# v27 + write-through (sc0 sc1) stores in all GEMM epilogues so the grid barrier's L2 write-back has less to flush
# baseline (speedup 1.0000x reference)
; __device__ __forceinline__ unsigned cvt_pk_bf16(float lo, float hi) { unsigned r; asm volatile("v_cvt_pk_bf16_f32 %0, %1, %2" : "=v"(r) : "v"(lo), "v"(hi)); return r; }
; __device__ __forceinline__ float gelu_tanh(float x) { const float y = x + 0.044715f * x * x * x; return x * __builtin_amdgcn_rcpf(1.0f + __builtin_amdgcn_exp2f(-2.302208198f * y)); }
;     __device__ __forceinline__ void operator()(const f32x4 (&acc)[2][2][4][2], const Unit& u, int wr, int wc, int fr, int fq) const {
;         const int row0 = u.pm * BM + wr * 64 + fr, col0 = u.pn * BM + wc * 32 + 8 * fq; const bool act = u.pn < nact;
; #pragma unroll
;         for (int ai = 0; ai < 2; ++ai)
; #pragma unroll
;             for (int m = 0; m < 4; ++m) { bf16_t* rowp = O + (size_t)u.ks * ks_stride + (size_t)(row0 + ai * HALF + m * 16) * ldc + col0;
; #pragma unroll
;                 for (int bj = 0; bj < 2; ++bj) { f32x4 v0 = acc[ai][bj][m][0] * ascale, v1 = acc[ai][bj][m][1] * ascale;
;                     if (act) {
; #pragma unroll
;                         for (int j = 0; j < 4; ++j) { v0[j] = gelu_tanh(v0[j]); v1[j] = gelu_tanh(v1[j]); } }
;                     u32x4 w; w.x = cvt_pk_bf16(v0[0], v0[1]); w.y = cvt_pk_bf16(v0[2], v0[3]); w.z = cvt_pk_bf16(v1[0], v1[1]); w.w = cvt_pk_bf16(v1[2], v1[3]);
;                     *(u32x4*)(rowp + bj * HALF) = w; } }
.LBB0_260:
	v_lshl_or_b32 v146, s22, 8, v151
	v_lshl_add_u32 v155, s2, 8, v1
	v_mov_b64_e32 v[148:149], s[8:9]
	v_ashrrev_i32_e32 v147, 31, v146
	v_mad_i64_i32 v[148:149], s[2:3], v155, s44, v[148:149]
	v_cvt_pk_bf16_f32 v126, v126, v127
	v_cvt_pk_bf16_f32 v127, v128, v129
	v_cvt_pk_bf16_f32 v128, v122, v123
	v_cndmask_b32_e64 v122, 0, 1, s[24:25]
	v_lshl_add_u64 v[148:149], v[146:147], 1, v[148:149]
	v_cmp_ne_u32_e64 s[2:3], 1, v122
	s_andn2_b64 vcc, exec, s[24:25]
	v_cvt_pk_bf16_f32 v129, v124, v125
	global_store_dwordx4 v[148:149], v[126:129], off sc0 sc1
	s_cbranch_vccnz .LBB0_262
	v_mul_f32_e32 v123, 0x3d372713, v114
	v_mul_f32_e32 v123, v114, v123
	v_mul_f32_e32 v124, 0x3d372713, v119
	v_fma_f32 v123, v114, v123, v114
	v_mul_f32_e32 v124, v119, v124
	v_mul_f32_e32 v123, 0xc0135761, v123
	v_fma_f32 v124, v119, v124, v119
	v_exp_f32_e32 v123, v123
	v_mul_f32_e32 v124, 0xc0135761, v124
	v_exp_f32_e32 v125, v124
	v_mul_f32_e32 v128, 0x3d372713, v121
	v_mul_f32_e32 v128, v121, v128
	v_fma_f32 v128, v121, v128, v121
	v_add_f32_e32 v123, 1.0, v123
	v_mul_f32_e32 v127, 0x3d372713, v116
	v_mul_f32_e32 v128, 0xc0135761, v128
	v_mul_f32_e32 v122, 0x3d372713, v118
	v_rcp_f32_e32 v124, v123
	v_add_f32_e32 v123, 1.0, v125
	v_mul_f32_e32 v125, 0x3d372713, v115
	v_mul_f32_e32 v126, 0x3d372713, v120
	v_mul_f32_e32 v127, v116, v127
	v_exp_f32_e32 v129, v128
	v_mul_f32_e32 v128, 0x3d372713, v117
	v_mul_f32_e32 v122, v118, v122
	v_mul_f32_e32 v125, v115, v125
	v_mul_f32_e32 v126, v120, v126
	v_fma_f32 v127, v116, v127, v116
	v_mul_f32_e32 v128, v117, v128
	v_fma_f32 v122, v118, v122, v118
	v_fma_f32 v125, v115, v125, v115
	v_fma_f32 v126, v120, v126, v120
	v_mul_f32_e32 v127, 0xc0135761, v127
	v_fma_f32 v128, v117, v128, v117
	v_mul_f32_e32 v122, 0xc0135761, v122
	v_mul_f32_e32 v125, 0xc0135761, v125
	v_mul_f32_e32 v126, 0xc0135761, v126
	v_exp_f32_e32 v127, v127
	v_mul_f32_e32 v128, 0xc0135761, v128
	v_exp_f32_e32 v122, v122
	v_exp_f32_e32 v125, v125
	v_exp_f32_e32 v126, v126
	v_exp_f32_e32 v156, v128
	v_add_f32_e32 v127, 1.0, v127
	v_add_f32_e32 v122, 1.0, v122
	v_add_f32_e32 v125, 1.0, v125
	v_add_f32_e32 v126, 1.0, v126
	v_rcp_f32_e32 v128, v127
	v_add_f32_e32 v127, 1.0, v129
	v_add_f32_e32 v129, 1.0, v156
	v_rcp_f32_e32 v122, v122
	v_rcp_f32_e32 v123, v123
	v_rcp_f32_e32 v126, v126
	v_rcp_f32_e32 v127, v127
	v_rcp_f32_e32 v129, v129
	v_rcp_f32_e32 v125, v125
	v_pk_mul_f32 v[118:119], v[118:119], v[122:123]
	v_pk_mul_f32 v[120:121], v[120:121], v[126:127]
	v_pk_mul_f32 v[116:117], v[116:117], v[128:129]
	v_pk_mul_f32 v[114:115], v[114:115], v[124:125]
.LBB0_262:
	s_and_b64 vcc, exec, s[2:3]
	v_cvt_pk_bf16_f32 v118, v118, v119
	v_cvt_pk_bf16_f32 v119, v120, v121
	v_cvt_pk_bf16_f32 v120, v114, v115
	v_cvt_pk_bf16_f32 v121, v116, v117
	global_store_dwordx4 v[148:149], v[118:121], off offset:256 sc0 sc1
	s_cbranch_vccnz .LBB0_264
	v_mul_f32_e32 v115, 0x3d372713, v106
	v_mul_f32_e32 v115, v106, v115
	v_mul_f32_e32 v116, 0x3d372713, v111
	v_fma_f32 v115, v106, v115, v106
	v_mul_f32_e32 v116, v111, v116
	v_mul_f32_e32 v115, 0xc0135761, v115
	v_fma_f32 v116, v111, v116, v111
	v_exp_f32_e32 v115, v115
	v_mul_f32_e32 v116, 0xc0135761, v116
	v_exp_f32_e32 v117, v116
	v_mul_f32_e32 v120, 0x3d372713, v113
	v_mul_f32_e32 v120, v113, v120
	v_fma_f32 v120, v113, v120, v113
	v_add_f32_e32 v115, 1.0, v115
	v_mul_f32_e32 v119, 0x3d372713, v108
	v_mul_f32_e32 v120, 0xc0135761, v120
	v_mul_f32_e32 v114, 0x3d372713, v110
	v_rcp_f32_e32 v116, v115
	v_add_f32_e32 v115, 1.0, v117
	v_mul_f32_e32 v117, 0x3d372713, v107
	v_mul_f32_e32 v118, 0x3d372713, v112
	v_mul_f32_e32 v119, v108, v119
	v_exp_f32_e32 v121, v120
	v_mul_f32_e32 v120, 0x3d372713, v109
	v_mul_f32_e32 v114, v110, v114
	v_mul_f32_e32 v117, v107, v117
	v_mul_f32_e32 v118, v112, v118
	v_fma_f32 v119, v108, v119, v108
	v_mul_f32_e32 v120, v109, v120
	v_fma_f32 v114, v110, v114, v110
	v_fma_f32 v117, v107, v117, v107
	v_fma_f32 v118, v112, v118, v112
	v_mul_f32_e32 v119, 0xc0135761, v119
	v_fma_f32 v120, v109, v120, v109
	v_mul_f32_e32 v114, 0xc0135761, v114
	v_mul_f32_e32 v117, 0xc0135761, v117
	v_mul_f32_e32 v118, 0xc0135761, v118
	v_exp_f32_e32 v119, v119
	v_mul_f32_e32 v120, 0xc0135761, v120
	v_exp_f32_e32 v114, v114
	v_exp_f32_e32 v117, v117
	v_exp_f32_e32 v118, v118
	v_exp_f32_e32 v122, v120
	v_add_f32_e32 v119, 1.0, v119
	v_add_f32_e32 v114, 1.0, v114
	v_add_f32_e32 v117, 1.0, v117
	v_add_f32_e32 v118, 1.0, v118
	v_rcp_f32_e32 v120, v119
	v_add_f32_e32 v119, 1.0, v121
	v_add_f32_e32 v121, 1.0, v122
	v_rcp_f32_e32 v114, v114
	v_rcp_f32_e32 v115, v115
	v_rcp_f32_e32 v118, v118
	v_rcp_f32_e32 v119, v119
	v_rcp_f32_e32 v121, v121
	v_rcp_f32_e32 v117, v117
	v_pk_mul_f32 v[110:111], v[110:111], v[114:115]
	v_pk_mul_f32 v[112:113], v[112:113], v[118:119]
	v_pk_mul_f32 v[108:109], v[108:109], v[120:121]
	v_pk_mul_f32 v[106:107], v[106:107], v[116:117]
; __device__ __forceinline__ unsigned cvt_pk_bf16(float lo, float hi) { unsigned r; asm volatile("v_cvt_pk_bf16_f32 %0, %1, %2" : "=v"(r) : "v"(lo), "v"(hi)); return r; }
; __device__ __forceinline__ float gelu_tanh(float x) { const float y = x + 0.044715f * x * x * x; return x * __builtin_amdgcn_rcpf(1.0f + __builtin_amdgcn_exp2f(-2.302208198f * y)); }
;     __device__ __forceinline__ void operator()(const f32x4 (&acc)[2][2][4][2], const Unit& u, int wr, int wc, int fr, int fq) const {
;         const int row0 = u.pm * BM + wr * 64 + fr, col0 = u.pn * BM + wc * 32 + 8 * fq; const bool act = u.pn < nact;
; #pragma unroll
;         for (int ai = 0; ai < 2; ++ai)
; #pragma unroll
;             for (int m = 0; m < 4; ++m) { bf16_t* rowp = O + (size_t)u.ks * ks_stride + (size_t)(row0 + ai * HALF + m * 16) * ldc + col0;
; #pragma unroll
;                 for (int bj = 0; bj < 2; ++bj) { f32x4 v0 = acc[ai][bj][m][0] * ascale, v1 = acc[ai][bj][m][1] * ascale;
;                     if (act) {
; #pragma unroll
;                         for (int j = 0; j < 4; ++j) { v0[j] = gelu_tanh(v0[j]); v1[j] = gelu_tanh(v1[j]); } }
;                     u32x4 w; w.x = cvt_pk_bf16(v0[0], v0[1]); w.y = cvt_pk_bf16(v0[2], v0[3]); w.z = cvt_pk_bf16(v1[0], v1[1]); w.w = cvt_pk_bf16(v1[2], v1[3]);
;                     *(u32x4*)(rowp + bj * HALF) = w; } }
.LBB0_264:
	v_or_b32_e32 v116, 16, v155
	v_mov_b64_e32 v[114:115], s[8:9]
	v_mad_i64_i32 v[114:115], s[24:25], v116, s44, v[114:115]
	v_lshl_add_u64 v[114:115], v[146:147], 1, v[114:115]
	s_and_b64 vcc, exec, s[2:3]
	v_cvt_pk_bf16_f32 v110, v110, v111
	v_cvt_pk_bf16_f32 v111, v112, v113
	v_cvt_pk_bf16_f32 v112, v106, v107
	v_cvt_pk_bf16_f32 v113, v108, v109
	global_store_dwordx4 v[114:115], v[110:113], off sc0 sc1
	s_cbranch_vccnz .LBB0_266
	v_mul_f32_e32 v107, 0x3d372713, v98
	v_mul_f32_e32 v107, v98, v107
	v_mul_f32_e32 v108, 0x3d372713, v103
	v_fma_f32 v107, v98, v107, v98
	v_mul_f32_e32 v108, v103, v108
	v_mul_f32_e32 v107, 0xc0135761, v107
	v_fma_f32 v108, v103, v108, v103
	v_exp_f32_e32 v107, v107
	v_mul_f32_e32 v108, 0xc0135761, v108
	v_exp_f32_e32 v109, v108
	v_mul_f32_e32 v112, 0x3d372713, v105
	v_mul_f32_e32 v112, v105, v112
	v_fma_f32 v112, v105, v112, v105
	v_add_f32_e32 v107, 1.0, v107
	v_mul_f32_e32 v111, 0x3d372713, v100
	v_mul_f32_e32 v112, 0xc0135761, v112
	v_mul_f32_e32 v106, 0x3d372713, v102
	v_rcp_f32_e32 v108, v107
	v_add_f32_e32 v107, 1.0, v109
	v_mul_f32_e32 v109, 0x3d372713, v99
	v_mul_f32_e32 v110, 0x3d372713, v104
	v_mul_f32_e32 v111, v100, v111
	v_exp_f32_e32 v113, v112
	v_mul_f32_e32 v112, 0x3d372713, v101
	v_mul_f32_e32 v106, v102, v106
	v_mul_f32_e32 v109, v99, v109
	v_mul_f32_e32 v110, v104, v110
	v_fma_f32 v111, v100, v111, v100
	v_mul_f32_e32 v112, v101, v112
	v_fma_f32 v106, v102, v106, v102
	v_fma_f32 v109, v99, v109, v99
	v_fma_f32 v110, v104, v110, v104
	v_mul_f32_e32 v111, 0xc0135761, v111
	v_fma_f32 v112, v101, v112, v101
	v_mul_f32_e32 v106, 0xc0135761, v106
	v_mul_f32_e32 v109, 0xc0135761, v109
	v_mul_f32_e32 v110, 0xc0135761, v110
	v_exp_f32_e32 v111, v111
	v_mul_f32_e32 v112, 0xc0135761, v112
	v_exp_f32_e32 v106, v106
	v_exp_f32_e32 v109, v109
	v_exp_f32_e32 v110, v110
	v_exp_f32_e32 v116, v112
	v_add_f32_e32 v111, 1.0, v111
	v_add_f32_e32 v106, 1.0, v106
	v_add_f32_e32 v109, 1.0, v109
	v_add_f32_e32 v110, 1.0, v110
	v_rcp_f32_e32 v112, v111
	v_add_f32_e32 v111, 1.0, v113
	v_add_f32_e32 v113, 1.0, v116
	v_rcp_f32_e32 v106, v106
	v_rcp_f32_e32 v107, v107
	v_rcp_f32_e32 v110, v110
	v_rcp_f32_e32 v111, v111
	v_rcp_f32_e32 v113, v113
	v_rcp_f32_e32 v109, v109
	v_pk_mul_f32 v[102:103], v[102:103], v[106:107]
	v_pk_mul_f32 v[104:105], v[104:105], v[110:111]
	v_pk_mul_f32 v[100:101], v[100:101], v[112:113]
	v_pk_mul_f32 v[98:99], v[98:99], v[108:109]
.LBB0_266:
	s_and_b64 vcc, exec, s[2:3]
	v_cvt_pk_bf16_f32 v102, v102, v103
	v_cvt_pk_bf16_f32 v103, v104, v105
	v_cvt_pk_bf16_f32 v104, v98, v99
	v_cvt_pk_bf16_f32 v105, v100, v101
	global_store_dwordx4 v[114:115], v[102:105], off offset:256 sc0 sc1
	s_cbranch_vccnz .LBB0_268
	v_mul_f32_e32 v99, 0x3d372713, v90
	v_mul_f32_e32 v99, v90, v99
	v_mul_f32_e32 v100, 0x3d372713, v95
	v_fma_f32 v99, v90, v99, v90
	v_mul_f32_e32 v100, v95, v100
	v_mul_f32_e32 v99, 0xc0135761, v99
	v_fma_f32 v100, v95, v100, v95
	v_exp_f32_e32 v99, v99
	v_mul_f32_e32 v100, 0xc0135761, v100
	v_exp_f32_e32 v101, v100
	v_mul_f32_e32 v104, 0x3d372713, v97
	v_mul_f32_e32 v104, v97, v104
	v_fma_f32 v104, v97, v104, v97
	v_add_f32_e32 v99, 1.0, v99
	v_mul_f32_e32 v103, 0x3d372713, v92
	v_mul_f32_e32 v104, 0xc0135761, v104
	v_mul_f32_e32 v98, 0x3d372713, v94
	v_rcp_f32_e32 v100, v99
	v_add_f32_e32 v99, 1.0, v101
	v_mul_f32_e32 v101, 0x3d372713, v91
	v_mul_f32_e32 v102, 0x3d372713, v96
	v_mul_f32_e32 v103, v92, v103
	v_exp_f32_e32 v105, v104
	v_mul_f32_e32 v104, 0x3d372713, v93
	v_mul_f32_e32 v98, v94, v98
	v_mul_f32_e32 v101, v91, v101
	v_mul_f32_e32 v102, v96, v102
	v_fma_f32 v103, v92, v103, v92
	v_mul_f32_e32 v104, v93, v104
	v_fma_f32 v98, v94, v98, v94
	v_fma_f32 v101, v91, v101, v91
	v_fma_f32 v102, v96, v102, v96
	v_mul_f32_e32 v103, 0xc0135761, v103
	v_fma_f32 v104, v93, v104, v93
	v_mul_f32_e32 v98, 0xc0135761, v98
	v_mul_f32_e32 v101, 0xc0135761, v101
	v_mul_f32_e32 v102, 0xc0135761, v102
	v_exp_f32_e32 v103, v103
	v_mul_f32_e32 v104, 0xc0135761, v104
	v_exp_f32_e32 v98, v98
	v_exp_f32_e32 v101, v101
	v_exp_f32_e32 v102, v102
	v_exp_f32_e32 v106, v104
	v_add_f32_e32 v103, 1.0, v103
	v_add_f32_e32 v98, 1.0, v98
	v_add_f32_e32 v101, 1.0, v101
	v_add_f32_e32 v102, 1.0, v102
	v_rcp_f32_e32 v104, v103
	v_add_f32_e32 v103, 1.0, v105
	v_add_f32_e32 v105, 1.0, v106
	v_rcp_f32_e32 v98, v98
	v_rcp_f32_e32 v99, v99
	v_rcp_f32_e32 v102, v102
	v_rcp_f32_e32 v103, v103
	v_rcp_f32_e32 v105, v105
	v_rcp_f32_e32 v101, v101
	v_pk_mul_f32 v[94:95], v[94:95], v[98:99]
	v_pk_mul_f32 v[96:97], v[96:97], v[102:103]
	v_pk_mul_f32 v[92:93], v[92:93], v[104:105]
	v_pk_mul_f32 v[90:91], v[90:91], v[100:101]
; __device__ __forceinline__ unsigned cvt_pk_bf16(float lo, float hi) { unsigned r; asm volatile("v_cvt_pk_bf16_f32 %0, %1, %2" : "=v"(r) : "v"(lo), "v"(hi)); return r; }
; __device__ __forceinline__ float gelu_tanh(float x) { const float y = x + 0.044715f * x * x * x; return x * __builtin_amdgcn_rcpf(1.0f + __builtin_amdgcn_exp2f(-2.302208198f * y)); }
;     __device__ __forceinline__ void operator()(const f32x4 (&acc)[2][2][4][2], const Unit& u, int wr, int wc, int fr, int fq) const {
;         const int row0 = u.pm * BM + wr * 64 + fr, col0 = u.pn * BM + wc * 32 + 8 * fq; const bool act = u.pn < nact;
; #pragma unroll
;         for (int ai = 0; ai < 2; ++ai)
; #pragma unroll
;             for (int m = 0; m < 4; ++m) { bf16_t* rowp = O + (size_t)u.ks * ks_stride + (size_t)(row0 + ai * HALF + m * 16) * ldc + col0;
; #pragma unroll
;                 for (int bj = 0; bj < 2; ++bj) { f32x4 v0 = acc[ai][bj][m][0] * ascale, v1 = acc[ai][bj][m][1] * ascale;
;                     if (act) {
; #pragma unroll
;                         for (int j = 0; j < 4; ++j) { v0[j] = gelu_tanh(v0[j]); v1[j] = gelu_tanh(v1[j]); } }
;                     u32x4 w; w.x = cvt_pk_bf16(v0[0], v0[1]); w.y = cvt_pk_bf16(v0[2], v0[3]); w.z = cvt_pk_bf16(v1[0], v1[1]); w.w = cvt_pk_bf16(v1[2], v1[3]);
;                     *(u32x4*)(rowp + bj * HALF) = w; } }
.LBB0_268:
	v_or_b32_e32 v100, 32, v155
	v_mov_b64_e32 v[98:99], s[8:9]
	v_mad_i64_i32 v[98:99], s[24:25], v100, s44, v[98:99]
	v_lshl_add_u64 v[98:99], v[146:147], 1, v[98:99]
	s_and_b64 vcc, exec, s[2:3]
	v_cvt_pk_bf16_f32 v94, v94, v95
	v_cvt_pk_bf16_f32 v95, v96, v97
	v_cvt_pk_bf16_f32 v96, v90, v91
	v_cvt_pk_bf16_f32 v97, v92, v93
	global_store_dwordx4 v[98:99], v[94:97], off sc0 sc1
	s_cbranch_vccnz .LBB0_270
	v_mul_f32_e32 v91, 0x3d372713, v82
	v_mul_f32_e32 v91, v82, v91
	v_mul_f32_e32 v92, 0x3d372713, v87
	v_fma_f32 v91, v82, v91, v82
	v_mul_f32_e32 v92, v87, v92
	v_mul_f32_e32 v91, 0xc0135761, v91
	v_fma_f32 v92, v87, v92, v87
	v_exp_f32_e32 v91, v91
	v_mul_f32_e32 v92, 0xc0135761, v92
	v_exp_f32_e32 v93, v92
	v_mul_f32_e32 v96, 0x3d372713, v89
	v_mul_f32_e32 v96, v89, v96
	v_fma_f32 v96, v89, v96, v89
	v_add_f32_e32 v91, 1.0, v91
	v_mul_f32_e32 v95, 0x3d372713, v84
	v_mul_f32_e32 v96, 0xc0135761, v96
	v_mul_f32_e32 v90, 0x3d372713, v86
	v_rcp_f32_e32 v92, v91
	v_add_f32_e32 v91, 1.0, v93
	v_mul_f32_e32 v93, 0x3d372713, v83
	v_mul_f32_e32 v94, 0x3d372713, v88
	v_mul_f32_e32 v95, v84, v95
	v_exp_f32_e32 v97, v96
	v_mul_f32_e32 v96, 0x3d372713, v85
	v_mul_f32_e32 v90, v86, v90
	v_mul_f32_e32 v93, v83, v93
	v_mul_f32_e32 v94, v88, v94
	v_fma_f32 v95, v84, v95, v84
	v_mul_f32_e32 v96, v85, v96
	v_fma_f32 v90, v86, v90, v86
	v_fma_f32 v93, v83, v93, v83
	v_fma_f32 v94, v88, v94, v88
	v_mul_f32_e32 v95, 0xc0135761, v95
	v_fma_f32 v96, v85, v96, v85
	v_mul_f32_e32 v90, 0xc0135761, v90
	v_mul_f32_e32 v93, 0xc0135761, v93
	v_mul_f32_e32 v94, 0xc0135761, v94
	v_exp_f32_e32 v95, v95
	v_mul_f32_e32 v96, 0xc0135761, v96
	v_exp_f32_e32 v90, v90
	v_exp_f32_e32 v93, v93
	v_exp_f32_e32 v94, v94
	v_exp_f32_e32 v100, v96
	v_add_f32_e32 v95, 1.0, v95
	v_add_f32_e32 v90, 1.0, v90
	v_add_f32_e32 v93, 1.0, v93
	v_add_f32_e32 v94, 1.0, v94
	v_rcp_f32_e32 v96, v95
	v_add_f32_e32 v95, 1.0, v97
	v_add_f32_e32 v97, 1.0, v100
	v_rcp_f32_e32 v90, v90
	v_rcp_f32_e32 v91, v91
	v_rcp_f32_e32 v94, v94
	v_rcp_f32_e32 v95, v95
	v_rcp_f32_e32 v97, v97
	v_rcp_f32_e32 v93, v93
	v_pk_mul_f32 v[86:87], v[86:87], v[90:91]
	v_pk_mul_f32 v[88:89], v[88:89], v[94:95]
	v_pk_mul_f32 v[84:85], v[84:85], v[96:97]
	v_pk_mul_f32 v[82:83], v[82:83], v[92:93]
.LBB0_270:
	s_and_b64 vcc, exec, s[2:3]
	v_cvt_pk_bf16_f32 v86, v86, v87
	v_cvt_pk_bf16_f32 v87, v88, v89
	v_cvt_pk_bf16_f32 v88, v82, v83
	v_cvt_pk_bf16_f32 v89, v84, v85
	global_store_dwordx4 v[98:99], v[86:89], off offset:256 sc0 sc1
	s_cbranch_vccnz .LBB0_272
	v_mul_f32_e32 v83, 0x3d372713, v74
	v_mul_f32_e32 v83, v74, v83
	v_mul_f32_e32 v84, 0x3d372713, v79
	v_fma_f32 v83, v74, v83, v74
	v_mul_f32_e32 v84, v79, v84
	v_mul_f32_e32 v83, 0xc0135761, v83
	v_fma_f32 v84, v79, v84, v79
	v_exp_f32_e32 v83, v83
	v_mul_f32_e32 v84, 0xc0135761, v84
	v_exp_f32_e32 v85, v84
	v_mul_f32_e32 v88, 0x3d372713, v81
	v_mul_f32_e32 v88, v81, v88
	v_fma_f32 v88, v81, v88, v81
	v_add_f32_e32 v83, 1.0, v83
	v_mul_f32_e32 v87, 0x3d372713, v76
	v_mul_f32_e32 v88, 0xc0135761, v88
	v_mul_f32_e32 v82, 0x3d372713, v78
	v_rcp_f32_e32 v84, v83
	v_add_f32_e32 v83, 1.0, v85
	v_mul_f32_e32 v85, 0x3d372713, v75
	v_mul_f32_e32 v86, 0x3d372713, v80
	v_mul_f32_e32 v87, v76, v87
	v_exp_f32_e32 v89, v88
	v_mul_f32_e32 v88, 0x3d372713, v77
	v_mul_f32_e32 v82, v78, v82
	v_mul_f32_e32 v85, v75, v85
	v_mul_f32_e32 v86, v80, v86
	v_fma_f32 v87, v76, v87, v76
	v_mul_f32_e32 v88, v77, v88
	v_fma_f32 v82, v78, v82, v78
	v_fma_f32 v85, v75, v85, v75
	v_fma_f32 v86, v80, v86, v80
	v_mul_f32_e32 v87, 0xc0135761, v87
	v_fma_f32 v88, v77, v88, v77
	v_mul_f32_e32 v82, 0xc0135761, v82
	v_mul_f32_e32 v85, 0xc0135761, v85
	v_mul_f32_e32 v86, 0xc0135761, v86
	v_exp_f32_e32 v87, v87
	v_mul_f32_e32 v88, 0xc0135761, v88
	v_exp_f32_e32 v82, v82
	v_exp_f32_e32 v85, v85
	v_exp_f32_e32 v86, v86
	v_exp_f32_e32 v90, v88
	v_add_f32_e32 v87, 1.0, v87
	v_add_f32_e32 v82, 1.0, v82
	v_add_f32_e32 v85, 1.0, v85
	v_add_f32_e32 v86, 1.0, v86
	v_rcp_f32_e32 v88, v87
	v_add_f32_e32 v87, 1.0, v89
	v_add_f32_e32 v89, 1.0, v90
	v_rcp_f32_e32 v82, v82
	v_rcp_f32_e32 v83, v83
	v_rcp_f32_e32 v86, v86
	v_rcp_f32_e32 v87, v87
	v_rcp_f32_e32 v89, v89
	v_rcp_f32_e32 v85, v85
	v_pk_mul_f32 v[78:79], v[78:79], v[82:83]
	v_pk_mul_f32 v[80:81], v[80:81], v[86:87]
	v_pk_mul_f32 v[76:77], v[76:77], v[88:89]
	v_pk_mul_f32 v[74:75], v[74:75], v[84:85]
.LBB0_272:
	v_or_b32_e32 v84, 48, v155
	v_mov_b64_e32 v[82:83], s[8:9]
	v_mad_i64_i32 v[82:83], s[24:25], v84, s44, v[82:83]
	v_lshl_add_u64 v[82:83], v[146:147], 1, v[82:83]
	s_and_b64 vcc, exec, s[2:3]
	v_cvt_pk_bf16_f32 v78, v78, v79
	v_cvt_pk_bf16_f32 v79, v80, v81
	v_cvt_pk_bf16_f32 v80, v74, v75
	v_cvt_pk_bf16_f32 v81, v76, v77
	global_store_dwordx4 v[82:83], v[78:81], off sc0 sc1
	s_cbranch_vccnz .LBB0_274
	v_mul_f32_e32 v75, 0x3d372713, v66
	v_mul_f32_e32 v75, v66, v75
	v_mul_f32_e32 v76, 0x3d372713, v71
	v_fma_f32 v75, v66, v75, v66
	v_mul_f32_e32 v76, v71, v76
	v_mul_f32_e32 v75, 0xc0135761, v75
	v_fma_f32 v76, v71, v76, v71
	v_exp_f32_e32 v75, v75
	v_mul_f32_e32 v76, 0xc0135761, v76
	v_exp_f32_e32 v77, v76
	v_mul_f32_e32 v80, 0x3d372713, v73
	v_mul_f32_e32 v80, v73, v80
	v_fma_f32 v80, v73, v80, v73
	v_add_f32_e32 v75, 1.0, v75
	v_mul_f32_e32 v79, 0x3d372713, v68
	v_mul_f32_e32 v80, 0xc0135761, v80
	v_mul_f32_e32 v74, 0x3d372713, v70
	v_rcp_f32_e32 v76, v75
	v_add_f32_e32 v75, 1.0, v77
	v_mul_f32_e32 v77, 0x3d372713, v67
	v_mul_f32_e32 v78, 0x3d372713, v72
	v_mul_f32_e32 v79, v68, v79
	v_exp_f32_e32 v81, v80
	v_mul_f32_e32 v80, 0x3d372713, v69
	v_mul_f32_e32 v74, v70, v74
	v_mul_f32_e32 v77, v67, v77
	v_mul_f32_e32 v78, v72, v78
	v_fma_f32 v79, v68, v79, v68
	v_mul_f32_e32 v80, v69, v80
	v_fma_f32 v74, v70, v74, v70
	v_fma_f32 v77, v67, v77, v67
	v_fma_f32 v78, v72, v78, v72
	v_mul_f32_e32 v79, 0xc0135761, v79
	v_fma_f32 v80, v69, v80, v69
	v_mul_f32_e32 v74, 0xc0135761, v74
	v_mul_f32_e32 v77, 0xc0135761, v77
	v_mul_f32_e32 v78, 0xc0135761, v78
	v_exp_f32_e32 v79, v79
	v_mul_f32_e32 v80, 0xc0135761, v80
	v_exp_f32_e32 v74, v74
	v_exp_f32_e32 v77, v77
	v_exp_f32_e32 v78, v78
	v_exp_f32_e32 v84, v80
	v_add_f32_e32 v79, 1.0, v79
	v_add_f32_e32 v74, 1.0, v74
	v_add_f32_e32 v77, 1.0, v77
	v_add_f32_e32 v78, 1.0, v78
	v_rcp_f32_e32 v80, v79
	v_add_f32_e32 v79, 1.0, v81
	v_add_f32_e32 v81, 1.0, v84
	v_rcp_f32_e32 v74, v74
	v_rcp_f32_e32 v75, v75
	v_rcp_f32_e32 v78, v78
	v_rcp_f32_e32 v79, v79
	v_rcp_f32_e32 v81, v81
	v_rcp_f32_e32 v77, v77
	v_pk_mul_f32 v[70:71], v[70:71], v[74:75]
	v_pk_mul_f32 v[72:73], v[72:73], v[78:79]
	v_pk_mul_f32 v[68:69], v[68:69], v[80:81]
	v_pk_mul_f32 v[66:67], v[66:67], v[76:77]
; __device__ __forceinline__ unsigned cvt_pk_bf16(float lo, float hi) { unsigned r; asm volatile("v_cvt_pk_bf16_f32 %0, %1, %2" : "=v"(r) : "v"(lo), "v"(hi)); return r; }
; __device__ __forceinline__ float gelu_tanh(float x) { const float y = x + 0.044715f * x * x * x; return x * __builtin_amdgcn_rcpf(1.0f + __builtin_amdgcn_exp2f(-2.302208198f * y)); }
;     __device__ __forceinline__ void operator()(const f32x4 (&acc)[2][2][4][2], const Unit& u, int wr, int wc, int fr, int fq) const {
;         const int row0 = u.pm * BM + wr * 64 + fr, col0 = u.pn * BM + wc * 32 + 8 * fq; const bool act = u.pn < nact;
; #pragma unroll
;         for (int ai = 0; ai < 2; ++ai)
; #pragma unroll
;             for (int m = 0; m < 4; ++m) { bf16_t* rowp = O + (size_t)u.ks * ks_stride + (size_t)(row0 + ai * HALF + m * 16) * ldc + col0;
; #pragma unroll
;                 for (int bj = 0; bj < 2; ++bj) { f32x4 v0 = acc[ai][bj][m][0] * ascale, v1 = acc[ai][bj][m][1] * ascale;
;                     if (act) {
; #pragma unroll
;                         for (int j = 0; j < 4; ++j) { v0[j] = gelu_tanh(v0[j]); v1[j] = gelu_tanh(v1[j]); } }
;                     u32x4 w; w.x = cvt_pk_bf16(v0[0], v0[1]); w.y = cvt_pk_bf16(v0[2], v0[3]); w.z = cvt_pk_bf16(v1[0], v1[1]); w.w = cvt_pk_bf16(v1[2], v1[3]);
;                     *(u32x4*)(rowp + bj * HALF) = w; } }
.LBB0_274:
	s_and_b64 vcc, exec, s[2:3]
	v_cvt_pk_bf16_f32 v70, v70, v71
	v_cvt_pk_bf16_f32 v71, v72, v73
	v_cvt_pk_bf16_f32 v72, v66, v67
	v_cvt_pk_bf16_f32 v73, v68, v69
	global_store_dwordx4 v[82:83], v[70:73], off offset:256 sc0 sc1
	s_cbranch_vccnz .LBB0_276
	v_mul_f32_e32 v67, 0x3d372713, v58
	v_mul_f32_e32 v67, v58, v67
	v_mul_f32_e32 v68, 0x3d372713, v63
	v_fma_f32 v67, v58, v67, v58
	v_mul_f32_e32 v68, v63, v68
	v_mul_f32_e32 v67, 0xc0135761, v67
	v_fma_f32 v68, v63, v68, v63
	v_exp_f32_e32 v67, v67
	v_mul_f32_e32 v68, 0xc0135761, v68
	v_exp_f32_e32 v69, v68
	v_mul_f32_e32 v72, 0x3d372713, v65
	v_mul_f32_e32 v72, v65, v72
	v_fma_f32 v72, v65, v72, v65
	v_add_f32_e32 v67, 1.0, v67
	v_mul_f32_e32 v71, 0x3d372713, v60
	v_mul_f32_e32 v72, 0xc0135761, v72
	v_mul_f32_e32 v66, 0x3d372713, v62
	v_rcp_f32_e32 v68, v67
	v_add_f32_e32 v67, 1.0, v69
	v_mul_f32_e32 v69, 0x3d372713, v59
	v_mul_f32_e32 v70, 0x3d372713, v64
	v_mul_f32_e32 v71, v60, v71
	v_exp_f32_e32 v73, v72
	v_mul_f32_e32 v72, 0x3d372713, v61
	v_mul_f32_e32 v66, v62, v66
	v_mul_f32_e32 v69, v59, v69
	v_mul_f32_e32 v70, v64, v70
	v_fma_f32 v71, v60, v71, v60
	v_mul_f32_e32 v72, v61, v72
	v_fma_f32 v66, v62, v66, v62
	v_fma_f32 v69, v59, v69, v59
	v_fma_f32 v70, v64, v70, v64
	v_mul_f32_e32 v71, 0xc0135761, v71
	v_fma_f32 v72, v61, v72, v61
	v_mul_f32_e32 v66, 0xc0135761, v66
	v_mul_f32_e32 v69, 0xc0135761, v69
	v_mul_f32_e32 v70, 0xc0135761, v70
	v_exp_f32_e32 v71, v71
	v_mul_f32_e32 v72, 0xc0135761, v72
	v_exp_f32_e32 v66, v66
	v_exp_f32_e32 v69, v69
	v_exp_f32_e32 v70, v70
	v_exp_f32_e32 v74, v72
	v_add_f32_e32 v71, 1.0, v71
	v_add_f32_e32 v66, 1.0, v66
	v_add_f32_e32 v69, 1.0, v69
	v_add_f32_e32 v70, 1.0, v70
	v_rcp_f32_e32 v72, v71
	v_add_f32_e32 v71, 1.0, v73
	v_add_f32_e32 v73, 1.0, v74
	v_rcp_f32_e32 v66, v66
	v_rcp_f32_e32 v67, v67
	v_rcp_f32_e32 v70, v70
	v_rcp_f32_e32 v71, v71
	v_rcp_f32_e32 v73, v73
	v_rcp_f32_e32 v69, v69
	v_pk_mul_f32 v[62:63], v[62:63], v[66:67]
	v_pk_mul_f32 v[64:65], v[64:65], v[70:71]
	v_pk_mul_f32 v[60:61], v[60:61], v[72:73]
	v_pk_mul_f32 v[58:59], v[58:59], v[68:69]
.LBB0_276:
	v_add_u32_e32 v68, 0x80, v155
	v_mov_b64_e32 v[66:67], s[8:9]
	v_mad_i64_i32 v[66:67], s[24:25], v68, s44, v[66:67]
	v_lshl_add_u64 v[66:67], v[146:147], 1, v[66:67]
	s_and_b64 vcc, exec, s[2:3]
	v_cvt_pk_bf16_f32 v62, v62, v63
	v_cvt_pk_bf16_f32 v63, v64, v65
	v_cvt_pk_bf16_f32 v64, v58, v59
	v_cvt_pk_bf16_f32 v65, v60, v61
	global_store_dwordx4 v[66:67], v[62:65], off sc0 sc1
	s_cbranch_vccnz .LBB0_278
	v_mul_f32_e32 v59, 0x3d372713, v50
	v_mul_f32_e32 v59, v50, v59
	v_mul_f32_e32 v60, 0x3d372713, v55
	v_fma_f32 v59, v50, v59, v50
	v_mul_f32_e32 v60, v55, v60
	v_mul_f32_e32 v59, 0xc0135761, v59
	v_fma_f32 v60, v55, v60, v55
	v_exp_f32_e32 v59, v59
	v_mul_f32_e32 v60, 0xc0135761, v60
	v_exp_f32_e32 v61, v60
	v_mul_f32_e32 v64, 0x3d372713, v57
	v_mul_f32_e32 v64, v57, v64
	v_fma_f32 v64, v57, v64, v57
	v_add_f32_e32 v59, 1.0, v59
	v_mul_f32_e32 v63, 0x3d372713, v52
	v_mul_f32_e32 v64, 0xc0135761, v64
	v_mul_f32_e32 v58, 0x3d372713, v54
	v_rcp_f32_e32 v60, v59
	v_add_f32_e32 v59, 1.0, v61
	v_mul_f32_e32 v61, 0x3d372713, v51
	v_mul_f32_e32 v62, 0x3d372713, v56
	v_mul_f32_e32 v63, v52, v63
	v_exp_f32_e32 v65, v64
	v_mul_f32_e32 v64, 0x3d372713, v53
	v_mul_f32_e32 v58, v54, v58
	v_mul_f32_e32 v61, v51, v61
	v_mul_f32_e32 v62, v56, v62
	v_fma_f32 v63, v52, v63, v52
	v_mul_f32_e32 v64, v53, v64
	v_fma_f32 v58, v54, v58, v54
	v_fma_f32 v61, v51, v61, v51
	v_fma_f32 v62, v56, v62, v56
	v_mul_f32_e32 v63, 0xc0135761, v63
	v_fma_f32 v64, v53, v64, v53
	v_mul_f32_e32 v58, 0xc0135761, v58
	v_mul_f32_e32 v61, 0xc0135761, v61
	v_mul_f32_e32 v62, 0xc0135761, v62
	v_exp_f32_e32 v63, v63
	v_mul_f32_e32 v64, 0xc0135761, v64
	v_exp_f32_e32 v58, v58
	v_exp_f32_e32 v61, v61
	v_exp_f32_e32 v62, v62
	v_exp_f32_e32 v68, v64
	v_add_f32_e32 v63, 1.0, v63
	v_add_f32_e32 v58, 1.0, v58
	v_add_f32_e32 v61, 1.0, v61
	v_add_f32_e32 v62, 1.0, v62
	v_rcp_f32_e32 v64, v63
	v_add_f32_e32 v63, 1.0, v65
	v_add_f32_e32 v65, 1.0, v68
	v_rcp_f32_e32 v58, v58
	v_rcp_f32_e32 v59, v59
	v_rcp_f32_e32 v62, v62
	v_rcp_f32_e32 v63, v63
	v_rcp_f32_e32 v65, v65
	v_rcp_f32_e32 v61, v61
	v_pk_mul_f32 v[54:55], v[54:55], v[58:59]
	v_pk_mul_f32 v[56:57], v[56:57], v[62:63]
	v_pk_mul_f32 v[52:53], v[52:53], v[64:65]
	v_pk_mul_f32 v[50:51], v[50:51], v[60:61]
.LBB0_278:
	s_and_b64 vcc, exec, s[2:3]
	v_cvt_pk_bf16_f32 v54, v54, v55
	v_cvt_pk_bf16_f32 v55, v56, v57
	v_cvt_pk_bf16_f32 v56, v50, v51
	v_cvt_pk_bf16_f32 v57, v52, v53
	global_store_dwordx4 v[66:67], v[54:57], off offset:256 sc0 sc1
	s_cbranch_vccnz .LBB0_280
	v_mul_f32_e32 v51, 0x3d372713, v42
	v_mul_f32_e32 v51, v42, v51
	v_mul_f32_e32 v52, 0x3d372713, v47
	v_fma_f32 v51, v42, v51, v42
	v_mul_f32_e32 v52, v47, v52
	v_mul_f32_e32 v51, 0xc0135761, v51
	v_fma_f32 v52, v47, v52, v47
	v_exp_f32_e32 v51, v51
	v_mul_f32_e32 v52, 0xc0135761, v52
	v_exp_f32_e32 v53, v52
	v_mul_f32_e32 v56, 0x3d372713, v49
	v_mul_f32_e32 v56, v49, v56
	v_fma_f32 v56, v49, v56, v49
	v_add_f32_e32 v51, 1.0, v51
	v_mul_f32_e32 v55, 0x3d372713, v44
	v_mul_f32_e32 v56, 0xc0135761, v56
	v_mul_f32_e32 v50, 0x3d372713, v46
	v_rcp_f32_e32 v52, v51
	v_add_f32_e32 v51, 1.0, v53
	v_mul_f32_e32 v53, 0x3d372713, v43
	v_mul_f32_e32 v54, 0x3d372713, v48
	v_mul_f32_e32 v55, v44, v55
	v_exp_f32_e32 v57, v56
	v_mul_f32_e32 v56, 0x3d372713, v45
	v_mul_f32_e32 v50, v46, v50
	v_mul_f32_e32 v53, v43, v53
	v_mul_f32_e32 v54, v48, v54
	v_fma_f32 v55, v44, v55, v44
	v_mul_f32_e32 v56, v45, v56
	v_fma_f32 v50, v46, v50, v46
	v_fma_f32 v53, v43, v53, v43
	v_fma_f32 v54, v48, v54, v48
	v_mul_f32_e32 v55, 0xc0135761, v55
	v_fma_f32 v56, v45, v56, v45
	v_mul_f32_e32 v50, 0xc0135761, v50
	v_mul_f32_e32 v53, 0xc0135761, v53
	v_mul_f32_e32 v54, 0xc0135761, v54
	v_exp_f32_e32 v55, v55
	v_mul_f32_e32 v56, 0xc0135761, v56
	v_exp_f32_e32 v50, v50
	v_exp_f32_e32 v53, v53
	v_exp_f32_e32 v54, v54
	v_exp_f32_e32 v58, v56
	v_add_f32_e32 v55, 1.0, v55
	v_add_f32_e32 v50, 1.0, v50
	v_add_f32_e32 v53, 1.0, v53
	v_add_f32_e32 v54, 1.0, v54
	v_rcp_f32_e32 v56, v55
	v_add_f32_e32 v55, 1.0, v57
	v_add_f32_e32 v57, 1.0, v58
	v_rcp_f32_e32 v50, v50
	v_rcp_f32_e32 v51, v51
	v_rcp_f32_e32 v54, v54
	v_rcp_f32_e32 v55, v55
	v_rcp_f32_e32 v57, v57
	v_rcp_f32_e32 v53, v53
	v_pk_mul_f32 v[46:47], v[46:47], v[50:51]
	v_pk_mul_f32 v[48:49], v[48:49], v[54:55]
	v_pk_mul_f32 v[44:45], v[44:45], v[56:57]
	v_pk_mul_f32 v[42:43], v[42:43], v[52:53]
; __device__ __forceinline__ unsigned cvt_pk_bf16(float lo, float hi) { unsigned r; asm volatile("v_cvt_pk_bf16_f32 %0, %1, %2" : "=v"(r) : "v"(lo), "v"(hi)); return r; }
; __device__ __forceinline__ float gelu_tanh(float x) { const float y = x + 0.044715f * x * x * x; return x * __builtin_amdgcn_rcpf(1.0f + __builtin_amdgcn_exp2f(-2.302208198f * y)); }
;     __device__ __forceinline__ void operator()(const f32x4 (&acc)[2][2][4][2], const Unit& u, int wr, int wc, int fr, int fq) const {
;         const int row0 = u.pm * BM + wr * 64 + fr, col0 = u.pn * BM + wc * 32 + 8 * fq; const bool act = u.pn < nact;
; #pragma unroll
;         for (int ai = 0; ai < 2; ++ai)
; #pragma unroll
;             for (int m = 0; m < 4; ++m) { bf16_t* rowp = O + (size_t)u.ks * ks_stride + (size_t)(row0 + ai * HALF + m * 16) * ldc + col0;
; #pragma unroll
;                 for (int bj = 0; bj < 2; ++bj) { f32x4 v0 = acc[ai][bj][m][0] * ascale, v1 = acc[ai][bj][m][1] * ascale;
;                     if (act) {
; #pragma unroll
;                         for (int j = 0; j < 4; ++j) { v0[j] = gelu_tanh(v0[j]); v1[j] = gelu_tanh(v1[j]); } }
;                     u32x4 w; w.x = cvt_pk_bf16(v0[0], v0[1]); w.y = cvt_pk_bf16(v0[2], v0[3]); w.z = cvt_pk_bf16(v1[0], v1[1]); w.w = cvt_pk_bf16(v1[2], v1[3]);
;                     *(u32x4*)(rowp + bj * HALF) = w; } }
.LBB0_280:
	v_add_u32_e32 v52, 0x90, v155
	v_mov_b64_e32 v[50:51], s[8:9]
	v_mad_i64_i32 v[50:51], s[24:25], v52, s44, v[50:51]
	v_lshl_add_u64 v[50:51], v[146:147], 1, v[50:51]
	s_and_b64 vcc, exec, s[2:3]
	v_cvt_pk_bf16_f32 v46, v46, v47
	v_cvt_pk_bf16_f32 v47, v48, v49
	v_cvt_pk_bf16_f32 v48, v42, v43
	v_cvt_pk_bf16_f32 v49, v44, v45
	global_store_dwordx4 v[50:51], v[46:49], off sc0 sc1
	s_cbranch_vccnz .LBB0_282
	v_mul_f32_e32 v43, 0x3d372713, v34
	v_mul_f32_e32 v43, v34, v43
	v_mul_f32_e32 v44, 0x3d372713, v39
	v_fma_f32 v43, v34, v43, v34
	v_mul_f32_e32 v44, v39, v44
	v_mul_f32_e32 v43, 0xc0135761, v43
	v_fma_f32 v44, v39, v44, v39
	v_exp_f32_e32 v43, v43
	v_mul_f32_e32 v44, 0xc0135761, v44
	v_exp_f32_e32 v45, v44
	v_mul_f32_e32 v48, 0x3d372713, v41
	v_mul_f32_e32 v48, v41, v48
	v_fma_f32 v48, v41, v48, v41
	v_add_f32_e32 v43, 1.0, v43
	v_mul_f32_e32 v47, 0x3d372713, v36
	v_mul_f32_e32 v48, 0xc0135761, v48
	v_mul_f32_e32 v42, 0x3d372713, v38
	v_rcp_f32_e32 v44, v43
	v_add_f32_e32 v43, 1.0, v45
	v_mul_f32_e32 v45, 0x3d372713, v35
	v_mul_f32_e32 v46, 0x3d372713, v40
	v_mul_f32_e32 v47, v36, v47
	v_exp_f32_e32 v49, v48
	v_mul_f32_e32 v48, 0x3d372713, v37
	v_mul_f32_e32 v42, v38, v42
	v_mul_f32_e32 v45, v35, v45
	v_mul_f32_e32 v46, v40, v46
	v_fma_f32 v47, v36, v47, v36
	v_mul_f32_e32 v48, v37, v48
	v_fma_f32 v42, v38, v42, v38
	v_fma_f32 v45, v35, v45, v35
	v_fma_f32 v46, v40, v46, v40
	v_mul_f32_e32 v47, 0xc0135761, v47
	v_fma_f32 v48, v37, v48, v37
	v_mul_f32_e32 v42, 0xc0135761, v42
	v_mul_f32_e32 v45, 0xc0135761, v45
	v_mul_f32_e32 v46, 0xc0135761, v46
	v_exp_f32_e32 v47, v47
	v_mul_f32_e32 v48, 0xc0135761, v48
	v_exp_f32_e32 v42, v42
	v_exp_f32_e32 v45, v45
	v_exp_f32_e32 v46, v46
	v_exp_f32_e32 v52, v48
	v_add_f32_e32 v47, 1.0, v47
	v_add_f32_e32 v42, 1.0, v42
	v_add_f32_e32 v45, 1.0, v45
	v_add_f32_e32 v46, 1.0, v46
	v_rcp_f32_e32 v48, v47
	v_add_f32_e32 v47, 1.0, v49
	v_add_f32_e32 v49, 1.0, v52
	v_rcp_f32_e32 v42, v42
	v_rcp_f32_e32 v43, v43
	v_rcp_f32_e32 v46, v46
	v_rcp_f32_e32 v47, v47
	v_rcp_f32_e32 v49, v49
	v_rcp_f32_e32 v45, v45
	v_pk_mul_f32 v[38:39], v[38:39], v[42:43]
	v_pk_mul_f32 v[40:41], v[40:41], v[46:47]
	v_pk_mul_f32 v[36:37], v[36:37], v[48:49]
	v_pk_mul_f32 v[34:35], v[34:35], v[44:45]
.LBB0_282:
	s_and_b64 vcc, exec, s[2:3]
	v_cvt_pk_bf16_f32 v38, v38, v39
	v_cvt_pk_bf16_f32 v39, v40, v41
	v_cvt_pk_bf16_f32 v40, v34, v35
	v_cvt_pk_bf16_f32 v41, v36, v37
	global_store_dwordx4 v[50:51], v[38:41], off offset:256 sc0 sc1
	s_cbranch_vccnz .LBB0_284
	v_mul_f32_e32 v35, 0x3d372713, v26
	v_mul_f32_e32 v35, v26, v35
	v_mul_f32_e32 v36, 0x3d372713, v31
	v_fma_f32 v35, v26, v35, v26
	v_mul_f32_e32 v36, v31, v36
	v_mul_f32_e32 v35, 0xc0135761, v35
	v_fma_f32 v36, v31, v36, v31
	v_exp_f32_e32 v35, v35
	v_mul_f32_e32 v36, 0xc0135761, v36
	v_exp_f32_e32 v37, v36
	v_mul_f32_e32 v40, 0x3d372713, v33
	v_mul_f32_e32 v40, v33, v40
	v_fma_f32 v40, v33, v40, v33
	v_add_f32_e32 v35, 1.0, v35
	v_mul_f32_e32 v39, 0x3d372713, v28
	v_mul_f32_e32 v40, 0xc0135761, v40
	v_mul_f32_e32 v34, 0x3d372713, v30
	v_rcp_f32_e32 v36, v35
	v_add_f32_e32 v35, 1.0, v37
	v_mul_f32_e32 v37, 0x3d372713, v27
	v_mul_f32_e32 v38, 0x3d372713, v32
	v_mul_f32_e32 v39, v28, v39
	v_exp_f32_e32 v41, v40
	v_mul_f32_e32 v40, 0x3d372713, v29
	v_mul_f32_e32 v34, v30, v34
	v_mul_f32_e32 v37, v27, v37
	v_mul_f32_e32 v38, v32, v38
	v_fma_f32 v39, v28, v39, v28
	v_mul_f32_e32 v40, v29, v40
	v_fma_f32 v34, v30, v34, v30
	v_fma_f32 v37, v27, v37, v27
	v_fma_f32 v38, v32, v38, v32
	v_mul_f32_e32 v39, 0xc0135761, v39
	v_fma_f32 v40, v29, v40, v29
	v_mul_f32_e32 v34, 0xc0135761, v34
	v_mul_f32_e32 v37, 0xc0135761, v37
	v_mul_f32_e32 v38, 0xc0135761, v38
	v_exp_f32_e32 v39, v39
	v_mul_f32_e32 v40, 0xc0135761, v40
	v_exp_f32_e32 v34, v34
	v_exp_f32_e32 v37, v37
	v_exp_f32_e32 v38, v38
	v_exp_f32_e32 v42, v40
	v_add_f32_e32 v39, 1.0, v39
	v_add_f32_e32 v34, 1.0, v34
	v_add_f32_e32 v37, 1.0, v37
	v_add_f32_e32 v38, 1.0, v38
	v_rcp_f32_e32 v40, v39
	v_add_f32_e32 v39, 1.0, v41
	v_add_f32_e32 v41, 1.0, v42
	v_rcp_f32_e32 v34, v34
	v_rcp_f32_e32 v35, v35
	v_rcp_f32_e32 v38, v38
	v_rcp_f32_e32 v39, v39
	v_rcp_f32_e32 v41, v41
	v_rcp_f32_e32 v37, v37
	v_pk_mul_f32 v[30:31], v[30:31], v[34:35]
	v_pk_mul_f32 v[32:33], v[32:33], v[38:39]
	v_pk_mul_f32 v[28:29], v[28:29], v[40:41]
	v_pk_mul_f32 v[26:27], v[26:27], v[36:37]
.LBB0_284:
	v_add_u32_e32 v36, 0xa0, v155
	v_mov_b64_e32 v[34:35], s[8:9]
	v_mad_i64_i32 v[34:35], s[24:25], v36, s44, v[34:35]
	v_lshl_add_u64 v[34:35], v[146:147], 1, v[34:35]
	s_and_b64 vcc, exec, s[2:3]
	v_cvt_pk_bf16_f32 v30, v30, v31
	v_cvt_pk_bf16_f32 v31, v32, v33
	v_cvt_pk_bf16_f32 v32, v26, v27
	v_cvt_pk_bf16_f32 v33, v28, v29
	global_store_dwordx4 v[34:35], v[30:33], off sc0 sc1
	s_cbranch_vccnz .LBB0_286
	v_mul_f32_e32 v27, 0x3d372713, v18
	v_mul_f32_e32 v27, v18, v27
	v_mul_f32_e32 v28, 0x3d372713, v23
	v_fma_f32 v27, v18, v27, v18
	v_mul_f32_e32 v28, v23, v28
	v_mul_f32_e32 v27, 0xc0135761, v27
	v_fma_f32 v28, v23, v28, v23
	v_exp_f32_e32 v27, v27
	v_mul_f32_e32 v28, 0xc0135761, v28
	v_exp_f32_e32 v29, v28
	v_mul_f32_e32 v32, 0x3d372713, v25
	v_mul_f32_e32 v32, v25, v32
	v_fma_f32 v32, v25, v32, v25
	v_add_f32_e32 v27, 1.0, v27
	v_mul_f32_e32 v31, 0x3d372713, v20
	v_mul_f32_e32 v32, 0xc0135761, v32
	v_mul_f32_e32 v26, 0x3d372713, v22
	v_rcp_f32_e32 v28, v27
	v_add_f32_e32 v27, 1.0, v29
	v_mul_f32_e32 v29, 0x3d372713, v19
	v_mul_f32_e32 v30, 0x3d372713, v24
	v_mul_f32_e32 v31, v20, v31
	v_exp_f32_e32 v33, v32
	v_mul_f32_e32 v32, 0x3d372713, v21
	v_mul_f32_e32 v26, v22, v26
	v_mul_f32_e32 v29, v19, v29
	v_mul_f32_e32 v30, v24, v30
	v_fma_f32 v31, v20, v31, v20
	v_mul_f32_e32 v32, v21, v32
	v_fma_f32 v26, v22, v26, v22
	v_fma_f32 v29, v19, v29, v19
	v_fma_f32 v30, v24, v30, v24
	v_mul_f32_e32 v31, 0xc0135761, v31
	v_fma_f32 v32, v21, v32, v21
	v_mul_f32_e32 v26, 0xc0135761, v26
	v_mul_f32_e32 v29, 0xc0135761, v29
	v_mul_f32_e32 v30, 0xc0135761, v30
	v_exp_f32_e32 v31, v31
	v_mul_f32_e32 v32, 0xc0135761, v32
	v_exp_f32_e32 v26, v26
	v_exp_f32_e32 v29, v29
	v_exp_f32_e32 v30, v30
	v_exp_f32_e32 v36, v32
	v_add_f32_e32 v31, 1.0, v31
	v_add_f32_e32 v26, 1.0, v26
	v_add_f32_e32 v29, 1.0, v29
	v_add_f32_e32 v30, 1.0, v30
	v_rcp_f32_e32 v32, v31
	v_add_f32_e32 v31, 1.0, v33
	v_add_f32_e32 v33, 1.0, v36
	v_rcp_f32_e32 v26, v26
	v_rcp_f32_e32 v27, v27
	v_rcp_f32_e32 v30, v30
	v_rcp_f32_e32 v31, v31
	v_rcp_f32_e32 v33, v33
	v_rcp_f32_e32 v29, v29
	v_pk_mul_f32 v[22:23], v[22:23], v[26:27]
	v_pk_mul_f32 v[24:25], v[24:25], v[30:31]
	v_pk_mul_f32 v[20:21], v[20:21], v[32:33]
	v_pk_mul_f32 v[18:19], v[18:19], v[28:29]
; __device__ __forceinline__ unsigned cvt_pk_bf16(float lo, float hi) { unsigned r; asm volatile("v_cvt_pk_bf16_f32 %0, %1, %2" : "=v"(r) : "v"(lo), "v"(hi)); return r; }
; __device__ __forceinline__ float gelu_tanh(float x) { const float y = x + 0.044715f * x * x * x; return x * __builtin_amdgcn_rcpf(1.0f + __builtin_amdgcn_exp2f(-2.302208198f * y)); }
;     __device__ __forceinline__ void operator()(const f32x4 (&acc)[2][2][4][2], const Unit& u, int wr, int wc, int fr, int fq) const {
;         const int row0 = u.pm * BM + wr * 64 + fr, col0 = u.pn * BM + wc * 32 + 8 * fq; const bool act = u.pn < nact;
; #pragma unroll
;         for (int ai = 0; ai < 2; ++ai)
; #pragma unroll
;             for (int m = 0; m < 4; ++m) { bf16_t* rowp = O + (size_t)u.ks * ks_stride + (size_t)(row0 + ai * HALF + m * 16) * ldc + col0;
; #pragma unroll
;                 for (int bj = 0; bj < 2; ++bj) { f32x4 v0 = acc[ai][bj][m][0] * ascale, v1 = acc[ai][bj][m][1] * ascale;
;                     if (act) {
; #pragma unroll
;                         for (int j = 0; j < 4; ++j) { v0[j] = gelu_tanh(v0[j]); v1[j] = gelu_tanh(v1[j]); } }
;                     u32x4 w; w.x = cvt_pk_bf16(v0[0], v0[1]); w.y = cvt_pk_bf16(v0[2], v0[3]); w.z = cvt_pk_bf16(v1[0], v1[1]); w.w = cvt_pk_bf16(v1[2], v1[3]);
;                     *(u32x4*)(rowp + bj * HALF) = w; } }
.LBB0_286:
	s_and_b64 vcc, exec, s[2:3]
	v_cvt_pk_bf16_f32 v22, v22, v23
	v_cvt_pk_bf16_f32 v23, v24, v25
	v_cvt_pk_bf16_f32 v24, v18, v19
	v_cvt_pk_bf16_f32 v25, v20, v21
	global_store_dwordx4 v[34:35], v[22:25], off offset:256 sc0 sc1
	s_cbranch_vccnz .LBB0_288
	v_mul_f32_e32 v19, 0x3d372713, v10
	v_mul_f32_e32 v19, v10, v19
	v_mul_f32_e32 v20, 0x3d372713, v15
	v_fma_f32 v19, v10, v19, v10
	v_mul_f32_e32 v20, v15, v20
	v_mul_f32_e32 v19, 0xc0135761, v19
	v_fma_f32 v20, v15, v20, v15
	v_exp_f32_e32 v19, v19
	v_mul_f32_e32 v20, 0xc0135761, v20
	v_exp_f32_e32 v21, v20
	v_mul_f32_e32 v24, 0x3d372713, v17
	v_mul_f32_e32 v24, v17, v24
	v_fma_f32 v24, v17, v24, v17
	v_add_f32_e32 v19, 1.0, v19
	v_mul_f32_e32 v23, 0x3d372713, v12
	v_mul_f32_e32 v24, 0xc0135761, v24
	v_mul_f32_e32 v18, 0x3d372713, v14
	v_rcp_f32_e32 v20, v19
	v_add_f32_e32 v19, 1.0, v21
	v_mul_f32_e32 v21, 0x3d372713, v11
	v_mul_f32_e32 v22, 0x3d372713, v16
	v_mul_f32_e32 v23, v12, v23
	v_exp_f32_e32 v25, v24
	v_mul_f32_e32 v24, 0x3d372713, v13
	v_mul_f32_e32 v18, v14, v18
	v_mul_f32_e32 v21, v11, v21
	v_mul_f32_e32 v22, v16, v22
	v_fma_f32 v23, v12, v23, v12
	v_mul_f32_e32 v24, v13, v24
	v_fma_f32 v18, v14, v18, v14
	v_fma_f32 v21, v11, v21, v11
	v_fma_f32 v22, v16, v22, v16
	v_mul_f32_e32 v23, 0xc0135761, v23
	v_fma_f32 v24, v13, v24, v13
	v_mul_f32_e32 v18, 0xc0135761, v18
	v_mul_f32_e32 v21, 0xc0135761, v21
	v_mul_f32_e32 v22, 0xc0135761, v22
	v_exp_f32_e32 v23, v23
	v_mul_f32_e32 v24, 0xc0135761, v24
	v_exp_f32_e32 v18, v18
	v_exp_f32_e32 v21, v21
	v_exp_f32_e32 v22, v22
	v_exp_f32_e32 v26, v24
	v_add_f32_e32 v23, 1.0, v23
	v_add_f32_e32 v18, 1.0, v18
	v_add_f32_e32 v21, 1.0, v21
	v_add_f32_e32 v22, 1.0, v22
	v_rcp_f32_e32 v24, v23
	v_add_f32_e32 v23, 1.0, v25
	v_add_f32_e32 v25, 1.0, v26
	v_rcp_f32_e32 v18, v18
	v_rcp_f32_e32 v19, v19
	v_rcp_f32_e32 v22, v22
	v_rcp_f32_e32 v23, v23
	v_rcp_f32_e32 v25, v25
	v_rcp_f32_e32 v21, v21
	v_pk_mul_f32 v[14:15], v[14:15], v[18:19]
	v_pk_mul_f32 v[16:17], v[16:17], v[22:23]
	v_pk_mul_f32 v[12:13], v[12:13], v[24:25]
	v_pk_mul_f32 v[10:11], v[10:11], v[20:21]
.LBB0_288:
	v_add_u32_e32 v20, 0xb0, v155
	v_mov_b64_e32 v[18:19], s[8:9]
	v_mad_i64_i32 v[18:19], s[24:25], v20, s44, v[18:19]
	v_lshl_add_u64 v[18:19], v[146:147], 1, v[18:19]
	s_and_b64 vcc, exec, s[2:3]
	v_cvt_pk_bf16_f32 v14, v14, v15
	v_cvt_pk_bf16_f32 v15, v16, v17
	v_cvt_pk_bf16_f32 v16, v10, v11
	v_cvt_pk_bf16_f32 v17, v12, v13
	global_store_dwordx4 v[18:19], v[14:17], off sc0 sc1
	s_cbranch_vccnz .LBB0_290
	v_mul_f32_e32 v11, 0x3d372713, v2
	v_mul_f32_e32 v11, v2, v11
	v_mul_f32_e32 v12, 0x3d372713, v7
	v_fma_f32 v11, v2, v11, v2
	v_mul_f32_e32 v12, v7, v12
	v_mul_f32_e32 v11, 0xc0135761, v11
	v_fma_f32 v12, v7, v12, v7
	v_exp_f32_e32 v11, v11
	v_mul_f32_e32 v12, 0xc0135761, v12
	v_exp_f32_e32 v13, v12
	v_mul_f32_e32 v16, 0x3d372713, v9
	v_mul_f32_e32 v16, v9, v16
	v_fma_f32 v16, v9, v16, v9
	v_add_f32_e32 v11, 1.0, v11
	v_mul_f32_e32 v15, 0x3d372713, v4
	v_mul_f32_e32 v16, 0xc0135761, v16
	v_mul_f32_e32 v10, 0x3d372713, v6
	v_rcp_f32_e32 v12, v11
	v_add_f32_e32 v11, 1.0, v13
	v_mul_f32_e32 v13, 0x3d372713, v3
	v_mul_f32_e32 v14, 0x3d372713, v8
	v_mul_f32_e32 v15, v4, v15
	v_exp_f32_e32 v17, v16
	v_mul_f32_e32 v16, 0x3d372713, v5
	v_mul_f32_e32 v10, v6, v10
	v_mul_f32_e32 v13, v3, v13
	v_mul_f32_e32 v14, v8, v14
	v_fma_f32 v15, v4, v15, v4
	v_mul_f32_e32 v16, v5, v16
	v_fma_f32 v10, v6, v10, v6
	v_fma_f32 v13, v3, v13, v3
	v_fma_f32 v14, v8, v14, v8
	v_mul_f32_e32 v15, 0xc0135761, v15
	v_fma_f32 v16, v5, v16, v5
	v_mul_f32_e32 v10, 0xc0135761, v10
	v_mul_f32_e32 v13, 0xc0135761, v13
	v_mul_f32_e32 v14, 0xc0135761, v14
	v_exp_f32_e32 v15, v15
	v_mul_f32_e32 v16, 0xc0135761, v16
	v_exp_f32_e32 v10, v10
	v_exp_f32_e32 v13, v13
	v_exp_f32_e32 v14, v14
	v_exp_f32_e32 v20, v16
	v_add_f32_e32 v15, 1.0, v15
	v_add_f32_e32 v10, 1.0, v10
	v_add_f32_e32 v13, 1.0, v13
	v_add_f32_e32 v14, 1.0, v14
	v_rcp_f32_e32 v16, v15
	v_add_f32_e32 v15, 1.0, v17
	v_add_f32_e32 v17, 1.0, v20
	v_rcp_f32_e32 v10, v10
	v_rcp_f32_e32 v11, v11
	v_rcp_f32_e32 v14, v14
	v_rcp_f32_e32 v15, v15
	v_rcp_f32_e32 v17, v17
	v_rcp_f32_e32 v13, v13
	v_pk_mul_f32 v[6:7], v[6:7], v[10:11]
	v_pk_mul_f32 v[8:9], v[8:9], v[14:15]
	v_pk_mul_f32 v[4:5], v[4:5], v[16:17]
	v_pk_mul_f32 v[2:3], v[2:3], v[12:13]
.LBB0_290:
	s_andn2_b64 vcc, exec, s[0:1]
	s_mov_b64 s[0:1], -1
	v_cvt_pk_bf16_f32 v6, v6, v7
	v_cvt_pk_bf16_f32 v7, v8, v9
	v_cvt_pk_bf16_f32 v8, v2, v3
	v_cvt_pk_bf16_f32 v9, v4, v5
	global_store_dwordx4 v[18:19], v[6:9], off offset:256 sc0 sc1
	s_cbranch_vccnz .LBB0_248
	s_andn2_b64 vcc, exec, s[6:7]
	s_cbranch_vccnz .LBB0_247
	s_barrier
	s_branch .LBB0_247

; __device__ __forceinline__ unsigned cvt_pk_bf16(float lo, float hi) { unsigned r; asm volatile("v_cvt_pk_bf16_f32 %0, %1, %2" : "=v"(r) : "v"(lo), "v"(hi)); return r; }
;     __device__ __forceinline__ void operator()(const f32x4 (&acc)[2][2][4][2], const Unit& u, int wr, int wc, int fr, int fq) const {
;     ...
;                 const float* res = isc ? resC - (size_t)16384 * 2048 : resL;
;                 f32x4 bs[4][2][2];
; #pragma unroll
;                 for (int m = 0; m < 4; ++m)
; #pragma unroll
;                     for (int bj = 0; bj < 2; ++bj)
; #pragma unroll
;                         for (int n = 0; n < 2; ++n) bs[m][bj][n] = *(const f32x4*)(res + (size_t)(row0 + ai * HALF + m * 16) * 2048 + col0 + bj * HALF + n * 4);
; #pragma unroll
;                 for (int m = 0; m < 4; ++m)
; #pragma unroll
;                     for (int bj = 0; bj < 2; ++bj) { const f32x4 r0 = bs[m][bj][0] + gg[bj][0] * acc[ai][bj][m][0], r1 = bs[m][bj][1] + gg[bj][1] * acc[ai][bj][m][1];
;                         u32x4 w; w.x = cvt_pk_bf16(r0[0], r0[1]); w.y = cvt_pk_bf16(r0[2], r0[3]); w.z = cvt_pk_bf16(r1[0], r1[1]); w.w = cvt_pk_bf16(r1[2], r1[3]);
;                         *(u32x4*)(H + (size_t)(row0 + ai * HALF + m * 16) * 2048 + col0 + bj * HALF) = w; }
.LBB0_542:
	s_lshl_b64 s[28:29], s[28:29], 2
	v_lshl_or_b32 v170, s24, 8, v177
	s_add_u32 s28, s41, s28
	v_ashrrev_i32_e32 v171, 31, v170
	v_lshl_add_u32 v174, s22, 8, v1
	s_addc_u32 s29, s42, s29
	v_lshlrev_b64 v[130:131], 2, v[170:171]
	v_ashrrev_i32_e32 v175, 31, v174
	v_lshl_add_u64 v[134:135], s[28:29], 0, v[130:131]
	v_lshl_add_u64 v[172:173], s[26:27], 0, v[130:131]
	v_lshlrev_b64 v[130:131], 13, v[174:175]
	v_or_b32_e32 v240, 16, v174
	v_lshl_add_u64 v[146:147], v[172:173], 0, v[130:131]
	v_ashrrev_i32_e32 v241, 31, v240
	global_load_dwordx4 v[138:141], v[134:135], off offset:16
	global_load_dwordx4 v[142:145], v[134:135], off
	global_load_dwordx4 v[184:187], v[146:147], off offset:16
	global_load_dwordx4 v[188:191], v[146:147], off
	global_load_dwordx4 v[130:133], v[134:135], off offset:528
	s_nop 0
	global_load_dwordx4 v[134:137], v[134:135], off offset:512
	s_nop 0
	global_load_dwordx4 v[192:195], v[146:147], off offset:528
	global_load_dwordx4 v[196:199], v[146:147], off offset:512
	v_lshlrev_b64 v[146:147], 13, v[240:241]
	v_or_b32_e32 v242, 32, v174
	v_lshl_add_u64 v[146:147], v[172:173], 0, v[146:147]
	v_ashrrev_i32_e32 v243, 31, v242
	global_load_dwordx4 v[200:203], v[146:147], off
	global_load_dwordx4 v[204:207], v[146:147], off offset:16
	global_load_dwordx4 v[208:211], v[146:147], off offset:528
	global_load_dwordx4 v[212:215], v[146:147], off offset:512
	v_lshlrev_b64 v[146:147], 13, v[242:243]
	v_lshl_add_u64 v[146:147], v[172:173], 0, v[146:147]
	global_load_dwordx4 v[216:219], v[146:147], off
	global_load_dwordx4 v[220:223], v[146:147], off offset:16
	global_load_dwordx4 v[224:227], v[146:147], off offset:512
	global_load_dwordx4 v[228:231], v[146:147], off offset:528
	v_or_b32_e32 v244, 48, v174
	v_ashrrev_i32_e32 v245, 31, v244
	v_lshlrev_b64 v[146:147], 13, v[244:245]
	v_lshl_add_u64 v[146:147], v[172:173], 0, v[146:147]
	global_load_dwordx4 v[232:235], v[146:147], off
	global_load_dwordx4 v[236:239], v[146:147], off offset:16
	global_load_dwordx4 v[150:153], v[146:147], off offset:512
	s_nop 0
	global_load_dwordx4 v[146:149], v[146:147], off offset:528
	v_lshlrev_b64 v[246:247], 12, v[174:175]
	v_lshlrev_b64 v[170:171], 1, v[170:171]
	v_lshl_add_u64 v[246:247], s[6:7], 0, v[246:247]
	v_lshlrev_b64 v[240:241], 12, v[240:241]
	v_lshl_add_u64 v[246:247], v[246:247], 0, v[170:171]
	v_lshl_add_u64 v[240:241], s[6:7], 0, v[240:241]
	v_lshl_add_u64 v[240:241], v[240:241], 0, v[170:171]
	v_lshlrev_b64 v[242:243], 12, v[242:243]
	s_andn2_b64 vcc, exec, s[0:1]
	s_mov_b64 s[0:1], -1
	s_waitcnt vmcnt(0)
	v_pk_fma_f32 v[124:125], v[124:125], v[140:141], v[186:187]
	v_pk_fma_f32 v[128:129], v[128:129], v[144:145], v[190:191]
	v_pk_fma_f32 v[126:127], v[126:127], v[142:143], v[188:189]
	v_pk_fma_f32 v[122:123], v[122:123], v[138:139], v[184:185]
	v_pk_fma_f32 v[108:109], v[108:109], v[136:137], v[198:199]
	v_pk_fma_f32 v[106:107], v[106:107], v[134:135], v[196:197]
	v_pk_fma_f32 v[184:185], v[94:95], v[130:131], v[208:209]
	v_pk_fma_f32 v[104:105], v[104:105], v[132:133], v[194:195]
	v_pk_fma_f32 v[186:187], v[92:93], v[140:141], v[222:223]
	v_cvt_pk_bf16_f32 v92, v126, v127
	v_cvt_pk_bf16_f32 v93, v128, v129
	v_cvt_pk_bf16_f32 v94, v122, v123
	v_cvt_pk_bf16_f32 v95, v124, v125
	v_pk_fma_f32 v[102:103], v[102:103], v[130:131], v[192:193]
	global_store_dwordx4 v[246:247], v[92:95], off sc0 sc1
	v_pk_fma_f32 v[120:121], v[120:121], v[144:145], v[202:203]
	v_pk_fma_f32 v[118:119], v[118:119], v[142:143], v[200:201]
	v_cvt_pk_bf16_f32 v92, v106, v107
	v_cvt_pk_bf16_f32 v93, v108, v109
	v_cvt_pk_bf16_f32 v94, v102, v103
	v_cvt_pk_bf16_f32 v95, v104, v105
	v_pk_fma_f32 v[116:117], v[116:117], v[140:141], v[206:207]
	v_pk_fma_f32 v[114:115], v[114:115], v[138:139], v[204:205]
	global_store_dwordx4 v[246:247], v[92:95], off offset:256 sc0 sc1
	v_pk_fma_f32 v[100:101], v[100:101], v[136:137], v[214:215]
	v_pk_fma_f32 v[98:99], v[98:99], v[134:135], v[212:213]
	v_cvt_pk_bf16_f32 v92, v118, v119
	v_cvt_pk_bf16_f32 v93, v120, v121
	v_cvt_pk_bf16_f32 v94, v114, v115
	v_cvt_pk_bf16_f32 v95, v116, v117
	v_pk_fma_f32 v[96:97], v[96:97], v[132:133], v[210:211]
	global_store_dwordx4 v[240:241], v[92:95], off sc0 sc1
	v_pk_fma_f32 v[112:113], v[112:113], v[144:145], v[218:219]
	v_pk_fma_f32 v[110:111], v[110:111], v[142:143], v[216:217]
	v_cvt_pk_bf16_f32 v92, v98, v99
	v_cvt_pk_bf16_f32 v93, v100, v101
	v_cvt_pk_bf16_f32 v94, v184, v185
	v_cvt_pk_bf16_f32 v95, v96, v97
	global_store_dwordx4 v[240:241], v[92:95], off offset:256 sc0 sc1
	v_pk_fma_f32 v[88:89], v[88:89], v[136:137], v[226:227]
	v_pk_fma_f32 v[86:87], v[86:87], v[134:135], v[224:225]
	v_lshl_add_u64 v[94:95], s[6:7], 0, v[242:243]
	v_pk_fma_f32 v[92:93], v[90:91], v[138:139], v[220:221]
	v_cvt_pk_bf16_f32 v90, v110, v111
	v_cvt_pk_bf16_f32 v91, v112, v113
	v_lshl_add_u64 v[94:95], v[94:95], 0, v[170:171]
	v_cvt_pk_bf16_f32 v92, v92, v93
	v_cvt_pk_bf16_f32 v93, v186, v187
	global_store_dwordx4 v[94:95], v[90:93], off sc0 sc1
	v_pk_fma_f32 v[82:83], v[82:83], v[142:143], v[232:233]
	v_pk_fma_f32 v[72:73], v[72:73], v[136:137], v[152:153]
	v_pk_fma_f32 v[90:91], v[80:81], v[132:133], v[230:231]
	v_pk_fma_f32 v[80:81], v[78:79], v[130:131], v[228:229]
	v_cvt_pk_bf16_f32 v78, v86, v87
	v_cvt_pk_bf16_f32 v79, v88, v89
	v_pk_fma_f32 v[70:71], v[70:71], v[134:135], v[150:151]
	v_cvt_pk_bf16_f32 v80, v80, v81
	v_cvt_pk_bf16_f32 v81, v90, v91
	global_store_dwordx4 v[94:95], v[78:81], off offset:256 sc0 sc1
	v_add_u32_e32 v150, 0xa0, v174
	v_ashrrev_i32_e32 v151, 31, v150
	v_lshlrev_b64 v[78:79], 12, v[244:245]
	v_lshl_add_u64 v[78:79], s[6:7], 0, v[78:79]
	v_pk_fma_f32 v[80:81], v[84:85], v[144:145], v[234:235]
; __device__ __forceinline__ unsigned cvt_pk_bf16(float lo, float hi) { unsigned r; asm volatile("v_cvt_pk_bf16_f32 %0, %1, %2" : "=v"(r) : "v"(lo), "v"(hi)); return r; }
;     __device__ __forceinline__ void operator()(const f32x4 (&acc)[2][2][4][2], const Unit& u, int wr, int wc, int fr, int fq) const {
;     ...
;                         for (int n = 0; n < 2; ++n) bs[m][bj][n] = *(const f32x4*)(res + (size_t)(row0 + ai * HALF + m * 16) * 2048 + col0 + bj * HALF + n * 4);
; #pragma unroll
;                 for (int m = 0; m < 4; ++m)
; #pragma unroll
;                     for (int bj = 0; bj < 2; ++bj) { const f32x4 r0 = bs[m][bj][0] + gg[bj][0] * acc[ai][bj][m][0], r1 = bs[m][bj][1] + gg[bj][1] * acc[ai][bj][m][1];
;                         u32x4 w; w.x = cvt_pk_bf16(r0[0], r0[1]); w.y = cvt_pk_bf16(r0[2], r0[3]); w.z = cvt_pk_bf16(r1[0], r1[1]); w.w = cvt_pk_bf16(r1[2], r1[3]);
;                         *(u32x4*)(H + (size_t)(row0 + ai * HALF + m * 16) * 2048 + col0 + bj * HALF) = w; }
	v_pk_fma_f32 v[84:85], v[76:77], v[140:141], v[238:239]
	v_pk_fma_f32 v[76:77], v[74:75], v[138:139], v[236:237]
	v_cvt_pk_bf16_f32 v74, v82, v83
	v_cvt_pk_bf16_f32 v75, v80, v81
	v_lshl_add_u64 v[78:79], v[78:79], 0, v[170:171]
	v_cvt_pk_bf16_f32 v76, v76, v77
	v_cvt_pk_bf16_f32 v77, v84, v85
	global_store_dwordx4 v[78:79], v[74:77], off sc0 sc1
	v_lshlrev_b64 v[98:99], 13, v[150:151]
	v_lshl_add_u64 v[110:111], v[172:173], 0, v[98:99]
	v_pk_fma_f32 v[74:75], v[68:69], v[132:133], v[148:149]
	v_pk_fma_f32 v[68:69], v[66:67], v[130:131], v[146:147]
	v_add_u32_e32 v146, 0x80, v174
	v_cvt_pk_bf16_f32 v66, v70, v71
	v_cvt_pk_bf16_f32 v67, v72, v73
	v_ashrrev_i32_e32 v147, 31, v146
	v_cvt_pk_bf16_f32 v68, v68, v69
	v_cvt_pk_bf16_f32 v69, v74, v75
	global_store_dwordx4 v[78:79], v[66:69], off offset:256 sc0 sc1
	v_add_u32_e32 v148, 0x90, v174
	v_ashrrev_i32_e32 v149, 31, v148
	v_lshlrev_b64 v[66:67], 13, v[146:147]
	v_lshl_add_u64 v[78:79], v[172:173], 0, v[66:67]
	global_load_dwordx4 v[66:69], v[78:79], off
	global_load_dwordx4 v[70:73], v[78:79], off offset:16
	global_load_dwordx4 v[74:77], v[78:79], off offset:512
	s_nop 0
	global_load_dwordx4 v[78:81], v[78:79], off offset:528
	v_lshlrev_b64 v[82:83], 13, v[148:149]
	v_lshl_add_u64 v[94:95], v[172:173], 0, v[82:83]
	global_load_dwordx4 v[82:85], v[94:95], off
	global_load_dwordx4 v[86:89], v[94:95], off offset:16
	global_load_dwordx4 v[90:93], v[94:95], off offset:512
	s_nop 0
	global_load_dwordx4 v[94:97], v[94:95], off offset:528
	s_nop 0
	global_load_dwordx4 v[98:101], v[110:111], off
	global_load_dwordx4 v[102:105], v[110:111], off offset:16
	global_load_dwordx4 v[106:109], v[110:111], off offset:512
	s_nop 0
	global_load_dwordx4 v[110:113], v[110:111], off offset:528
	v_add_u32_e32 v152, 0xb0, v174
	v_ashrrev_i32_e32 v153, 31, v152
	v_lshlrev_b64 v[114:115], 13, v[152:153]
	v_lshl_add_u64 v[126:127], v[172:173], 0, v[114:115]
	global_load_dwordx4 v[114:117], v[126:127], off
	global_load_dwordx4 v[118:121], v[126:127], off offset:16
	global_load_dwordx4 v[122:125], v[126:127], off offset:512
	s_nop 0
	global_load_dwordx4 v[126:129], v[126:127], off offset:528
	v_lshlrev_b64 v[146:147], 12, v[146:147]
	v_lshl_add_u64 v[146:147], s[6:7], 0, v[146:147]
	v_lshl_add_u64 v[146:147], v[146:147], 0, v[170:171]
	s_waitcnt vmcnt(15)
	v_pk_fma_f32 v[64:65], v[64:65], v[144:145], v[68:69]
	v_pk_fma_f32 v[62:63], v[62:63], v[142:143], v[66:67]
	s_waitcnt vmcnt(14)
	v_pk_fma_f32 v[60:61], v[60:61], v[140:141], v[72:73]
	s_waitcnt vmcnt(12)
	v_pk_fma_f32 v[68:69], v[50:51], v[130:131], v[78:79]
	v_cvt_pk_bf16_f32 v50, v62, v63
	v_cvt_pk_bf16_f32 v51, v64, v65
	v_pk_fma_f32 v[58:59], v[58:59], v[138:139], v[70:71]
	v_pk_fma_f32 v[56:57], v[56:57], v[136:137], v[76:77]
	v_pk_fma_f32 v[54:55], v[54:55], v[134:135], v[74:75]
	v_pk_fma_f32 v[66:67], v[52:53], v[132:133], v[80:81]
	v_cvt_pk_bf16_f32 v52, v58, v59
	v_cvt_pk_bf16_f32 v53, v60, v61
	global_store_dwordx4 v[146:147], v[50:53], off sc0 sc1
	s_waitcnt vmcnt(12)
	v_pk_fma_f32 v[46:47], v[46:47], v[142:143], v[82:83]
	v_pk_fma_f32 v[48:49], v[48:49], v[144:145], v[84:85]
	v_cvt_pk_bf16_f32 v50, v54, v55
	v_cvt_pk_bf16_f32 v51, v56, v57
	v_cvt_pk_bf16_f32 v52, v68, v69
	v_cvt_pk_bf16_f32 v53, v66, v67
	global_store_dwordx4 v[146:147], v[50:53], off offset:256 sc0 sc1
	s_waitcnt vmcnt(11)
	v_pk_fma_f32 v[40:41], v[40:41], v[136:137], v[92:93]
	v_pk_fma_f32 v[38:39], v[38:39], v[134:135], v[90:91]
	v_lshlrev_b64 v[50:51], 12, v[148:149]
	v_pk_fma_f32 v[52:53], v[44:45], v[140:141], v[88:89]
	v_pk_fma_f32 v[44:45], v[42:43], v[138:139], v[86:87]
	v_cvt_pk_bf16_f32 v42, v46, v47
	v_lshl_add_u64 v[46:47], s[6:7], 0, v[50:51]
	v_cvt_pk_bf16_f32 v43, v48, v49
	v_lshl_add_u64 v[46:47], v[46:47], 0, v[170:171]
	v_cvt_pk_bf16_f32 v44, v44, v45
	v_cvt_pk_bf16_f32 v45, v52, v53
	global_store_dwordx4 v[46:47], v[42:45], off sc0 sc1
	s_waitcnt vmcnt(10)
	v_pk_fma_f32 v[34:35], v[34:35], v[142:143], v[98:99]
	s_waitcnt vmcnt(8)
	v_pk_fma_f32 v[24:25], v[24:25], v[136:137], v[108:109]
	v_pk_fma_f32 v[42:43], v[32:33], v[132:133], v[96:97]
	v_pk_fma_f32 v[32:33], v[30:31], v[130:131], v[94:95]
	v_cvt_pk_bf16_f32 v30, v38, v39
	v_cvt_pk_bf16_f32 v31, v40, v41
	v_pk_fma_f32 v[22:23], v[22:23], v[134:135], v[106:107]
	v_cvt_pk_bf16_f32 v32, v32, v33
	v_cvt_pk_bf16_f32 v33, v42, v43
	global_store_dwordx4 v[46:47], v[30:33], off offset:256 sc0 sc1
	s_waitcnt vmcnt(7)
	v_pk_fma_f32 v[18:19], v[18:19], v[142:143], v[114:115]
	s_waitcnt vmcnt(5)
	v_pk_fma_f32 v[8:9], v[8:9], v[136:137], v[124:125]
	v_lshlrev_b64 v[30:31], 12, v[150:151]
	v_lshl_add_u64 v[30:31], s[6:7], 0, v[30:31]
	v_pk_fma_f32 v[32:33], v[36:37], v[144:145], v[100:101]
	v_pk_fma_f32 v[36:37], v[28:29], v[140:141], v[104:105]
	v_pk_fma_f32 v[28:29], v[26:27], v[138:139], v[102:103]
	v_cvt_pk_bf16_f32 v26, v34, v35
	v_cvt_pk_bf16_f32 v27, v32, v33
	v_lshl_add_u64 v[30:31], v[30:31], 0, v[170:171]
	v_cvt_pk_bf16_f32 v28, v28, v29
	v_cvt_pk_bf16_f32 v29, v36, v37
	global_store_dwordx4 v[30:31], v[26:29], off sc0 sc1
	v_pk_fma_f32 v[6:7], v[6:7], v[134:135], v[122:123]
	s_nop 0
	v_pk_fma_f32 v[26:27], v[16:17], v[132:133], v[112:113]
	v_pk_fma_f32 v[16:17], v[14:15], v[130:131], v[110:111]
	v_cvt_pk_bf16_f32 v14, v22, v23
	v_cvt_pk_bf16_f32 v15, v24, v25
	s_nop 0
	v_cvt_pk_bf16_f32 v16, v16, v17
	v_cvt_pk_bf16_f32 v17, v26, v27
	global_store_dwordx4 v[30:31], v[14:17], off offset:256 sc0 sc1
	s_nop 1
	v_lshlrev_b64 v[14:15], 12, v[152:153]
	v_lshl_add_u64 v[14:15], s[6:7], 0, v[14:15]
	v_pk_fma_f32 v[16:17], v[20:21], v[144:145], v[116:117]
	v_pk_fma_f32 v[20:21], v[12:13], v[140:141], v[120:121]
	v_pk_fma_f32 v[12:13], v[10:11], v[138:139], v[118:119]
	v_cvt_pk_bf16_f32 v10, v18, v19
	v_cvt_pk_bf16_f32 v11, v16, v17
	v_lshl_add_u64 v[14:15], v[14:15], 0, v[170:171]
	v_cvt_pk_bf16_f32 v12, v12, v13
	v_cvt_pk_bf16_f32 v13, v20, v21
	global_store_dwordx4 v[14:15], v[10:13], off sc0 sc1
	s_waitcnt vmcnt(7)
	s_nop 0
	v_pk_fma_f32 v[10:11], v[4:5], v[132:133], v[128:129]
	v_pk_fma_f32 v[4:5], v[2:3], v[130:131], v[126:127]
	v_cvt_pk_bf16_f32 v2, v6, v7
	v_cvt_pk_bf16_f32 v3, v8, v9
	s_nop 0
	v_cvt_pk_bf16_f32 v4, v4, v5
	v_cvt_pk_bf16_f32 v5, v10, v11
	global_store_dwordx4 v[14:15], v[2:5], off offset:256 sc0 sc1
	s_cbranch_vccnz .LBB0_530
	s_andn2_b64 vcc, exec, s[4:5]
	s_cbranch_vccnz .LBB0_529
	s_barrier
	s_branch .LBB0_529

;     __device__ __forceinline__ f2 swi2(f2 G, f2 U, float kexp, float kout) const {
;         const f2 t = G * kexp; f2 e; e.x = __builtin_amdgcn_exp2f(t.x); e.y = __builtin_amdgcn_exp2f(t.y);
;         const f2 d = e + 1.0f; f2 r; r.x = __builtin_amdgcn_rcpf(d.x); r.y = __builtin_amdgcn_rcpf(d.y);
;         f2 h = (G * U) * r * kout; h.x = __builtin_amdgcn_fmed3f(h.x, -448.f, 448.f); h.y = __builtin_amdgcn_fmed3f(h.y, -448.f, 448.f); return h; }
;     __device__ __forceinline__ void operator()(const f32x4 (&acc)[2][2][4][2], const Unit& u, int wr, int wc, int fr, int fq) const {
;         const int row0 = u.pm * BM + wr * 64 + fr, col0 = u.pn * HALF + wc * 32 + 8 * fq;
;         const float kexp = -1.4426950408889634f * ascale, kout = ascale * ascale * scale;
; #pragma unroll
;         for (int ai = 0; ai < 2; ++ai)
; #pragma unroll
;             for (int m = 0; m < 4; ++m) { unsigned char* rowp = O + (size_t)(row0 + ai * HALF + m * 16) * ldc + col0;
;                 const f32x4 g0 = acc[ai][0][m][0], g1 = acc[ai][0][m][1], u0 = acc[ai][1][m][0], u1 = acc[ai][1][m][1];
;                 const f2 a = swi2((f2){g0[0], g0[1]}, (f2){u0[0], u0[1]}, kexp, kout), b = swi2((f2){g0[2], g0[3]}, (f2){u0[2], u0[3]}, kexp, kout);
;                 const f2 c = swi2((f2){g1[0], g1[1]}, (f2){u1[0], u1[1]}, kexp, kout), d = swi2((f2){g1[2], g1[3]}, (f2){u1[2], u1[3]}, kexp, kout);
;                 int p0 = 0, p1 = 0;
;                 p0 = __builtin_amdgcn_cvt_pk_fp8_f32(a.x, a.y, p0, false); p0 = __builtin_amdgcn_cvt_pk_fp8_f32(b.x, b.y, p0, true);
;                 p1 = __builtin_amdgcn_cvt_pk_fp8_f32(c.x, c.y, p1, false); p1 = __builtin_amdgcn_cvt_pk_fp8_f32(d.x, d.y, p1, true);
;                 typedef unsigned u32x2 __attribute__((ext_vector_type(2))); u32x2 w; w.x = (unsigned)p0; w.y = (unsigned)p1; *(u32x2*)rowp = w; }
.LBB0_678:
	v_pk_mul_f32 v[4:5], v[158:159], s[12:13] op_sel_hi:[1,0]
	v_pk_mul_f32 v[12:13], v[160:161], s[12:13] op_sel_hi:[1,0]
	v_exp_f32_e32 v8, v4
	v_exp_f32_e32 v9, v5
	v_exp_f32_e32 v12, v12
	v_exp_f32_e32 v13, v13
	v_pk_mul_f32 v[16:17], v[158:159], v[154:155]
	v_pk_add_f32 v[8:9], v[8:9], 1.0 op_sel_hi:[1,0]
	v_pk_mul_f32 v[14:15], v[160:161], v[156:157]
	v_rcp_f32_e32 v8, v8
	v_rcp_f32_e32 v9, v9
	v_pk_add_f32 v[12:13], v[12:13], 1.0 op_sel_hi:[1,0]
	v_lshl_add_u32 v6, s24, 8, v1
	v_rcp_f32_e32 v12, v12
	v_rcp_f32_e32 v13, v13
	v_pk_mul_f32 v[8:9], v[8:9], v[16:17]
	v_pk_mul_f32 v[16:17], v[150:151], v[146:147]
	v_pk_mul_f32 v[8:9], v[8:9], s[14:15] op_sel_hi:[1,0]
	v_lshl_or_b32 v2, s26, 7, v181
	v_med3_f32 v7, v8, s47, v193
	v_med3_f32 v18, v9, s47, v193
	v_pk_mul_f32 v[8:9], v[12:13], v[14:15]
	v_pk_mul_f32 v[12:13], v[150:151], s[12:13] op_sel_hi:[1,0]
	v_pk_mul_f32 v[8:9], v[8:9], s[14:15] op_sel_hi:[1,0]
	v_exp_f32_e32 v12, v12
	v_exp_f32_e32 v13, v13
	v_med3_f32 v19, v8, s47, v193
	v_med3_f32 v20, v9, s47, v193
	v_pk_mul_f32 v[14:15], v[152:153], v[148:149]
	v_pk_add_f32 v[8:9], v[12:13], 1.0 op_sel_hi:[1,0]
	v_pk_mul_f32 v[12:13], v[152:153], s[12:13] op_sel_hi:[1,0]
	v_rcp_f32_e32 v8, v8
	v_exp_f32_e32 v12, v12
	v_exp_f32_e32 v13, v13
	v_rcp_f32_e32 v9, v9
	v_mov_b64_e32 v[4:5], s[6:7]
	v_ashrrev_i32_e32 v3, 31, v2
	v_pk_add_f32 v[12:13], v[12:13], 1.0 op_sel_hi:[1,0]
	v_pk_mul_f32 v[8:9], v[8:9], v[16:17]
	v_rcp_f32_e32 v12, v12
	v_rcp_f32_e32 v13, v13
	v_pk_mul_f32 v[8:9], v[8:9], s[14:15] op_sel_hi:[1,0]
	v_mad_i64_i32 v[10:11], s[28:29], v6, s46, v[4:5]
	v_med3_f32 v16, v8, s47, v193
	v_med3_f32 v17, v9, s47, v193
	v_pk_mul_f32 v[8:9], v[12:13], v[14:15]
	v_mov_b32_e32 v12, 0
	v_mov_b32_e32 v13, 0
	v_cvt_pk_fp8_f32 v12, v7, v18
	v_cvt_pk_fp8_f32 v13, v16, v17
	v_pk_mul_f32 v[8:9], v[8:9], s[14:15] op_sel_hi:[1,0]
	v_lshl_add_u64 v[10:11], v[10:11], 0, v[2:3]
	v_med3_f32 v7, v8, s47, v193
	v_med3_f32 v8, v9, s47, v193
	v_cvt_pk_fp8_f32 v12, v19, v20 op_sel:[0,0,1]
	v_cvt_pk_fp8_f32 v13, v7, v8 op_sel:[0,0,1]
	v_pk_mul_f32 v[8:9], v[142:143], s[12:13] op_sel_hi:[1,0]
	s_nop 15
	s_nop 15
	v_pk_mul_f32 v[14:15], v[142:143], v[138:139]
	v_exp_f32_e32 v8, v8
	v_exp_f32_e32 v9, v9
	global_store_dwordx2 v[10:11], v[12:13], off sc0 sc1
	v_pk_mul_f32 v[10:11], v[144:145], s[12:13] op_sel_hi:[1,0]
	v_pk_mul_f32 v[12:13], v[144:145], v[140:141]
	v_exp_f32_e32 v10, v10
	v_exp_f32_e32 v11, v11
	v_pk_add_f32 v[8:9], v[8:9], 1.0 op_sel_hi:[1,0]
	v_or_b32_e32 v7, 16, v6
	v_rcp_f32_e32 v8, v8
	v_rcp_f32_e32 v9, v9
	v_pk_add_f32 v[10:11], v[10:11], 1.0 op_sel_hi:[1,0]
	s_andn2_b64 vcc, exec, s[0:1]
	v_rcp_f32_e32 v10, v10
	v_rcp_f32_e32 v11, v11
	v_pk_mul_f32 v[8:9], v[8:9], v[14:15]
	v_pk_mul_f32 v[14:15], v[134:135], v[130:131]
	v_pk_mul_f32 v[8:9], v[8:9], s[14:15] op_sel_hi:[1,0]
	s_mov_b64 s[0:1], -1
	v_med3_f32 v16, v8, s47, v193
	v_med3_f32 v17, v9, s47, v193
	v_pk_mul_f32 v[8:9], v[10:11], v[12:13]
	v_pk_mul_f32 v[10:11], v[134:135], s[12:13] op_sel_hi:[1,0]
	v_pk_mul_f32 v[8:9], v[8:9], s[14:15] op_sel_hi:[1,0]
	v_exp_f32_e32 v10, v10
	v_exp_f32_e32 v11, v11
	v_med3_f32 v18, v8, s47, v193
	v_med3_f32 v19, v9, s47, v193
	v_pk_mul_f32 v[12:13], v[136:137], v[132:133]
	v_pk_add_f32 v[8:9], v[10:11], 1.0 op_sel_hi:[1,0]
	v_pk_mul_f32 v[10:11], v[136:137], s[12:13] op_sel_hi:[1,0]
	v_rcp_f32_e32 v8, v8
	v_exp_f32_e32 v10, v10
	v_exp_f32_e32 v11, v11
	v_rcp_f32_e32 v9, v9
	v_pk_add_f32 v[10:11], v[10:11], 1.0 op_sel_hi:[1,0]
	s_nop 0
	v_rcp_f32_e32 v10, v10
	v_rcp_f32_e32 v11, v11
	v_pk_mul_f32 v[8:9], v[8:9], v[14:15]
	s_nop 0
	v_pk_mul_f32 v[8:9], v[8:9], s[14:15] op_sel_hi:[1,0]
	s_nop 0
	v_med3_f32 v14, v8, s47, v193
	v_med3_f32 v15, v9, s47, v193
	v_pk_mul_f32 v[8:9], v[10:11], v[12:13]
	v_mov_b32_e32 v10, 0
	v_mov_b32_e32 v11, 0
	v_cvt_pk_fp8_f32 v10, v16, v17
	v_cvt_pk_fp8_f32 v11, v14, v15
	v_pk_mul_f32 v[8:9], v[8:9], s[14:15] op_sel_hi:[1,0]
	v_pk_mul_f32 v[12:13], v[128:129], s[12:13] op_sel_hi:[1,0]
	v_med3_f32 v8, v8, s47, v193
	v_med3_f32 v9, v9, s47, v193
	v_cvt_pk_fp8_f32 v10, v18, v19 op_sel:[0,0,1]
	v_cvt_pk_fp8_f32 v11, v8, v9 op_sel:[0,0,1]
	v_mad_i64_i32 v[8:9], s[28:29], v7, s46, v[4:5]
	v_lshl_add_u64 v[8:9], v[8:9], 0, v[2:3]
	global_store_dwordx2 v[8:9], v[10:11], off sc0 sc1
	v_pk_mul_f32 v[8:9], v[126:127], s[12:13] op_sel_hi:[1,0]
	v_exp_f32_e32 v12, v12
	v_exp_f32_e32 v8, v8
	v_exp_f32_e32 v9, v9
	v_exp_f32_e32 v13, v13
	v_pk_mul_f32 v[16:17], v[126:127], v[122:123]
	v_or_b32_e32 v7, 32, v6
	v_pk_add_f32 v[8:9], v[8:9], 1.0 op_sel_hi:[1,0]
	v_pk_add_f32 v[12:13], v[12:13], 1.0 op_sel_hi:[1,0]
	v_rcp_f32_e32 v8, v8
	v_rcp_f32_e32 v9, v9
	v_rcp_f32_e32 v12, v12
	v_rcp_f32_e32 v13, v13
	v_pk_mul_f32 v[14:15], v[128:129], v[124:125]
	v_pk_mul_f32 v[8:9], v[8:9], v[16:17]
	v_mad_i64_i32 v[10:11], s[28:29], v7, s46, v[4:5]
	v_pk_mul_f32 v[8:9], v[8:9], s[14:15] op_sel_hi:[1,0]
	v_pk_mul_f32 v[16:17], v[118:119], v[114:115]
	v_med3_f32 v7, v8, s47, v193
	v_med3_f32 v18, v9, s47, v193
	v_pk_mul_f32 v[8:9], v[12:13], v[14:15]
	v_pk_mul_f32 v[12:13], v[118:119], s[12:13] op_sel_hi:[1,0]
	v_pk_mul_f32 v[8:9], v[8:9], s[14:15] op_sel_hi:[1,0]
	v_exp_f32_e32 v12, v12
	v_exp_f32_e32 v13, v13
	v_med3_f32 v19, v8, s47, v193
	v_med3_f32 v20, v9, s47, v193
	v_pk_mul_f32 v[14:15], v[120:121], v[116:117]
	v_pk_add_f32 v[8:9], v[12:13], 1.0 op_sel_hi:[1,0]
	v_pk_mul_f32 v[12:13], v[120:121], s[12:13] op_sel_hi:[1,0]
	v_rcp_f32_e32 v8, v8
	v_exp_f32_e32 v12, v12
	v_exp_f32_e32 v13, v13
	v_rcp_f32_e32 v9, v9
	v_lshl_add_u64 v[10:11], v[10:11], 0, v[2:3]
	v_pk_add_f32 v[12:13], v[12:13], 1.0 op_sel_hi:[1,0]
	s_nop 0
;     __device__ __forceinline__ f2 swi2(f2 G, f2 U, float kexp, float kout) const {
;         const f2 t = G * kexp; f2 e; e.x = __builtin_amdgcn_exp2f(t.x); e.y = __builtin_amdgcn_exp2f(t.y);
;         const f2 d = e + 1.0f; f2 r; r.x = __builtin_amdgcn_rcpf(d.x); r.y = __builtin_amdgcn_rcpf(d.y);
;         f2 h = (G * U) * r * kout; h.x = __builtin_amdgcn_fmed3f(h.x, -448.f, 448.f); h.y = __builtin_amdgcn_fmed3f(h.y, -448.f, 448.f); return h; }
;     __device__ __forceinline__ void operator()(const f32x4 (&acc)[2][2][4][2], const Unit& u, int wr, int wc, int fr, int fq) const {
;         const int row0 = u.pm * BM + wr * 64 + fr, col0 = u.pn * HALF + wc * 32 + 8 * fq;
;         const float kexp = -1.4426950408889634f * ascale, kout = ascale * ascale * scale;
; #pragma unroll
;         for (int ai = 0; ai < 2; ++ai)
; #pragma unroll
;             for (int m = 0; m < 4; ++m) { unsigned char* rowp = O + (size_t)(row0 + ai * HALF + m * 16) * ldc + col0;
;                 const f32x4 g0 = acc[ai][0][m][0], g1 = acc[ai][0][m][1], u0 = acc[ai][1][m][0], u1 = acc[ai][1][m][1];
;                 const f2 a = swi2((f2){g0[0], g0[1]}, (f2){u0[0], u0[1]}, kexp, kout), b = swi2((f2){g0[2], g0[3]}, (f2){u0[2], u0[3]}, kexp, kout);
;                 const f2 c = swi2((f2){g1[0], g1[1]}, (f2){u1[0], u1[1]}, kexp, kout), d = swi2((f2){g1[2], g1[3]}, (f2){u1[2], u1[3]}, kexp, kout);
;                 int p0 = 0, p1 = 0;
;                 p0 = __builtin_amdgcn_cvt_pk_fp8_f32(a.x, a.y, p0, false); p0 = __builtin_amdgcn_cvt_pk_fp8_f32(b.x, b.y, p0, true);
;                 p1 = __builtin_amdgcn_cvt_pk_fp8_f32(c.x, c.y, p1, false); p1 = __builtin_amdgcn_cvt_pk_fp8_f32(d.x, d.y, p1, true);
;                 typedef unsigned u32x2 __attribute__((ext_vector_type(2))); u32x2 w; w.x = (unsigned)p0; w.y = (unsigned)p1; *(u32x2*)rowp = w; }
	v_rcp_f32_e32 v12, v12
	v_rcp_f32_e32 v13, v13
	v_pk_mul_f32 v[8:9], v[8:9], v[16:17]
	s_nop 0
	v_pk_mul_f32 v[8:9], v[8:9], s[14:15] op_sel_hi:[1,0]
	s_nop 0
	v_med3_f32 v16, v8, s47, v193
	v_med3_f32 v17, v9, s47, v193
	v_pk_mul_f32 v[8:9], v[12:13], v[14:15]
	v_mov_b32_e32 v12, 0
	v_mov_b32_e32 v13, 0
	v_cvt_pk_fp8_f32 v12, v7, v18
	v_cvt_pk_fp8_f32 v13, v16, v17
	v_pk_mul_f32 v[8:9], v[8:9], s[14:15] op_sel_hi:[1,0]
	v_pk_mul_f32 v[14:15], v[110:111], v[106:107]
	v_med3_f32 v7, v8, s47, v193
	v_med3_f32 v8, v9, s47, v193
	v_cvt_pk_fp8_f32 v12, v19, v20 op_sel:[0,0,1]
	v_cvt_pk_fp8_f32 v13, v7, v8 op_sel:[0,0,1]
	v_pk_mul_f32 v[8:9], v[110:111], s[12:13] op_sel_hi:[1,0]
	v_or_b32_e32 v7, 48, v6
	v_exp_f32_e32 v8, v8
	v_exp_f32_e32 v9, v9
	global_store_dwordx2 v[10:11], v[12:13], off sc0 sc1
	v_pk_mul_f32 v[10:11], v[112:113], s[12:13] op_sel_hi:[1,0]
	v_pk_mul_f32 v[12:13], v[112:113], v[108:109]
	v_exp_f32_e32 v10, v10
	v_exp_f32_e32 v11, v11
	v_pk_add_f32 v[8:9], v[8:9], 1.0 op_sel_hi:[1,0]
	v_pk_add_f32 v[10:11], v[10:11], 1.0 op_sel_hi:[1,0]
	v_rcp_f32_e32 v8, v8
	v_rcp_f32_e32 v9, v9
	v_rcp_f32_e32 v10, v10
	v_rcp_f32_e32 v11, v11
	v_pk_mul_f32 v[8:9], v[8:9], v[14:15]
	s_nop 0
	v_pk_mul_f32 v[8:9], v[8:9], s[14:15] op_sel_hi:[1,0]
	v_pk_mul_f32 v[14:15], v[102:103], v[98:99]
	v_med3_f32 v16, v8, s47, v193
	v_med3_f32 v17, v9, s47, v193
	v_pk_mul_f32 v[8:9], v[10:11], v[12:13]
	v_pk_mul_f32 v[10:11], v[102:103], s[12:13] op_sel_hi:[1,0]
	v_pk_mul_f32 v[8:9], v[8:9], s[14:15] op_sel_hi:[1,0]
	v_exp_f32_e32 v10, v10
	v_exp_f32_e32 v11, v11
	v_med3_f32 v18, v8, s47, v193
	v_med3_f32 v19, v9, s47, v193
	v_pk_mul_f32 v[12:13], v[104:105], v[100:101]
	v_pk_add_f32 v[8:9], v[10:11], 1.0 op_sel_hi:[1,0]
	v_pk_mul_f32 v[10:11], v[104:105], s[12:13] op_sel_hi:[1,0]
	v_rcp_f32_e32 v8, v8
	v_exp_f32_e32 v10, v10
	v_exp_f32_e32 v11, v11
	v_rcp_f32_e32 v9, v9
	v_pk_add_f32 v[10:11], v[10:11], 1.0 op_sel_hi:[1,0]
	s_nop 0
	v_rcp_f32_e32 v10, v10
	v_rcp_f32_e32 v11, v11
	v_pk_mul_f32 v[8:9], v[8:9], v[14:15]
	s_nop 0
	v_pk_mul_f32 v[8:9], v[8:9], s[14:15] op_sel_hi:[1,0]
	s_nop 0
	v_med3_f32 v14, v8, s47, v193
	v_med3_f32 v15, v9, s47, v193
	v_pk_mul_f32 v[8:9], v[10:11], v[12:13]
	v_mov_b32_e32 v10, 0
	v_mov_b32_e32 v11, 0
	v_cvt_pk_fp8_f32 v10, v16, v17
	v_cvt_pk_fp8_f32 v11, v14, v15
	v_pk_mul_f32 v[8:9], v[8:9], s[14:15] op_sel_hi:[1,0]
	v_pk_mul_f32 v[12:13], v[96:97], s[12:13] op_sel_hi:[1,0]
	v_med3_f32 v8, v8, s47, v193
	v_med3_f32 v9, v9, s47, v193
	v_cvt_pk_fp8_f32 v10, v18, v19 op_sel:[0,0,1]
	v_cvt_pk_fp8_f32 v11, v8, v9 op_sel:[0,0,1]
	v_mad_i64_i32 v[8:9], s[28:29], v7, s46, v[4:5]
	v_lshl_add_u64 v[8:9], v[8:9], 0, v[2:3]
	global_store_dwordx2 v[8:9], v[10:11], off sc0 sc1
	v_pk_mul_f32 v[8:9], v[94:95], s[12:13] op_sel_hi:[1,0]
	v_exp_f32_e32 v12, v12
	v_exp_f32_e32 v8, v8
	v_exp_f32_e32 v9, v9
	v_exp_f32_e32 v13, v13
	v_pk_mul_f32 v[16:17], v[94:95], v[90:91]
	v_add_u32_e32 v7, 0x80, v6
	v_pk_add_f32 v[8:9], v[8:9], 1.0 op_sel_hi:[1,0]
	v_pk_add_f32 v[12:13], v[12:13], 1.0 op_sel_hi:[1,0]
	v_rcp_f32_e32 v8, v8
	v_rcp_f32_e32 v9, v9
	v_rcp_f32_e32 v12, v12
	v_rcp_f32_e32 v13, v13
	v_pk_mul_f32 v[14:15], v[96:97], v[92:93]
	v_pk_mul_f32 v[8:9], v[8:9], v[16:17]
	v_mad_i64_i32 v[10:11], s[28:29], v7, s46, v[4:5]
	v_pk_mul_f32 v[8:9], v[8:9], s[14:15] op_sel_hi:[1,0]
	v_pk_mul_f32 v[16:17], v[86:87], v[82:83]
	v_med3_f32 v7, v8, s47, v193
	v_med3_f32 v18, v9, s47, v193
	v_pk_mul_f32 v[8:9], v[12:13], v[14:15]
	v_pk_mul_f32 v[12:13], v[86:87], s[12:13] op_sel_hi:[1,0]
	v_pk_mul_f32 v[8:9], v[8:9], s[14:15] op_sel_hi:[1,0]
	v_exp_f32_e32 v12, v12
	v_exp_f32_e32 v13, v13
	v_med3_f32 v19, v8, s47, v193
	v_med3_f32 v20, v9, s47, v193
	v_pk_mul_f32 v[14:15], v[88:89], v[84:85]
	v_pk_add_f32 v[8:9], v[12:13], 1.0 op_sel_hi:[1,0]
	v_pk_mul_f32 v[12:13], v[88:89], s[12:13] op_sel_hi:[1,0]
	v_rcp_f32_e32 v8, v8
	v_exp_f32_e32 v12, v12
	v_exp_f32_e32 v13, v13
	v_rcp_f32_e32 v9, v9
	v_lshl_add_u64 v[10:11], v[10:11], 0, v[2:3]
	v_pk_add_f32 v[12:13], v[12:13], 1.0 op_sel_hi:[1,0]
	s_nop 0
	v_rcp_f32_e32 v12, v12
	v_rcp_f32_e32 v13, v13
	v_pk_mul_f32 v[8:9], v[8:9], v[16:17]
	s_nop 0
	v_pk_mul_f32 v[8:9], v[8:9], s[14:15] op_sel_hi:[1,0]
	s_nop 0
	v_med3_f32 v16, v8, s47, v193
	v_med3_f32 v17, v9, s47, v193
	v_pk_mul_f32 v[8:9], v[12:13], v[14:15]
	v_mov_b32_e32 v12, 0
	v_mov_b32_e32 v13, 0
	v_cvt_pk_fp8_f32 v12, v7, v18
	v_cvt_pk_fp8_f32 v13, v16, v17
	v_pk_mul_f32 v[8:9], v[8:9], s[14:15] op_sel_hi:[1,0]
	v_pk_mul_f32 v[14:15], v[78:79], v[74:75]
	v_med3_f32 v7, v8, s47, v193
	v_med3_f32 v8, v9, s47, v193
	v_cvt_pk_fp8_f32 v12, v19, v20 op_sel:[0,0,1]
	v_cvt_pk_fp8_f32 v13, v7, v8 op_sel:[0,0,1]
	v_pk_mul_f32 v[8:9], v[78:79], s[12:13] op_sel_hi:[1,0]
	v_add_u32_e32 v7, 0x90, v6
	v_exp_f32_e32 v8, v8
	v_exp_f32_e32 v9, v9
	global_store_dwordx2 v[10:11], v[12:13], off sc0 sc1
	v_pk_mul_f32 v[10:11], v[80:81], s[12:13] op_sel_hi:[1,0]
	v_pk_mul_f32 v[12:13], v[80:81], v[76:77]
	v_exp_f32_e32 v10, v10
	v_exp_f32_e32 v11, v11
	v_pk_add_f32 v[8:9], v[8:9], 1.0 op_sel_hi:[1,0]
	v_pk_add_f32 v[10:11], v[10:11], 1.0 op_sel_hi:[1,0]
	v_rcp_f32_e32 v8, v8
	v_rcp_f32_e32 v9, v9
	v_rcp_f32_e32 v10, v10
	v_rcp_f32_e32 v11, v11
	v_pk_mul_f32 v[8:9], v[8:9], v[14:15]
	s_nop 0
	v_pk_mul_f32 v[8:9], v[8:9], s[14:15] op_sel_hi:[1,0]
	v_pk_mul_f32 v[14:15], v[70:71], v[66:67]
	v_med3_f32 v16, v8, s47, v193
	v_med3_f32 v17, v9, s47, v193
;     __device__ __forceinline__ f2 swi2(f2 G, f2 U, float kexp, float kout) const {
;         const f2 t = G * kexp; f2 e; e.x = __builtin_amdgcn_exp2f(t.x); e.y = __builtin_amdgcn_exp2f(t.y);
;         const f2 d = e + 1.0f; f2 r; r.x = __builtin_amdgcn_rcpf(d.x); r.y = __builtin_amdgcn_rcpf(d.y);
;         f2 h = (G * U) * r * kout; h.x = __builtin_amdgcn_fmed3f(h.x, -448.f, 448.f); h.y = __builtin_amdgcn_fmed3f(h.y, -448.f, 448.f); return h; }
;     __device__ __forceinline__ void operator()(const f32x4 (&acc)[2][2][4][2], const Unit& u, int wr, int wc, int fr, int fq) const {
;         const int row0 = u.pm * BM + wr * 64 + fr, col0 = u.pn * HALF + wc * 32 + 8 * fq;
;         const float kexp = -1.4426950408889634f * ascale, kout = ascale * ascale * scale;
; #pragma unroll
;         for (int ai = 0; ai < 2; ++ai)
; #pragma unroll
;             for (int m = 0; m < 4; ++m) { unsigned char* rowp = O + (size_t)(row0 + ai * HALF + m * 16) * ldc + col0;
;                 const f32x4 g0 = acc[ai][0][m][0], g1 = acc[ai][0][m][1], u0 = acc[ai][1][m][0], u1 = acc[ai][1][m][1];
;                 const f2 a = swi2((f2){g0[0], g0[1]}, (f2){u0[0], u0[1]}, kexp, kout), b = swi2((f2){g0[2], g0[3]}, (f2){u0[2], u0[3]}, kexp, kout);
;                 const f2 c = swi2((f2){g1[0], g1[1]}, (f2){u1[0], u1[1]}, kexp, kout), d = swi2((f2){g1[2], g1[3]}, (f2){u1[2], u1[3]}, kexp, kout);
;                 int p0 = 0, p1 = 0;
;                 p0 = __builtin_amdgcn_cvt_pk_fp8_f32(a.x, a.y, p0, false); p0 = __builtin_amdgcn_cvt_pk_fp8_f32(b.x, b.y, p0, true);
;                 p1 = __builtin_amdgcn_cvt_pk_fp8_f32(c.x, c.y, p1, false); p1 = __builtin_amdgcn_cvt_pk_fp8_f32(d.x, d.y, p1, true);
;                 typedef unsigned u32x2 __attribute__((ext_vector_type(2))); u32x2 w; w.x = (unsigned)p0; w.y = (unsigned)p1; *(u32x2*)rowp = w; }
	v_pk_mul_f32 v[8:9], v[10:11], v[12:13]
	v_pk_mul_f32 v[10:11], v[70:71], s[12:13] op_sel_hi:[1,0]
	v_pk_mul_f32 v[8:9], v[8:9], s[14:15] op_sel_hi:[1,0]
	v_exp_f32_e32 v10, v10
	v_exp_f32_e32 v11, v11
	v_med3_f32 v18, v8, s47, v193
	v_med3_f32 v19, v9, s47, v193
	v_pk_mul_f32 v[12:13], v[72:73], v[68:69]
	v_pk_add_f32 v[8:9], v[10:11], 1.0 op_sel_hi:[1,0]
	v_pk_mul_f32 v[10:11], v[72:73], s[12:13] op_sel_hi:[1,0]
	v_rcp_f32_e32 v8, v8
	v_exp_f32_e32 v10, v10
	v_exp_f32_e32 v11, v11
	v_rcp_f32_e32 v9, v9
	v_pk_add_f32 v[10:11], v[10:11], 1.0 op_sel_hi:[1,0]
	s_nop 0
	v_rcp_f32_e32 v10, v10
	v_rcp_f32_e32 v11, v11
	v_pk_mul_f32 v[8:9], v[8:9], v[14:15]
	s_nop 0
	v_pk_mul_f32 v[8:9], v[8:9], s[14:15] op_sel_hi:[1,0]
	s_nop 0
	v_med3_f32 v14, v8, s47, v193
	v_med3_f32 v15, v9, s47, v193
	v_pk_mul_f32 v[8:9], v[10:11], v[12:13]
	v_mov_b32_e32 v10, 0
	v_mov_b32_e32 v11, 0
	v_cvt_pk_fp8_f32 v10, v16, v17
	v_cvt_pk_fp8_f32 v11, v14, v15
	v_pk_mul_f32 v[8:9], v[8:9], s[14:15] op_sel_hi:[1,0]
	v_pk_mul_f32 v[12:13], v[64:65], s[12:13] op_sel_hi:[1,0]
	v_med3_f32 v8, v8, s47, v193
	v_med3_f32 v9, v9, s47, v193
	v_cvt_pk_fp8_f32 v10, v18, v19 op_sel:[0,0,1]
	v_cvt_pk_fp8_f32 v11, v8, v9 op_sel:[0,0,1]
	v_mad_i64_i32 v[8:9], s[28:29], v7, s46, v[4:5]
	v_lshl_add_u64 v[8:9], v[8:9], 0, v[2:3]
	global_store_dwordx2 v[8:9], v[10:11], off sc0 sc1
	v_pk_mul_f32 v[8:9], v[62:63], s[12:13] op_sel_hi:[1,0]
	v_exp_f32_e32 v12, v12
	v_exp_f32_e32 v8, v8
	v_exp_f32_e32 v9, v9
	v_exp_f32_e32 v13, v13
	v_pk_mul_f32 v[16:17], v[62:63], v[58:59]
	v_add_u32_e32 v7, 0xa0, v6
	v_pk_add_f32 v[8:9], v[8:9], 1.0 op_sel_hi:[1,0]
	v_pk_add_f32 v[12:13], v[12:13], 1.0 op_sel_hi:[1,0]
	v_rcp_f32_e32 v8, v8
	v_rcp_f32_e32 v9, v9
	v_rcp_f32_e32 v12, v12
	v_rcp_f32_e32 v13, v13
	v_pk_mul_f32 v[14:15], v[64:65], v[60:61]
	v_pk_mul_f32 v[8:9], v[8:9], v[16:17]
	v_mad_i64_i32 v[10:11], s[28:29], v7, s46, v[4:5]
	v_pk_mul_f32 v[8:9], v[8:9], s[14:15] op_sel_hi:[1,0]
	v_pk_mul_f32 v[16:17], v[54:55], v[50:51]
	v_med3_f32 v7, v8, s47, v193
	v_med3_f32 v18, v9, s47, v193
	v_pk_mul_f32 v[8:9], v[12:13], v[14:15]
	v_pk_mul_f32 v[12:13], v[54:55], s[12:13] op_sel_hi:[1,0]
	v_pk_mul_f32 v[8:9], v[8:9], s[14:15] op_sel_hi:[1,0]
	v_exp_f32_e32 v12, v12
	v_exp_f32_e32 v13, v13
	v_med3_f32 v19, v8, s47, v193
	v_med3_f32 v20, v9, s47, v193
	v_pk_mul_f32 v[14:15], v[56:57], v[52:53]
	v_pk_add_f32 v[8:9], v[12:13], 1.0 op_sel_hi:[1,0]
	v_pk_mul_f32 v[12:13], v[56:57], s[12:13] op_sel_hi:[1,0]
	v_rcp_f32_e32 v8, v8
	v_exp_f32_e32 v12, v12
	v_exp_f32_e32 v13, v13
	v_rcp_f32_e32 v9, v9
	v_lshl_add_u64 v[10:11], v[10:11], 0, v[2:3]
	v_pk_add_f32 v[12:13], v[12:13], 1.0 op_sel_hi:[1,0]
	s_nop 0
	v_rcp_f32_e32 v12, v12
	v_rcp_f32_e32 v13, v13
	v_pk_mul_f32 v[8:9], v[8:9], v[16:17]
	s_nop 0
	v_pk_mul_f32 v[8:9], v[8:9], s[14:15] op_sel_hi:[1,0]
	s_nop 0
	v_med3_f32 v16, v8, s47, v193
	v_med3_f32 v17, v9, s47, v193
	v_pk_mul_f32 v[8:9], v[12:13], v[14:15]
	v_mov_b32_e32 v13, 0
	v_cvt_pk_fp8_f32 v13, v16, v17
	v_pk_mul_f32 v[8:9], v[8:9], s[14:15] op_sel_hi:[1,0]
	v_mov_b32_e32 v12, 0
	v_cvt_pk_fp8_f32 v12, v7, v18
	v_med3_f32 v7, v8, s47, v193
	v_med3_f32 v8, v9, s47, v193
	v_cvt_pk_fp8_f32 v13, v7, v8 op_sel:[0,0,1]
	v_pk_mul_f32 v[8:9], v[46:47], s[12:13] op_sel_hi:[1,0]
	v_add_u32_e32 v14, 0xb0, v6
	v_exp_f32_e32 v8, v8
	v_exp_f32_e32 v9, v9
	v_cvt_pk_fp8_f32 v12, v19, v20 op_sel:[0,0,1]
	v_mad_i64_i32 v[4:5], s[28:29], v14, s46, v[4:5]
	v_pk_add_f32 v[6:7], v[8:9], 1.0 op_sel_hi:[1,0]
	v_pk_mul_f32 v[8:9], v[48:49], s[12:13] op_sel_hi:[1,0]
	v_rcp_f32_e32 v6, v6
	v_exp_f32_e32 v8, v8
	v_exp_f32_e32 v9, v9
	v_rcp_f32_e32 v7, v7
	global_store_dwordx2 v[10:11], v[12:13], off sc0 sc1
	v_pk_mul_f32 v[12:13], v[46:47], v[42:43]
	v_pk_add_f32 v[8:9], v[8:9], 1.0 op_sel_hi:[1,0]
	v_pk_mul_f32 v[6:7], v[6:7], v[12:13]
	v_rcp_f32_e32 v8, v8
	v_rcp_f32_e32 v9, v9
	v_pk_mul_f32 v[10:11], v[48:49], v[44:45]
	v_pk_mul_f32 v[6:7], v[6:7], s[14:15] op_sel_hi:[1,0]
	v_pk_mul_f32 v[12:13], v[38:39], v[34:35]
	v_med3_f32 v15, v6, s47, v193
	v_med3_f32 v16, v7, s47, v193
	v_pk_mul_f32 v[6:7], v[8:9], v[10:11]
	v_pk_mul_f32 v[8:9], v[38:39], s[12:13] op_sel_hi:[1,0]
	v_pk_mul_f32 v[6:7], v[6:7], s[14:15] op_sel_hi:[1,0]
	v_exp_f32_e32 v8, v8
	v_exp_f32_e32 v9, v9
	v_med3_f32 v17, v6, s47, v193
	v_med3_f32 v18, v7, s47, v193
	v_pk_mul_f32 v[10:11], v[40:41], v[36:37]
	v_pk_add_f32 v[6:7], v[8:9], 1.0 op_sel_hi:[1,0]
	v_pk_mul_f32 v[8:9], v[40:41], s[12:13] op_sel_hi:[1,0]
	v_rcp_f32_e32 v6, v6
	v_exp_f32_e32 v8, v8
	v_exp_f32_e32 v9, v9
	v_rcp_f32_e32 v7, v7
	v_lshl_add_u64 v[2:3], v[4:5], 0, v[2:3]
	v_pk_add_f32 v[8:9], v[8:9], 1.0 op_sel_hi:[1,0]
	s_nop 0
	v_rcp_f32_e32 v8, v8
	v_rcp_f32_e32 v9, v9
	v_pk_mul_f32 v[6:7], v[6:7], v[12:13]
	s_nop 0
	v_pk_mul_f32 v[6:7], v[6:7], s[14:15] op_sel_hi:[1,0]
	s_nop 0
	v_med3_f32 v12, v6, s47, v193
	v_med3_f32 v13, v7, s47, v193
	v_pk_mul_f32 v[6:7], v[8:9], v[10:11]
	v_mov_b32_e32 v8, 0
	v_mov_b32_e32 v9, 0
	v_cvt_pk_fp8_f32 v8, v15, v16
	v_cvt_pk_fp8_f32 v9, v12, v13
	v_pk_mul_f32 v[6:7], v[6:7], s[14:15] op_sel_hi:[1,0]
	v_cvt_pk_fp8_f32 v8, v17, v18 op_sel:[0,0,1]
	v_med3_f32 v6, v6, s47, v193
	v_med3_f32 v7, v7, s47, v193
	v_cvt_pk_fp8_f32 v9, v6, v7 op_sel:[0,0,1]
	global_store_dwordx2 v[2:3], v[8:9], off sc0 sc1
	s_cbranch_vccnz .LBB0_668
	s_andn2_b64 vcc, exec, s[4:5]
	s_cbranch_vccnz .LBB0_667
	s_barrier
	s_branch .LBB0_667

; __device__ __forceinline__ unsigned cvt_pk_bf16(float lo, float hi) { unsigned r; asm volatile("v_cvt_pk_bf16_f32 %0, %1, %2" : "=v"(r) : "v"(lo), "v"(hi)); return r; }
;     __device__ __forceinline__ void operator()(const f32x4 (&acc)[2][2][4][2], const Unit& u, int wr, int wc, int fr, int fq) const {
;     ...
;         const int row0 = u.pm * BM + wr * 64 + fr, col0 = u.pn * BM + wc * 32 + 8 * fq;
;         f32x4 gg[2][2];
; #pragma unroll
;         for (int bj = 0; bj < 2; ++bj)
; #pragma unroll
;             for (int n = 0; n < 2; ++n) gg[bj][n] = *(const f32x4*)(gv + col0 + bj * HALF + n * 4) * ascale;
; #pragma unroll
;         for (int ai = 0; ai < 2; ++ai) {
;             if constexpr (RB) {
;                 u32x4 bs[4][2];
; #pragma unroll
;                 for (int m = 0; m < 4; ++m)
; #pragma unroll
;                     for (int bj = 0; bj < 2; ++bj) bs[m][bj] = *(const u32x4*)(H + (size_t)(row0 + ai * HALF + m * 16) * 2048 + col0 + bj * HALF);
; #pragma unroll
;                 for (int m = 0; m < 4; ++m)
; #pragma unroll
;                     for (int bj = 0; bj < 2; ++bj) { const u32x4 b = bs[m][bj];
;                         f32x4 r0, r1; r0.x = __builtin_bit_cast(float, b.x << 16); r0.y = __builtin_bit_cast(float, b.x & 0xffff0000u); r0.z = __builtin_bit_cast(float, b.y << 16); r0.w = __builtin_bit_cast(float, b.y & 0xffff0000u);
;                         r1.x = __builtin_bit_cast(float, b.z << 16); r1.y = __builtin_bit_cast(float, b.z & 0xffff0000u); r1.z = __builtin_bit_cast(float, b.w << 16); r1.w = __builtin_bit_cast(float, b.w & 0xffff0000u);
;                         r0 += gg[bj][0] * acc[ai][bj][m][0]; r1 += gg[bj][1] * acc[ai][bj][m][1];
;                         u32x4 w; w.x = cvt_pk_bf16(r0[0], r0[1]); w.y = cvt_pk_bf16(r0[2], r0[3]); w.z = cvt_pk_bf16(r1[0], r1[1]); w.w = cvt_pk_bf16(r1[2], r1[3]);
;                         *(u32x4*)(H + (size_t)(row0 + ai * HALF + m * 16) * 2048 + col0 + bj * HALF) = w; }
.LBB0_884:
	s_lshl_b64 s[18:19], s[18:19], 2
	s_add_u32 s18, s37, s18
	v_lshl_or_b32 v10, s48, 8, v181
	s_addc_u32 s19, s38, s19
	v_ashrrev_i32_e32 v11, 31, v10
	v_lshl_add_u64 v[12:13], v[10:11], 2, s[18:19]
	global_load_dwordx4 v[2:5], v[12:13], off offset:16
	global_load_dwordx4 v[6:9], v[12:13], off
	v_lshlrev_b64 v[194:195], 1, v[10:11]
	v_lshl_add_u64 v[196:197], s[8:9], 0, v[194:195]
	s_mov_b64 s[18:19], 0x80000
	s_and_b64 vcc, exec, s[0:1]
	s_waitcnt vmcnt(0)
	v_pk_mul_f32 v[188:189], v[4:5], s[14:15] op_sel_hi:[1,0]
	v_pk_mul_f32 v[192:193], v[8:9], s[14:15] op_sel_hi:[1,0]
	v_pk_mul_f32 v[190:191], v[6:7], s[14:15] op_sel_hi:[1,0]
	v_pk_mul_f32 v[186:187], v[2:3], s[14:15] op_sel_hi:[1,0]
	global_load_dwordx4 v[2:5], v[12:13], off offset:528
	global_load_dwordx4 v[6:9], v[12:13], off offset:512
	s_waitcnt vmcnt(1)
	v_pk_mul_f32 v[30:31], v[2:3], s[14:15] op_sel_hi:[1,0]
	v_lshl_add_u32 v2, s47, 8, v1
	v_ashrrev_i32_e32 v3, 31, v2
	v_lshlrev_b64 v[198:199], 12, v[2:3]
	v_pk_mul_f32 v[32:33], v[4:5], s[14:15] op_sel_hi:[1,0]
	v_lshl_add_u64 v[4:5], v[196:197], 0, v[198:199]
	global_load_dwordx4 v[210:213], v[4:5], off
	global_load_dwordx4 v[26:29], v[4:5], off offset:256
	v_or_b32_e32 v4, 16, v2
	v_ashrrev_i32_e32 v5, 31, v4
	v_lshlrev_b64 v[204:205], 12, v[4:5]
	v_lshl_add_u64 v[4:5], v[196:197], 0, v[204:205]
	global_load_dwordx4 v[22:25], v[4:5], off
	global_load_dwordx4 v[18:21], v[4:5], off offset:256
	v_or_b32_e32 v4, 32, v2
	v_ashrrev_i32_e32 v5, 31, v4
	v_lshlrev_b64 v[202:203], 12, v[4:5]
	v_lshl_add_u64 v[4:5], v[196:197], 0, v[202:203]
	global_load_dwordx4 v[14:17], v[4:5], off
	global_load_dwordx4 v[10:13], v[4:5], off offset:256
	v_or_b32_e32 v2, 48, v2
	v_ashrrev_i32_e32 v3, 31, v2
	v_lshlrev_b64 v[200:201], 12, v[2:3]
	v_lshl_add_u64 v[2:3], v[196:197], 0, v[200:201]
	s_waitcnt vmcnt(6)
	v_pk_mul_f32 v[184:185], v[8:9], s[14:15] op_sel_hi:[1,0]
	v_pk_mul_f32 v[182:183], v[6:7], s[14:15] op_sel_hi:[1,0]
	global_load_dwordx4 v[6:9], v[2:3], off
	s_nop 0
	global_load_dwordx4 v[2:5], v[2:3], off offset:256
	s_waitcnt vmcnt(7)
	v_lshlrev_b32_e32 v214, 16, v210
	v_and_b32_e32 v215, 0xffff0000, v210
	v_lshlrev_b32_e32 v210, 16, v211
	v_and_b32_e32 v211, 0xffff0000, v211
	v_lshlrev_b32_e32 v216, 16, v212
	v_and_b32_e32 v217, 0xffff0000, v212
	v_lshlrev_b32_e32 v212, 16, v213
	v_and_b32_e32 v213, 0xffff0000, v213
	v_pk_fma_f32 v[158:159], v[158:159], v[190:191], v[214:215]
	v_pk_fma_f32 v[160:161], v[160:161], v[192:193], v[210:211]
	v_pk_fma_f32 v[210:211], v[156:157], v[188:189], v[212:213]
	v_pk_fma_f32 v[156:157], v[154:155], v[186:187], v[216:217]
	v_cvt_pk_bf16_f32 v154, v158, v159
	v_lshl_add_u64 v[158:159], s[8:9], 0, v[198:199]
	v_cvt_pk_bf16_f32 v155, v160, v161
	v_cvt_pk_bf16_f32 v156, v156, v157
	v_cvt_pk_bf16_f32 v157, v210, v211
	v_lshl_add_u64 v[158:159], v[158:159], 0, v[194:195]
	global_store_dwordx4 v[158:159], v[154:157], off sc0 sc1
	s_waitcnt vmcnt(7)
	s_nop 0
	v_lshlrev_b32_e32 v154, 16, v26
	v_and_b32_e32 v155, 0xffff0000, v26
	v_lshlrev_b32_e32 v26, 16, v27
	v_and_b32_e32 v27, 0xffff0000, v27
	v_lshlrev_b32_e32 v156, 16, v28
	v_and_b32_e32 v157, 0xffff0000, v28
	v_lshlrev_b32_e32 v28, 16, v29
	v_and_b32_e32 v29, 0xffff0000, v29
	v_pk_fma_f32 v[152:153], v[152:153], v[184:185], v[26:27]
	v_pk_fma_f32 v[26:27], v[150:151], v[182:183], v[154:155]
	v_pk_fma_f32 v[148:149], v[148:149], v[32:33], v[28:29]
	v_pk_fma_f32 v[28:29], v[146:147], v[30:31], v[156:157]
	v_cvt_pk_bf16_f32 v26, v26, v27
	v_cvt_pk_bf16_f32 v27, v152, v153
	s_nop 0
	v_cvt_pk_bf16_f32 v28, v28, v29
	v_cvt_pk_bf16_f32 v29, v148, v149
	global_store_dwordx4 v[158:159], v[26:29], off offset:256 sc0 sc1
	s_waitcnt vmcnt(7)
	s_nop 0
	v_lshlrev_b32_e32 v26, 16, v22
	v_and_b32_e32 v27, 0xffff0000, v22
	v_lshlrev_b32_e32 v22, 16, v23
	v_and_b32_e32 v23, 0xffff0000, v23
	v_lshlrev_b32_e32 v28, 16, v24
	v_and_b32_e32 v29, 0xffff0000, v24
	v_lshlrev_b32_e32 v24, 16, v25
	v_and_b32_e32 v25, 0xffff0000, v25
	v_pk_fma_f32 v[144:145], v[144:145], v[192:193], v[22:23]
	v_pk_fma_f32 v[22:23], v[142:143], v[190:191], v[26:27]
	v_pk_fma_f32 v[26:27], v[140:141], v[188:189], v[24:25]
	v_pk_fma_f32 v[24:25], v[138:139], v[186:187], v[28:29]
	v_cvt_pk_bf16_f32 v22, v22, v23
	v_cvt_pk_bf16_f32 v23, v144, v145
	s_nop 0
	v_cvt_pk_bf16_f32 v24, v24, v25
	v_cvt_pk_bf16_f32 v25, v26, v27
	v_lshl_add_u64 v[26:27], s[8:9], 0, v[204:205]
	v_lshl_add_u64 v[26:27], v[26:27], 0, v[194:195]
	global_store_dwordx4 v[26:27], v[22:25], off sc0 sc1
	s_waitcnt vmcnt(7)
	s_nop 0
	v_lshlrev_b32_e32 v22, 16, v18
	v_and_b32_e32 v23, 0xffff0000, v18
	v_lshlrev_b32_e32 v18, 16, v19
	v_and_b32_e32 v19, 0xffff0000, v19
	v_lshlrev_b32_e32 v24, 16, v20
	v_and_b32_e32 v25, 0xffff0000, v20
	v_lshlrev_b32_e32 v20, 16, v21
	v_and_b32_e32 v21, 0xffff0000, v21
	v_pk_fma_f32 v[28:29], v[136:137], v[184:185], v[18:19]
	v_pk_fma_f32 v[18:19], v[134:135], v[182:183], v[22:23]
	v_pk_fma_f32 v[22:23], v[132:133], v[32:33], v[20:21]
	v_pk_fma_f32 v[20:21], v[130:131], v[30:31], v[24:25]
	v_cvt_pk_bf16_f32 v18, v18, v19
	v_cvt_pk_bf16_f32 v19, v28, v29
	v_lshl_add_u64 v[28:29], v[198:199], 0, s[18:19]
	v_cvt_pk_bf16_f32 v20, v20, v21
	v_cvt_pk_bf16_f32 v21, v22, v23
	global_store_dwordx4 v[26:27], v[18:21], off offset:256 sc0 sc1
	s_mov_b64 s[18:19], 0x90000
	s_waitcnt vmcnt(7)
; __device__ __forceinline__ unsigned cvt_pk_bf16(float lo, float hi) { unsigned r; asm volatile("v_cvt_pk_bf16_f32 %0, %1, %2" : "=v"(r) : "v"(lo), "v"(hi)); return r; }
;     __device__ __forceinline__ void operator()(const f32x4 (&acc)[2][2][4][2], const Unit& u, int wr, int wc, int fr, int fq) const {
;     ...
;                     for (int bj = 0; bj < 2; ++bj) bs[m][bj] = *(const u32x4*)(H + (size_t)(row0 + ai * HALF + m * 16) * 2048 + col0 + bj * HALF);
; #pragma unroll
;                 for (int m = 0; m < 4; ++m)
; #pragma unroll
;                     for (int bj = 0; bj < 2; ++bj) { const u32x4 b = bs[m][bj];
;                         f32x4 r0, r1; r0.x = __builtin_bit_cast(float, b.x << 16); r0.y = __builtin_bit_cast(float, b.x & 0xffff0000u); r0.z = __builtin_bit_cast(float, b.y << 16); r0.w = __builtin_bit_cast(float, b.y & 0xffff0000u);
;                         r1.x = __builtin_bit_cast(float, b.z << 16); r1.y = __builtin_bit_cast(float, b.z & 0xffff0000u); r1.z = __builtin_bit_cast(float, b.w << 16); r1.w = __builtin_bit_cast(float, b.w & 0xffff0000u);
;                         r0 += gg[bj][0] * acc[ai][bj][m][0]; r1 += gg[bj][1] * acc[ai][bj][m][1];
;                         u32x4 w; w.x = cvt_pk_bf16(r0[0], r0[1]); w.y = cvt_pk_bf16(r0[2], r0[3]); w.z = cvt_pk_bf16(r1[0], r1[1]); w.w = cvt_pk_bf16(r1[2], r1[3]);
;                         *(u32x4*)(H + (size_t)(row0 + ai * HALF + m * 16) * 2048 + col0 + bj * HALF) = w; }
	v_lshlrev_b32_e32 v18, 16, v14
	v_and_b32_e32 v19, 0xffff0000, v14
	v_lshlrev_b32_e32 v14, 16, v15
	v_and_b32_e32 v15, 0xffff0000, v15
	v_lshlrev_b32_e32 v20, 16, v16
	v_and_b32_e32 v21, 0xffff0000, v16
	v_lshlrev_b32_e32 v16, 16, v17
	v_and_b32_e32 v17, 0xffff0000, v17
	v_pk_fma_f32 v[22:23], v[128:129], v[192:193], v[14:15]
	v_pk_fma_f32 v[14:15], v[126:127], v[190:191], v[18:19]
	v_pk_fma_f32 v[18:19], v[124:125], v[188:189], v[16:17]
	v_pk_fma_f32 v[16:17], v[122:123], v[186:187], v[20:21]
	v_cvt_pk_bf16_f32 v14, v14, v15
	v_cvt_pk_bf16_f32 v15, v22, v23
	s_nop 0
	v_cvt_pk_bf16_f32 v16, v16, v17
	v_cvt_pk_bf16_f32 v17, v18, v19
	v_lshl_add_u64 v[18:19], s[8:9], 0, v[202:203]
	v_lshl_add_u64 v[18:19], v[18:19], 0, v[194:195]
	global_store_dwordx4 v[18:19], v[14:17], off sc0 sc1
	s_waitcnt vmcnt(7)
	s_nop 0
	v_lshlrev_b32_e32 v14, 16, v10
	v_and_b32_e32 v15, 0xffff0000, v10
	v_lshlrev_b32_e32 v10, 16, v11
	v_and_b32_e32 v11, 0xffff0000, v11
	v_lshlrev_b32_e32 v16, 16, v12
	v_and_b32_e32 v17, 0xffff0000, v12
	v_lshlrev_b32_e32 v12, 16, v13
	v_and_b32_e32 v13, 0xffff0000, v13
	v_pk_fma_f32 v[20:21], v[120:121], v[184:185], v[10:11]
	v_pk_fma_f32 v[10:11], v[118:119], v[182:183], v[14:15]
	v_pk_fma_f32 v[14:15], v[116:117], v[32:33], v[12:13]
	v_pk_fma_f32 v[12:13], v[114:115], v[30:31], v[16:17]
	v_cvt_pk_bf16_f32 v10, v10, v11
	v_cvt_pk_bf16_f32 v11, v20, v21
	s_nop 0
	v_cvt_pk_bf16_f32 v12, v12, v13
	v_cvt_pk_bf16_f32 v13, v14, v15
	global_store_dwordx4 v[18:19], v[10:13], off offset:256 sc0 sc1
	s_waitcnt vmcnt(7)
	s_nop 0
	v_lshlrev_b32_e32 v10, 16, v6
	v_and_b32_e32 v11, 0xffff0000, v6
	v_lshlrev_b32_e32 v6, 16, v7
	v_and_b32_e32 v7, 0xffff0000, v7
	v_lshlrev_b32_e32 v12, 16, v8
	v_and_b32_e32 v13, 0xffff0000, v8
	v_lshlrev_b32_e32 v8, 16, v9
	v_and_b32_e32 v9, 0xffff0000, v9
	v_pk_fma_f32 v[14:15], v[112:113], v[192:193], v[6:7]
	v_pk_fma_f32 v[6:7], v[110:111], v[190:191], v[10:11]
	v_pk_fma_f32 v[10:11], v[108:109], v[188:189], v[8:9]
	v_pk_fma_f32 v[8:9], v[106:107], v[186:187], v[12:13]
	v_cvt_pk_bf16_f32 v6, v6, v7
	v_cvt_pk_bf16_f32 v7, v14, v15
	v_lshl_add_u64 v[106:107], v[198:199], 0, s[18:19]
	v_cvt_pk_bf16_f32 v8, v8, v9
	v_cvt_pk_bf16_f32 v9, v10, v11
	v_lshl_add_u64 v[10:11], s[8:9], 0, v[200:201]
	v_lshl_add_u64 v[10:11], v[10:11], 0, v[194:195]
	global_store_dwordx4 v[10:11], v[6:9], off sc0 sc1
	s_mov_b64 s[18:19], 0xa0000
	v_lshl_add_u64 v[108:109], v[198:199], 0, s[18:19]
	s_waitcnt vmcnt(7)
	v_lshlrev_b32_e32 v6, 16, v2
	v_and_b32_e32 v7, 0xffff0000, v2
	v_lshlrev_b32_e32 v2, 16, v3
	v_and_b32_e32 v3, 0xffff0000, v3
	v_lshlrev_b32_e32 v8, 16, v4
	v_and_b32_e32 v9, 0xffff0000, v4
	v_lshlrev_b32_e32 v4, 16, v5
	v_and_b32_e32 v5, 0xffff0000, v5
	v_pk_fma_f32 v[12:13], v[104:105], v[184:185], v[2:3]
	v_pk_fma_f32 v[2:3], v[102:103], v[182:183], v[6:7]
	v_pk_fma_f32 v[6:7], v[100:101], v[32:33], v[4:5]
	v_pk_fma_f32 v[4:5], v[98:99], v[30:31], v[8:9]
	v_cvt_pk_bf16_f32 v2, v2, v3
	v_cvt_pk_bf16_f32 v3, v12, v13
	s_mov_b64 s[18:19], 0xb0000
	v_cvt_pk_bf16_f32 v4, v4, v5
	v_cvt_pk_bf16_f32 v5, v6, v7
	global_store_dwordx4 v[10:11], v[2:5], off offset:256 sc0 sc1
	v_lshl_add_u64 v[10:11], v[198:199], 0, s[18:19]
	s_mov_b64 s[18:19], -1
	v_lshl_add_u64 v[2:3], v[196:197], 0, v[28:29]
	global_load_dwordx4 v[12:15], v[2:3], off
	global_load_dwordx4 v[16:19], v[2:3], off offset:256
	v_lshl_add_u64 v[2:3], v[196:197], 0, v[106:107]
	global_load_dwordx4 v[20:23], v[2:3], off
	global_load_dwordx4 v[24:27], v[2:3], off offset:256
	v_lshl_add_u64 v[2:3], v[196:197], 0, v[108:109]
	global_load_dwordx4 v[98:101], v[2:3], off
	global_load_dwordx4 v[102:105], v[2:3], off offset:256
	v_lshl_add_u64 v[2:3], v[196:197], 0, v[10:11]
	global_load_dwordx4 v[6:9], v[2:3], off
	s_nop 0
	global_load_dwordx4 v[2:5], v[2:3], off offset:256
	v_lshl_add_u64 v[28:29], s[8:9], 0, v[28:29]
	v_lshl_add_u64 v[28:29], v[28:29], 0, v[194:195]
	v_lshl_add_u64 v[10:11], s[8:9], 0, v[10:11]
	v_lshl_add_u64 v[10:11], v[10:11], 0, v[194:195]
	s_waitcnt vmcnt(7)
	v_lshlrev_b32_e32 v110, 16, v12
	v_and_b32_e32 v111, 0xffff0000, v12
	v_lshlrev_b32_e32 v12, 16, v13
	v_and_b32_e32 v13, 0xffff0000, v13
	v_lshlrev_b32_e32 v112, 16, v14
	v_and_b32_e32 v113, 0xffff0000, v14
	v_lshlrev_b32_e32 v14, 16, v15
	v_and_b32_e32 v15, 0xffff0000, v15
	v_pk_fma_f32 v[96:97], v[96:97], v[192:193], v[12:13]
	v_pk_fma_f32 v[12:13], v[94:95], v[190:191], v[110:111]
	v_pk_fma_f32 v[92:93], v[92:93], v[188:189], v[14:15]
	v_pk_fma_f32 v[14:15], v[90:91], v[186:187], v[112:113]
	v_cvt_pk_bf16_f32 v12, v12, v13
	v_cvt_pk_bf16_f32 v13, v96, v97
	s_nop 0
	v_cvt_pk_bf16_f32 v14, v14, v15
	v_cvt_pk_bf16_f32 v15, v92, v93
	global_store_dwordx4 v[28:29], v[12:15], off sc0 sc1
	s_waitcnt vmcnt(7)
; __device__ __forceinline__ unsigned cvt_pk_bf16(float lo, float hi) { unsigned r; asm volatile("v_cvt_pk_bf16_f32 %0, %1, %2" : "=v"(r) : "v"(lo), "v"(hi)); return r; }
;     __device__ __forceinline__ void operator()(const f32x4 (&acc)[2][2][4][2], const Unit& u, int wr, int wc, int fr, int fq) const {
;     ...
;                     for (int bj = 0; bj < 2; ++bj) bs[m][bj] = *(const u32x4*)(H + (size_t)(row0 + ai * HALF + m * 16) * 2048 + col0 + bj * HALF);
; #pragma unroll
;                 for (int m = 0; m < 4; ++m)
; #pragma unroll
;                     for (int bj = 0; bj < 2; ++bj) { const u32x4 b = bs[m][bj];
;                         f32x4 r0, r1; r0.x = __builtin_bit_cast(float, b.x << 16); r0.y = __builtin_bit_cast(float, b.x & 0xffff0000u); r0.z = __builtin_bit_cast(float, b.y << 16); r0.w = __builtin_bit_cast(float, b.y & 0xffff0000u);
;                         r1.x = __builtin_bit_cast(float, b.z << 16); r1.y = __builtin_bit_cast(float, b.z & 0xffff0000u); r1.z = __builtin_bit_cast(float, b.w << 16); r1.w = __builtin_bit_cast(float, b.w & 0xffff0000u);
;                         r0 += gg[bj][0] * acc[ai][bj][m][0]; r1 += gg[bj][1] * acc[ai][bj][m][1];
;                         u32x4 w; w.x = cvt_pk_bf16(r0[0], r0[1]); w.y = cvt_pk_bf16(r0[2], r0[3]); w.z = cvt_pk_bf16(r1[0], r1[1]); w.w = cvt_pk_bf16(r1[2], r1[3]);
;                         *(u32x4*)(H + (size_t)(row0 + ai * HALF + m * 16) * 2048 + col0 + bj * HALF) = w; }
	s_nop 0
	v_lshlrev_b32_e32 v12, 16, v16
	v_and_b32_e32 v13, 0xffff0000, v16
	v_lshlrev_b32_e32 v14, 16, v17
	v_and_b32_e32 v15, 0xffff0000, v17
	v_lshlrev_b32_e32 v16, 16, v18
	v_and_b32_e32 v17, 0xffff0000, v18
	v_lshlrev_b32_e32 v18, 16, v19
	v_and_b32_e32 v19, 0xffff0000, v19
	v_pk_fma_f32 v[14:15], v[88:89], v[184:185], v[14:15]
	v_pk_fma_f32 v[12:13], v[86:87], v[182:183], v[12:13]
	v_pk_fma_f32 v[18:19], v[84:85], v[32:33], v[18:19]
	v_pk_fma_f32 v[16:17], v[82:83], v[30:31], v[16:17]
	v_cvt_pk_bf16_f32 v12, v12, v13
	v_cvt_pk_bf16_f32 v13, v14, v15
	s_nop 0
	v_cvt_pk_bf16_f32 v14, v16, v17
	v_cvt_pk_bf16_f32 v15, v18, v19
	global_store_dwordx4 v[28:29], v[12:15], off offset:256 sc0 sc1
	s_waitcnt vmcnt(7)
	v_lshlrev_b32_e32 v16, 16, v22
	v_and_b32_e32 v17, 0xffff0000, v22
	v_lshlrev_b32_e32 v12, 16, v20
	v_and_b32_e32 v13, 0xffff0000, v20
	v_lshlrev_b32_e32 v14, 16, v21
	v_and_b32_e32 v15, 0xffff0000, v21
	v_pk_fma_f32 v[14:15], v[80:81], v[192:193], v[14:15]
	v_pk_fma_f32 v[12:13], v[78:79], v[190:191], v[12:13]
	v_pk_fma_f32 v[16:17], v[74:75], v[186:187], v[16:17]
	v_lshlrev_b32_e32 v18, 16, v23
	v_and_b32_e32 v19, 0xffff0000, v23
	v_cvt_pk_bf16_f32 v12, v12, v13
	v_cvt_pk_bf16_f32 v13, v14, v15
	v_cvt_pk_bf16_f32 v14, v16, v17
	v_lshl_add_u64 v[16:17], s[8:9], 0, v[106:107]
	v_pk_fma_f32 v[18:19], v[76:77], v[188:189], v[18:19]
	v_lshl_add_u64 v[16:17], v[16:17], 0, v[194:195]
	v_cvt_pk_bf16_f32 v15, v18, v19
	global_store_dwordx4 v[16:17], v[12:15], off sc0 sc1
	s_waitcnt vmcnt(7)
	v_lshlrev_b32_e32 v18, 16, v26
	v_and_b32_e32 v19, 0xffff0000, v26
	v_lshlrev_b32_e32 v12, 16, v24
	v_and_b32_e32 v13, 0xffff0000, v24
	v_lshlrev_b32_e32 v14, 16, v25
	v_and_b32_e32 v15, 0xffff0000, v25
	v_lshlrev_b32_e32 v20, 16, v27
	v_and_b32_e32 v21, 0xffff0000, v27
	v_pk_fma_f32 v[14:15], v[72:73], v[184:185], v[14:15]
	v_pk_fma_f32 v[12:13], v[70:71], v[182:183], v[12:13]
	v_pk_fma_f32 v[20:21], v[68:69], v[32:33], v[20:21]
	v_pk_fma_f32 v[18:19], v[66:67], v[30:31], v[18:19]
	v_cvt_pk_bf16_f32 v12, v12, v13
	v_cvt_pk_bf16_f32 v13, v14, v15
	s_nop 0
	v_cvt_pk_bf16_f32 v14, v18, v19
	v_cvt_pk_bf16_f32 v15, v20, v21
	global_store_dwordx4 v[16:17], v[12:15], off offset:256 sc0 sc1
	s_waitcnt vmcnt(7)
	v_lshlrev_b32_e32 v16, 16, v100
	v_and_b32_e32 v17, 0xffff0000, v100
	v_lshlrev_b32_e32 v12, 16, v98
	v_and_b32_e32 v13, 0xffff0000, v98
	v_lshlrev_b32_e32 v14, 16, v99
	v_and_b32_e32 v15, 0xffff0000, v99
	v_pk_fma_f32 v[14:15], v[64:65], v[192:193], v[14:15]
	v_pk_fma_f32 v[12:13], v[62:63], v[190:191], v[12:13]
	v_pk_fma_f32 v[16:17], v[58:59], v[186:187], v[16:17]
	v_lshlrev_b32_e32 v18, 16, v101
	v_and_b32_e32 v19, 0xffff0000, v101
	v_cvt_pk_bf16_f32 v12, v12, v13
	v_cvt_pk_bf16_f32 v13, v14, v15
	v_cvt_pk_bf16_f32 v14, v16, v17
	v_lshl_add_u64 v[16:17], s[8:9], 0, v[108:109]
	v_pk_fma_f32 v[18:19], v[60:61], v[188:189], v[18:19]
	v_lshl_add_u64 v[16:17], v[16:17], 0, v[194:195]
	v_cvt_pk_bf16_f32 v15, v18, v19
	global_store_dwordx4 v[16:17], v[12:15], off sc0 sc1
	s_waitcnt vmcnt(7)
	v_lshlrev_b32_e32 v18, 16, v104
	v_and_b32_e32 v19, 0xffff0000, v104
	v_lshlrev_b32_e32 v12, 16, v102
	v_and_b32_e32 v13, 0xffff0000, v102
	v_lshlrev_b32_e32 v14, 16, v103
	v_and_b32_e32 v15, 0xffff0000, v103
	v_lshlrev_b32_e32 v20, 16, v105
	v_and_b32_e32 v21, 0xffff0000, v105
	v_pk_fma_f32 v[14:15], v[56:57], v[184:185], v[14:15]
	v_pk_fma_f32 v[12:13], v[54:55], v[182:183], v[12:13]
	v_pk_fma_f32 v[20:21], v[52:53], v[32:33], v[20:21]
	v_pk_fma_f32 v[18:19], v[50:51], v[30:31], v[18:19]
	v_cvt_pk_bf16_f32 v12, v12, v13
	v_cvt_pk_bf16_f32 v13, v14, v15
	s_nop 0
	v_cvt_pk_bf16_f32 v14, v18, v19
	v_cvt_pk_bf16_f32 v15, v20, v21
	global_store_dwordx4 v[16:17], v[12:15], off offset:256 sc0 sc1
	s_waitcnt vmcnt(7)
	s_nop 0
	v_lshlrev_b32_e32 v12, 16, v6
	v_and_b32_e32 v13, 0xffff0000, v6
	v_lshlrev_b32_e32 v6, 16, v7
	v_and_b32_e32 v7, 0xffff0000, v7
	v_lshlrev_b32_e32 v14, 16, v8
	v_and_b32_e32 v15, 0xffff0000, v8
	v_lshlrev_b32_e32 v8, 16, v9
	v_and_b32_e32 v9, 0xffff0000, v9
	v_pk_fma_f32 v[16:17], v[48:49], v[192:193], v[6:7]
	v_pk_fma_f32 v[6:7], v[46:47], v[190:191], v[12:13]
	v_pk_fma_f32 v[12:13], v[44:45], v[188:189], v[8:9]
	v_pk_fma_f32 v[8:9], v[42:43], v[186:187], v[14:15]
	v_cvt_pk_bf16_f32 v6, v6, v7
	v_cvt_pk_bf16_f32 v7, v16, v17
	s_nop 0
	v_cvt_pk_bf16_f32 v8, v8, v9
	v_cvt_pk_bf16_f32 v9, v12, v13
	global_store_dwordx4 v[10:11], v[6:9], off sc0 sc1
	s_waitcnt vmcnt(7)
	s_nop 0
	v_lshlrev_b32_e32 v6, 16, v2
	v_and_b32_e32 v7, 0xffff0000, v2
	v_lshlrev_b32_e32 v2, 16, v3
	v_and_b32_e32 v3, 0xffff0000, v3
	v_lshlrev_b32_e32 v8, 16, v4
	v_and_b32_e32 v9, 0xffff0000, v4
	v_lshlrev_b32_e32 v4, 16, v5
	v_and_b32_e32 v5, 0xffff0000, v5
	v_pk_fma_f32 v[12:13], v[40:41], v[184:185], v[2:3]
	v_pk_fma_f32 v[2:3], v[38:39], v[182:183], v[6:7]
	v_pk_fma_f32 v[6:7], v[36:37], v[32:33], v[4:5]
	v_pk_fma_f32 v[4:5], v[34:35], v[30:31], v[8:9]
	v_cvt_pk_bf16_f32 v2, v2, v3
	v_cvt_pk_bf16_f32 v3, v12, v13
	s_nop 0
	v_cvt_pk_bf16_f32 v4, v4, v5
	v_cvt_pk_bf16_f32 v5, v6, v7
	global_store_dwordx4 v[10:11], v[2:5], off offset:256 sc0 sc1
	s_cbranch_vccnz .LBB0_868
	s_andn2_b64 vcc, exec, s[4:5]
	s_cbranch_vccnz .LBB0_867
	s_barrier
	s_branch .LBB0_867

; __device__ __forceinline__ unsigned cvt_pk_bf16(float lo, float hi) { unsigned r; asm volatile("v_cvt_pk_bf16_f32 %0, %1, %2" : "=v"(r) : "v"(lo), "v"(hi)); return r; }
; __device__ __forceinline__ float gelu_tanh(float x) { const float y = x + 0.044715f * x * x * x; return x * __builtin_amdgcn_rcpf(1.0f + __builtin_amdgcn_exp2f(-2.302208198f * y)); }
;     __device__ __forceinline__ void operator()(const f32x4 (&acc)[2][2][4][2], const Unit& u, int wr, int wc, int fr, int fq) const {
;         const int row0 = u.pm * BM + wr * 64 + fr, col0 = u.pn * BM + wc * 32 + 8 * fq; const bool act = u.pn < nact;
; #pragma unroll
;         for (int ai = 0; ai < 2; ++ai)
; #pragma unroll
;             for (int m = 0; m < 4; ++m) { bf16_t* rowp = O + (size_t)u.ks * ks_stride + (size_t)(row0 + ai * HALF + m * 16) * ldc + col0;
; #pragma unroll
;                 for (int bj = 0; bj < 2; ++bj) { f32x4 v0 = acc[ai][bj][m][0] * ascale, v1 = acc[ai][bj][m][1] * ascale;
;                     if (act) {
; #pragma unroll
;                         for (int j = 0; j < 4; ++j) { v0[j] = gelu_tanh(v0[j]); v1[j] = gelu_tanh(v1[j]); } }
;                     u32x4 w; w.x = cvt_pk_bf16(v0[0], v0[1]); w.y = cvt_pk_bf16(v0[2], v0[3]); w.z = cvt_pk_bf16(v1[0], v1[1]); w.w = cvt_pk_bf16(v1[2], v1[3]);
;                     *(u32x4*)(rowp + bj * HALF) = w; } }
.LBB0_1263:
	v_lshl_add_u32 v148, s2, 8, v1
	v_ashrrev_i32_e32 v149, 31, v148
	v_lshl_or_b32 v146, s22, 8, v153
	v_lshlrev_b64 v[150:151], 13, v[148:149]
	v_ashrrev_i32_e32 v147, 31, v146
	v_lshl_add_u64 v[150:151], s[8:9], 0, v[150:151]
	v_cvt_pk_bf16_f32 v126, v126, v127
	v_cvt_pk_bf16_f32 v127, v128, v129
	v_cvt_pk_bf16_f32 v128, v122, v123
	v_cndmask_b32_e64 v122, 0, 1, s[24:25]
	v_lshl_add_u64 v[150:151], v[146:147], 1, v[150:151]
	v_cmp_ne_u32_e64 s[2:3], 1, v122
	s_andn2_b64 vcc, exec, s[24:25]
	v_cvt_pk_bf16_f32 v129, v124, v125
	global_store_dwordx4 v[150:151], v[126:129], off sc0 sc1
	s_cbranch_vccnz .LBB0_1265
	v_mul_f32_e32 v123, 0x3d372713, v114
	v_mul_f32_e32 v123, v114, v123
	v_mul_f32_e32 v124, 0x3d372713, v119
	v_fma_f32 v123, v114, v123, v114
	v_mul_f32_e32 v124, v119, v124
	v_mul_f32_e32 v123, 0xc0135761, v123
	v_fma_f32 v124, v119, v124, v119
	v_exp_f32_e32 v123, v123
	v_mul_f32_e32 v124, 0xc0135761, v124
	v_exp_f32_e32 v125, v124
	v_mul_f32_e32 v128, 0x3d372713, v121
	v_mul_f32_e32 v128, v121, v128
	v_fma_f32 v128, v121, v128, v121
	v_add_f32_e32 v123, 1.0, v123
	v_mul_f32_e32 v127, 0x3d372713, v116
	v_mul_f32_e32 v128, 0xc0135761, v128
	v_mul_f32_e32 v122, 0x3d372713, v118
	v_rcp_f32_e32 v124, v123
	v_add_f32_e32 v123, 1.0, v125
	v_mul_f32_e32 v125, 0x3d372713, v115
	v_mul_f32_e32 v126, 0x3d372713, v120
	v_mul_f32_e32 v127, v116, v127
	v_exp_f32_e32 v129, v128
	v_mul_f32_e32 v128, 0x3d372713, v117
	v_mul_f32_e32 v122, v118, v122
	v_mul_f32_e32 v125, v115, v125
	v_mul_f32_e32 v126, v120, v126
	v_fma_f32 v127, v116, v127, v116
	v_mul_f32_e32 v128, v117, v128
	v_fma_f32 v122, v118, v122, v118
	v_fma_f32 v125, v115, v125, v115
	v_fma_f32 v126, v120, v126, v120
	v_mul_f32_e32 v127, 0xc0135761, v127
	v_fma_f32 v128, v117, v128, v117
	v_mul_f32_e32 v122, 0xc0135761, v122
	v_mul_f32_e32 v125, 0xc0135761, v125
	v_mul_f32_e32 v126, 0xc0135761, v126
	v_exp_f32_e32 v127, v127
	v_mul_f32_e32 v128, 0xc0135761, v128
	v_exp_f32_e32 v122, v122
	v_exp_f32_e32 v125, v125
	v_exp_f32_e32 v126, v126
	v_exp_f32_e32 v157, v128
	v_add_f32_e32 v127, 1.0, v127
	v_add_f32_e32 v122, 1.0, v122
	v_add_f32_e32 v125, 1.0, v125
	v_add_f32_e32 v126, 1.0, v126
	v_rcp_f32_e32 v128, v127
	v_add_f32_e32 v127, 1.0, v129
	v_add_f32_e32 v129, 1.0, v157
	v_rcp_f32_e32 v122, v122
	v_rcp_f32_e32 v123, v123
	v_rcp_f32_e32 v126, v126
	v_rcp_f32_e32 v127, v127
	v_rcp_f32_e32 v129, v129
	v_rcp_f32_e32 v125, v125
	v_pk_mul_f32 v[118:119], v[118:119], v[122:123]
	v_pk_mul_f32 v[120:121], v[120:121], v[126:127]
	v_pk_mul_f32 v[116:117], v[116:117], v[128:129]
	v_pk_mul_f32 v[114:115], v[114:115], v[124:125]
; __device__ __forceinline__ unsigned cvt_pk_bf16(float lo, float hi) { unsigned r; asm volatile("v_cvt_pk_bf16_f32 %0, %1, %2" : "=v"(r) : "v"(lo), "v"(hi)); return r; }
; __device__ __forceinline__ float gelu_tanh(float x) { const float y = x + 0.044715f * x * x * x; return x * __builtin_amdgcn_rcpf(1.0f + __builtin_amdgcn_exp2f(-2.302208198f * y)); }
;     __device__ __forceinline__ void operator()(const f32x4 (&acc)[2][2][4][2], const Unit& u, int wr, int wc, int fr, int fq) const {
;         const int row0 = u.pm * BM + wr * 64 + fr, col0 = u.pn * BM + wc * 32 + 8 * fq; const bool act = u.pn < nact;
; #pragma unroll
;         for (int ai = 0; ai < 2; ++ai)
; #pragma unroll
;             for (int m = 0; m < 4; ++m) { bf16_t* rowp = O + (size_t)u.ks * ks_stride + (size_t)(row0 + ai * HALF + m * 16) * ldc + col0;
; #pragma unroll
;                 for (int bj = 0; bj < 2; ++bj) { f32x4 v0 = acc[ai][bj][m][0] * ascale, v1 = acc[ai][bj][m][1] * ascale;
;                     if (act) {
; #pragma unroll
;                         for (int j = 0; j < 4; ++j) { v0[j] = gelu_tanh(v0[j]); v1[j] = gelu_tanh(v1[j]); } }
;                     u32x4 w; w.x = cvt_pk_bf16(v0[0], v0[1]); w.y = cvt_pk_bf16(v0[2], v0[3]); w.z = cvt_pk_bf16(v1[0], v1[1]); w.w = cvt_pk_bf16(v1[2], v1[3]);
;                     *(u32x4*)(rowp + bj * HALF) = w; } }
.LBB0_1265:
	s_and_b64 vcc, exec, s[2:3]
	v_cvt_pk_bf16_f32 v118, v118, v119
	v_cvt_pk_bf16_f32 v119, v120, v121
	v_cvt_pk_bf16_f32 v120, v114, v115
	v_cvt_pk_bf16_f32 v121, v116, v117
	global_store_dwordx4 v[150:151], v[118:121], off offset:256 sc0 sc1
	s_cbranch_vccnz .LBB0_1267
	v_mul_f32_e32 v115, 0x3d372713, v106
	v_mul_f32_e32 v115, v106, v115
	v_mul_f32_e32 v116, 0x3d372713, v111
	v_fma_f32 v115, v106, v115, v106
	v_mul_f32_e32 v116, v111, v116
	v_mul_f32_e32 v115, 0xc0135761, v115
	v_fma_f32 v116, v111, v116, v111
	v_exp_f32_e32 v115, v115
	v_mul_f32_e32 v116, 0xc0135761, v116
	v_exp_f32_e32 v117, v116
	v_mul_f32_e32 v120, 0x3d372713, v113
	v_mul_f32_e32 v120, v113, v120
	v_fma_f32 v120, v113, v120, v113
	v_add_f32_e32 v115, 1.0, v115
	v_mul_f32_e32 v119, 0x3d372713, v108
	v_mul_f32_e32 v120, 0xc0135761, v120
	v_mul_f32_e32 v114, 0x3d372713, v110
	v_rcp_f32_e32 v116, v115
	v_add_f32_e32 v115, 1.0, v117
	v_mul_f32_e32 v117, 0x3d372713, v107
	v_mul_f32_e32 v118, 0x3d372713, v112
	v_mul_f32_e32 v119, v108, v119
	v_exp_f32_e32 v121, v120
	v_mul_f32_e32 v120, 0x3d372713, v109
	v_mul_f32_e32 v114, v110, v114
	v_mul_f32_e32 v117, v107, v117
	v_mul_f32_e32 v118, v112, v118
	v_fma_f32 v119, v108, v119, v108
	v_mul_f32_e32 v120, v109, v120
	v_fma_f32 v114, v110, v114, v110
	v_fma_f32 v117, v107, v117, v107
	v_fma_f32 v118, v112, v118, v112
	v_mul_f32_e32 v119, 0xc0135761, v119
	v_fma_f32 v120, v109, v120, v109
	v_mul_f32_e32 v114, 0xc0135761, v114
	v_mul_f32_e32 v117, 0xc0135761, v117
	v_mul_f32_e32 v118, 0xc0135761, v118
	v_exp_f32_e32 v119, v119
	v_mul_f32_e32 v120, 0xc0135761, v120
	v_exp_f32_e32 v114, v114
	v_exp_f32_e32 v117, v117
	v_exp_f32_e32 v118, v118
	v_exp_f32_e32 v122, v120
	v_add_f32_e32 v119, 1.0, v119
	v_add_f32_e32 v114, 1.0, v114
	v_add_f32_e32 v117, 1.0, v117
	v_add_f32_e32 v118, 1.0, v118
	v_rcp_f32_e32 v120, v119
	v_add_f32_e32 v119, 1.0, v121
	v_add_f32_e32 v121, 1.0, v122
	v_rcp_f32_e32 v114, v114
	v_rcp_f32_e32 v115, v115
	v_rcp_f32_e32 v118, v118
	v_rcp_f32_e32 v119, v119
	v_rcp_f32_e32 v121, v121
	v_rcp_f32_e32 v117, v117
	v_pk_mul_f32 v[110:111], v[110:111], v[114:115]
	v_pk_mul_f32 v[112:113], v[112:113], v[118:119]
	v_pk_mul_f32 v[108:109], v[108:109], v[120:121]
	v_pk_mul_f32 v[106:107], v[106:107], v[116:117]
.LBB0_1267:
	v_or_b32_e32 v114, 16, v148
	v_ashrrev_i32_e32 v115, 31, v114
	v_lshlrev_b64 v[114:115], 13, v[114:115]
	v_lshl_add_u64 v[114:115], s[8:9], 0, v[114:115]
	v_lshl_add_u64 v[114:115], v[146:147], 1, v[114:115]
	s_and_b64 vcc, exec, s[2:3]
	v_cvt_pk_bf16_f32 v110, v110, v111
	v_cvt_pk_bf16_f32 v111, v112, v113
	v_cvt_pk_bf16_f32 v112, v106, v107
	v_cvt_pk_bf16_f32 v113, v108, v109
	global_store_dwordx4 v[114:115], v[110:113], off sc0 sc1
	s_cbranch_vccnz .LBB0_1269
	v_mul_f32_e32 v107, 0x3d372713, v98
	v_mul_f32_e32 v107, v98, v107
	v_mul_f32_e32 v108, 0x3d372713, v103
	v_fma_f32 v107, v98, v107, v98
	v_mul_f32_e32 v108, v103, v108
	v_mul_f32_e32 v107, 0xc0135761, v107
	v_fma_f32 v108, v103, v108, v103
	v_exp_f32_e32 v107, v107
	v_mul_f32_e32 v108, 0xc0135761, v108
	v_exp_f32_e32 v109, v108
	v_mul_f32_e32 v112, 0x3d372713, v105
	v_mul_f32_e32 v112, v105, v112
	v_fma_f32 v112, v105, v112, v105
	v_add_f32_e32 v107, 1.0, v107
	v_mul_f32_e32 v111, 0x3d372713, v100
	v_mul_f32_e32 v112, 0xc0135761, v112
	v_mul_f32_e32 v106, 0x3d372713, v102
	v_rcp_f32_e32 v108, v107
	v_add_f32_e32 v107, 1.0, v109
	v_mul_f32_e32 v109, 0x3d372713, v99
	v_mul_f32_e32 v110, 0x3d372713, v104
	v_mul_f32_e32 v111, v100, v111
	v_exp_f32_e32 v113, v112
	v_mul_f32_e32 v112, 0x3d372713, v101
	v_mul_f32_e32 v106, v102, v106
	v_mul_f32_e32 v109, v99, v109
	v_mul_f32_e32 v110, v104, v110
	v_fma_f32 v111, v100, v111, v100
	v_mul_f32_e32 v112, v101, v112
	v_fma_f32 v106, v102, v106, v102
	v_fma_f32 v109, v99, v109, v99
	v_fma_f32 v110, v104, v110, v104
	v_mul_f32_e32 v111, 0xc0135761, v111
	v_fma_f32 v112, v101, v112, v101
	v_mul_f32_e32 v106, 0xc0135761, v106
	v_mul_f32_e32 v109, 0xc0135761, v109
	v_mul_f32_e32 v110, 0xc0135761, v110
	v_exp_f32_e32 v111, v111
	v_mul_f32_e32 v112, 0xc0135761, v112
	v_exp_f32_e32 v106, v106
	v_exp_f32_e32 v109, v109
	v_exp_f32_e32 v110, v110
	v_exp_f32_e32 v116, v112
	v_add_f32_e32 v111, 1.0, v111
	v_add_f32_e32 v106, 1.0, v106
	v_add_f32_e32 v109, 1.0, v109
	v_add_f32_e32 v110, 1.0, v110
	v_rcp_f32_e32 v112, v111
	v_add_f32_e32 v111, 1.0, v113
	v_add_f32_e32 v113, 1.0, v116
	v_rcp_f32_e32 v106, v106
	v_rcp_f32_e32 v107, v107
	v_rcp_f32_e32 v110, v110
	v_rcp_f32_e32 v111, v111
	v_rcp_f32_e32 v113, v113
	v_rcp_f32_e32 v109, v109
	v_pk_mul_f32 v[102:103], v[102:103], v[106:107]
	v_pk_mul_f32 v[104:105], v[104:105], v[110:111]
	v_pk_mul_f32 v[100:101], v[100:101], v[112:113]
	v_pk_mul_f32 v[98:99], v[98:99], v[108:109]

; __device__ __forceinline__ unsigned cvt_pk_bf16(float lo, float hi) { unsigned r; asm volatile("v_cvt_pk_bf16_f32 %0, %1, %2" : "=v"(r) : "v"(lo), "v"(hi)); return r; }
; __device__ __forceinline__ float gelu_tanh(float x) { const float y = x + 0.044715f * x * x * x; return x * __builtin_amdgcn_rcpf(1.0f + __builtin_amdgcn_exp2f(-2.302208198f * y)); }
;     __device__ __forceinline__ void operator()(const f32x4 (&acc)[2][2][4][2], const Unit& u, int wr, int wc, int fr, int fq) const {
;         const int row0 = u.pm * BM + wr * 64 + fr, col0 = u.pn * BM + wc * 32 + 8 * fq; const bool act = u.pn < nact;
; #pragma unroll
;         for (int ai = 0; ai < 2; ++ai)
; #pragma unroll
;             for (int m = 0; m < 4; ++m) { bf16_t* rowp = O + (size_t)u.ks * ks_stride + (size_t)(row0 + ai * HALF + m * 16) * ldc + col0;
; #pragma unroll
;                 for (int bj = 0; bj < 2; ++bj) { f32x4 v0 = acc[ai][bj][m][0] * ascale, v1 = acc[ai][bj][m][1] * ascale;
;                     if (act) {
; #pragma unroll
;                         for (int j = 0; j < 4; ++j) { v0[j] = gelu_tanh(v0[j]); v1[j] = gelu_tanh(v1[j]); } }
;                     u32x4 w; w.x = cvt_pk_bf16(v0[0], v0[1]); w.y = cvt_pk_bf16(v0[2], v0[3]); w.z = cvt_pk_bf16(v1[0], v1[1]); w.w = cvt_pk_bf16(v1[2], v1[3]);
;                     *(u32x4*)(rowp + bj * HALF) = w; } }
.LBB0_1271:
	v_or_b32_e32 v98, 32, v148
	v_ashrrev_i32_e32 v99, 31, v98
	v_lshlrev_b64 v[98:99], 13, v[98:99]
	v_lshl_add_u64 v[98:99], s[8:9], 0, v[98:99]
	v_lshl_add_u64 v[98:99], v[146:147], 1, v[98:99]
	s_and_b64 vcc, exec, s[2:3]
	v_cvt_pk_bf16_f32 v94, v94, v95
	v_cvt_pk_bf16_f32 v95, v96, v97
	v_cvt_pk_bf16_f32 v96, v90, v91
	v_cvt_pk_bf16_f32 v97, v92, v93
	global_store_dwordx4 v[98:99], v[94:97], off sc0 sc1
	s_cbranch_vccnz .LBB0_1273
	v_mul_f32_e32 v91, 0x3d372713, v82
	v_mul_f32_e32 v91, v82, v91
	v_mul_f32_e32 v92, 0x3d372713, v87
	v_fma_f32 v91, v82, v91, v82
	v_mul_f32_e32 v92, v87, v92
	v_mul_f32_e32 v91, 0xc0135761, v91
	v_fma_f32 v92, v87, v92, v87
	v_exp_f32_e32 v91, v91
	v_mul_f32_e32 v92, 0xc0135761, v92
	v_exp_f32_e32 v93, v92
	v_mul_f32_e32 v96, 0x3d372713, v89
	v_mul_f32_e32 v96, v89, v96
	v_fma_f32 v96, v89, v96, v89
	v_add_f32_e32 v91, 1.0, v91
	v_mul_f32_e32 v95, 0x3d372713, v84
	v_mul_f32_e32 v96, 0xc0135761, v96
	v_mul_f32_e32 v90, 0x3d372713, v86
	v_rcp_f32_e32 v92, v91
	v_add_f32_e32 v91, 1.0, v93
	v_mul_f32_e32 v93, 0x3d372713, v83
	v_mul_f32_e32 v94, 0x3d372713, v88
	v_mul_f32_e32 v95, v84, v95
	v_exp_f32_e32 v97, v96
	v_mul_f32_e32 v96, 0x3d372713, v85
	v_mul_f32_e32 v90, v86, v90
	v_mul_f32_e32 v93, v83, v93
	v_mul_f32_e32 v94, v88, v94
	v_fma_f32 v95, v84, v95, v84
	v_mul_f32_e32 v96, v85, v96
	v_fma_f32 v90, v86, v90, v86
	v_fma_f32 v93, v83, v93, v83
	v_fma_f32 v94, v88, v94, v88
	v_mul_f32_e32 v95, 0xc0135761, v95
	v_fma_f32 v96, v85, v96, v85
	v_mul_f32_e32 v90, 0xc0135761, v90
	v_mul_f32_e32 v93, 0xc0135761, v93
	v_mul_f32_e32 v94, 0xc0135761, v94
	v_exp_f32_e32 v95, v95
	v_mul_f32_e32 v96, 0xc0135761, v96
	v_exp_f32_e32 v90, v90
	v_exp_f32_e32 v93, v93
	v_exp_f32_e32 v94, v94
	v_exp_f32_e32 v100, v96
	v_add_f32_e32 v95, 1.0, v95
	v_add_f32_e32 v90, 1.0, v90
	v_add_f32_e32 v93, 1.0, v93
	v_add_f32_e32 v94, 1.0, v94
	v_rcp_f32_e32 v96, v95
	v_add_f32_e32 v95, 1.0, v97
	v_add_f32_e32 v97, 1.0, v100
	v_rcp_f32_e32 v90, v90
	v_rcp_f32_e32 v91, v91
	v_rcp_f32_e32 v94, v94
	v_rcp_f32_e32 v95, v95
	v_rcp_f32_e32 v97, v97
	v_rcp_f32_e32 v93, v93
	v_pk_mul_f32 v[86:87], v[86:87], v[90:91]
	v_pk_mul_f32 v[88:89], v[88:89], v[94:95]
	v_pk_mul_f32 v[84:85], v[84:85], v[96:97]
	v_pk_mul_f32 v[82:83], v[82:83], v[92:93]

; __device__ __forceinline__ unsigned cvt_pk_bf16(float lo, float hi) { unsigned r; asm volatile("v_cvt_pk_bf16_f32 %0, %1, %2" : "=v"(r) : "v"(lo), "v"(hi)); return r; }
; __device__ __forceinline__ float gelu_tanh(float x) { const float y = x + 0.044715f * x * x * x; return x * __builtin_amdgcn_rcpf(1.0f + __builtin_amdgcn_exp2f(-2.302208198f * y)); }
;     __device__ __forceinline__ void operator()(const f32x4 (&acc)[2][2][4][2], const Unit& u, int wr, int wc, int fr, int fq) const {
;         const int row0 = u.pm * BM + wr * 64 + fr, col0 = u.pn * BM + wc * 32 + 8 * fq; const bool act = u.pn < nact;
; #pragma unroll
;         for (int ai = 0; ai < 2; ++ai)
; #pragma unroll
;             for (int m = 0; m < 4; ++m) { bf16_t* rowp = O + (size_t)u.ks * ks_stride + (size_t)(row0 + ai * HALF + m * 16) * ldc + col0;
; #pragma unroll
;                 for (int bj = 0; bj < 2; ++bj) { f32x4 v0 = acc[ai][bj][m][0] * ascale, v1 = acc[ai][bj][m][1] * ascale;
;                     if (act) {
; #pragma unroll
;                         for (int j = 0; j < 4; ++j) { v0[j] = gelu_tanh(v0[j]); v1[j] = gelu_tanh(v1[j]); } }
;                     u32x4 w; w.x = cvt_pk_bf16(v0[0], v0[1]); w.y = cvt_pk_bf16(v0[2], v0[3]); w.z = cvt_pk_bf16(v1[0], v1[1]); w.w = cvt_pk_bf16(v1[2], v1[3]);
;                     *(u32x4*)(rowp + bj * HALF) = w; } }
.LBB0_1275:
	v_or_b32_e32 v82, 48, v148
	v_ashrrev_i32_e32 v83, 31, v82
	v_lshlrev_b64 v[82:83], 13, v[82:83]
	v_lshl_add_u64 v[82:83], s[8:9], 0, v[82:83]
	v_lshl_add_u64 v[82:83], v[146:147], 1, v[82:83]
	s_and_b64 vcc, exec, s[2:3]
	v_cvt_pk_bf16_f32 v78, v78, v79
	v_cvt_pk_bf16_f32 v79, v80, v81
	v_cvt_pk_bf16_f32 v80, v74, v75
	v_cvt_pk_bf16_f32 v81, v76, v77
	global_store_dwordx4 v[82:83], v[78:81], off sc0 sc1
	s_cbranch_vccnz .LBB0_1277
	v_mul_f32_e32 v75, 0x3d372713, v66
	v_mul_f32_e32 v75, v66, v75
	v_mul_f32_e32 v76, 0x3d372713, v71
	v_fma_f32 v75, v66, v75, v66
	v_mul_f32_e32 v76, v71, v76
	v_mul_f32_e32 v75, 0xc0135761, v75
	v_fma_f32 v76, v71, v76, v71
	v_exp_f32_e32 v75, v75
	v_mul_f32_e32 v76, 0xc0135761, v76
	v_exp_f32_e32 v77, v76
	v_mul_f32_e32 v80, 0x3d372713, v73
	v_mul_f32_e32 v80, v73, v80
	v_fma_f32 v80, v73, v80, v73
	v_add_f32_e32 v75, 1.0, v75
	v_mul_f32_e32 v79, 0x3d372713, v68
	v_mul_f32_e32 v80, 0xc0135761, v80
	v_mul_f32_e32 v74, 0x3d372713, v70
	v_rcp_f32_e32 v76, v75
	v_add_f32_e32 v75, 1.0, v77
	v_mul_f32_e32 v77, 0x3d372713, v67
	v_mul_f32_e32 v78, 0x3d372713, v72
	v_mul_f32_e32 v79, v68, v79
	v_exp_f32_e32 v81, v80
	v_mul_f32_e32 v80, 0x3d372713, v69
	v_mul_f32_e32 v74, v70, v74
	v_mul_f32_e32 v77, v67, v77
	v_mul_f32_e32 v78, v72, v78
	v_fma_f32 v79, v68, v79, v68
	v_mul_f32_e32 v80, v69, v80
	v_fma_f32 v74, v70, v74, v70
	v_fma_f32 v77, v67, v77, v67
	v_fma_f32 v78, v72, v78, v72
	v_mul_f32_e32 v79, 0xc0135761, v79
	v_fma_f32 v80, v69, v80, v69
	v_mul_f32_e32 v74, 0xc0135761, v74
	v_mul_f32_e32 v77, 0xc0135761, v77
	v_mul_f32_e32 v78, 0xc0135761, v78
	v_exp_f32_e32 v79, v79
	v_mul_f32_e32 v80, 0xc0135761, v80
	v_exp_f32_e32 v74, v74
	v_exp_f32_e32 v77, v77
	v_exp_f32_e32 v78, v78
	v_exp_f32_e32 v84, v80
	v_add_f32_e32 v79, 1.0, v79
	v_add_f32_e32 v74, 1.0, v74
	v_add_f32_e32 v77, 1.0, v77
	v_add_f32_e32 v78, 1.0, v78
	v_rcp_f32_e32 v80, v79
	v_add_f32_e32 v79, 1.0, v81
	v_add_f32_e32 v81, 1.0, v84
	v_rcp_f32_e32 v74, v74
	v_rcp_f32_e32 v75, v75
	v_rcp_f32_e32 v78, v78
	v_rcp_f32_e32 v79, v79
	v_rcp_f32_e32 v81, v81
	v_rcp_f32_e32 v77, v77
	v_pk_mul_f32 v[70:71], v[70:71], v[74:75]
	v_pk_mul_f32 v[72:73], v[72:73], v[78:79]
	v_pk_mul_f32 v[68:69], v[68:69], v[80:81]
	v_pk_mul_f32 v[66:67], v[66:67], v[76:77]

; __device__ __forceinline__ unsigned cvt_pk_bf16(float lo, float hi) { unsigned r; asm volatile("v_cvt_pk_bf16_f32 %0, %1, %2" : "=v"(r) : "v"(lo), "v"(hi)); return r; }
; __device__ __forceinline__ float gelu_tanh(float x) { const float y = x + 0.044715f * x * x * x; return x * __builtin_amdgcn_rcpf(1.0f + __builtin_amdgcn_exp2f(-2.302208198f * y)); }
;     __device__ __forceinline__ void operator()(const f32x4 (&acc)[2][2][4][2], const Unit& u, int wr, int wc, int fr, int fq) const {
;         const int row0 = u.pm * BM + wr * 64 + fr, col0 = u.pn * BM + wc * 32 + 8 * fq; const bool act = u.pn < nact;
; #pragma unroll
;         for (int ai = 0; ai < 2; ++ai)
; #pragma unroll
;             for (int m = 0; m < 4; ++m) { bf16_t* rowp = O + (size_t)u.ks * ks_stride + (size_t)(row0 + ai * HALF + m * 16) * ldc + col0;
; #pragma unroll
;                 for (int bj = 0; bj < 2; ++bj) { f32x4 v0 = acc[ai][bj][m][0] * ascale, v1 = acc[ai][bj][m][1] * ascale;
;                     if (act) {
; #pragma unroll
;                         for (int j = 0; j < 4; ++j) { v0[j] = gelu_tanh(v0[j]); v1[j] = gelu_tanh(v1[j]); } }
;                     u32x4 w; w.x = cvt_pk_bf16(v0[0], v0[1]); w.y = cvt_pk_bf16(v0[2], v0[3]); w.z = cvt_pk_bf16(v1[0], v1[1]); w.w = cvt_pk_bf16(v1[2], v1[3]);
;                     *(u32x4*)(rowp + bj * HALF) = w; } }
.LBB0_1279:
	v_lshlrev_b64 v[66:67], 13, v[148:149]
	v_lshl_add_u64 v[66:67], s[8:9], 0, v[66:67]
	v_lshl_add_u64 v[66:67], v[146:147], 1, v[66:67]
	v_cvt_pk_bf16_f32 v62, v62, v63
	v_cvt_pk_bf16_f32 v63, v64, v65
	v_cvt_pk_bf16_f32 v64, v58, v59
	v_add_co_u32_e32 v58, vcc, 0x100000, v66
	v_cvt_pk_bf16_f32 v65, v60, v61
	s_nop 1
	v_addc_co_u32_e32 v59, vcc, 0, v67, vcc
	s_and_b64 vcc, exec, s[2:3]
	global_store_dwordx4 v[58:59], v[62:65], off sc0 sc1
	s_cbranch_vccnz .LBB0_1281
	v_mul_f32_e32 v59, 0x3d372713, v50
	v_mul_f32_e32 v59, v50, v59
	v_mul_f32_e32 v60, 0x3d372713, v55
	v_fma_f32 v59, v50, v59, v50
	v_mul_f32_e32 v60, v55, v60
	v_mul_f32_e32 v59, 0xc0135761, v59
	v_fma_f32 v60, v55, v60, v55
	v_exp_f32_e32 v59, v59
	v_mul_f32_e32 v60, 0xc0135761, v60
	v_exp_f32_e32 v61, v60
	v_mul_f32_e32 v64, 0x3d372713, v57
	v_mul_f32_e32 v64, v57, v64
	v_fma_f32 v64, v57, v64, v57
	v_add_f32_e32 v59, 1.0, v59
	v_mul_f32_e32 v63, 0x3d372713, v52
	v_mul_f32_e32 v64, 0xc0135761, v64
	v_mul_f32_e32 v58, 0x3d372713, v54
	v_rcp_f32_e32 v60, v59
	v_add_f32_e32 v59, 1.0, v61
	v_mul_f32_e32 v61, 0x3d372713, v51
	v_mul_f32_e32 v62, 0x3d372713, v56
	v_mul_f32_e32 v63, v52, v63
	v_exp_f32_e32 v65, v64
	v_mul_f32_e32 v64, 0x3d372713, v53
	v_mul_f32_e32 v58, v54, v58
	v_mul_f32_e32 v61, v51, v61
	v_mul_f32_e32 v62, v56, v62
	v_fma_f32 v63, v52, v63, v52
	v_mul_f32_e32 v64, v53, v64
	v_fma_f32 v58, v54, v58, v54
	v_fma_f32 v61, v51, v61, v51
	v_fma_f32 v62, v56, v62, v56
	v_mul_f32_e32 v63, 0xc0135761, v63
	v_fma_f32 v64, v53, v64, v53
	v_mul_f32_e32 v58, 0xc0135761, v58
	v_mul_f32_e32 v61, 0xc0135761, v61
	v_mul_f32_e32 v62, 0xc0135761, v62
	v_exp_f32_e32 v63, v63
	v_mul_f32_e32 v64, 0xc0135761, v64
	v_exp_f32_e32 v58, v58
	v_exp_f32_e32 v61, v61
	v_exp_f32_e32 v62, v62
	v_exp_f32_e32 v68, v64
	v_add_f32_e32 v63, 1.0, v63
	v_add_f32_e32 v58, 1.0, v58
	v_add_f32_e32 v61, 1.0, v61
	v_add_f32_e32 v62, 1.0, v62
	v_rcp_f32_e32 v64, v63
	v_add_f32_e32 v63, 1.0, v65
	v_add_f32_e32 v65, 1.0, v68
	v_rcp_f32_e32 v58, v58
	v_rcp_f32_e32 v59, v59
	v_rcp_f32_e32 v62, v62
	v_rcp_f32_e32 v63, v63
	v_rcp_f32_e32 v65, v65
	v_rcp_f32_e32 v61, v61
	v_pk_mul_f32 v[54:55], v[54:55], v[58:59]
	v_pk_mul_f32 v[56:57], v[56:57], v[62:63]
	v_pk_mul_f32 v[52:53], v[52:53], v[64:65]
	v_pk_mul_f32 v[50:51], v[50:51], v[60:61]
.LBB0_1281:
	s_mov_b64 s[24:25], 0x100000
	v_lshl_add_u64 v[58:59], v[66:67], 0, s[24:25]
	s_and_b64 vcc, exec, s[2:3]
	v_cvt_pk_bf16_f32 v54, v54, v55
	v_cvt_pk_bf16_f32 v55, v56, v57
	v_cvt_pk_bf16_f32 v56, v50, v51
	v_cvt_pk_bf16_f32 v57, v52, v53
	global_store_dwordx4 v[58:59], v[54:57], off offset:256 sc0 sc1
	s_cbranch_vccnz .LBB0_1283
	v_mul_f32_e32 v51, 0x3d372713, v42
	v_mul_f32_e32 v51, v42, v51
	v_mul_f32_e32 v52, 0x3d372713, v47
	v_fma_f32 v51, v42, v51, v42
	v_mul_f32_e32 v52, v47, v52
	v_mul_f32_e32 v51, 0xc0135761, v51
	v_fma_f32 v52, v47, v52, v47
	v_exp_f32_e32 v51, v51
	v_mul_f32_e32 v52, 0xc0135761, v52
	v_exp_f32_e32 v53, v52
	v_mul_f32_e32 v56, 0x3d372713, v49
	v_mul_f32_e32 v56, v49, v56
	v_fma_f32 v56, v49, v56, v49
	v_add_f32_e32 v51, 1.0, v51
	v_mul_f32_e32 v55, 0x3d372713, v44
	v_mul_f32_e32 v56, 0xc0135761, v56
	v_mul_f32_e32 v50, 0x3d372713, v46
	v_rcp_f32_e32 v52, v51
	v_add_f32_e32 v51, 1.0, v53
	v_mul_f32_e32 v53, 0x3d372713, v43
	v_mul_f32_e32 v54, 0x3d372713, v48
	v_mul_f32_e32 v55, v44, v55
	v_exp_f32_e32 v57, v56
	v_mul_f32_e32 v56, 0x3d372713, v45
	v_mul_f32_e32 v50, v46, v50
	v_mul_f32_e32 v53, v43, v53
	v_mul_f32_e32 v54, v48, v54
	v_fma_f32 v55, v44, v55, v44
	v_mul_f32_e32 v56, v45, v56
	v_fma_f32 v50, v46, v50, v46
	v_fma_f32 v53, v43, v53, v43
	v_fma_f32 v54, v48, v54, v48
	v_mul_f32_e32 v55, 0xc0135761, v55
	v_fma_f32 v56, v45, v56, v45
	v_mul_f32_e32 v50, 0xc0135761, v50
	v_mul_f32_e32 v53, 0xc0135761, v53
	v_mul_f32_e32 v54, 0xc0135761, v54
	v_exp_f32_e32 v55, v55
	v_mul_f32_e32 v56, 0xc0135761, v56
	v_exp_f32_e32 v50, v50
	v_exp_f32_e32 v53, v53
	v_exp_f32_e32 v54, v54
	v_exp_f32_e32 v58, v56
	v_add_f32_e32 v55, 1.0, v55
	v_add_f32_e32 v50, 1.0, v50
	v_add_f32_e32 v53, 1.0, v53
	v_add_f32_e32 v54, 1.0, v54
	v_rcp_f32_e32 v56, v55
	v_add_f32_e32 v55, 1.0, v57
	v_add_f32_e32 v57, 1.0, v58
	v_rcp_f32_e32 v50, v50
	v_rcp_f32_e32 v51, v51
	v_rcp_f32_e32 v54, v54
	v_rcp_f32_e32 v55, v55
	v_rcp_f32_e32 v57, v57
	v_rcp_f32_e32 v53, v53
	v_pk_mul_f32 v[46:47], v[46:47], v[50:51]
	v_pk_mul_f32 v[48:49], v[48:49], v[54:55]
	v_pk_mul_f32 v[44:45], v[44:45], v[56:57]
	v_pk_mul_f32 v[42:43], v[42:43], v[52:53]
; __device__ __forceinline__ unsigned cvt_pk_bf16(float lo, float hi) { unsigned r; asm volatile("v_cvt_pk_bf16_f32 %0, %1, %2" : "=v"(r) : "v"(lo), "v"(hi)); return r; }
; __device__ __forceinline__ float gelu_tanh(float x) { const float y = x + 0.044715f * x * x * x; return x * __builtin_amdgcn_rcpf(1.0f + __builtin_amdgcn_exp2f(-2.302208198f * y)); }
;     __device__ __forceinline__ void operator()(const f32x4 (&acc)[2][2][4][2], const Unit& u, int wr, int wc, int fr, int fq) const {
;         const int row0 = u.pm * BM + wr * 64 + fr, col0 = u.pn * BM + wc * 32 + 8 * fq; const bool act = u.pn < nact;
; #pragma unroll
;         for (int ai = 0; ai < 2; ++ai)
; #pragma unroll
;             for (int m = 0; m < 4; ++m) { bf16_t* rowp = O + (size_t)u.ks * ks_stride + (size_t)(row0 + ai * HALF + m * 16) * ldc + col0;
; #pragma unroll
;                 for (int bj = 0; bj < 2; ++bj) { f32x4 v0 = acc[ai][bj][m][0] * ascale, v1 = acc[ai][bj][m][1] * ascale;
;                     if (act) {
; #pragma unroll
;                         for (int j = 0; j < 4; ++j) { v0[j] = gelu_tanh(v0[j]); v1[j] = gelu_tanh(v1[j]); } }
;                     u32x4 w; w.x = cvt_pk_bf16(v0[0], v0[1]); w.y = cvt_pk_bf16(v0[2], v0[3]); w.z = cvt_pk_bf16(v1[0], v1[1]); w.w = cvt_pk_bf16(v1[2], v1[3]);
;                     *(u32x4*)(rowp + bj * HALF) = w; } }
.LBB0_1283:
	v_lshlrev_b64 v[50:51], 13, v[148:149]
	v_lshl_add_u64 v[50:51], s[8:9], 0, v[50:51]
	v_lshl_add_u64 v[50:51], v[146:147], 1, v[50:51]
	v_cvt_pk_bf16_f32 v46, v46, v47
	v_cvt_pk_bf16_f32 v47, v48, v49
	v_cvt_pk_bf16_f32 v48, v42, v43
	v_add_co_u32_e32 v42, vcc, 0x120000, v50
	v_cvt_pk_bf16_f32 v49, v44, v45
	s_nop 1
	v_addc_co_u32_e32 v43, vcc, 0, v51, vcc
	s_and_b64 vcc, exec, s[2:3]
	global_store_dwordx4 v[42:43], v[46:49], off sc0 sc1
	s_cbranch_vccnz .LBB0_1285
	v_mul_f32_e32 v43, 0x3d372713, v34
	v_mul_f32_e32 v43, v34, v43
	v_mul_f32_e32 v44, 0x3d372713, v39
	v_fma_f32 v43, v34, v43, v34
	v_mul_f32_e32 v44, v39, v44
	v_mul_f32_e32 v43, 0xc0135761, v43
	v_fma_f32 v44, v39, v44, v39
	v_exp_f32_e32 v43, v43
	v_mul_f32_e32 v44, 0xc0135761, v44
	v_exp_f32_e32 v45, v44
	v_mul_f32_e32 v48, 0x3d372713, v41
	v_mul_f32_e32 v48, v41, v48
	v_fma_f32 v48, v41, v48, v41
	v_add_f32_e32 v43, 1.0, v43
	v_mul_f32_e32 v47, 0x3d372713, v36
	v_mul_f32_e32 v48, 0xc0135761, v48
	v_mul_f32_e32 v42, 0x3d372713, v38
	v_rcp_f32_e32 v44, v43
	v_add_f32_e32 v43, 1.0, v45
	v_mul_f32_e32 v45, 0x3d372713, v35
	v_mul_f32_e32 v46, 0x3d372713, v40
	v_mul_f32_e32 v47, v36, v47
	v_exp_f32_e32 v49, v48
	v_mul_f32_e32 v48, 0x3d372713, v37
	v_mul_f32_e32 v42, v38, v42
	v_mul_f32_e32 v45, v35, v45
	v_mul_f32_e32 v46, v40, v46
	v_fma_f32 v47, v36, v47, v36
	v_mul_f32_e32 v48, v37, v48
	v_fma_f32 v42, v38, v42, v38
	v_fma_f32 v45, v35, v45, v35
	v_fma_f32 v46, v40, v46, v40
	v_mul_f32_e32 v47, 0xc0135761, v47
	v_fma_f32 v48, v37, v48, v37
	v_mul_f32_e32 v42, 0xc0135761, v42
	v_mul_f32_e32 v45, 0xc0135761, v45
	v_mul_f32_e32 v46, 0xc0135761, v46
	v_exp_f32_e32 v47, v47
	v_mul_f32_e32 v48, 0xc0135761, v48
	v_exp_f32_e32 v42, v42
	v_exp_f32_e32 v45, v45
	v_exp_f32_e32 v46, v46
	v_exp_f32_e32 v52, v48
	v_add_f32_e32 v47, 1.0, v47
	v_add_f32_e32 v42, 1.0, v42
	v_add_f32_e32 v45, 1.0, v45
	v_add_f32_e32 v46, 1.0, v46
	v_rcp_f32_e32 v48, v47
	v_add_f32_e32 v47, 1.0, v49
	v_add_f32_e32 v49, 1.0, v52
	v_rcp_f32_e32 v42, v42
	v_rcp_f32_e32 v43, v43
	v_rcp_f32_e32 v46, v46
	v_rcp_f32_e32 v47, v47
	v_rcp_f32_e32 v49, v49
	v_rcp_f32_e32 v45, v45
	v_pk_mul_f32 v[38:39], v[38:39], v[42:43]
	v_pk_mul_f32 v[40:41], v[40:41], v[46:47]
	v_pk_mul_f32 v[36:37], v[36:37], v[48:49]
	v_pk_mul_f32 v[34:35], v[34:35], v[44:45]
.LBB0_1285:
	s_mov_b64 s[24:25], 0x120000
	v_lshl_add_u64 v[42:43], v[50:51], 0, s[24:25]
	s_and_b64 vcc, exec, s[2:3]
	v_cvt_pk_bf16_f32 v38, v38, v39
	v_cvt_pk_bf16_f32 v39, v40, v41
	v_cvt_pk_bf16_f32 v40, v34, v35
	v_cvt_pk_bf16_f32 v41, v36, v37
	global_store_dwordx4 v[42:43], v[38:41], off offset:256 sc0 sc1
	s_cbranch_vccnz .LBB0_1287
	v_mul_f32_e32 v35, 0x3d372713, v26
	v_mul_f32_e32 v35, v26, v35
	v_mul_f32_e32 v36, 0x3d372713, v31
	v_fma_f32 v35, v26, v35, v26
	v_mul_f32_e32 v36, v31, v36
	v_mul_f32_e32 v35, 0xc0135761, v35
	v_fma_f32 v36, v31, v36, v31
	v_exp_f32_e32 v35, v35
	v_mul_f32_e32 v36, 0xc0135761, v36
	v_exp_f32_e32 v37, v36
	v_mul_f32_e32 v40, 0x3d372713, v33
	v_mul_f32_e32 v40, v33, v40
	v_fma_f32 v40, v33, v40, v33
	v_add_f32_e32 v35, 1.0, v35
	v_mul_f32_e32 v39, 0x3d372713, v28
	v_mul_f32_e32 v40, 0xc0135761, v40
	v_mul_f32_e32 v34, 0x3d372713, v30
	v_rcp_f32_e32 v36, v35
	v_add_f32_e32 v35, 1.0, v37
	v_mul_f32_e32 v37, 0x3d372713, v27
	v_mul_f32_e32 v38, 0x3d372713, v32
	v_mul_f32_e32 v39, v28, v39
	v_exp_f32_e32 v41, v40
	v_mul_f32_e32 v40, 0x3d372713, v29
	v_mul_f32_e32 v34, v30, v34
	v_mul_f32_e32 v37, v27, v37
	v_mul_f32_e32 v38, v32, v38
	v_fma_f32 v39, v28, v39, v28
	v_mul_f32_e32 v40, v29, v40
	v_fma_f32 v34, v30, v34, v30
	v_fma_f32 v37, v27, v37, v27
	v_fma_f32 v38, v32, v38, v32
	v_mul_f32_e32 v39, 0xc0135761, v39
	v_fma_f32 v40, v29, v40, v29
	v_mul_f32_e32 v34, 0xc0135761, v34
	v_mul_f32_e32 v37, 0xc0135761, v37
	v_mul_f32_e32 v38, 0xc0135761, v38
	v_exp_f32_e32 v39, v39
	v_mul_f32_e32 v40, 0xc0135761, v40
	v_exp_f32_e32 v34, v34
	v_exp_f32_e32 v37, v37
	v_exp_f32_e32 v38, v38
	v_exp_f32_e32 v42, v40
	v_add_f32_e32 v39, 1.0, v39
	v_add_f32_e32 v34, 1.0, v34
	v_add_f32_e32 v37, 1.0, v37
	v_add_f32_e32 v38, 1.0, v38
	v_rcp_f32_e32 v40, v39
	v_add_f32_e32 v39, 1.0, v41
	v_add_f32_e32 v41, 1.0, v42
	v_rcp_f32_e32 v34, v34
	v_rcp_f32_e32 v35, v35
	v_rcp_f32_e32 v38, v38
	v_rcp_f32_e32 v39, v39
	v_rcp_f32_e32 v41, v41
	v_rcp_f32_e32 v37, v37
	v_pk_mul_f32 v[30:31], v[30:31], v[34:35]
	v_pk_mul_f32 v[32:33], v[32:33], v[38:39]
	v_pk_mul_f32 v[28:29], v[28:29], v[40:41]
	v_pk_mul_f32 v[26:27], v[26:27], v[36:37]
; __device__ __forceinline__ unsigned cvt_pk_bf16(float lo, float hi) { unsigned r; asm volatile("v_cvt_pk_bf16_f32 %0, %1, %2" : "=v"(r) : "v"(lo), "v"(hi)); return r; }
; __device__ __forceinline__ float gelu_tanh(float x) { const float y = x + 0.044715f * x * x * x; return x * __builtin_amdgcn_rcpf(1.0f + __builtin_amdgcn_exp2f(-2.302208198f * y)); }
;     __device__ __forceinline__ void operator()(const f32x4 (&acc)[2][2][4][2], const Unit& u, int wr, int wc, int fr, int fq) const {
;         const int row0 = u.pm * BM + wr * 64 + fr, col0 = u.pn * BM + wc * 32 + 8 * fq; const bool act = u.pn < nact;
; #pragma unroll
;         for (int ai = 0; ai < 2; ++ai)
; #pragma unroll
;             for (int m = 0; m < 4; ++m) { bf16_t* rowp = O + (size_t)u.ks * ks_stride + (size_t)(row0 + ai * HALF + m * 16) * ldc + col0;
; #pragma unroll
;                 for (int bj = 0; bj < 2; ++bj) { f32x4 v0 = acc[ai][bj][m][0] * ascale, v1 = acc[ai][bj][m][1] * ascale;
;                     if (act) {
; #pragma unroll
;                         for (int j = 0; j < 4; ++j) { v0[j] = gelu_tanh(v0[j]); v1[j] = gelu_tanh(v1[j]); } }
;                     u32x4 w; w.x = cvt_pk_bf16(v0[0], v0[1]); w.y = cvt_pk_bf16(v0[2], v0[3]); w.z = cvt_pk_bf16(v1[0], v1[1]); w.w = cvt_pk_bf16(v1[2], v1[3]);
;                     *(u32x4*)(rowp + bj * HALF) = w; } }
.LBB0_1287:
	v_lshlrev_b64 v[34:35], 13, v[148:149]
	v_lshl_add_u64 v[34:35], s[8:9], 0, v[34:35]
	v_lshl_add_u64 v[34:35], v[146:147], 1, v[34:35]
	v_cvt_pk_bf16_f32 v30, v30, v31
	v_cvt_pk_bf16_f32 v31, v32, v33
	v_cvt_pk_bf16_f32 v32, v26, v27
	v_add_co_u32_e32 v26, vcc, 0x140000, v34
	v_cvt_pk_bf16_f32 v33, v28, v29
	s_nop 1
	v_addc_co_u32_e32 v27, vcc, 0, v35, vcc
	s_and_b64 vcc, exec, s[2:3]
	global_store_dwordx4 v[26:27], v[30:33], off sc0 sc1
	s_cbranch_vccnz .LBB0_1289
	v_mul_f32_e32 v27, 0x3d372713, v18
	v_mul_f32_e32 v27, v18, v27
	v_mul_f32_e32 v28, 0x3d372713, v23
	v_fma_f32 v27, v18, v27, v18
	v_mul_f32_e32 v28, v23, v28
	v_mul_f32_e32 v27, 0xc0135761, v27
	v_fma_f32 v28, v23, v28, v23
	v_exp_f32_e32 v27, v27
	v_mul_f32_e32 v28, 0xc0135761, v28
	v_exp_f32_e32 v29, v28
	v_mul_f32_e32 v32, 0x3d372713, v25
	v_mul_f32_e32 v32, v25, v32
	v_fma_f32 v32, v25, v32, v25
	v_add_f32_e32 v27, 1.0, v27
	v_mul_f32_e32 v31, 0x3d372713, v20
	v_mul_f32_e32 v32, 0xc0135761, v32
	v_mul_f32_e32 v26, 0x3d372713, v22
	v_rcp_f32_e32 v28, v27
	v_add_f32_e32 v27, 1.0, v29
	v_mul_f32_e32 v29, 0x3d372713, v19
	v_mul_f32_e32 v30, 0x3d372713, v24
	v_mul_f32_e32 v31, v20, v31
	v_exp_f32_e32 v33, v32
	v_mul_f32_e32 v32, 0x3d372713, v21
	v_mul_f32_e32 v26, v22, v26
	v_mul_f32_e32 v29, v19, v29
	v_mul_f32_e32 v30, v24, v30
	v_fma_f32 v31, v20, v31, v20
	v_mul_f32_e32 v32, v21, v32
	v_fma_f32 v26, v22, v26, v22
	v_fma_f32 v29, v19, v29, v19
	v_fma_f32 v30, v24, v30, v24
	v_mul_f32_e32 v31, 0xc0135761, v31
	v_fma_f32 v32, v21, v32, v21
	v_mul_f32_e32 v26, 0xc0135761, v26
	v_mul_f32_e32 v29, 0xc0135761, v29
	v_mul_f32_e32 v30, 0xc0135761, v30
	v_exp_f32_e32 v31, v31
	v_mul_f32_e32 v32, 0xc0135761, v32
	v_exp_f32_e32 v26, v26
	v_exp_f32_e32 v29, v29
	v_exp_f32_e32 v30, v30
	v_exp_f32_e32 v36, v32
	v_add_f32_e32 v31, 1.0, v31
	v_add_f32_e32 v26, 1.0, v26
	v_add_f32_e32 v29, 1.0, v29
	v_add_f32_e32 v30, 1.0, v30
	v_rcp_f32_e32 v32, v31
	v_add_f32_e32 v31, 1.0, v33
	v_add_f32_e32 v33, 1.0, v36
	v_rcp_f32_e32 v26, v26
	v_rcp_f32_e32 v27, v27
	v_rcp_f32_e32 v30, v30
	v_rcp_f32_e32 v31, v31
	v_rcp_f32_e32 v33, v33
	v_rcp_f32_e32 v29, v29
	v_pk_mul_f32 v[22:23], v[22:23], v[26:27]
	v_pk_mul_f32 v[24:25], v[24:25], v[30:31]
	v_pk_mul_f32 v[20:21], v[20:21], v[32:33]
	v_pk_mul_f32 v[18:19], v[18:19], v[28:29]
.LBB0_1289:
	s_mov_b64 s[24:25], 0x140000
	v_lshl_add_u64 v[26:27], v[34:35], 0, s[24:25]
	s_and_b64 vcc, exec, s[2:3]
	v_cvt_pk_bf16_f32 v22, v22, v23
	v_cvt_pk_bf16_f32 v23, v24, v25
	v_cvt_pk_bf16_f32 v24, v18, v19
	v_cvt_pk_bf16_f32 v25, v20, v21
	global_store_dwordx4 v[26:27], v[22:25], off offset:256 sc0 sc1
	s_cbranch_vccnz .LBB0_1291
	v_mul_f32_e32 v19, 0x3d372713, v10
	v_mul_f32_e32 v19, v10, v19
	v_mul_f32_e32 v20, 0x3d372713, v15
	v_fma_f32 v19, v10, v19, v10
	v_mul_f32_e32 v20, v15, v20
	v_mul_f32_e32 v19, 0xc0135761, v19
	v_fma_f32 v20, v15, v20, v15
	v_exp_f32_e32 v19, v19
	v_mul_f32_e32 v20, 0xc0135761, v20
	v_exp_f32_e32 v21, v20
	v_mul_f32_e32 v24, 0x3d372713, v17
	v_mul_f32_e32 v24, v17, v24
	v_fma_f32 v24, v17, v24, v17
	v_add_f32_e32 v19, 1.0, v19
	v_mul_f32_e32 v23, 0x3d372713, v12
	v_mul_f32_e32 v24, 0xc0135761, v24
	v_mul_f32_e32 v18, 0x3d372713, v14
	v_rcp_f32_e32 v20, v19
	v_add_f32_e32 v19, 1.0, v21
	v_mul_f32_e32 v21, 0x3d372713, v11
	v_mul_f32_e32 v22, 0x3d372713, v16
	v_mul_f32_e32 v23, v12, v23
	v_exp_f32_e32 v25, v24
	v_mul_f32_e32 v24, 0x3d372713, v13
	v_mul_f32_e32 v18, v14, v18
	v_mul_f32_e32 v21, v11, v21
	v_mul_f32_e32 v22, v16, v22
	v_fma_f32 v23, v12, v23, v12
	v_mul_f32_e32 v24, v13, v24
	v_fma_f32 v18, v14, v18, v14
	v_fma_f32 v21, v11, v21, v11
	v_fma_f32 v22, v16, v22, v16
	v_mul_f32_e32 v23, 0xc0135761, v23
	v_fma_f32 v24, v13, v24, v13
	v_mul_f32_e32 v18, 0xc0135761, v18
	v_mul_f32_e32 v21, 0xc0135761, v21
	v_mul_f32_e32 v22, 0xc0135761, v22
	v_exp_f32_e32 v23, v23
	v_mul_f32_e32 v24, 0xc0135761, v24
	v_exp_f32_e32 v18, v18
	v_exp_f32_e32 v21, v21
	v_exp_f32_e32 v22, v22
	v_exp_f32_e32 v26, v24
	v_add_f32_e32 v23, 1.0, v23
	v_add_f32_e32 v18, 1.0, v18
	v_add_f32_e32 v21, 1.0, v21
	v_add_f32_e32 v22, 1.0, v22
	v_rcp_f32_e32 v24, v23
	v_add_f32_e32 v23, 1.0, v25
	v_add_f32_e32 v25, 1.0, v26
	v_rcp_f32_e32 v18, v18
	v_rcp_f32_e32 v19, v19
	v_rcp_f32_e32 v22, v22
	v_rcp_f32_e32 v23, v23
	v_rcp_f32_e32 v25, v25
	v_rcp_f32_e32 v21, v21
	v_pk_mul_f32 v[14:15], v[14:15], v[18:19]
	v_pk_mul_f32 v[16:17], v[16:17], v[22:23]
	v_pk_mul_f32 v[12:13], v[12:13], v[24:25]
	v_pk_mul_f32 v[10:11], v[10:11], v[20:21]
; __device__ __forceinline__ unsigned cvt_pk_bf16(float lo, float hi) { unsigned r; asm volatile("v_cvt_pk_bf16_f32 %0, %1, %2" : "=v"(r) : "v"(lo), "v"(hi)); return r; }
; __device__ __forceinline__ float gelu_tanh(float x) { const float y = x + 0.044715f * x * x * x; return x * __builtin_amdgcn_rcpf(1.0f + __builtin_amdgcn_exp2f(-2.302208198f * y)); }
; #define PG8_BAR __builtin_amdgcn_s_barrier()
;     __device__ __forceinline__ void operator()(const f32x4 (&acc)[2][2][4][2], const Unit& u, int wr, int wc, int fr, int fq) const {
;         const int row0 = u.pm * BM + wr * 64 + fr, col0 = u.pn * BM + wc * 32 + 8 * fq; const bool act = u.pn < nact;
; #pragma unroll
;         for (int ai = 0; ai < 2; ++ai)
; #pragma unroll
;             for (int m = 0; m < 4; ++m) { bf16_t* rowp = O + (size_t)u.ks * ks_stride + (size_t)(row0 + ai * HALF + m * 16) * ldc + col0;
; #pragma unroll
;                 for (int bj = 0; bj < 2; ++bj) { f32x4 v0 = acc[ai][bj][m][0] * ascale, v1 = acc[ai][bj][m][1] * ascale;
;                     if (act) {
; #pragma unroll
;                         for (int j = 0; j < 4; ++j) { v0[j] = gelu_tanh(v0[j]); v1[j] = gelu_tanh(v1[j]); } }
;                     u32x4 w; w.x = cvt_pk_bf16(v0[0], v0[1]); w.y = cvt_pk_bf16(v0[2], v0[3]); w.z = cvt_pk_bf16(v1[0], v1[1]); w.w = cvt_pk_bf16(v1[2], v1[3]);
;                     *(u32x4*)(rowp + bj * HALF) = w; } }
; template <class Epi, class Sched, bool ALIGN_EPI = false, bool SP2 = false, bool FP8 = false>
; __device__ __forceinline__ void gemm_phase(PG8_LAS unsigned char* lds, const Gemm g, const Sched& S, const Epi& E) {
;     ...
;         if constexpr (!Epi::AFTER_DRAIN) { E(acc, cur, wr, wc, fr, fq); S.done(cur); }
;         if (!has_next) break;
; #pragma unroll
;         for (int a = 0; a < 2; ++a)
; #pragma unroll
;             for (int b = 0; b < 2; ++b)
; #pragma unroll
;                 for (int m = 0; m < 4; ++m)
; #pragma unroll
;                     for (int n = 0; n < 2; ++n) acc[a][b][m][n] = (f32x4){0.f, 0.f, 0.f, 0.f};
;         cur = nxt; cA = nA; cB = nB; ++ui;
;         if constexpr (ALIGN_EPI) { if (wr == 1) PG8_BAR; }
.LBB0_1291:
	v_lshlrev_b64 v[18:19], 13, v[148:149]
	v_lshl_add_u64 v[18:19], s[8:9], 0, v[18:19]
	v_lshl_add_u64 v[18:19], v[146:147], 1, v[18:19]
	v_cvt_pk_bf16_f32 v14, v14, v15
	v_cvt_pk_bf16_f32 v15, v16, v17
	v_cvt_pk_bf16_f32 v16, v10, v11
	v_add_co_u32_e32 v10, vcc, 0x160000, v18
	v_cvt_pk_bf16_f32 v17, v12, v13
	s_nop 1
	v_addc_co_u32_e32 v11, vcc, 0, v19, vcc
	s_and_b64 vcc, exec, s[2:3]
	global_store_dwordx4 v[10:11], v[14:17], off sc0 sc1
	s_cbranch_vccnz .LBB0_1293
	v_mul_f32_e32 v11, 0x3d372713, v2
	v_mul_f32_e32 v11, v2, v11
	v_mul_f32_e32 v12, 0x3d372713, v7
	v_fma_f32 v11, v2, v11, v2
	v_mul_f32_e32 v12, v7, v12
	v_mul_f32_e32 v11, 0xc0135761, v11
	v_fma_f32 v12, v7, v12, v7
	v_exp_f32_e32 v11, v11
	v_mul_f32_e32 v12, 0xc0135761, v12
	v_exp_f32_e32 v13, v12
	v_mul_f32_e32 v16, 0x3d372713, v9
	v_mul_f32_e32 v16, v9, v16
	v_fma_f32 v16, v9, v16, v9
	v_add_f32_e32 v11, 1.0, v11
	v_mul_f32_e32 v15, 0x3d372713, v4
	v_mul_f32_e32 v16, 0xc0135761, v16
	v_mul_f32_e32 v10, 0x3d372713, v6
	v_rcp_f32_e32 v12, v11
	v_add_f32_e32 v11, 1.0, v13
	v_mul_f32_e32 v13, 0x3d372713, v3
	v_mul_f32_e32 v14, 0x3d372713, v8
	v_mul_f32_e32 v15, v4, v15
	v_exp_f32_e32 v17, v16
	v_mul_f32_e32 v16, 0x3d372713, v5
	v_mul_f32_e32 v10, v6, v10
	v_mul_f32_e32 v13, v3, v13
	v_mul_f32_e32 v14, v8, v14
	v_fma_f32 v15, v4, v15, v4
	v_mul_f32_e32 v16, v5, v16
	v_fma_f32 v10, v6, v10, v6
	v_fma_f32 v13, v3, v13, v3
	v_fma_f32 v14, v8, v14, v8
	v_mul_f32_e32 v15, 0xc0135761, v15
	v_fma_f32 v16, v5, v16, v5
	v_mul_f32_e32 v10, 0xc0135761, v10
	v_mul_f32_e32 v13, 0xc0135761, v13
	v_mul_f32_e32 v14, 0xc0135761, v14
	v_exp_f32_e32 v15, v15
	v_mul_f32_e32 v16, 0xc0135761, v16
	v_exp_f32_e32 v10, v10
	v_exp_f32_e32 v13, v13
	v_exp_f32_e32 v14, v14
	v_exp_f32_e32 v20, v16
	v_add_f32_e32 v15, 1.0, v15
	v_add_f32_e32 v10, 1.0, v10
	v_add_f32_e32 v13, 1.0, v13
	v_add_f32_e32 v14, 1.0, v14
	v_rcp_f32_e32 v16, v15
	v_add_f32_e32 v15, 1.0, v17
	v_add_f32_e32 v17, 1.0, v20
	v_rcp_f32_e32 v10, v10
	v_rcp_f32_e32 v11, v11
	v_rcp_f32_e32 v14, v14
	v_rcp_f32_e32 v15, v15
	v_rcp_f32_e32 v17, v17
	v_rcp_f32_e32 v13, v13
	v_pk_mul_f32 v[6:7], v[6:7], v[10:11]
	v_pk_mul_f32 v[8:9], v[8:9], v[14:15]
	v_pk_mul_f32 v[4:5], v[4:5], v[16:17]
	v_pk_mul_f32 v[2:3], v[2:3], v[12:13]
.LBB0_1293:
	s_mov_b64 s[2:3], 0x160000
	v_lshl_add_u64 v[10:11], v[18:19], 0, s[2:3]
	s_andn2_b64 vcc, exec, s[0:1]
	s_mov_b64 s[0:1], -1
	v_cvt_pk_bf16_f32 v6, v6, v7
	v_cvt_pk_bf16_f32 v7, v8, v9
	v_cvt_pk_bf16_f32 v8, v2, v3
	v_cvt_pk_bf16_f32 v9, v4, v5
	global_store_dwordx4 v[10:11], v[6:9], off offset:256 sc0 sc1
	s_cbranch_vccnz .LBB0_1251
	s_andn2_b64 vcc, exec, s[6:7]
	s_cbranch_vccnz .LBB0_1250
	s_barrier
	s_branch .LBB0_1250

; __device__ __forceinline__ unsigned cvt_pk_bf16(float lo, float hi) { unsigned r; asm volatile("v_cvt_pk_bf16_f32 %0, %1, %2" : "=v"(r) : "v"(lo), "v"(hi)); return r; }
;     __device__ __forceinline__ void operator()(const f32x4 (&acc)[2][2][4][2], const Unit& u, int wr, int wc, int fr, int fq) const {
;     ...
;         const int row0 = u.pm * BM + wr * 64 + fr, col0 = u.pn * BM + wc * 32 + 8 * fq;
;         f32x4 gg[2][2];
; #pragma unroll
;         for (int bj = 0; bj < 2; ++bj)
; #pragma unroll
;             for (int n = 0; n < 2; ++n) gg[bj][n] = *(const f32x4*)(gv + col0 + bj * HALF + n * 4) * ascale;
; #pragma unroll
;         for (int ai = 0; ai < 2; ++ai) {
;             if constexpr (RB) {
;                 u32x4 bs[4][2];
; #pragma unroll
;                 for (int m = 0; m < 4; ++m)
; #pragma unroll
;                     for (int bj = 0; bj < 2; ++bj) bs[m][bj] = *(const u32x4*)(H + (size_t)(row0 + ai * HALF + m * 16) * 2048 + col0 + bj * HALF);
; #pragma unroll
;                 for (int m = 0; m < 4; ++m)
; #pragma unroll
;                     for (int bj = 0; bj < 2; ++bj) { const u32x4 b = bs[m][bj];
;                         f32x4 r0, r1; r0.x = __builtin_bit_cast(float, b.x << 16); r0.y = __builtin_bit_cast(float, b.x & 0xffff0000u); r0.z = __builtin_bit_cast(float, b.y << 16); r0.w = __builtin_bit_cast(float, b.y & 0xffff0000u);
;                         r1.x = __builtin_bit_cast(float, b.z << 16); r1.y = __builtin_bit_cast(float, b.z & 0xffff0000u); r1.z = __builtin_bit_cast(float, b.w << 16); r1.w = __builtin_bit_cast(float, b.w & 0xffff0000u);
;                         r0 += gg[bj][0] * acc[ai][bj][m][0]; r1 += gg[bj][1] * acc[ai][bj][m][1];
;                         u32x4 w; w.x = cvt_pk_bf16(r0[0], r0[1]); w.y = cvt_pk_bf16(r0[2], r0[3]); w.z = cvt_pk_bf16(r1[0], r1[1]); w.w = cvt_pk_bf16(r1[2], r1[3]);
;                         *(u32x4*)(H + (size_t)(row0 + ai * HALF + m * 16) * 2048 + col0 + bj * HALF) = w; }
.LBB0_1677:
	v_lshl_or_b32 v130, s28, 8, v173
	v_ashrrev_i32_e32 v131, 31, v130
	v_lshl_add_u32 v168, s26, 8, v1
	v_lshlrev_b64 v[162:163], 1, v[130:131]
	v_ashrrev_i32_e32 v169, 31, v168
	v_lshl_add_u64 v[164:165], s[6:7], 0, v[162:163]
	v_lshlrev_b64 v[166:167], 12, v[168:169]
	v_lshl_add_u64 v[132:133], v[164:165], 0, v[166:167]
	global_load_dwordx4 v[182:185], v[132:133], off
	global_load_dwordx4 v[186:189], v[132:133], off offset:256
	v_or_b32_e32 v132, 16, v168
	s_lshl_b64 s[30:31], s[30:31], 2
	v_ashrrev_i32_e32 v133, 31, v132
	s_add_u32 s30, s46, s30
	v_lshlrev_b64 v[202:203], 12, v[132:133]
	s_addc_u32 s31, s47, s31
	v_lshl_add_u64 v[170:171], v[164:165], 0, v[202:203]
	v_lshl_add_u64 v[130:131], v[130:131], 2, s[30:31]
	global_load_dwordx4 v[190:193], v[170:171], off
	global_load_dwordx4 v[142:145], v[130:131], off
	global_load_dwordx4 v[138:141], v[130:131], off offset:16
	global_load_dwordx4 v[134:137], v[130:131], off offset:512
	s_nop 0
	global_load_dwordx4 v[130:133], v[130:131], off offset:528
	s_nop 0
	global_load_dwordx4 v[194:197], v[170:171], off offset:256
	v_or_b32_e32 v170, 32, v168
	v_ashrrev_i32_e32 v171, 31, v170
	v_lshlrev_b64 v[170:171], 12, v[170:171]
	v_lshl_add_u64 v[204:205], v[164:165], 0, v[170:171]
	global_load_dwordx4 v[198:201], v[204:205], off
	v_or_b32_e32 v168, 48, v168
	v_ashrrev_i32_e32 v169, 31, v168
	v_lshlrev_b64 v[168:169], 12, v[168:169]
	v_lshl_add_u64 v[206:207], s[6:7], 0, v[166:167]
	v_lshl_add_u64 v[210:211], v[164:165], 0, v[168:169]
	v_lshl_add_u64 v[214:215], v[206:207], 0, v[162:163]
	v_lshl_add_u64 v[216:217], s[6:7], 0, v[202:203]
	global_load_dwordx4 v[202:205], v[204:205], off offset:256
	s_nop 0
	global_load_dwordx4 v[206:209], v[210:211], off
	s_nop 0
	global_load_dwordx4 v[210:213], v[210:211], off offset:256
	v_lshl_add_u64 v[216:217], v[216:217], 0, v[162:163]
	s_mov_b64 s[30:31], 0x80000
	s_andn2_b64 vcc, exec, s[0:1]
	s_mov_b64 s[0:1], -1
	s_waitcnt vmcnt(0)
	v_lshlrev_b32_e32 v218, 16, v182
	v_and_b32_e32 v219, 0xffff0000, v182
	v_lshlrev_b32_e32 v182, 16, v183
	v_and_b32_e32 v183, 0xffff0000, v183
	v_lshlrev_b32_e32 v220, 16, v184
	v_and_b32_e32 v221, 0xffff0000, v184
	v_lshlrev_b32_e32 v184, 16, v185
	v_and_b32_e32 v185, 0xffff0000, v185
	v_lshlrev_b32_e32 v224, 16, v188
	v_and_b32_e32 v225, 0xffff0000, v188
	v_lshlrev_b32_e32 v188, 16, v189
	v_and_b32_e32 v189, 0xffff0000, v189
	v_lshlrev_b32_e32 v222, 16, v186
	v_and_b32_e32 v223, 0xffff0000, v186
	v_lshlrev_b32_e32 v186, 16, v187
	v_and_b32_e32 v187, 0xffff0000, v187
	v_pk_fma_f32 v[128:129], v[128:129], v[144:145], v[182:183]
	v_pk_fma_f32 v[126:127], v[126:127], v[142:143], v[218:219]
	v_pk_fma_f32 v[124:125], v[124:125], v[140:141], v[184:185]
	v_pk_fma_f32 v[122:123], v[122:123], v[138:139], v[220:221]
	v_pk_fma_f32 v[182:183], v[108:109], v[132:133], v[188:189]
	v_pk_fma_f32 v[184:185], v[106:107], v[130:131], v[224:225]
	v_cvt_pk_bf16_f32 v106, v126, v127
	v_cvt_pk_bf16_f32 v107, v128, v129
	v_cvt_pk_bf16_f32 v108, v122, v123
	v_cvt_pk_bf16_f32 v109, v124, v125
	v_lshlrev_b32_e32 v226, 16, v190
	v_and_b32_e32 v227, 0xffff0000, v190
	v_lshlrev_b32_e32 v190, 16, v191
	v_and_b32_e32 v191, 0xffff0000, v191
	v_lshlrev_b32_e32 v228, 16, v192
	v_and_b32_e32 v229, 0xffff0000, v192
	v_lshlrev_b32_e32 v192, 16, v193
	v_and_b32_e32 v193, 0xffff0000, v193
	v_pk_fma_f32 v[112:113], v[112:113], v[136:137], v[186:187]
	v_pk_fma_f32 v[110:111], v[110:111], v[134:135], v[222:223]
	global_store_dwordx4 v[214:215], v[106:109], off sc0 sc1
	v_pk_fma_f32 v[120:121], v[120:121], v[144:145], v[190:191]
	v_pk_fma_f32 v[118:119], v[118:119], v[142:143], v[226:227]
	v_cvt_pk_bf16_f32 v106, v110, v111
	v_cvt_pk_bf16_f32 v107, v112, v113
	v_cvt_pk_bf16_f32 v108, v184, v185
	v_cvt_pk_bf16_f32 v109, v182, v183
	v_pk_fma_f32 v[116:117], v[116:117], v[140:141], v[192:193]
	v_pk_fma_f32 v[114:115], v[114:115], v[138:139], v[228:229]
	global_store_dwordx4 v[214:215], v[106:109], off offset:256 sc0 sc1
	v_lshlrev_b32_e32 v110, 16, v196
	v_and_b32_e32 v111, 0xffff0000, v196
	v_cvt_pk_bf16_f32 v106, v118, v119
	v_cvt_pk_bf16_f32 v107, v120, v121
	v_cvt_pk_bf16_f32 v108, v114, v115
	v_cvt_pk_bf16_f32 v109, v116, v117
	global_store_dwordx4 v[216:217], v[106:109], off sc0 sc1
	v_lshlrev_b32_e32 v112, 16, v197
	v_and_b32_e32 v113, 0xffff0000, v197
	v_lshlrev_b32_e32 v106, 16, v194
	v_and_b32_e32 v107, 0xffff0000, v194
	v_lshlrev_b32_e32 v108, 16, v195
	v_and_b32_e32 v109, 0xffff0000, v195
	v_pk_fma_f32 v[104:105], v[104:105], v[136:137], v[108:109]
	v_pk_fma_f32 v[102:103], v[102:103], v[134:135], v[106:107]
	v_pk_fma_f32 v[106:107], v[100:101], v[132:133], v[112:113]
	v_pk_fma_f32 v[100:101], v[98:99], v[130:131], v[110:111]
	v_cvt_pk_bf16_f32 v98, v102, v103
	v_cvt_pk_bf16_f32 v99, v104, v105
	v_lshlrev_b32_e32 v102, 16, v200
	v_cvt_pk_bf16_f32 v100, v100, v101
	v_cvt_pk_bf16_f32 v101, v106, v107
	global_store_dwordx4 v[216:217], v[98:101], off offset:256 sc0 sc1
	v_and_b32_e32 v103, 0xffff0000, v200
	v_lshlrev_b32_e32 v104, 16, v201
	v_lshlrev_b32_e32 v98, 16, v198
	v_and_b32_e32 v99, 0xffff0000, v198
	v_and_b32_e32 v105, 0xffff0000, v201
	v_pk_fma_f32 v[94:95], v[94:95], v[142:143], v[98:99]
	v_lshlrev_b32_e32 v100, 16, v199
	v_and_b32_e32 v101, 0xffff0000, v199
	v_pk_fma_f32 v[98:99], v[92:93], v[140:141], v[104:105]
	v_pk_fma_f32 v[92:93], v[90:91], v[138:139], v[102:103]
	v_cvt_pk_bf16_f32 v90, v94, v95
	v_lshl_add_u64 v[94:95], s[6:7], 0, v[170:171]
	v_pk_fma_f32 v[96:97], v[96:97], v[144:145], v[100:101]
	v_lshl_add_u64 v[94:95], v[94:95], 0, v[162:163]
	v_cvt_pk_bf16_f32 v91, v96, v97
	v_cvt_pk_bf16_f32 v92, v92, v93
	v_cvt_pk_bf16_f32 v93, v98, v99
; __device__ __forceinline__ unsigned cvt_pk_bf16(float lo, float hi) { unsigned r; asm volatile("v_cvt_pk_bf16_f32 %0, %1, %2" : "=v"(r) : "v"(lo), "v"(hi)); return r; }
;     __device__ __forceinline__ void operator()(const f32x4 (&acc)[2][2][4][2], const Unit& u, int wr, int wc, int fr, int fq) const {
;     ...
;                     for (int bj = 0; bj < 2; ++bj) bs[m][bj] = *(const u32x4*)(H + (size_t)(row0 + ai * HALF + m * 16) * 2048 + col0 + bj * HALF);
; #pragma unroll
;                 for (int m = 0; m < 4; ++m)
; #pragma unroll
;                     for (int bj = 0; bj < 2; ++bj) { const u32x4 b = bs[m][bj];
;                         f32x4 r0, r1; r0.x = __builtin_bit_cast(float, b.x << 16); r0.y = __builtin_bit_cast(float, b.x & 0xffff0000u); r0.z = __builtin_bit_cast(float, b.y << 16); r0.w = __builtin_bit_cast(float, b.y & 0xffff0000u);
;                         r1.x = __builtin_bit_cast(float, b.z << 16); r1.y = __builtin_bit_cast(float, b.z & 0xffff0000u); r1.z = __builtin_bit_cast(float, b.w << 16); r1.w = __builtin_bit_cast(float, b.w & 0xffff0000u);
;                         r0 += gg[bj][0] * acc[ai][bj][m][0]; r1 += gg[bj][1] * acc[ai][bj][m][1];
;                         u32x4 w; w.x = cvt_pk_bf16(r0[0], r0[1]); w.y = cvt_pk_bf16(r0[2], r0[3]); w.z = cvt_pk_bf16(r1[0], r1[1]); w.w = cvt_pk_bf16(r1[2], r1[3]);
;                         *(u32x4*)(H + (size_t)(row0 + ai * HALF + m * 16) * 2048 + col0 + bj * HALF) = w; }
	global_store_dwordx4 v[94:95], v[90:93], off sc0 sc1
	v_lshlrev_b32_e32 v96, 16, v204
	v_and_b32_e32 v97, 0xffff0000, v204
	v_lshlrev_b32_e32 v90, 16, v202
	v_and_b32_e32 v91, 0xffff0000, v202
	v_lshlrev_b32_e32 v92, 16, v203
	v_and_b32_e32 v93, 0xffff0000, v203
	v_lshlrev_b32_e32 v98, 16, v205
	v_and_b32_e32 v99, 0xffff0000, v205
	v_pk_fma_f32 v[88:89], v[88:89], v[136:137], v[92:93]
	v_pk_fma_f32 v[86:87], v[86:87], v[134:135], v[90:91]
	v_pk_fma_f32 v[90:91], v[84:85], v[132:133], v[98:99]
	v_pk_fma_f32 v[84:85], v[82:83], v[130:131], v[96:97]
	v_cvt_pk_bf16_f32 v82, v86, v87
	v_cvt_pk_bf16_f32 v83, v88, v89
	v_lshlrev_b32_e32 v86, 16, v208
	v_cvt_pk_bf16_f32 v84, v84, v85
	v_cvt_pk_bf16_f32 v85, v90, v91
	global_store_dwordx4 v[94:95], v[82:85], off offset:256 sc0 sc1
	v_and_b32_e32 v87, 0xffff0000, v208
	v_lshlrev_b32_e32 v88, 16, v209
	v_lshlrev_b32_e32 v82, 16, v206
	v_and_b32_e32 v83, 0xffff0000, v206
	v_and_b32_e32 v89, 0xffff0000, v209
	v_pk_fma_f32 v[78:79], v[78:79], v[142:143], v[82:83]
	v_lshlrev_b32_e32 v84, 16, v207
	v_and_b32_e32 v85, 0xffff0000, v207
	v_pk_fma_f32 v[82:83], v[76:77], v[140:141], v[88:89]
	v_pk_fma_f32 v[76:77], v[74:75], v[138:139], v[86:87]
	v_cvt_pk_bf16_f32 v74, v78, v79
	v_lshl_add_u64 v[78:79], s[6:7], 0, v[168:169]
	v_pk_fma_f32 v[80:81], v[80:81], v[144:145], v[84:85]
	v_lshl_add_u64 v[78:79], v[78:79], 0, v[162:163]
	v_cvt_pk_bf16_f32 v75, v80, v81
	v_cvt_pk_bf16_f32 v76, v76, v77
	v_cvt_pk_bf16_f32 v77, v82, v83
	global_store_dwordx4 v[78:79], v[74:77], off sc0 sc1
	v_lshlrev_b32_e32 v80, 16, v212
	v_and_b32_e32 v81, 0xffff0000, v212
	v_lshlrev_b32_e32 v74, 16, v210
	v_and_b32_e32 v75, 0xffff0000, v210
	v_lshlrev_b32_e32 v82, 16, v213
	v_and_b32_e32 v83, 0xffff0000, v213
	v_lshlrev_b32_e32 v76, 16, v211
	v_and_b32_e32 v77, 0xffff0000, v211
	v_pk_fma_f32 v[70:71], v[70:71], v[134:135], v[74:75]
	v_pk_fma_f32 v[74:75], v[68:69], v[132:133], v[82:83]
	v_pk_fma_f32 v[68:69], v[66:67], v[130:131], v[80:81]
	v_pk_fma_f32 v[72:73], v[72:73], v[136:137], v[76:77]
	v_cvt_pk_bf16_f32 v66, v70, v71
	v_lshl_add_u64 v[100:101], v[166:167], 0, s[30:31]
	v_cvt_pk_bf16_f32 v67, v72, v73
	v_cvt_pk_bf16_f32 v68, v68, v69
	v_cvt_pk_bf16_f32 v69, v74, v75
	global_store_dwordx4 v[78:79], v[66:69], off offset:256 sc0 sc1
	v_lshl_add_u64 v[102:103], v[166:167], 0, s[12:13]
	v_lshl_add_u64 v[104:105], v[166:167], 0, s[14:15]
	v_lshl_add_u64 v[66:67], v[164:165], 0, v[100:101]
	global_load_dwordx4 v[76:79], v[66:67], off
	global_load_dwordx4 v[80:83], v[66:67], off offset:256
	v_lshl_add_u64 v[66:67], v[164:165], 0, v[102:103]
	global_load_dwordx4 v[84:87], v[66:67], off
	global_load_dwordx4 v[88:91], v[66:67], off offset:256
	v_lshl_add_u64 v[66:67], v[164:165], 0, v[104:105]
	global_load_dwordx4 v[92:95], v[66:67], off
	global_load_dwordx4 v[96:99], v[66:67], off offset:256
	v_lshl_add_u64 v[74:75], v[166:167], 0, s[16:17]
	v_lshl_add_u64 v[66:67], v[164:165], 0, v[74:75]
	global_load_dwordx4 v[70:73], v[66:67], off
	s_nop 0
	global_load_dwordx4 v[66:69], v[66:67], off offset:256
	s_waitcnt vmcnt(7)
	v_lshlrev_b32_e32 v106, 16, v76
	v_and_b32_e32 v107, 0xffff0000, v76
	v_lshlrev_b32_e32 v76, 16, v77
	v_and_b32_e32 v77, 0xffff0000, v77
	v_lshlrev_b32_e32 v108, 16, v78
	v_and_b32_e32 v109, 0xffff0000, v78
	v_lshlrev_b32_e32 v78, 16, v79
	v_and_b32_e32 v79, 0xffff0000, v79
	v_pk_fma_f32 v[62:63], v[62:63], v[142:143], v[106:107]
	v_pk_fma_f32 v[64:65], v[64:65], v[144:145], v[76:77]
	v_pk_fma_f32 v[76:77], v[60:61], v[140:141], v[78:79]
	v_pk_fma_f32 v[60:61], v[58:59], v[138:139], v[108:109]
	v_cvt_pk_bf16_f32 v58, v62, v63
	v_lshl_add_u64 v[62:63], s[6:7], 0, v[100:101]
	v_cvt_pk_bf16_f32 v59, v64, v65
	v_cvt_pk_bf16_f32 v60, v60, v61
	v_cvt_pk_bf16_f32 v61, v76, v77
	v_lshl_add_u64 v[62:63], v[62:63], 0, v[162:163]
	global_store_dwordx4 v[62:63], v[58:61], off sc0 sc1
	s_waitcnt vmcnt(7)
	v_lshlrev_b32_e32 v64, 16, v82
	v_and_b32_e32 v65, 0xffff0000, v82
	v_lshlrev_b32_e32 v58, 16, v80
	v_and_b32_e32 v59, 0xffff0000, v80
	v_lshlrev_b32_e32 v60, 16, v81
	v_and_b32_e32 v61, 0xffff0000, v81
	v_lshlrev_b32_e32 v76, 16, v83
	v_and_b32_e32 v77, 0xffff0000, v83
	v_pk_fma_f32 v[56:57], v[56:57], v[136:137], v[60:61]
	v_pk_fma_f32 v[54:55], v[54:55], v[134:135], v[58:59]
	v_pk_fma_f32 v[58:59], v[52:53], v[132:133], v[76:77]
	v_pk_fma_f32 v[52:53], v[50:51], v[130:131], v[64:65]
	v_cvt_pk_bf16_f32 v50, v54, v55
	v_cvt_pk_bf16_f32 v51, v56, v57
	s_waitcnt vmcnt(6)
; __device__ __forceinline__ unsigned cvt_pk_bf16(float lo, float hi) { unsigned r; asm volatile("v_cvt_pk_bf16_f32 %0, %1, %2" : "=v"(r) : "v"(lo), "v"(hi)); return r; }
;     __device__ __forceinline__ void operator()(const f32x4 (&acc)[2][2][4][2], const Unit& u, int wr, int wc, int fr, int fq) const {
;     ...
;                     for (int bj = 0; bj < 2; ++bj) bs[m][bj] = *(const u32x4*)(H + (size_t)(row0 + ai * HALF + m * 16) * 2048 + col0 + bj * HALF);
; #pragma unroll
;                 for (int m = 0; m < 4; ++m)
; #pragma unroll
;                     for (int bj = 0; bj < 2; ++bj) { const u32x4 b = bs[m][bj];
;                         f32x4 r0, r1; r0.x = __builtin_bit_cast(float, b.x << 16); r0.y = __builtin_bit_cast(float, b.x & 0xffff0000u); r0.z = __builtin_bit_cast(float, b.y << 16); r0.w = __builtin_bit_cast(float, b.y & 0xffff0000u);
;                         r1.x = __builtin_bit_cast(float, b.z << 16); r1.y = __builtin_bit_cast(float, b.z & 0xffff0000u); r1.z = __builtin_bit_cast(float, b.w << 16); r1.w = __builtin_bit_cast(float, b.w & 0xffff0000u);
;                         r0 += gg[bj][0] * acc[ai][bj][m][0]; r1 += gg[bj][1] * acc[ai][bj][m][1];
;                         u32x4 w; w.x = cvt_pk_bf16(r0[0], r0[1]); w.y = cvt_pk_bf16(r0[2], r0[3]); w.z = cvt_pk_bf16(r1[0], r1[1]); w.w = cvt_pk_bf16(r1[2], r1[3]);
;                         *(u32x4*)(H + (size_t)(row0 + ai * HALF + m * 16) * 2048 + col0 + bj * HALF) = w; }
	v_lshlrev_b32_e32 v54, 16, v86
	v_cvt_pk_bf16_f32 v52, v52, v53
	v_cvt_pk_bf16_f32 v53, v58, v59
	global_store_dwordx4 v[62:63], v[50:53], off offset:256 sc0 sc1
	v_and_b32_e32 v55, 0xffff0000, v86
	v_lshlrev_b32_e32 v56, 16, v87
	v_lshlrev_b32_e32 v50, 16, v84
	v_and_b32_e32 v51, 0xffff0000, v84
	v_and_b32_e32 v57, 0xffff0000, v87
	v_pk_fma_f32 v[46:47], v[46:47], v[142:143], v[50:51]
	v_lshlrev_b32_e32 v52, 16, v85
	v_and_b32_e32 v53, 0xffff0000, v85
	v_pk_fma_f32 v[50:51], v[44:45], v[140:141], v[56:57]
	v_pk_fma_f32 v[44:45], v[42:43], v[138:139], v[54:55]
	v_cvt_pk_bf16_f32 v42, v46, v47
	v_lshl_add_u64 v[46:47], s[6:7], 0, v[102:103]
	v_pk_fma_f32 v[48:49], v[48:49], v[144:145], v[52:53]
	v_lshl_add_u64 v[46:47], v[46:47], 0, v[162:163]
	v_cvt_pk_bf16_f32 v43, v48, v49
	v_cvt_pk_bf16_f32 v44, v44, v45
	v_cvt_pk_bf16_f32 v45, v50, v51
	global_store_dwordx4 v[46:47], v[42:45], off sc0 sc1
	s_waitcnt vmcnt(7)
	v_lshlrev_b32_e32 v48, 16, v90
	v_and_b32_e32 v49, 0xffff0000, v90
	v_lshlrev_b32_e32 v42, 16, v88
	v_and_b32_e32 v43, 0xffff0000, v88
	v_lshlrev_b32_e32 v44, 16, v89
	v_and_b32_e32 v45, 0xffff0000, v89
	v_lshlrev_b32_e32 v50, 16, v91
	v_and_b32_e32 v51, 0xffff0000, v91
	v_pk_fma_f32 v[40:41], v[40:41], v[136:137], v[44:45]
	v_pk_fma_f32 v[38:39], v[38:39], v[134:135], v[42:43]
	v_pk_fma_f32 v[42:43], v[36:37], v[132:133], v[50:51]
	v_pk_fma_f32 v[36:37], v[34:35], v[130:131], v[48:49]
	v_cvt_pk_bf16_f32 v34, v38, v39
	v_cvt_pk_bf16_f32 v35, v40, v41
	s_waitcnt vmcnt(6)
	v_lshlrev_b32_e32 v38, 16, v94
	v_cvt_pk_bf16_f32 v36, v36, v37
	v_cvt_pk_bf16_f32 v37, v42, v43
	global_store_dwordx4 v[46:47], v[34:37], off offset:256 sc0 sc1
	v_and_b32_e32 v39, 0xffff0000, v94
	v_lshlrev_b32_e32 v40, 16, v95
	v_lshlrev_b32_e32 v34, 16, v92
	v_and_b32_e32 v35, 0xffff0000, v92
	v_and_b32_e32 v41, 0xffff0000, v95
	v_pk_fma_f32 v[30:31], v[30:31], v[142:143], v[34:35]
	v_lshlrev_b32_e32 v36, 16, v93
	v_and_b32_e32 v37, 0xffff0000, v93
	v_pk_fma_f32 v[34:35], v[28:29], v[140:141], v[40:41]
	v_pk_fma_f32 v[28:29], v[26:27], v[138:139], v[38:39]
	v_cvt_pk_bf16_f32 v26, v30, v31
	v_lshl_add_u64 v[30:31], s[6:7], 0, v[104:105]
	v_pk_fma_f32 v[32:33], v[32:33], v[144:145], v[36:37]
	v_lshl_add_u64 v[30:31], v[30:31], 0, v[162:163]
	v_cvt_pk_bf16_f32 v27, v32, v33
	v_cvt_pk_bf16_f32 v28, v28, v29
	v_cvt_pk_bf16_f32 v29, v34, v35
	global_store_dwordx4 v[30:31], v[26:29], off sc0 sc1
	s_waitcnt vmcnt(7)
	v_lshlrev_b32_e32 v32, 16, v98
	v_and_b32_e32 v33, 0xffff0000, v98
	v_lshlrev_b32_e32 v26, 16, v96
	v_and_b32_e32 v27, 0xffff0000, v96
	v_lshlrev_b32_e32 v28, 16, v97
	v_and_b32_e32 v29, 0xffff0000, v97
	v_lshlrev_b32_e32 v34, 16, v99
	v_and_b32_e32 v35, 0xffff0000, v99
	v_pk_fma_f32 v[24:25], v[24:25], v[136:137], v[28:29]
	v_pk_fma_f32 v[22:23], v[22:23], v[134:135], v[26:27]
	v_pk_fma_f32 v[26:27], v[20:21], v[132:133], v[34:35]
	v_pk_fma_f32 v[20:21], v[18:19], v[130:131], v[32:33]
	v_cvt_pk_bf16_f32 v18, v22, v23
	v_cvt_pk_bf16_f32 v19, v24, v25
	s_waitcnt vmcnt(6)
	v_lshlrev_b32_e32 v22, 16, v72
	v_cvt_pk_bf16_f32 v20, v20, v21
	v_cvt_pk_bf16_f32 v21, v26, v27
	global_store_dwordx4 v[30:31], v[18:21], off offset:256 sc0 sc1
	v_and_b32_e32 v23, 0xffff0000, v72
	v_lshlrev_b32_e32 v24, 16, v73
	v_lshlrev_b32_e32 v18, 16, v70
	v_and_b32_e32 v19, 0xffff0000, v70
	v_and_b32_e32 v25, 0xffff0000, v73
	v_pk_fma_f32 v[14:15], v[14:15], v[142:143], v[18:19]
	v_lshlrev_b32_e32 v20, 16, v71
	v_and_b32_e32 v21, 0xffff0000, v71
	v_pk_fma_f32 v[18:19], v[12:13], v[140:141], v[24:25]
	v_pk_fma_f32 v[12:13], v[10:11], v[138:139], v[22:23]
	v_cvt_pk_bf16_f32 v10, v14, v15
	v_lshl_add_u64 v[14:15], s[6:7], 0, v[74:75]
	v_pk_fma_f32 v[16:17], v[16:17], v[144:145], v[20:21]
	v_lshl_add_u64 v[14:15], v[14:15], 0, v[162:163]
	v_cvt_pk_bf16_f32 v11, v16, v17
	v_cvt_pk_bf16_f32 v12, v12, v13
	v_cvt_pk_bf16_f32 v13, v18, v19
	global_store_dwordx4 v[14:15], v[10:13], off sc0 sc1
	s_waitcnt vmcnt(7)
	v_lshlrev_b32_e32 v16, 16, v68
	v_and_b32_e32 v17, 0xffff0000, v68
	v_lshlrev_b32_e32 v10, 16, v66
	v_and_b32_e32 v11, 0xffff0000, v66
	v_lshlrev_b32_e32 v18, 16, v69
	v_and_b32_e32 v19, 0xffff0000, v69
	v_lshlrev_b32_e32 v12, 16, v67
	v_and_b32_e32 v13, 0xffff0000, v67
	v_pk_fma_f32 v[6:7], v[6:7], v[134:135], v[10:11]
	v_pk_fma_f32 v[10:11], v[4:5], v[132:133], v[18:19]
	v_pk_fma_f32 v[4:5], v[2:3], v[130:131], v[16:17]
	v_pk_fma_f32 v[8:9], v[8:9], v[136:137], v[12:13]
	v_cvt_pk_bf16_f32 v2, v6, v7
	s_nop 0
	v_cvt_pk_bf16_f32 v3, v8, v9
	v_cvt_pk_bf16_f32 v4, v4, v5
	v_cvt_pk_bf16_f32 v5, v10, v11
	global_store_dwordx4 v[14:15], v[2:5], off offset:256 sc0 sc1
	s_cbranch_vccnz .LBB0_1667
	s_andn2_b64 vcc, exec, s[4:5]
	s_cbranch_vccnz .LBB0_1666
	s_barrier
	s_branch .LBB0_1666

;     __device__ __forceinline__ f2 swi2(f2 G, f2 U, float kexp, float kout) const {
;         const f2 t = G * kexp; f2 e; e.x = __builtin_amdgcn_exp2f(t.x); e.y = __builtin_amdgcn_exp2f(t.y);
;         const f2 d = e + 1.0f; f2 r; r.x = __builtin_amdgcn_rcpf(d.x); r.y = __builtin_amdgcn_rcpf(d.y);
;         f2 h = (G * U) * r * kout; h.x = __builtin_amdgcn_fmed3f(h.x, -448.f, 448.f); h.y = __builtin_amdgcn_fmed3f(h.y, -448.f, 448.f); return h; }
;     __device__ __forceinline__ void operator()(const f32x4 (&acc)[2][2][4][2], const Unit& u, int wr, int wc, int fr, int fq) const {
;         const int row0 = u.pm * BM + wr * 64 + fr, col0 = u.pn * HALF + wc * 32 + 8 * fq;
;         const float kexp = -1.4426950408889634f * ascale, kout = ascale * ascale * scale;
; #pragma unroll
;         for (int ai = 0; ai < 2; ++ai)
; #pragma unroll
;             for (int m = 0; m < 4; ++m) { unsigned char* rowp = O + (size_t)(row0 + ai * HALF + m * 16) * ldc + col0;
;                 const f32x4 g0 = acc[ai][0][m][0], g1 = acc[ai][0][m][1], u0 = acc[ai][1][m][0], u1 = acc[ai][1][m][1];
;                 const f2 a = swi2((f2){g0[0], g0[1]}, (f2){u0[0], u0[1]}, kexp, kout), b = swi2((f2){g0[2], g0[3]}, (f2){u0[2], u0[3]}, kexp, kout);
;                 const f2 c = swi2((f2){g1[0], g1[1]}, (f2){u1[0], u1[1]}, kexp, kout), d = swi2((f2){g1[2], g1[3]}, (f2){u1[2], u1[3]}, kexp, kout);
;                 int p0 = 0, p1 = 0;
;                 p0 = __builtin_amdgcn_cvt_pk_fp8_f32(a.x, a.y, p0, false); p0 = __builtin_amdgcn_cvt_pk_fp8_f32(b.x, b.y, p0, true);
;                 p1 = __builtin_amdgcn_cvt_pk_fp8_f32(c.x, c.y, p1, false); p1 = __builtin_amdgcn_cvt_pk_fp8_f32(d.x, d.y, p1, true);
;                 typedef unsigned u32x2 __attribute__((ext_vector_type(2))); u32x2 w; w.x = (unsigned)p0; w.y = (unsigned)p1; *(u32x2*)rowp = w; }
.LBB0_1948:
	v_pk_mul_f32 v[4:5], v[142:143], s[14:15] op_sel_hi:[1,0]
	v_pk_mul_f32 v[12:13], v[144:145], s[14:15] op_sel_hi:[1,0]
	v_exp_f32_e32 v8, v4
	v_exp_f32_e32 v9, v5
	v_exp_f32_e32 v12, v12
	v_exp_f32_e32 v13, v13
	v_pk_mul_f32 v[16:17], v[142:143], v[138:139]
	v_pk_add_f32 v[8:9], v[8:9], 1.0 op_sel_hi:[1,0]
	v_pk_mul_f32 v[14:15], v[144:145], v[140:141]
	v_rcp_f32_e32 v8, v8
	v_rcp_f32_e32 v9, v9
	v_pk_add_f32 v[12:13], v[12:13], 1.0 op_sel_hi:[1,0]
	v_lshl_add_u32 v6, s63, 8, v1
	v_rcp_f32_e32 v12, v12
	v_rcp_f32_e32 v13, v13
	v_pk_mul_f32 v[8:9], v[8:9], v[16:17]
	v_pk_mul_f32 v[16:17], v[134:135], v[130:131]
	v_pk_mul_f32 v[8:9], v[8:9], s[16:17] op_sel_hi:[1,0]
	v_lshl_or_b32 v2, s28, 7, v169
	v_med3_f32 v7, v8, s60, v173
	v_med3_f32 v138, v9, s60, v173
	v_pk_mul_f32 v[8:9], v[12:13], v[14:15]
	v_pk_mul_f32 v[12:13], v[134:135], s[14:15] op_sel_hi:[1,0]
	v_pk_mul_f32 v[8:9], v[8:9], s[16:17] op_sel_hi:[1,0]
	v_exp_f32_e32 v12, v12
	v_exp_f32_e32 v13, v13
	v_med3_f32 v139, v8, s60, v173
	v_med3_f32 v140, v9, s60, v173
	v_pk_mul_f32 v[14:15], v[136:137], v[132:133]
	v_pk_add_f32 v[8:9], v[12:13], 1.0 op_sel_hi:[1,0]
	v_pk_mul_f32 v[12:13], v[136:137], s[14:15] op_sel_hi:[1,0]
	v_rcp_f32_e32 v8, v8
	v_exp_f32_e32 v12, v12
	v_exp_f32_e32 v13, v13
	v_rcp_f32_e32 v9, v9
	v_mov_b64_e32 v[4:5], s[8:9]
	v_ashrrev_i32_e32 v3, 31, v2
	v_pk_add_f32 v[12:13], v[12:13], 1.0 op_sel_hi:[1,0]
	v_pk_mul_f32 v[8:9], v[8:9], v[16:17]
	v_rcp_f32_e32 v12, v12
	v_rcp_f32_e32 v13, v13
	v_pk_mul_f32 v[8:9], v[8:9], s[16:17] op_sel_hi:[1,0]
	v_mad_i64_i32 v[10:11], s[2:3], v6, s59, v[4:5]
	v_med3_f32 v16, v8, s60, v173
	v_med3_f32 v17, v9, s60, v173
	v_pk_mul_f32 v[8:9], v[12:13], v[14:15]
	v_mov_b32_e32 v12, 0
	v_mov_b32_e32 v13, 0
	v_cvt_pk_fp8_f32 v12, v7, v138
	v_cvt_pk_fp8_f32 v13, v16, v17
	v_pk_mul_f32 v[8:9], v[8:9], s[16:17] op_sel_hi:[1,0]
	v_lshl_add_u64 v[10:11], v[10:11], 0, v[2:3]
	v_med3_f32 v7, v8, s60, v173
	v_med3_f32 v8, v9, s60, v173
	v_cvt_pk_fp8_f32 v12, v139, v140 op_sel:[0,0,1]
	v_cvt_pk_fp8_f32 v13, v7, v8 op_sel:[0,0,1]
	v_pk_mul_f32 v[8:9], v[126:127], s[14:15] op_sel_hi:[1,0]
	s_nop 15
	s_nop 15
	v_pk_mul_f32 v[14:15], v[126:127], v[122:123]
	v_exp_f32_e32 v8, v8
	v_exp_f32_e32 v9, v9
	global_store_dwordx2 v[10:11], v[12:13], off sc0 sc1
	v_pk_mul_f32 v[10:11], v[128:129], s[14:15] op_sel_hi:[1,0]
	v_pk_mul_f32 v[12:13], v[128:129], v[124:125]
	v_exp_f32_e32 v10, v10
	v_exp_f32_e32 v11, v11
	v_pk_add_f32 v[8:9], v[8:9], 1.0 op_sel_hi:[1,0]
	v_or_b32_e32 v7, 16, v6
	v_rcp_f32_e32 v8, v8
	v_rcp_f32_e32 v9, v9
	v_pk_add_f32 v[10:11], v[10:11], 1.0 op_sel_hi:[1,0]
	s_and_b64 vcc, exec, s[0:1]
	v_rcp_f32_e32 v10, v10
	v_rcp_f32_e32 v11, v11
	v_pk_mul_f32 v[8:9], v[8:9], v[14:15]
	v_pk_mul_f32 v[14:15], v[118:119], v[114:115]
	v_pk_mul_f32 v[8:9], v[8:9], s[16:17] op_sel_hi:[1,0]
	s_mov_b64 s[0:1], -1
	v_med3_f32 v16, v8, s60, v173
	v_med3_f32 v17, v9, s60, v173
	v_pk_mul_f32 v[8:9], v[10:11], v[12:13]
	v_pk_mul_f32 v[10:11], v[118:119], s[14:15] op_sel_hi:[1,0]
	v_pk_mul_f32 v[8:9], v[8:9], s[16:17] op_sel_hi:[1,0]
	v_exp_f32_e32 v10, v10
	v_exp_f32_e32 v11, v11
	v_med3_f32 v122, v8, s60, v173
	v_med3_f32 v123, v9, s60, v173
	v_pk_mul_f32 v[12:13], v[120:121], v[116:117]
	v_pk_add_f32 v[8:9], v[10:11], 1.0 op_sel_hi:[1,0]
	v_pk_mul_f32 v[10:11], v[120:121], s[14:15] op_sel_hi:[1,0]
	v_rcp_f32_e32 v8, v8
	v_exp_f32_e32 v10, v10
	v_exp_f32_e32 v11, v11
	v_rcp_f32_e32 v9, v9
	v_pk_add_f32 v[10:11], v[10:11], 1.0 op_sel_hi:[1,0]
	s_nop 0
	v_rcp_f32_e32 v10, v10
	v_rcp_f32_e32 v11, v11
	v_pk_mul_f32 v[8:9], v[8:9], v[14:15]
	s_nop 0
	v_pk_mul_f32 v[8:9], v[8:9], s[16:17] op_sel_hi:[1,0]
	s_nop 0
	v_med3_f32 v14, v8, s60, v173
	v_med3_f32 v15, v9, s60, v173
	v_pk_mul_f32 v[8:9], v[10:11], v[12:13]
	v_mov_b32_e32 v10, 0
	v_mov_b32_e32 v11, 0
	v_cvt_pk_fp8_f32 v10, v16, v17
	v_cvt_pk_fp8_f32 v11, v14, v15
	v_pk_mul_f32 v[8:9], v[8:9], s[16:17] op_sel_hi:[1,0]
	v_pk_mul_f32 v[12:13], v[112:113], s[14:15] op_sel_hi:[1,0]
	v_med3_f32 v8, v8, s60, v173
	v_med3_f32 v9, v9, s60, v173
	v_cvt_pk_fp8_f32 v10, v122, v123 op_sel:[0,0,1]
	v_cvt_pk_fp8_f32 v11, v8, v9 op_sel:[0,0,1]
	v_mad_i64_i32 v[8:9], s[2:3], v7, s59, v[4:5]
	v_lshl_add_u64 v[8:9], v[8:9], 0, v[2:3]
	global_store_dwordx2 v[8:9], v[10:11], off sc0 sc1
	v_pk_mul_f32 v[8:9], v[110:111], s[14:15] op_sel_hi:[1,0]
	v_exp_f32_e32 v12, v12
	v_exp_f32_e32 v8, v8
	v_exp_f32_e32 v9, v9
	v_exp_f32_e32 v13, v13
	v_pk_mul_f32 v[16:17], v[110:111], v[106:107]
	v_or_b32_e32 v7, 32, v6
	v_pk_add_f32 v[8:9], v[8:9], 1.0 op_sel_hi:[1,0]
	v_pk_add_f32 v[12:13], v[12:13], 1.0 op_sel_hi:[1,0]
	v_rcp_f32_e32 v8, v8
	v_rcp_f32_e32 v9, v9
	v_rcp_f32_e32 v12, v12
	v_rcp_f32_e32 v13, v13
	v_pk_mul_f32 v[14:15], v[112:113], v[108:109]
	v_pk_mul_f32 v[8:9], v[8:9], v[16:17]
	v_mad_i64_i32 v[10:11], s[2:3], v7, s59, v[4:5]
	v_pk_mul_f32 v[8:9], v[8:9], s[16:17] op_sel_hi:[1,0]
	v_pk_mul_f32 v[16:17], v[102:103], v[98:99]
	v_med3_f32 v7, v8, s60, v173
	v_med3_f32 v106, v9, s60, v173
	v_pk_mul_f32 v[8:9], v[12:13], v[14:15]
	v_pk_mul_f32 v[12:13], v[102:103], s[14:15] op_sel_hi:[1,0]
	v_pk_mul_f32 v[8:9], v[8:9], s[16:17] op_sel_hi:[1,0]
	v_exp_f32_e32 v12, v12
	v_exp_f32_e32 v13, v13
	v_med3_f32 v107, v8, s60, v173
	v_med3_f32 v108, v9, s60, v173
	v_pk_mul_f32 v[14:15], v[104:105], v[100:101]
	v_pk_add_f32 v[8:9], v[12:13], 1.0 op_sel_hi:[1,0]
	v_pk_mul_f32 v[12:13], v[104:105], s[14:15] op_sel_hi:[1,0]
	v_rcp_f32_e32 v8, v8
	v_exp_f32_e32 v12, v12
	v_exp_f32_e32 v13, v13
	v_rcp_f32_e32 v9, v9
	v_lshl_add_u64 v[10:11], v[10:11], 0, v[2:3]
	v_pk_add_f32 v[12:13], v[12:13], 1.0 op_sel_hi:[1,0]
	s_nop 0
;     __device__ __forceinline__ f2 swi2(f2 G, f2 U, float kexp, float kout) const {
;         const f2 t = G * kexp; f2 e; e.x = __builtin_amdgcn_exp2f(t.x); e.y = __builtin_amdgcn_exp2f(t.y);
;         const f2 d = e + 1.0f; f2 r; r.x = __builtin_amdgcn_rcpf(d.x); r.y = __builtin_amdgcn_rcpf(d.y);
;         f2 h = (G * U) * r * kout; h.x = __builtin_amdgcn_fmed3f(h.x, -448.f, 448.f); h.y = __builtin_amdgcn_fmed3f(h.y, -448.f, 448.f); return h; }
;     __device__ __forceinline__ void operator()(const f32x4 (&acc)[2][2][4][2], const Unit& u, int wr, int wc, int fr, int fq) const {
;         const int row0 = u.pm * BM + wr * 64 + fr, col0 = u.pn * HALF + wc * 32 + 8 * fq;
;         const float kexp = -1.4426950408889634f * ascale, kout = ascale * ascale * scale;
; #pragma unroll
;         for (int ai = 0; ai < 2; ++ai)
; #pragma unroll
;             for (int m = 0; m < 4; ++m) { unsigned char* rowp = O + (size_t)(row0 + ai * HALF + m * 16) * ldc + col0;
;                 const f32x4 g0 = acc[ai][0][m][0], g1 = acc[ai][0][m][1], u0 = acc[ai][1][m][0], u1 = acc[ai][1][m][1];
;                 const f2 a = swi2((f2){g0[0], g0[1]}, (f2){u0[0], u0[1]}, kexp, kout), b = swi2((f2){g0[2], g0[3]}, (f2){u0[2], u0[3]}, kexp, kout);
;                 const f2 c = swi2((f2){g1[0], g1[1]}, (f2){u1[0], u1[1]}, kexp, kout), d = swi2((f2){g1[2], g1[3]}, (f2){u1[2], u1[3]}, kexp, kout);
;                 int p0 = 0, p1 = 0;
;                 p0 = __builtin_amdgcn_cvt_pk_fp8_f32(a.x, a.y, p0, false); p0 = __builtin_amdgcn_cvt_pk_fp8_f32(b.x, b.y, p0, true);
;                 p1 = __builtin_amdgcn_cvt_pk_fp8_f32(c.x, c.y, p1, false); p1 = __builtin_amdgcn_cvt_pk_fp8_f32(d.x, d.y, p1, true);
;                 typedef unsigned u32x2 __attribute__((ext_vector_type(2))); u32x2 w; w.x = (unsigned)p0; w.y = (unsigned)p1; *(u32x2*)rowp = w; }
	v_rcp_f32_e32 v12, v12
	v_rcp_f32_e32 v13, v13
	v_pk_mul_f32 v[8:9], v[8:9], v[16:17]
	s_nop 0
	v_pk_mul_f32 v[8:9], v[8:9], s[16:17] op_sel_hi:[1,0]
	s_nop 0
	v_med3_f32 v16, v8, s60, v173
	v_med3_f32 v17, v9, s60, v173
	v_pk_mul_f32 v[8:9], v[12:13], v[14:15]
	v_mov_b32_e32 v12, 0
	v_mov_b32_e32 v13, 0
	v_cvt_pk_fp8_f32 v12, v7, v106
	v_cvt_pk_fp8_f32 v13, v16, v17
	v_pk_mul_f32 v[8:9], v[8:9], s[16:17] op_sel_hi:[1,0]
	v_pk_mul_f32 v[14:15], v[94:95], v[90:91]
	v_med3_f32 v7, v8, s60, v173
	v_med3_f32 v8, v9, s60, v173
	v_cvt_pk_fp8_f32 v12, v107, v108 op_sel:[0,0,1]
	v_cvt_pk_fp8_f32 v13, v7, v8 op_sel:[0,0,1]
	v_pk_mul_f32 v[8:9], v[94:95], s[14:15] op_sel_hi:[1,0]
	v_or_b32_e32 v7, 48, v6
	v_exp_f32_e32 v8, v8
	v_exp_f32_e32 v9, v9
	global_store_dwordx2 v[10:11], v[12:13], off sc0 sc1
	v_pk_mul_f32 v[10:11], v[96:97], s[14:15] op_sel_hi:[1,0]
	v_pk_mul_f32 v[12:13], v[96:97], v[92:93]
	v_exp_f32_e32 v10, v10
	v_exp_f32_e32 v11, v11
	v_pk_add_f32 v[8:9], v[8:9], 1.0 op_sel_hi:[1,0]
	v_pk_add_f32 v[10:11], v[10:11], 1.0 op_sel_hi:[1,0]
	v_rcp_f32_e32 v8, v8
	v_rcp_f32_e32 v9, v9
	v_rcp_f32_e32 v10, v10
	v_rcp_f32_e32 v11, v11
	v_pk_mul_f32 v[8:9], v[8:9], v[14:15]
	s_nop 0
	v_pk_mul_f32 v[8:9], v[8:9], s[16:17] op_sel_hi:[1,0]
	v_pk_mul_f32 v[14:15], v[86:87], v[82:83]
	v_med3_f32 v16, v8, s60, v173
	v_med3_f32 v17, v9, s60, v173
	v_pk_mul_f32 v[8:9], v[10:11], v[12:13]
	v_pk_mul_f32 v[10:11], v[86:87], s[14:15] op_sel_hi:[1,0]
	v_pk_mul_f32 v[8:9], v[8:9], s[16:17] op_sel_hi:[1,0]
	v_exp_f32_e32 v10, v10
	v_exp_f32_e32 v11, v11
	v_med3_f32 v90, v8, s60, v173
	v_med3_f32 v91, v9, s60, v173
	v_pk_mul_f32 v[12:13], v[88:89], v[84:85]
	v_pk_add_f32 v[8:9], v[10:11], 1.0 op_sel_hi:[1,0]
	v_pk_mul_f32 v[10:11], v[88:89], s[14:15] op_sel_hi:[1,0]
	v_rcp_f32_e32 v8, v8
	v_exp_f32_e32 v10, v10
	v_exp_f32_e32 v11, v11
	v_rcp_f32_e32 v9, v9
	v_pk_add_f32 v[10:11], v[10:11], 1.0 op_sel_hi:[1,0]
	s_nop 0
	v_rcp_f32_e32 v10, v10
	v_rcp_f32_e32 v11, v11
	v_pk_mul_f32 v[8:9], v[8:9], v[14:15]
	s_nop 0
	v_pk_mul_f32 v[8:9], v[8:9], s[16:17] op_sel_hi:[1,0]
	s_nop 0
	v_med3_f32 v14, v8, s60, v173
	v_med3_f32 v15, v9, s60, v173
	v_pk_mul_f32 v[8:9], v[10:11], v[12:13]
	v_mov_b32_e32 v10, 0
	v_mov_b32_e32 v11, 0
	v_cvt_pk_fp8_f32 v10, v16, v17
	v_cvt_pk_fp8_f32 v11, v14, v15
	v_pk_mul_f32 v[8:9], v[8:9], s[16:17] op_sel_hi:[1,0]
	v_pk_mul_f32 v[12:13], v[80:81], s[14:15] op_sel_hi:[1,0]
	v_med3_f32 v8, v8, s60, v173
	v_med3_f32 v9, v9, s60, v173
	v_cvt_pk_fp8_f32 v10, v90, v91 op_sel:[0,0,1]
	v_cvt_pk_fp8_f32 v11, v8, v9 op_sel:[0,0,1]
	v_mad_i64_i32 v[8:9], s[2:3], v7, s59, v[4:5]
	v_lshl_add_u64 v[8:9], v[8:9], 0, v[2:3]
	global_store_dwordx2 v[8:9], v[10:11], off sc0 sc1
	v_pk_mul_f32 v[8:9], v[78:79], s[14:15] op_sel_hi:[1,0]
	v_exp_f32_e32 v12, v12
	v_exp_f32_e32 v8, v8
	v_exp_f32_e32 v9, v9
	v_exp_f32_e32 v13, v13
	v_pk_mul_f32 v[16:17], v[78:79], v[74:75]
	v_add_u32_e32 v7, 0x80, v6
	v_pk_add_f32 v[8:9], v[8:9], 1.0 op_sel_hi:[1,0]
	v_pk_add_f32 v[12:13], v[12:13], 1.0 op_sel_hi:[1,0]
	v_rcp_f32_e32 v8, v8
	v_rcp_f32_e32 v9, v9
	v_rcp_f32_e32 v12, v12
	v_rcp_f32_e32 v13, v13
	v_pk_mul_f32 v[14:15], v[80:81], v[76:77]
	v_pk_mul_f32 v[8:9], v[8:9], v[16:17]
	v_mad_i64_i32 v[10:11], s[2:3], v7, s59, v[4:5]
	v_pk_mul_f32 v[8:9], v[8:9], s[16:17] op_sel_hi:[1,0]
	v_pk_mul_f32 v[16:17], v[70:71], v[66:67]
	v_med3_f32 v7, v8, s60, v173
	v_med3_f32 v74, v9, s60, v173
	v_pk_mul_f32 v[8:9], v[12:13], v[14:15]
	v_pk_mul_f32 v[12:13], v[70:71], s[14:15] op_sel_hi:[1,0]
	v_pk_mul_f32 v[8:9], v[8:9], s[16:17] op_sel_hi:[1,0]
	v_exp_f32_e32 v12, v12
	v_exp_f32_e32 v13, v13
	v_med3_f32 v75, v8, s60, v173
	v_med3_f32 v76, v9, s60, v173
	v_pk_mul_f32 v[14:15], v[72:73], v[68:69]
	v_pk_add_f32 v[8:9], v[12:13], 1.0 op_sel_hi:[1,0]
	v_pk_mul_f32 v[12:13], v[72:73], s[14:15] op_sel_hi:[1,0]
	v_rcp_f32_e32 v8, v8
	v_exp_f32_e32 v12, v12
	v_exp_f32_e32 v13, v13
	v_rcp_f32_e32 v9, v9
	v_lshl_add_u64 v[10:11], v[10:11], 0, v[2:3]
	v_pk_add_f32 v[12:13], v[12:13], 1.0 op_sel_hi:[1,0]
	s_nop 0
	v_rcp_f32_e32 v12, v12
	v_rcp_f32_e32 v13, v13
	v_pk_mul_f32 v[8:9], v[8:9], v[16:17]
	s_nop 0
	v_pk_mul_f32 v[8:9], v[8:9], s[16:17] op_sel_hi:[1,0]
	s_nop 0
	v_med3_f32 v16, v8, s60, v173
	v_med3_f32 v17, v9, s60, v173
	v_pk_mul_f32 v[8:9], v[12:13], v[14:15]
	v_mov_b32_e32 v12, 0
	v_mov_b32_e32 v13, 0
	v_cvt_pk_fp8_f32 v12, v7, v74
	v_cvt_pk_fp8_f32 v13, v16, v17
	v_pk_mul_f32 v[8:9], v[8:9], s[16:17] op_sel_hi:[1,0]
	v_pk_mul_f32 v[14:15], v[62:63], v[58:59]
	v_med3_f32 v7, v8, s60, v173
	v_med3_f32 v8, v9, s60, v173
	v_cvt_pk_fp8_f32 v12, v75, v76 op_sel:[0,0,1]
	v_cvt_pk_fp8_f32 v13, v7, v8 op_sel:[0,0,1]
	v_pk_mul_f32 v[8:9], v[62:63], s[14:15] op_sel_hi:[1,0]
	v_add_u32_e32 v7, 0x90, v6
	v_exp_f32_e32 v8, v8
	v_exp_f32_e32 v9, v9
	global_store_dwordx2 v[10:11], v[12:13], off sc0 sc1
	v_pk_mul_f32 v[10:11], v[64:65], s[14:15] op_sel_hi:[1,0]
	v_pk_mul_f32 v[12:13], v[64:65], v[60:61]
	v_exp_f32_e32 v10, v10
	v_exp_f32_e32 v11, v11
	v_pk_add_f32 v[8:9], v[8:9], 1.0 op_sel_hi:[1,0]
	v_pk_add_f32 v[10:11], v[10:11], 1.0 op_sel_hi:[1,0]
	v_rcp_f32_e32 v8, v8
	v_rcp_f32_e32 v9, v9
	v_rcp_f32_e32 v10, v10
	v_rcp_f32_e32 v11, v11
	v_pk_mul_f32 v[8:9], v[8:9], v[14:15]
	s_nop 0
	v_pk_mul_f32 v[8:9], v[8:9], s[16:17] op_sel_hi:[1,0]
	v_pk_mul_f32 v[14:15], v[54:55], v[50:51]
	v_med3_f32 v16, v8, s60, v173
	v_med3_f32 v17, v9, s60, v173
;     __device__ __forceinline__ f2 swi2(f2 G, f2 U, float kexp, float kout) const {
;         const f2 t = G * kexp; f2 e; e.x = __builtin_amdgcn_exp2f(t.x); e.y = __builtin_amdgcn_exp2f(t.y);
;         const f2 d = e + 1.0f; f2 r; r.x = __builtin_amdgcn_rcpf(d.x); r.y = __builtin_amdgcn_rcpf(d.y);
;         f2 h = (G * U) * r * kout; h.x = __builtin_amdgcn_fmed3f(h.x, -448.f, 448.f); h.y = __builtin_amdgcn_fmed3f(h.y, -448.f, 448.f); return h; }
;     __device__ __forceinline__ void operator()(const f32x4 (&acc)[2][2][4][2], const Unit& u, int wr, int wc, int fr, int fq) const {
;         const int row0 = u.pm * BM + wr * 64 + fr, col0 = u.pn * HALF + wc * 32 + 8 * fq;
;         const float kexp = -1.4426950408889634f * ascale, kout = ascale * ascale * scale;
; #pragma unroll
;         for (int ai = 0; ai < 2; ++ai)
; #pragma unroll
;             for (int m = 0; m < 4; ++m) { unsigned char* rowp = O + (size_t)(row0 + ai * HALF + m * 16) * ldc + col0;
;                 const f32x4 g0 = acc[ai][0][m][0], g1 = acc[ai][0][m][1], u0 = acc[ai][1][m][0], u1 = acc[ai][1][m][1];
;                 const f2 a = swi2((f2){g0[0], g0[1]}, (f2){u0[0], u0[1]}, kexp, kout), b = swi2((f2){g0[2], g0[3]}, (f2){u0[2], u0[3]}, kexp, kout);
;                 const f2 c = swi2((f2){g1[0], g1[1]}, (f2){u1[0], u1[1]}, kexp, kout), d = swi2((f2){g1[2], g1[3]}, (f2){u1[2], u1[3]}, kexp, kout);
;                 int p0 = 0, p1 = 0;
;                 p0 = __builtin_amdgcn_cvt_pk_fp8_f32(a.x, a.y, p0, false); p0 = __builtin_amdgcn_cvt_pk_fp8_f32(b.x, b.y, p0, true);
;                 p1 = __builtin_amdgcn_cvt_pk_fp8_f32(c.x, c.y, p1, false); p1 = __builtin_amdgcn_cvt_pk_fp8_f32(d.x, d.y, p1, true);
;                 typedef unsigned u32x2 __attribute__((ext_vector_type(2))); u32x2 w; w.x = (unsigned)p0; w.y = (unsigned)p1; *(u32x2*)rowp = w; }
	v_pk_mul_f32 v[8:9], v[10:11], v[12:13]
	v_pk_mul_f32 v[10:11], v[54:55], s[14:15] op_sel_hi:[1,0]
	v_pk_mul_f32 v[8:9], v[8:9], s[16:17] op_sel_hi:[1,0]
	v_exp_f32_e32 v10, v10
	v_exp_f32_e32 v11, v11
	v_med3_f32 v58, v8, s60, v173
	v_med3_f32 v59, v9, s60, v173
	v_pk_mul_f32 v[12:13], v[56:57], v[52:53]
	v_pk_add_f32 v[8:9], v[10:11], 1.0 op_sel_hi:[1,0]
	v_pk_mul_f32 v[10:11], v[56:57], s[14:15] op_sel_hi:[1,0]
	v_rcp_f32_e32 v8, v8
	v_exp_f32_e32 v10, v10
	v_exp_f32_e32 v11, v11
	v_rcp_f32_e32 v9, v9
	v_pk_add_f32 v[10:11], v[10:11], 1.0 op_sel_hi:[1,0]
	s_nop 0
	v_rcp_f32_e32 v10, v10
	v_rcp_f32_e32 v11, v11
	v_pk_mul_f32 v[8:9], v[8:9], v[14:15]
	s_nop 0
	v_pk_mul_f32 v[8:9], v[8:9], s[16:17] op_sel_hi:[1,0]
	s_nop 0
	v_med3_f32 v14, v8, s60, v173
	v_med3_f32 v15, v9, s60, v173
	v_pk_mul_f32 v[8:9], v[10:11], v[12:13]
	v_mov_b32_e32 v10, 0
	v_mov_b32_e32 v11, 0
	v_cvt_pk_fp8_f32 v10, v16, v17
	v_cvt_pk_fp8_f32 v11, v14, v15
	v_pk_mul_f32 v[8:9], v[8:9], s[16:17] op_sel_hi:[1,0]
	v_pk_mul_f32 v[12:13], v[48:49], s[14:15] op_sel_hi:[1,0]
	v_med3_f32 v8, v8, s60, v173
	v_med3_f32 v9, v9, s60, v173
	v_cvt_pk_fp8_f32 v10, v58, v59 op_sel:[0,0,1]
	v_cvt_pk_fp8_f32 v11, v8, v9 op_sel:[0,0,1]
	v_mad_i64_i32 v[8:9], s[2:3], v7, s59, v[4:5]
	v_lshl_add_u64 v[8:9], v[8:9], 0, v[2:3]
	global_store_dwordx2 v[8:9], v[10:11], off sc0 sc1
	v_pk_mul_f32 v[8:9], v[46:47], s[14:15] op_sel_hi:[1,0]
	v_exp_f32_e32 v12, v12
	v_exp_f32_e32 v8, v8
	v_exp_f32_e32 v9, v9
	v_exp_f32_e32 v13, v13
	v_pk_mul_f32 v[16:17], v[46:47], v[42:43]
	v_add_u32_e32 v7, 0xa0, v6
	v_pk_add_f32 v[8:9], v[8:9], 1.0 op_sel_hi:[1,0]
	v_pk_add_f32 v[12:13], v[12:13], 1.0 op_sel_hi:[1,0]
	v_rcp_f32_e32 v8, v8
	v_rcp_f32_e32 v9, v9
	v_rcp_f32_e32 v12, v12
	v_rcp_f32_e32 v13, v13
	v_pk_mul_f32 v[14:15], v[48:49], v[44:45]
	v_pk_mul_f32 v[8:9], v[8:9], v[16:17]
	v_mad_i64_i32 v[10:11], s[2:3], v7, s59, v[4:5]
	v_pk_mul_f32 v[8:9], v[8:9], s[16:17] op_sel_hi:[1,0]
	v_pk_mul_f32 v[16:17], v[38:39], v[34:35]
	v_med3_f32 v7, v8, s60, v173
	v_med3_f32 v42, v9, s60, v173
	v_pk_mul_f32 v[8:9], v[12:13], v[14:15]
	v_pk_mul_f32 v[12:13], v[38:39], s[14:15] op_sel_hi:[1,0]
	v_pk_mul_f32 v[8:9], v[8:9], s[16:17] op_sel_hi:[1,0]
	v_exp_f32_e32 v12, v12
	v_exp_f32_e32 v13, v13
	v_med3_f32 v43, v8, s60, v173
	v_med3_f32 v44, v9, s60, v173
	v_pk_mul_f32 v[14:15], v[40:41], v[36:37]
	v_pk_add_f32 v[8:9], v[12:13], 1.0 op_sel_hi:[1,0]
	v_pk_mul_f32 v[12:13], v[40:41], s[14:15] op_sel_hi:[1,0]
	v_rcp_f32_e32 v8, v8
	v_exp_f32_e32 v12, v12
	v_exp_f32_e32 v13, v13
	v_rcp_f32_e32 v9, v9
	v_lshl_add_u64 v[10:11], v[10:11], 0, v[2:3]
	v_pk_add_f32 v[12:13], v[12:13], 1.0 op_sel_hi:[1,0]
	s_nop 0
	v_rcp_f32_e32 v12, v12
	v_rcp_f32_e32 v13, v13
	v_pk_mul_f32 v[8:9], v[8:9], v[16:17]
	s_nop 0
	v_pk_mul_f32 v[8:9], v[8:9], s[16:17] op_sel_hi:[1,0]
	s_nop 0
	v_med3_f32 v16, v8, s60, v173
	v_med3_f32 v17, v9, s60, v173
	v_pk_mul_f32 v[8:9], v[12:13], v[14:15]
	v_mov_b32_e32 v13, 0
	v_cvt_pk_fp8_f32 v13, v16, v17
	v_pk_mul_f32 v[8:9], v[8:9], s[16:17] op_sel_hi:[1,0]
	v_mov_b32_e32 v12, 0
	v_cvt_pk_fp8_f32 v12, v7, v42
	v_med3_f32 v7, v8, s60, v173
	v_med3_f32 v8, v9, s60, v173
	v_cvt_pk_fp8_f32 v13, v7, v8 op_sel:[0,0,1]
	v_pk_mul_f32 v[8:9], v[30:31], s[14:15] op_sel_hi:[1,0]
	v_add_u32_e32 v14, 0xb0, v6
	v_exp_f32_e32 v8, v8
	v_exp_f32_e32 v9, v9
	v_cvt_pk_fp8_f32 v12, v43, v44 op_sel:[0,0,1]
	v_mad_i64_i32 v[4:5], s[2:3], v14, s59, v[4:5]
	v_pk_add_f32 v[6:7], v[8:9], 1.0 op_sel_hi:[1,0]
	v_pk_mul_f32 v[8:9], v[32:33], s[14:15] op_sel_hi:[1,0]
	v_rcp_f32_e32 v6, v6
	v_exp_f32_e32 v8, v8
	v_exp_f32_e32 v9, v9
	v_rcp_f32_e32 v7, v7
	global_store_dwordx2 v[10:11], v[12:13], off sc0 sc1
	v_pk_mul_f32 v[12:13], v[30:31], v[26:27]
	v_pk_add_f32 v[8:9], v[8:9], 1.0 op_sel_hi:[1,0]
	v_pk_mul_f32 v[6:7], v[6:7], v[12:13]
	v_rcp_f32_e32 v8, v8
	v_rcp_f32_e32 v9, v9
	v_pk_mul_f32 v[10:11], v[32:33], v[28:29]
	v_pk_mul_f32 v[6:7], v[6:7], s[16:17] op_sel_hi:[1,0]
	v_pk_mul_f32 v[12:13], v[22:23], v[18:19]
	v_med3_f32 v15, v6, s60, v173
	v_med3_f32 v16, v7, s60, v173
	v_pk_mul_f32 v[6:7], v[8:9], v[10:11]
	v_pk_mul_f32 v[8:9], v[22:23], s[14:15] op_sel_hi:[1,0]
	v_pk_mul_f32 v[6:7], v[6:7], s[16:17] op_sel_hi:[1,0]
	v_exp_f32_e32 v8, v8
	v_exp_f32_e32 v9, v9
	v_med3_f32 v17, v6, s60, v173
	v_med3_f32 v26, v7, s60, v173
	v_pk_mul_f32 v[10:11], v[24:25], v[20:21]
	v_pk_add_f32 v[6:7], v[8:9], 1.0 op_sel_hi:[1,0]
	v_pk_mul_f32 v[8:9], v[24:25], s[14:15] op_sel_hi:[1,0]
	v_rcp_f32_e32 v6, v6
	v_exp_f32_e32 v8, v8
	v_exp_f32_e32 v9, v9
	v_rcp_f32_e32 v7, v7
	v_lshl_add_u64 v[2:3], v[4:5], 0, v[2:3]
	v_pk_add_f32 v[8:9], v[8:9], 1.0 op_sel_hi:[1,0]
	s_nop 0
	v_rcp_f32_e32 v8, v8
	v_rcp_f32_e32 v9, v9
	v_pk_mul_f32 v[6:7], v[6:7], v[12:13]
	s_nop 0
	v_pk_mul_f32 v[6:7], v[6:7], s[16:17] op_sel_hi:[1,0]
	s_nop 0
	v_med3_f32 v12, v6, s60, v173
	v_med3_f32 v13, v7, s60, v173
	v_pk_mul_f32 v[6:7], v[8:9], v[10:11]
	v_mov_b32_e32 v8, 0
	v_mov_b32_e32 v9, 0
	v_cvt_pk_fp8_f32 v8, v15, v16
	v_cvt_pk_fp8_f32 v9, v12, v13
	v_pk_mul_f32 v[6:7], v[6:7], s[16:17] op_sel_hi:[1,0]
	v_cvt_pk_fp8_f32 v8, v17, v26 op_sel:[0,0,1]
	v_med3_f32 v6, v6, s60, v173
	v_med3_f32 v7, v7, s60, v173
	v_cvt_pk_fp8_f32 v9, v6, v7 op_sel:[0,0,1]
	global_store_dwordx2 v[2:3], v[8:9], off sc0 sc1
	s_cbranch_vccnz .LBB0_1935
	s_andn2_b64 vcc, exec, s[6:7]
	s_cbranch_vccnz .LBB0_1934
	s_barrier
	s_branch .LBB0_1934

; __device__ __forceinline__ unsigned cvt_pk_bf16(float lo, float hi) { unsigned r; asm volatile("v_cvt_pk_bf16_f32 %0, %1, %2" : "=v"(r) : "v"(lo), "v"(hi)); return r; }
; __device__ __forceinline__ float gelu_tanh(float x) { const float y = x + 0.044715f * x * x * x; return x * __builtin_amdgcn_rcpf(1.0f + __builtin_amdgcn_exp2f(-2.302208198f * y)); }
;     __device__ __forceinline__ void operator()(const f32x4 (&acc)[2][2][4][2], const Unit& u, int wr, int wc, int fr, int fq) const {
;         const int row0 = u.pm * BM + wr * 64 + fr, col0 = u.pn * BM + wc * 32 + 8 * fq; const bool act = u.pn < nact;
; #pragma unroll
;         for (int ai = 0; ai < 2; ++ai)
; #pragma unroll
;             for (int m = 0; m < 4; ++m) { bf16_t* rowp = O + (size_t)u.ks * ks_stride + (size_t)(row0 + ai * HALF + m * 16) * ldc + col0;
; #pragma unroll
;                 for (int bj = 0; bj < 2; ++bj) { f32x4 v0 = acc[ai][bj][m][0] * ascale, v1 = acc[ai][bj][m][1] * ascale;
;                     if (act) {
; #pragma unroll
;                         for (int j = 0; j < 4; ++j) { v0[j] = gelu_tanh(v0[j]); v1[j] = gelu_tanh(v1[j]); } }
;                     u32x4 w; w.x = cvt_pk_bf16(v0[0], v0[1]); w.y = cvt_pk_bf16(v0[2], v0[3]); w.z = cvt_pk_bf16(v1[0], v1[1]); w.w = cvt_pk_bf16(v1[2], v1[3]);
;                     *(u32x4*)(rowp + bj * HALF) = w; } }
.LBB0_2036:
	v_lshl_add_u32 v4, s73, 8, v1
	v_ashrrev_i32_e32 v5, 31, v4
	v_lshl_or_b32 v2, s74, 8, v192
	v_lshlrev_b64 v[6:7], 12, v[4:5]
	v_ashrrev_i32_e32 v3, 31, v2
	v_lshl_add_u64 v[6:7], s[16:17], 0, v[6:7]
	v_lshl_add_u64 v[6:7], v[2:3], 1, v[6:7]
	v_cvt_pk_bf16_f32 v12, v12, v13
	v_cvt_pk_bf16_f32 v13, v8, v9
	v_cvt_pk_bf16_f32 v14, v14, v15
	v_cvt_pk_bf16_f32 v15, v10, v11
	global_store_dwordx4 v[6:7], v[12:15], off sc0 sc1
	v_pk_mul_f32 v[8:9], v[152:153], s[10:11] op_sel_hi:[1,0]
	v_pk_mul_f32 v[10:11], v[148:149], s[10:11] op_sel_hi:[1,0]
	v_cndmask_b32_e64 v14, 0, 1, s[38:39]
	v_pk_mul_f32 v[12:13], v[150:151], s[10:11] op_sel_hi:[1,0]
	v_cmp_ne_u32_e64 s[2:3], 1, v14
	s_andn2_b64 vcc, exec, s[38:39]
	v_pk_mul_f32 v[14:15], v[146:147], s[10:11] op_sel_hi:[1,0]
	s_cbranch_vccnz .LBB0_2038
	v_mul_f32_e32 v17, 0x3d372713, v14
	v_mul_f32_e32 v17, v14, v17
	v_mul_f32_e32 v18, 0x3d372713, v13
	v_fma_f32 v17, v14, v17, v14
	v_mul_f32_e32 v18, v13, v18
	v_mov_b32_e32 v19, v13
	v_mul_f32_e32 v17, 0xc0135761, v17
	v_fmac_f32_e32 v19, v19, v18
	v_exp_f32_e32 v17, v17
	v_mul_f32_e32 v18, 0xc0135761, v19
	v_exp_f32_e32 v19, v18
	v_mul_f32_e32 v22, 0x3d372713, v9
	v_add_f32_e32 v17, 1.0, v17
	v_rcp_f32_e32 v18, v17
	v_add_f32_e32 v17, 1.0, v19
	v_mul_f32_e32 v19, 0x3d372713, v15
	v_mul_f32_e32 v22, v9, v22
	v_mul_f32_e32 v19, v15, v19
	v_mov_b32_e32 v20, v15
	v_fma_f32 v22, v9, v22, v9
	v_fmac_f32_e32 v20, v20, v19
	v_mul_f32_e32 v21, 0x3d372713, v10
	v_mul_f32_e32 v22, 0xc0135761, v22
	v_mul_f32_e32 v16, 0x3d372713, v12
	v_mul_f32_e32 v19, 0xc0135761, v20
	v_mul_f32_e32 v20, 0x3d372713, v8
	v_mul_f32_e32 v21, v10, v21
	v_exp_f32_e32 v23, v22
	v_mul_f32_e32 v22, 0x3d372713, v11
	v_mul_f32_e32 v16, v12, v16
	v_mul_f32_e32 v20, v8, v20
	v_fma_f32 v21, v10, v21, v10
	v_mul_f32_e32 v22, v11, v22
	v_fma_f32 v16, v12, v16, v12
	v_fma_f32 v20, v8, v20, v8
	v_mul_f32_e32 v21, 0xc0135761, v21
	v_fma_f32 v22, v11, v22, v11
	v_mul_f32_e32 v16, 0xc0135761, v16
	v_mul_f32_e32 v20, 0xc0135761, v20
	v_exp_f32_e32 v21, v21
	v_mul_f32_e32 v22, 0xc0135761, v22
	v_exp_f32_e32 v16, v16
	v_exp_f32_e32 v19, v19
	v_exp_f32_e32 v20, v20
	v_exp_f32_e32 v24, v22
	v_add_f32_e32 v21, 1.0, v21
	v_add_f32_e32 v16, 1.0, v16
	v_add_f32_e32 v19, 1.0, v19
	v_add_f32_e32 v20, 1.0, v20
	v_rcp_f32_e32 v22, v21
	v_add_f32_e32 v21, 1.0, v23
	v_add_f32_e32 v23, 1.0, v24
	v_rcp_f32_e32 v16, v16
	v_rcp_f32_e32 v17, v17
	v_rcp_f32_e32 v20, v20
	v_rcp_f32_e32 v21, v21
	v_rcp_f32_e32 v23, v23
	v_rcp_f32_e32 v19, v19
	v_pk_mul_f32 v[12:13], v[12:13], v[16:17]
	v_pk_mul_f32 v[8:9], v[8:9], v[20:21]
	v_pk_mul_f32 v[10:11], v[10:11], v[22:23]
	v_pk_mul_f32 v[14:15], v[14:15], v[18:19]
.LBB0_2038:
	v_cvt_pk_bf16_f32 v12, v12, v13
	v_cvt_pk_bf16_f32 v13, v8, v9
	s_nop 0
	v_cvt_pk_bf16_f32 v14, v14, v15
	v_cvt_pk_bf16_f32 v15, v10, v11
	global_store_dwordx4 v[6:7], v[12:15], off offset:256 sc0 sc1
	v_pk_mul_f32 v[8:9], v[144:145], s[10:11] op_sel_hi:[1,0]
	v_pk_mul_f32 v[10:11], v[140:141], s[10:11] op_sel_hi:[1,0]
	v_pk_mul_f32 v[12:13], v[142:143], s[10:11] op_sel_hi:[1,0]
	s_and_b64 vcc, exec, s[2:3]
	v_pk_mul_f32 v[14:15], v[138:139], s[10:11] op_sel_hi:[1,0]
	s_cbranch_vccnz .LBB0_2040
	v_mul_f32_e32 v7, 0x3d372713, v14
	v_mul_f32_e32 v7, v14, v7
	v_mul_f32_e32 v16, 0x3d372713, v13
	v_fma_f32 v7, v14, v7, v14
	v_mul_f32_e32 v16, v13, v16
	v_mov_b32_e32 v17, v13
	v_mul_f32_e32 v7, 0xc0135761, v7
	v_fmac_f32_e32 v17, v17, v16
	v_exp_f32_e32 v7, v7
	v_mul_f32_e32 v16, 0xc0135761, v17
	v_exp_f32_e32 v17, v16
	v_mul_f32_e32 v20, 0x3d372713, v9
	v_add_f32_e32 v7, 1.0, v7
	v_rcp_f32_e32 v16, v7
	v_add_f32_e32 v7, 1.0, v17
	v_mul_f32_e32 v17, 0x3d372713, v15
	v_mul_f32_e32 v20, v9, v20
	v_mul_f32_e32 v17, v15, v17
	v_mov_b32_e32 v18, v15
	v_fma_f32 v20, v9, v20, v9
	v_fmac_f32_e32 v18, v18, v17
	v_mul_f32_e32 v19, 0x3d372713, v10
	v_mul_f32_e32 v20, 0xc0135761, v20
	v_mul_f32_e32 v6, 0x3d372713, v12
	v_mul_f32_e32 v17, 0xc0135761, v18
	v_mul_f32_e32 v18, 0x3d372713, v8
	v_mul_f32_e32 v19, v10, v19
	v_exp_f32_e32 v21, v20
	v_mul_f32_e32 v20, 0x3d372713, v11
	v_mul_f32_e32 v6, v12, v6
	v_mul_f32_e32 v18, v8, v18
	v_fma_f32 v19, v10, v19, v10
	v_mul_f32_e32 v20, v11, v20
	v_fma_f32 v6, v12, v6, v12
	v_fma_f32 v18, v8, v18, v8
	v_mul_f32_e32 v19, 0xc0135761, v19
	v_fma_f32 v20, v11, v20, v11
	v_mul_f32_e32 v6, 0xc0135761, v6
	v_mul_f32_e32 v18, 0xc0135761, v18
	v_exp_f32_e32 v19, v19
	v_mul_f32_e32 v20, 0xc0135761, v20
	v_exp_f32_e32 v6, v6
	v_exp_f32_e32 v17, v17
	v_exp_f32_e32 v18, v18
	v_exp_f32_e32 v22, v20
	v_add_f32_e32 v19, 1.0, v19
	v_add_f32_e32 v6, 1.0, v6
	v_add_f32_e32 v17, 1.0, v17
	v_add_f32_e32 v18, 1.0, v18
	v_rcp_f32_e32 v20, v19
	v_add_f32_e32 v19, 1.0, v21
	v_add_f32_e32 v21, 1.0, v22
	v_rcp_f32_e32 v6, v6
	v_rcp_f32_e32 v7, v7
	v_rcp_f32_e32 v18, v18
	v_rcp_f32_e32 v19, v19
	v_rcp_f32_e32 v21, v21
	v_rcp_f32_e32 v17, v17
	v_pk_mul_f32 v[12:13], v[12:13], v[6:7]
	v_pk_mul_f32 v[8:9], v[8:9], v[18:19]
	v_pk_mul_f32 v[10:11], v[10:11], v[20:21]
	v_pk_mul_f32 v[14:15], v[14:15], v[16:17]
; __device__ __forceinline__ unsigned cvt_pk_bf16(float lo, float hi) { unsigned r; asm volatile("v_cvt_pk_bf16_f32 %0, %1, %2" : "=v"(r) : "v"(lo), "v"(hi)); return r; }
; __device__ __forceinline__ float gelu_tanh(float x) { const float y = x + 0.044715f * x * x * x; return x * __builtin_amdgcn_rcpf(1.0f + __builtin_amdgcn_exp2f(-2.302208198f * y)); }
;     __device__ __forceinline__ void operator()(const f32x4 (&acc)[2][2][4][2], const Unit& u, int wr, int wc, int fr, int fq) const {
;         const int row0 = u.pm * BM + wr * 64 + fr, col0 = u.pn * BM + wc * 32 + 8 * fq; const bool act = u.pn < nact;
; #pragma unroll
;         for (int ai = 0; ai < 2; ++ai)
; #pragma unroll
;             for (int m = 0; m < 4; ++m) { bf16_t* rowp = O + (size_t)u.ks * ks_stride + (size_t)(row0 + ai * HALF + m * 16) * ldc + col0;
; #pragma unroll
;                 for (int bj = 0; bj < 2; ++bj) { f32x4 v0 = acc[ai][bj][m][0] * ascale, v1 = acc[ai][bj][m][1] * ascale;
;                     if (act) {
; #pragma unroll
;                         for (int j = 0; j < 4; ++j) { v0[j] = gelu_tanh(v0[j]); v1[j] = gelu_tanh(v1[j]); } }
;                     u32x4 w; w.x = cvt_pk_bf16(v0[0], v0[1]); w.y = cvt_pk_bf16(v0[2], v0[3]); w.z = cvt_pk_bf16(v1[0], v1[1]); w.w = cvt_pk_bf16(v1[2], v1[3]);
;                     *(u32x4*)(rowp + bj * HALF) = w; } }
.LBB0_2040:
	v_or_b32_e32 v6, 16, v4
	v_ashrrev_i32_e32 v7, 31, v6
	v_lshlrev_b64 v[6:7], 12, v[6:7]
	v_lshl_add_u64 v[6:7], s[16:17], 0, v[6:7]
	v_lshl_add_u64 v[6:7], v[2:3], 1, v[6:7]
	v_cvt_pk_bf16_f32 v12, v12, v13
	v_cvt_pk_bf16_f32 v13, v8, v9
	v_cvt_pk_bf16_f32 v14, v14, v15
	v_cvt_pk_bf16_f32 v15, v10, v11
	global_store_dwordx4 v[6:7], v[12:15], off sc0 sc1
	v_pk_mul_f32 v[8:9], v[136:137], s[10:11] op_sel_hi:[1,0]
	v_pk_mul_f32 v[10:11], v[132:133], s[10:11] op_sel_hi:[1,0]
	v_pk_mul_f32 v[12:13], v[134:135], s[10:11] op_sel_hi:[1,0]
	s_and_b64 vcc, exec, s[2:3]
	v_pk_mul_f32 v[14:15], v[130:131], s[10:11] op_sel_hi:[1,0]
	s_cbranch_vccnz .LBB0_2042
	v_mul_f32_e32 v17, 0x3d372713, v14
	v_mul_f32_e32 v17, v14, v17
	v_mul_f32_e32 v18, 0x3d372713, v13
	v_fma_f32 v17, v14, v17, v14
	v_mul_f32_e32 v18, v13, v18
	v_mov_b32_e32 v19, v13
	v_mul_f32_e32 v17, 0xc0135761, v17
	v_fmac_f32_e32 v19, v19, v18
	v_exp_f32_e32 v17, v17
	v_mul_f32_e32 v18, 0xc0135761, v19
	v_exp_f32_e32 v19, v18
	v_mul_f32_e32 v22, 0x3d372713, v9
	v_add_f32_e32 v17, 1.0, v17
	v_rcp_f32_e32 v18, v17
	v_add_f32_e32 v17, 1.0, v19
	v_mul_f32_e32 v19, 0x3d372713, v15
	v_mul_f32_e32 v22, v9, v22
	v_mul_f32_e32 v19, v15, v19
	v_mov_b32_e32 v20, v15
	v_fma_f32 v22, v9, v22, v9
	v_fmac_f32_e32 v20, v20, v19
	v_mul_f32_e32 v21, 0x3d372713, v10
	v_mul_f32_e32 v22, 0xc0135761, v22
	v_mul_f32_e32 v16, 0x3d372713, v12
	v_mul_f32_e32 v19, 0xc0135761, v20
	v_mul_f32_e32 v20, 0x3d372713, v8
	v_mul_f32_e32 v21, v10, v21
	v_exp_f32_e32 v23, v22
	v_mul_f32_e32 v22, 0x3d372713, v11
	v_mul_f32_e32 v16, v12, v16
	v_mul_f32_e32 v20, v8, v20
	v_fma_f32 v21, v10, v21, v10
	v_mul_f32_e32 v22, v11, v22
	v_fma_f32 v16, v12, v16, v12
	v_fma_f32 v20, v8, v20, v8
	v_mul_f32_e32 v21, 0xc0135761, v21
	v_fma_f32 v22, v11, v22, v11
	v_mul_f32_e32 v16, 0xc0135761, v16
	v_mul_f32_e32 v20, 0xc0135761, v20
	v_exp_f32_e32 v21, v21
	v_mul_f32_e32 v22, 0xc0135761, v22
	v_exp_f32_e32 v16, v16
	v_exp_f32_e32 v19, v19
	v_exp_f32_e32 v20, v20
	v_exp_f32_e32 v24, v22
	v_add_f32_e32 v21, 1.0, v21
	v_add_f32_e32 v16, 1.0, v16
	v_add_f32_e32 v19, 1.0, v19
	v_add_f32_e32 v20, 1.0, v20
	v_rcp_f32_e32 v22, v21
	v_add_f32_e32 v21, 1.0, v23
	v_add_f32_e32 v23, 1.0, v24
	v_rcp_f32_e32 v16, v16
	v_rcp_f32_e32 v17, v17
	v_rcp_f32_e32 v20, v20
	v_rcp_f32_e32 v21, v21
	v_rcp_f32_e32 v23, v23
	v_rcp_f32_e32 v19, v19
	v_pk_mul_f32 v[12:13], v[12:13], v[16:17]
	v_pk_mul_f32 v[8:9], v[8:9], v[20:21]
	v_pk_mul_f32 v[10:11], v[10:11], v[22:23]
	v_pk_mul_f32 v[14:15], v[14:15], v[18:19]
.LBB0_2042:
	v_cvt_pk_bf16_f32 v12, v12, v13
	v_cvt_pk_bf16_f32 v13, v8, v9
	s_nop 0
	v_cvt_pk_bf16_f32 v14, v14, v15
	v_cvt_pk_bf16_f32 v15, v10, v11
	global_store_dwordx4 v[6:7], v[12:15], off offset:256 sc0 sc1
	v_pk_mul_f32 v[8:9], v[128:129], s[10:11] op_sel_hi:[1,0]
	v_pk_mul_f32 v[10:11], v[124:125], s[10:11] op_sel_hi:[1,0]
	v_pk_mul_f32 v[12:13], v[126:127], s[10:11] op_sel_hi:[1,0]
	s_and_b64 vcc, exec, s[2:3]
	v_pk_mul_f32 v[14:15], v[122:123], s[10:11] op_sel_hi:[1,0]
	s_cbranch_vccnz .LBB0_2044
	v_mul_f32_e32 v7, 0x3d372713, v14
	v_mul_f32_e32 v7, v14, v7
	v_mul_f32_e32 v16, 0x3d372713, v13
	v_fma_f32 v7, v14, v7, v14
	v_mul_f32_e32 v16, v13, v16
	v_mov_b32_e32 v17, v13
	v_mul_f32_e32 v7, 0xc0135761, v7
	v_fmac_f32_e32 v17, v17, v16
	v_exp_f32_e32 v7, v7
	v_mul_f32_e32 v16, 0xc0135761, v17
	v_exp_f32_e32 v17, v16
	v_mul_f32_e32 v20, 0x3d372713, v9
	v_add_f32_e32 v7, 1.0, v7
	v_rcp_f32_e32 v16, v7
	v_add_f32_e32 v7, 1.0, v17
	v_mul_f32_e32 v17, 0x3d372713, v15
	v_mul_f32_e32 v20, v9, v20
	v_mul_f32_e32 v17, v15, v17
	v_mov_b32_e32 v18, v15
	v_fma_f32 v20, v9, v20, v9
	v_fmac_f32_e32 v18, v18, v17
	v_mul_f32_e32 v19, 0x3d372713, v10
	v_mul_f32_e32 v20, 0xc0135761, v20
	v_mul_f32_e32 v6, 0x3d372713, v12
	v_mul_f32_e32 v17, 0xc0135761, v18
	v_mul_f32_e32 v18, 0x3d372713, v8
	v_mul_f32_e32 v19, v10, v19
	v_exp_f32_e32 v21, v20
	v_mul_f32_e32 v20, 0x3d372713, v11
	v_mul_f32_e32 v6, v12, v6
	v_mul_f32_e32 v18, v8, v18
	v_fma_f32 v19, v10, v19, v10
	v_mul_f32_e32 v20, v11, v20
	v_fma_f32 v6, v12, v6, v12
	v_fma_f32 v18, v8, v18, v8
	v_mul_f32_e32 v19, 0xc0135761, v19
	v_fma_f32 v20, v11, v20, v11
	v_mul_f32_e32 v6, 0xc0135761, v6
	v_mul_f32_e32 v18, 0xc0135761, v18
	v_exp_f32_e32 v19, v19
	v_mul_f32_e32 v20, 0xc0135761, v20
	v_exp_f32_e32 v6, v6
	v_exp_f32_e32 v17, v17
	v_exp_f32_e32 v18, v18
	v_exp_f32_e32 v22, v20
	v_add_f32_e32 v19, 1.0, v19
	v_add_f32_e32 v6, 1.0, v6
	v_add_f32_e32 v17, 1.0, v17
	v_add_f32_e32 v18, 1.0, v18
	v_rcp_f32_e32 v20, v19
	v_add_f32_e32 v19, 1.0, v21
	v_add_f32_e32 v21, 1.0, v22
	v_rcp_f32_e32 v6, v6
	v_rcp_f32_e32 v7, v7
	v_rcp_f32_e32 v18, v18
	v_rcp_f32_e32 v19, v19
	v_rcp_f32_e32 v21, v21
	v_rcp_f32_e32 v17, v17
	v_pk_mul_f32 v[12:13], v[12:13], v[6:7]
	v_pk_mul_f32 v[8:9], v[8:9], v[18:19]
	v_pk_mul_f32 v[10:11], v[10:11], v[20:21]
	v_pk_mul_f32 v[14:15], v[14:15], v[16:17]
; __device__ __forceinline__ unsigned cvt_pk_bf16(float lo, float hi) { unsigned r; asm volatile("v_cvt_pk_bf16_f32 %0, %1, %2" : "=v"(r) : "v"(lo), "v"(hi)); return r; }
; __device__ __forceinline__ float gelu_tanh(float x) { const float y = x + 0.044715f * x * x * x; return x * __builtin_amdgcn_rcpf(1.0f + __builtin_amdgcn_exp2f(-2.302208198f * y)); }
;     __device__ __forceinline__ void operator()(const f32x4 (&acc)[2][2][4][2], const Unit& u, int wr, int wc, int fr, int fq) const {
;         const int row0 = u.pm * BM + wr * 64 + fr, col0 = u.pn * BM + wc * 32 + 8 * fq; const bool act = u.pn < nact;
; #pragma unroll
;         for (int ai = 0; ai < 2; ++ai)
; #pragma unroll
;             for (int m = 0; m < 4; ++m) { bf16_t* rowp = O + (size_t)u.ks * ks_stride + (size_t)(row0 + ai * HALF + m * 16) * ldc + col0;
; #pragma unroll
;                 for (int bj = 0; bj < 2; ++bj) { f32x4 v0 = acc[ai][bj][m][0] * ascale, v1 = acc[ai][bj][m][1] * ascale;
;                     if (act) {
; #pragma unroll
;                         for (int j = 0; j < 4; ++j) { v0[j] = gelu_tanh(v0[j]); v1[j] = gelu_tanh(v1[j]); } }
;                     u32x4 w; w.x = cvt_pk_bf16(v0[0], v0[1]); w.y = cvt_pk_bf16(v0[2], v0[3]); w.z = cvt_pk_bf16(v1[0], v1[1]); w.w = cvt_pk_bf16(v1[2], v1[3]);
;                     *(u32x4*)(rowp + bj * HALF) = w; } }
.LBB0_2044:
	v_or_b32_e32 v6, 32, v4
	v_ashrrev_i32_e32 v7, 31, v6
	v_lshlrev_b64 v[6:7], 12, v[6:7]
	v_lshl_add_u64 v[6:7], s[16:17], 0, v[6:7]
	v_lshl_add_u64 v[6:7], v[2:3], 1, v[6:7]
	v_cvt_pk_bf16_f32 v12, v12, v13
	v_cvt_pk_bf16_f32 v13, v8, v9
	v_cvt_pk_bf16_f32 v14, v14, v15
	v_cvt_pk_bf16_f32 v15, v10, v11
	global_store_dwordx4 v[6:7], v[12:15], off sc0 sc1
	v_pk_mul_f32 v[8:9], v[120:121], s[10:11] op_sel_hi:[1,0]
	v_pk_mul_f32 v[10:11], v[116:117], s[10:11] op_sel_hi:[1,0]
	v_pk_mul_f32 v[12:13], v[118:119], s[10:11] op_sel_hi:[1,0]
	s_and_b64 vcc, exec, s[2:3]
	v_pk_mul_f32 v[14:15], v[114:115], s[10:11] op_sel_hi:[1,0]
	s_cbranch_vccnz .LBB0_2046
	v_mul_f32_e32 v17, 0x3d372713, v14
	v_mul_f32_e32 v17, v14, v17
	v_mul_f32_e32 v18, 0x3d372713, v13
	v_fma_f32 v17, v14, v17, v14
	v_mul_f32_e32 v18, v13, v18
	v_mov_b32_e32 v19, v13
	v_mul_f32_e32 v17, 0xc0135761, v17
	v_fmac_f32_e32 v19, v19, v18
	v_exp_f32_e32 v17, v17
	v_mul_f32_e32 v18, 0xc0135761, v19
	v_exp_f32_e32 v19, v18
	v_mul_f32_e32 v22, 0x3d372713, v9
	v_add_f32_e32 v17, 1.0, v17
	v_rcp_f32_e32 v18, v17
	v_add_f32_e32 v17, 1.0, v19
	v_mul_f32_e32 v19, 0x3d372713, v15
	v_mul_f32_e32 v22, v9, v22
	v_mul_f32_e32 v19, v15, v19
	v_mov_b32_e32 v20, v15
	v_fma_f32 v22, v9, v22, v9
	v_fmac_f32_e32 v20, v20, v19
	v_mul_f32_e32 v21, 0x3d372713, v10
	v_mul_f32_e32 v22, 0xc0135761, v22
	v_mul_f32_e32 v16, 0x3d372713, v12
	v_mul_f32_e32 v19, 0xc0135761, v20
	v_mul_f32_e32 v20, 0x3d372713, v8
	v_mul_f32_e32 v21, v10, v21
	v_exp_f32_e32 v23, v22
	v_mul_f32_e32 v22, 0x3d372713, v11
	v_mul_f32_e32 v16, v12, v16
	v_mul_f32_e32 v20, v8, v20
	v_fma_f32 v21, v10, v21, v10
	v_mul_f32_e32 v22, v11, v22
	v_fma_f32 v16, v12, v16, v12
	v_fma_f32 v20, v8, v20, v8
	v_mul_f32_e32 v21, 0xc0135761, v21
	v_fma_f32 v22, v11, v22, v11
	v_mul_f32_e32 v16, 0xc0135761, v16
	v_mul_f32_e32 v20, 0xc0135761, v20
	v_exp_f32_e32 v21, v21
	v_mul_f32_e32 v22, 0xc0135761, v22
	v_exp_f32_e32 v16, v16
	v_exp_f32_e32 v19, v19
	v_exp_f32_e32 v20, v20
	v_exp_f32_e32 v24, v22
	v_add_f32_e32 v21, 1.0, v21
	v_add_f32_e32 v16, 1.0, v16
	v_add_f32_e32 v19, 1.0, v19
	v_add_f32_e32 v20, 1.0, v20
	v_rcp_f32_e32 v22, v21
	v_add_f32_e32 v21, 1.0, v23
	v_add_f32_e32 v23, 1.0, v24
	v_rcp_f32_e32 v16, v16
	v_rcp_f32_e32 v17, v17
	v_rcp_f32_e32 v20, v20
	v_rcp_f32_e32 v21, v21
	v_rcp_f32_e32 v23, v23
	v_rcp_f32_e32 v19, v19
	v_pk_mul_f32 v[12:13], v[12:13], v[16:17]
	v_pk_mul_f32 v[8:9], v[8:9], v[20:21]
	v_pk_mul_f32 v[10:11], v[10:11], v[22:23]
	v_pk_mul_f32 v[14:15], v[14:15], v[18:19]
.LBB0_2046:
	v_cvt_pk_bf16_f32 v12, v12, v13
	v_cvt_pk_bf16_f32 v13, v8, v9
	s_nop 0
	v_cvt_pk_bf16_f32 v14, v14, v15
	v_cvt_pk_bf16_f32 v15, v10, v11
	global_store_dwordx4 v[6:7], v[12:15], off offset:256 sc0 sc1
	v_pk_mul_f32 v[8:9], v[112:113], s[10:11] op_sel_hi:[1,0]
	v_pk_mul_f32 v[10:11], v[108:109], s[10:11] op_sel_hi:[1,0]
	v_pk_mul_f32 v[12:13], v[110:111], s[10:11] op_sel_hi:[1,0]
	s_and_b64 vcc, exec, s[2:3]
	v_pk_mul_f32 v[14:15], v[106:107], s[10:11] op_sel_hi:[1,0]
	s_cbranch_vccnz .LBB0_2048
	v_mul_f32_e32 v7, 0x3d372713, v14
	v_mul_f32_e32 v7, v14, v7
	v_mul_f32_e32 v16, 0x3d372713, v13
	v_fma_f32 v7, v14, v7, v14
	v_mul_f32_e32 v16, v13, v16
	v_mov_b32_e32 v17, v13
	v_mul_f32_e32 v7, 0xc0135761, v7
	v_fmac_f32_e32 v17, v17, v16
	v_exp_f32_e32 v7, v7
	v_mul_f32_e32 v16, 0xc0135761, v17
	v_exp_f32_e32 v17, v16
	v_mul_f32_e32 v20, 0x3d372713, v9
	v_add_f32_e32 v7, 1.0, v7
	v_rcp_f32_e32 v16, v7
	v_add_f32_e32 v7, 1.0, v17
	v_mul_f32_e32 v17, 0x3d372713, v15
	v_mul_f32_e32 v20, v9, v20
	v_mul_f32_e32 v17, v15, v17
	v_mov_b32_e32 v18, v15
	v_fma_f32 v20, v9, v20, v9
	v_fmac_f32_e32 v18, v18, v17
	v_mul_f32_e32 v19, 0x3d372713, v10
	v_mul_f32_e32 v20, 0xc0135761, v20
	v_mul_f32_e32 v6, 0x3d372713, v12
	v_mul_f32_e32 v17, 0xc0135761, v18
	v_mul_f32_e32 v18, 0x3d372713, v8
	v_mul_f32_e32 v19, v10, v19
	v_exp_f32_e32 v21, v20
	v_mul_f32_e32 v20, 0x3d372713, v11
	v_mul_f32_e32 v6, v12, v6
	v_mul_f32_e32 v18, v8, v18
	v_fma_f32 v19, v10, v19, v10
	v_mul_f32_e32 v20, v11, v20
	v_fma_f32 v6, v12, v6, v12
	v_fma_f32 v18, v8, v18, v8
	v_mul_f32_e32 v19, 0xc0135761, v19
	v_fma_f32 v20, v11, v20, v11
	v_mul_f32_e32 v6, 0xc0135761, v6
	v_mul_f32_e32 v18, 0xc0135761, v18
	v_exp_f32_e32 v19, v19
	v_mul_f32_e32 v20, 0xc0135761, v20
	v_exp_f32_e32 v6, v6
	v_exp_f32_e32 v17, v17
	v_exp_f32_e32 v18, v18
	v_exp_f32_e32 v22, v20
	v_add_f32_e32 v19, 1.0, v19
	v_add_f32_e32 v6, 1.0, v6
	v_add_f32_e32 v17, 1.0, v17
	v_add_f32_e32 v18, 1.0, v18
	v_rcp_f32_e32 v20, v19
	v_add_f32_e32 v19, 1.0, v21
	v_add_f32_e32 v21, 1.0, v22
	v_rcp_f32_e32 v6, v6
	v_rcp_f32_e32 v7, v7
	v_rcp_f32_e32 v18, v18
	v_rcp_f32_e32 v19, v19
	v_rcp_f32_e32 v21, v21
	v_rcp_f32_e32 v17, v17
	v_pk_mul_f32 v[12:13], v[12:13], v[6:7]
	v_pk_mul_f32 v[8:9], v[8:9], v[18:19]
	v_pk_mul_f32 v[10:11], v[10:11], v[20:21]
	v_pk_mul_f32 v[14:15], v[14:15], v[16:17]
; __device__ __forceinline__ unsigned cvt_pk_bf16(float lo, float hi) { unsigned r; asm volatile("v_cvt_pk_bf16_f32 %0, %1, %2" : "=v"(r) : "v"(lo), "v"(hi)); return r; }
; __device__ __forceinline__ float gelu_tanh(float x) { const float y = x + 0.044715f * x * x * x; return x * __builtin_amdgcn_rcpf(1.0f + __builtin_amdgcn_exp2f(-2.302208198f * y)); }
;     __device__ __forceinline__ void operator()(const f32x4 (&acc)[2][2][4][2], const Unit& u, int wr, int wc, int fr, int fq) const {
;         const int row0 = u.pm * BM + wr * 64 + fr, col0 = u.pn * BM + wc * 32 + 8 * fq; const bool act = u.pn < nact;
; #pragma unroll
;         for (int ai = 0; ai < 2; ++ai)
; #pragma unroll
;             for (int m = 0; m < 4; ++m) { bf16_t* rowp = O + (size_t)u.ks * ks_stride + (size_t)(row0 + ai * HALF + m * 16) * ldc + col0;
; #pragma unroll
;                 for (int bj = 0; bj < 2; ++bj) { f32x4 v0 = acc[ai][bj][m][0] * ascale, v1 = acc[ai][bj][m][1] * ascale;
;                     if (act) {
; #pragma unroll
;                         for (int j = 0; j < 4; ++j) { v0[j] = gelu_tanh(v0[j]); v1[j] = gelu_tanh(v1[j]); } }
;                     u32x4 w; w.x = cvt_pk_bf16(v0[0], v0[1]); w.y = cvt_pk_bf16(v0[2], v0[3]); w.z = cvt_pk_bf16(v1[0], v1[1]); w.w = cvt_pk_bf16(v1[2], v1[3]);
;                     *(u32x4*)(rowp + bj * HALF) = w; } }
.LBB0_2048:
	v_or_b32_e32 v6, 48, v4
	v_ashrrev_i32_e32 v7, 31, v6
	v_lshlrev_b64 v[6:7], 12, v[6:7]
	v_lshl_add_u64 v[6:7], s[16:17], 0, v[6:7]
	v_lshl_add_u64 v[6:7], v[2:3], 1, v[6:7]
	v_cvt_pk_bf16_f32 v12, v12, v13
	v_cvt_pk_bf16_f32 v13, v8, v9
	v_cvt_pk_bf16_f32 v14, v14, v15
	v_cvt_pk_bf16_f32 v15, v10, v11
	global_store_dwordx4 v[6:7], v[12:15], off sc0 sc1
	v_pk_mul_f32 v[8:9], v[104:105], s[10:11] op_sel_hi:[1,0]
	v_pk_mul_f32 v[10:11], v[100:101], s[10:11] op_sel_hi:[1,0]
	v_pk_mul_f32 v[12:13], v[102:103], s[10:11] op_sel_hi:[1,0]
	s_and_b64 vcc, exec, s[2:3]
	v_pk_mul_f32 v[14:15], v[98:99], s[10:11] op_sel_hi:[1,0]
	s_cbranch_vccnz .LBB0_2050
	v_mul_f32_e32 v17, 0x3d372713, v14
	v_mul_f32_e32 v17, v14, v17
	v_mul_f32_e32 v18, 0x3d372713, v13
	v_fma_f32 v17, v14, v17, v14
	v_mul_f32_e32 v18, v13, v18
	v_mov_b32_e32 v19, v13
	v_mul_f32_e32 v17, 0xc0135761, v17
	v_fmac_f32_e32 v19, v19, v18
	v_exp_f32_e32 v17, v17
	v_mul_f32_e32 v18, 0xc0135761, v19
	v_exp_f32_e32 v19, v18
	v_mul_f32_e32 v22, 0x3d372713, v9
	v_add_f32_e32 v17, 1.0, v17
	v_rcp_f32_e32 v18, v17
	v_add_f32_e32 v17, 1.0, v19
	v_mul_f32_e32 v19, 0x3d372713, v15
	v_mul_f32_e32 v22, v9, v22
	v_mul_f32_e32 v19, v15, v19
	v_mov_b32_e32 v20, v15
	v_fma_f32 v22, v9, v22, v9
	v_fmac_f32_e32 v20, v20, v19
	v_mul_f32_e32 v21, 0x3d372713, v10
	v_mul_f32_e32 v22, 0xc0135761, v22
	v_mul_f32_e32 v16, 0x3d372713, v12
	v_mul_f32_e32 v19, 0xc0135761, v20
	v_mul_f32_e32 v20, 0x3d372713, v8
	v_mul_f32_e32 v21, v10, v21
	v_exp_f32_e32 v23, v22
	v_mul_f32_e32 v22, 0x3d372713, v11
	v_mul_f32_e32 v16, v12, v16
	v_mul_f32_e32 v20, v8, v20
	v_fma_f32 v21, v10, v21, v10
	v_mul_f32_e32 v22, v11, v22
	v_fma_f32 v16, v12, v16, v12
	v_fma_f32 v20, v8, v20, v8
	v_mul_f32_e32 v21, 0xc0135761, v21
	v_fma_f32 v22, v11, v22, v11
	v_mul_f32_e32 v16, 0xc0135761, v16
	v_mul_f32_e32 v20, 0xc0135761, v20
	v_exp_f32_e32 v21, v21
	v_mul_f32_e32 v22, 0xc0135761, v22
	v_exp_f32_e32 v16, v16
	v_exp_f32_e32 v19, v19
	v_exp_f32_e32 v20, v20
	v_exp_f32_e32 v24, v22
	v_add_f32_e32 v21, 1.0, v21
	v_add_f32_e32 v16, 1.0, v16
	v_add_f32_e32 v19, 1.0, v19
	v_add_f32_e32 v20, 1.0, v20
	v_rcp_f32_e32 v22, v21
	v_add_f32_e32 v21, 1.0, v23
	v_add_f32_e32 v23, 1.0, v24
	v_rcp_f32_e32 v16, v16
	v_rcp_f32_e32 v17, v17
	v_rcp_f32_e32 v20, v20
	v_rcp_f32_e32 v21, v21
	v_rcp_f32_e32 v23, v23
	v_rcp_f32_e32 v19, v19
	v_pk_mul_f32 v[12:13], v[12:13], v[16:17]
	v_pk_mul_f32 v[8:9], v[8:9], v[20:21]
	v_pk_mul_f32 v[10:11], v[10:11], v[22:23]
	v_pk_mul_f32 v[14:15], v[14:15], v[18:19]
.LBB0_2050:
	v_cvt_pk_bf16_f32 v12, v12, v13
	v_cvt_pk_bf16_f32 v13, v8, v9
	s_nop 0
	v_cvt_pk_bf16_f32 v14, v14, v15
	v_cvt_pk_bf16_f32 v15, v10, v11
	global_store_dwordx4 v[6:7], v[12:15], off offset:256 sc0 sc1
	v_pk_mul_f32 v[8:9], v[96:97], s[10:11] op_sel_hi:[1,0]
	v_pk_mul_f32 v[10:11], v[92:93], s[10:11] op_sel_hi:[1,0]
	v_pk_mul_f32 v[12:13], v[94:95], s[10:11] op_sel_hi:[1,0]
	s_and_b64 vcc, exec, s[2:3]
	v_pk_mul_f32 v[14:15], v[90:91], s[10:11] op_sel_hi:[1,0]
	s_cbranch_vccnz .LBB0_2052
	v_mul_f32_e32 v7, 0x3d372713, v14
	v_mul_f32_e32 v7, v14, v7
	v_mul_f32_e32 v16, 0x3d372713, v13
	v_fma_f32 v7, v14, v7, v14
	v_mul_f32_e32 v16, v13, v16
	v_mov_b32_e32 v17, v13
	v_mul_f32_e32 v7, 0xc0135761, v7
	v_fmac_f32_e32 v17, v17, v16
	v_exp_f32_e32 v7, v7
	v_mul_f32_e32 v16, 0xc0135761, v17
	v_exp_f32_e32 v17, v16
	v_mul_f32_e32 v20, 0x3d372713, v9
	v_add_f32_e32 v7, 1.0, v7
	v_rcp_f32_e32 v16, v7
	v_add_f32_e32 v7, 1.0, v17
	v_mul_f32_e32 v17, 0x3d372713, v15
	v_mul_f32_e32 v20, v9, v20
	v_mul_f32_e32 v17, v15, v17
	v_mov_b32_e32 v18, v15
	v_fma_f32 v20, v9, v20, v9
	v_fmac_f32_e32 v18, v18, v17
	v_mul_f32_e32 v19, 0x3d372713, v10
	v_mul_f32_e32 v20, 0xc0135761, v20
	v_mul_f32_e32 v6, 0x3d372713, v12
	v_mul_f32_e32 v17, 0xc0135761, v18
	v_mul_f32_e32 v18, 0x3d372713, v8
	v_mul_f32_e32 v19, v10, v19
	v_exp_f32_e32 v21, v20
	v_mul_f32_e32 v20, 0x3d372713, v11
	v_mul_f32_e32 v6, v12, v6
	v_mul_f32_e32 v18, v8, v18
	v_fma_f32 v19, v10, v19, v10
	v_mul_f32_e32 v20, v11, v20
	v_fma_f32 v6, v12, v6, v12
	v_fma_f32 v18, v8, v18, v8
	v_mul_f32_e32 v19, 0xc0135761, v19
	v_fma_f32 v20, v11, v20, v11
	v_mul_f32_e32 v6, 0xc0135761, v6
	v_mul_f32_e32 v18, 0xc0135761, v18
	v_exp_f32_e32 v19, v19
	v_mul_f32_e32 v20, 0xc0135761, v20
	v_exp_f32_e32 v6, v6
	v_exp_f32_e32 v17, v17
	v_exp_f32_e32 v18, v18
	v_exp_f32_e32 v22, v20
	v_add_f32_e32 v19, 1.0, v19
	v_add_f32_e32 v6, 1.0, v6
	v_add_f32_e32 v17, 1.0, v17
	v_add_f32_e32 v18, 1.0, v18
	v_rcp_f32_e32 v20, v19
	v_add_f32_e32 v19, 1.0, v21
	v_add_f32_e32 v21, 1.0, v22
	v_rcp_f32_e32 v6, v6
	v_rcp_f32_e32 v7, v7
	v_rcp_f32_e32 v18, v18
	v_rcp_f32_e32 v19, v19
	v_rcp_f32_e32 v21, v21
	v_rcp_f32_e32 v17, v17
	v_pk_mul_f32 v[12:13], v[12:13], v[6:7]
	v_pk_mul_f32 v[8:9], v[8:9], v[18:19]
	v_pk_mul_f32 v[10:11], v[10:11], v[20:21]
	v_pk_mul_f32 v[14:15], v[14:15], v[16:17]
; __device__ __forceinline__ unsigned cvt_pk_bf16(float lo, float hi) { unsigned r; asm volatile("v_cvt_pk_bf16_f32 %0, %1, %2" : "=v"(r) : "v"(lo), "v"(hi)); return r; }
; __device__ __forceinline__ float gelu_tanh(float x) { const float y = x + 0.044715f * x * x * x; return x * __builtin_amdgcn_rcpf(1.0f + __builtin_amdgcn_exp2f(-2.302208198f * y)); }
;     __device__ __forceinline__ void operator()(const f32x4 (&acc)[2][2][4][2], const Unit& u, int wr, int wc, int fr, int fq) const {
;         const int row0 = u.pm * BM + wr * 64 + fr, col0 = u.pn * BM + wc * 32 + 8 * fq; const bool act = u.pn < nact;
; #pragma unroll
;         for (int ai = 0; ai < 2; ++ai)
; #pragma unroll
;             for (int m = 0; m < 4; ++m) { bf16_t* rowp = O + (size_t)u.ks * ks_stride + (size_t)(row0 + ai * HALF + m * 16) * ldc + col0;
; #pragma unroll
;                 for (int bj = 0; bj < 2; ++bj) { f32x4 v0 = acc[ai][bj][m][0] * ascale, v1 = acc[ai][bj][m][1] * ascale;
;                     if (act) {
; #pragma unroll
;                         for (int j = 0; j < 4; ++j) { v0[j] = gelu_tanh(v0[j]); v1[j] = gelu_tanh(v1[j]); } }
;                     u32x4 w; w.x = cvt_pk_bf16(v0[0], v0[1]); w.y = cvt_pk_bf16(v0[2], v0[3]); w.z = cvt_pk_bf16(v1[0], v1[1]); w.w = cvt_pk_bf16(v1[2], v1[3]);
;                     *(u32x4*)(rowp + bj * HALF) = w; } }
.LBB0_2052:
	v_lshlrev_b64 v[6:7], 12, v[4:5]
	v_lshl_add_u64 v[6:7], s[16:17], 0, v[6:7]
	v_lshl_add_u64 v[6:7], v[2:3], 1, v[6:7]
	v_cvt_pk_bf16_f32 v12, v12, v13
	v_cvt_pk_bf16_f32 v13, v8, v9
	v_add_co_u32_e32 v8, vcc, s66, v6
	v_cvt_pk_bf16_f32 v14, v14, v15
	v_cvt_pk_bf16_f32 v15, v10, v11
	v_pk_mul_f32 v[10:11], v[84:85], s[10:11] op_sel_hi:[1,0]
	s_nop 0
	v_addc_co_u32_e32 v9, vcc, 0, v7, vcc
	global_store_dwordx4 v[8:9], v[12:15], off sc0 sc1
	v_pk_mul_f32 v[8:9], v[88:89], s[10:11] op_sel_hi:[1,0]
	s_and_b64 vcc, exec, s[2:3]
	v_pk_mul_f32 v[12:13], v[86:87], s[10:11] op_sel_hi:[1,0]
	v_pk_mul_f32 v[14:15], v[82:83], s[10:11] op_sel_hi:[1,0]
	s_cbranch_vccnz .LBB0_2054
	v_mul_f32_e32 v17, 0x3d372713, v14
	v_mul_f32_e32 v17, v14, v17
	v_mul_f32_e32 v18, 0x3d372713, v13
	v_fma_f32 v17, v14, v17, v14
	v_mul_f32_e32 v18, v13, v18
	v_mov_b32_e32 v19, v13
	v_mul_f32_e32 v17, 0xc0135761, v17
	v_fmac_f32_e32 v19, v19, v18
	v_exp_f32_e32 v17, v17
	v_mul_f32_e32 v18, 0xc0135761, v19
	v_exp_f32_e32 v19, v18
	v_mul_f32_e32 v22, 0x3d372713, v9
	v_add_f32_e32 v17, 1.0, v17
	v_rcp_f32_e32 v18, v17
	v_add_f32_e32 v17, 1.0, v19
	v_mul_f32_e32 v19, 0x3d372713, v15
	v_mul_f32_e32 v22, v9, v22
	v_mul_f32_e32 v19, v15, v19
	v_mov_b32_e32 v20, v15
	v_fma_f32 v22, v9, v22, v9
	v_fmac_f32_e32 v20, v20, v19
	v_mul_f32_e32 v21, 0x3d372713, v10
	v_mul_f32_e32 v22, 0xc0135761, v22
	v_mul_f32_e32 v16, 0x3d372713, v12
	v_mul_f32_e32 v19, 0xc0135761, v20
	v_mul_f32_e32 v20, 0x3d372713, v8
	v_mul_f32_e32 v21, v10, v21
	v_exp_f32_e32 v23, v22
	v_mul_f32_e32 v22, 0x3d372713, v11
	v_mul_f32_e32 v16, v12, v16
	v_mul_f32_e32 v20, v8, v20
	v_fma_f32 v21, v10, v21, v10
	v_mul_f32_e32 v22, v11, v22
	v_fma_f32 v16, v12, v16, v12
	v_fma_f32 v20, v8, v20, v8
	v_mul_f32_e32 v21, 0xc0135761, v21
	v_fma_f32 v22, v11, v22, v11
	v_mul_f32_e32 v16, 0xc0135761, v16
	v_mul_f32_e32 v20, 0xc0135761, v20
	v_exp_f32_e32 v21, v21
	v_mul_f32_e32 v22, 0xc0135761, v22
	v_exp_f32_e32 v16, v16
	v_exp_f32_e32 v19, v19
	v_exp_f32_e32 v20, v20
	v_exp_f32_e32 v24, v22
	v_add_f32_e32 v21, 1.0, v21
	v_add_f32_e32 v16, 1.0, v16
	v_add_f32_e32 v19, 1.0, v19
	v_add_f32_e32 v20, 1.0, v20
	v_rcp_f32_e32 v22, v21
	v_add_f32_e32 v21, 1.0, v23
	v_add_f32_e32 v23, 1.0, v24
	v_rcp_f32_e32 v16, v16
	v_rcp_f32_e32 v17, v17
	v_rcp_f32_e32 v20, v20
	v_rcp_f32_e32 v21, v21
	v_rcp_f32_e32 v23, v23
	v_rcp_f32_e32 v19, v19
	v_pk_mul_f32 v[12:13], v[12:13], v[16:17]
	v_pk_mul_f32 v[8:9], v[8:9], v[20:21]
	v_pk_mul_f32 v[10:11], v[10:11], v[22:23]
	v_pk_mul_f32 v[14:15], v[14:15], v[18:19]
.LBB0_2054:
	v_lshl_add_u64 v[16:17], v[6:7], 0, s[26:27]
	v_cvt_pk_bf16_f32 v6, v12, v13
	v_cvt_pk_bf16_f32 v7, v8, v9
	v_cvt_pk_bf16_f32 v8, v14, v15
	v_cvt_pk_bf16_f32 v9, v10, v11
	global_store_dwordx4 v[16:17], v[6:9], off offset:256 sc0 sc1
	v_pk_mul_f32 v[12:13], v[78:79], s[10:11] op_sel_hi:[1,0]
	v_pk_mul_f32 v[10:11], v[76:77], s[10:11] op_sel_hi:[1,0]
	v_pk_mul_f32 v[8:9], v[80:81], s[10:11] op_sel_hi:[1,0]
	s_and_b64 vcc, exec, s[2:3]
	v_pk_mul_f32 v[14:15], v[74:75], s[10:11] op_sel_hi:[1,0]
	s_cbranch_vccnz .LBB0_2056
	v_mul_f32_e32 v7, 0x3d372713, v14
	v_mul_f32_e32 v7, v14, v7
	v_mul_f32_e32 v16, 0x3d372713, v13
	v_fma_f32 v7, v14, v7, v14
	v_mul_f32_e32 v16, v13, v16
	v_mov_b32_e32 v17, v13
	v_mul_f32_e32 v7, 0xc0135761, v7
	v_fmac_f32_e32 v17, v17, v16
	v_exp_f32_e32 v7, v7
	v_mul_f32_e32 v16, 0xc0135761, v17
	v_exp_f32_e32 v17, v16
	v_mul_f32_e32 v20, 0x3d372713, v9
	v_add_f32_e32 v7, 1.0, v7
	v_rcp_f32_e32 v16, v7
	v_add_f32_e32 v7, 1.0, v17
	v_mul_f32_e32 v17, 0x3d372713, v15
	v_mul_f32_e32 v20, v9, v20
	v_mul_f32_e32 v17, v15, v17
	v_mov_b32_e32 v18, v15
	v_fma_f32 v20, v9, v20, v9
	v_fmac_f32_e32 v18, v18, v17
	v_mul_f32_e32 v19, 0x3d372713, v10
	v_mul_f32_e32 v20, 0xc0135761, v20
	v_mul_f32_e32 v6, 0x3d372713, v12
	v_mul_f32_e32 v17, 0xc0135761, v18
	v_mul_f32_e32 v18, 0x3d372713, v8
	v_mul_f32_e32 v19, v10, v19
	v_exp_f32_e32 v21, v20
	v_mul_f32_e32 v20, 0x3d372713, v11
	v_mul_f32_e32 v6, v12, v6
	v_mul_f32_e32 v18, v8, v18
	v_fma_f32 v19, v10, v19, v10
	v_mul_f32_e32 v20, v11, v20
	v_fma_f32 v6, v12, v6, v12
	v_fma_f32 v18, v8, v18, v8
	v_mul_f32_e32 v19, 0xc0135761, v19
	v_fma_f32 v20, v11, v20, v11
	v_mul_f32_e32 v6, 0xc0135761, v6
	v_mul_f32_e32 v18, 0xc0135761, v18
	v_exp_f32_e32 v19, v19
	v_mul_f32_e32 v20, 0xc0135761, v20
	v_exp_f32_e32 v6, v6
	v_exp_f32_e32 v17, v17
	v_exp_f32_e32 v18, v18
	v_exp_f32_e32 v22, v20
	v_add_f32_e32 v19, 1.0, v19
	v_add_f32_e32 v6, 1.0, v6
	v_add_f32_e32 v17, 1.0, v17
	v_add_f32_e32 v18, 1.0, v18
	v_rcp_f32_e32 v20, v19
	v_add_f32_e32 v19, 1.0, v21
	v_add_f32_e32 v21, 1.0, v22
	v_rcp_f32_e32 v6, v6
	v_rcp_f32_e32 v7, v7
	v_rcp_f32_e32 v18, v18
	v_rcp_f32_e32 v19, v19
	v_rcp_f32_e32 v21, v21
	v_rcp_f32_e32 v17, v17
	v_pk_mul_f32 v[12:13], v[12:13], v[6:7]
	v_pk_mul_f32 v[8:9], v[8:9], v[18:19]
	v_pk_mul_f32 v[10:11], v[10:11], v[20:21]
	v_pk_mul_f32 v[14:15], v[14:15], v[16:17]
; __device__ __forceinline__ unsigned cvt_pk_bf16(float lo, float hi) { unsigned r; asm volatile("v_cvt_pk_bf16_f32 %0, %1, %2" : "=v"(r) : "v"(lo), "v"(hi)); return r; }
; __device__ __forceinline__ float gelu_tanh(float x) { const float y = x + 0.044715f * x * x * x; return x * __builtin_amdgcn_rcpf(1.0f + __builtin_amdgcn_exp2f(-2.302208198f * y)); }
;     __device__ __forceinline__ void operator()(const f32x4 (&acc)[2][2][4][2], const Unit& u, int wr, int wc, int fr, int fq) const {
;     ...
;             for (int m = 0; m < 4; ++m) { bf16_t* rowp = O + (size_t)u.ks * ks_stride + (size_t)(row0 + ai * HALF + m * 16) * ldc + col0;
; #pragma unroll
;                 for (int bj = 0; bj < 2; ++bj) { f32x4 v0 = acc[ai][bj][m][0] * ascale, v1 = acc[ai][bj][m][1] * ascale;
;                     if (act) {
; #pragma unroll
;                         for (int j = 0; j < 4; ++j) { v0[j] = gelu_tanh(v0[j]); v1[j] = gelu_tanh(v1[j]); } }
;                     u32x4 w; w.x = cvt_pk_bf16(v0[0], v0[1]); w.y = cvt_pk_bf16(v0[2], v0[3]); w.z = cvt_pk_bf16(v1[0], v1[1]); w.w = cvt_pk_bf16(v1[2], v1[3]);
;                     *(u32x4*)(rowp + bj * HALF) = w; } }
.LBB0_2056:
	v_lshlrev_b64 v[6:7], 12, v[4:5]
	v_lshl_add_u64 v[6:7], s[16:17], 0, v[6:7]
	v_lshl_add_u64 v[6:7], v[2:3], 1, v[6:7]
	v_cvt_pk_bf16_f32 v12, v12, v13
	v_cvt_pk_bf16_f32 v13, v8, v9
	v_add_co_u32_e32 v8, vcc, s67, v6
	v_cvt_pk_bf16_f32 v14, v14, v15
	v_cvt_pk_bf16_f32 v15, v10, v11
	v_pk_mul_f32 v[10:11], v[68:69], s[10:11] op_sel_hi:[1,0]
	s_nop 0
	v_addc_co_u32_e32 v9, vcc, 0, v7, vcc
	global_store_dwordx4 v[8:9], v[12:15], off sc0 sc1
	v_pk_mul_f32 v[8:9], v[72:73], s[10:11] op_sel_hi:[1,0]
	s_and_b64 vcc, exec, s[2:3]
	v_pk_mul_f32 v[12:13], v[70:71], s[10:11] op_sel_hi:[1,0]
	v_pk_mul_f32 v[14:15], v[66:67], s[10:11] op_sel_hi:[1,0]
	s_cbranch_vccnz .LBB0_2058
	v_mul_f32_e32 v17, 0x3d372713, v14
	v_mul_f32_e32 v17, v14, v17
	v_mul_f32_e32 v18, 0x3d372713, v13
	v_fma_f32 v17, v14, v17, v14
	v_mul_f32_e32 v18, v13, v18
	v_mov_b32_e32 v19, v13
	v_mul_f32_e32 v17, 0xc0135761, v17
	v_fmac_f32_e32 v19, v19, v18
	v_exp_f32_e32 v17, v17
	v_mul_f32_e32 v18, 0xc0135761, v19
	v_exp_f32_e32 v19, v18
	v_mul_f32_e32 v22, 0x3d372713, v9
	v_add_f32_e32 v17, 1.0, v17
	v_rcp_f32_e32 v18, v17
	v_add_f32_e32 v17, 1.0, v19
	v_mul_f32_e32 v19, 0x3d372713, v15
	v_mul_f32_e32 v22, v9, v22
	v_mul_f32_e32 v19, v15, v19
	v_mov_b32_e32 v20, v15
	v_fma_f32 v22, v9, v22, v9
	v_fmac_f32_e32 v20, v20, v19
	v_mul_f32_e32 v21, 0x3d372713, v10
	v_mul_f32_e32 v22, 0xc0135761, v22
	v_mul_f32_e32 v16, 0x3d372713, v12
	v_mul_f32_e32 v19, 0xc0135761, v20
	v_mul_f32_e32 v20, 0x3d372713, v8
	v_mul_f32_e32 v21, v10, v21
	v_exp_f32_e32 v23, v22
	v_mul_f32_e32 v22, 0x3d372713, v11
	v_mul_f32_e32 v16, v12, v16
	v_mul_f32_e32 v20, v8, v20
	v_fma_f32 v21, v10, v21, v10
	v_mul_f32_e32 v22, v11, v22
	v_fma_f32 v16, v12, v16, v12
	v_fma_f32 v20, v8, v20, v8
	v_mul_f32_e32 v21, 0xc0135761, v21
	v_fma_f32 v22, v11, v22, v11
	v_mul_f32_e32 v16, 0xc0135761, v16
	v_mul_f32_e32 v20, 0xc0135761, v20
	v_exp_f32_e32 v21, v21
	v_mul_f32_e32 v22, 0xc0135761, v22
	v_exp_f32_e32 v16, v16
	v_exp_f32_e32 v19, v19
	v_exp_f32_e32 v20, v20
	v_exp_f32_e32 v24, v22
	v_add_f32_e32 v21, 1.0, v21
	v_add_f32_e32 v16, 1.0, v16
	v_add_f32_e32 v19, 1.0, v19
	v_add_f32_e32 v20, 1.0, v20
	v_rcp_f32_e32 v22, v21
	v_add_f32_e32 v21, 1.0, v23
	v_add_f32_e32 v23, 1.0, v24
	v_rcp_f32_e32 v16, v16
	v_rcp_f32_e32 v17, v17
	v_rcp_f32_e32 v20, v20
	v_rcp_f32_e32 v21, v21
	v_rcp_f32_e32 v23, v23
	v_rcp_f32_e32 v19, v19
	v_pk_mul_f32 v[12:13], v[12:13], v[16:17]
	v_pk_mul_f32 v[8:9], v[8:9], v[20:21]
	v_pk_mul_f32 v[10:11], v[10:11], v[22:23]
	v_pk_mul_f32 v[14:15], v[14:15], v[18:19]
.LBB0_2058:
	v_lshl_add_u64 v[16:17], v[6:7], 0, s[28:29]
	v_cvt_pk_bf16_f32 v6, v12, v13
	v_cvt_pk_bf16_f32 v7, v8, v9
	v_cvt_pk_bf16_f32 v8, v14, v15
	v_cvt_pk_bf16_f32 v9, v10, v11
	global_store_dwordx4 v[16:17], v[6:9], off offset:256 sc0 sc1
	v_pk_mul_f32 v[12:13], v[62:63], s[10:11] op_sel_hi:[1,0]
	v_pk_mul_f32 v[10:11], v[60:61], s[10:11] op_sel_hi:[1,0]
	v_pk_mul_f32 v[8:9], v[64:65], s[10:11] op_sel_hi:[1,0]
	s_and_b64 vcc, exec, s[2:3]
	v_pk_mul_f32 v[14:15], v[58:59], s[10:11] op_sel_hi:[1,0]
	s_cbranch_vccnz .LBB0_2060
	v_mul_f32_e32 v7, 0x3d372713, v14
	v_mul_f32_e32 v7, v14, v7
	v_mul_f32_e32 v16, 0x3d372713, v13
	v_fma_f32 v7, v14, v7, v14
	v_mul_f32_e32 v16, v13, v16
	v_mov_b32_e32 v17, v13
	v_mul_f32_e32 v7, 0xc0135761, v7
	v_fmac_f32_e32 v17, v17, v16
	v_exp_f32_e32 v7, v7
	v_mul_f32_e32 v16, 0xc0135761, v17
	v_exp_f32_e32 v17, v16
	v_mul_f32_e32 v20, 0x3d372713, v9
	v_add_f32_e32 v7, 1.0, v7
	v_rcp_f32_e32 v16, v7
	v_add_f32_e32 v7, 1.0, v17
	v_mul_f32_e32 v17, 0x3d372713, v15
	v_mul_f32_e32 v20, v9, v20
	v_mul_f32_e32 v17, v15, v17
	v_mov_b32_e32 v18, v15
	v_fma_f32 v20, v9, v20, v9
	v_fmac_f32_e32 v18, v18, v17
	v_mul_f32_e32 v19, 0x3d372713, v10
	v_mul_f32_e32 v20, 0xc0135761, v20
	v_mul_f32_e32 v6, 0x3d372713, v12
	v_mul_f32_e32 v17, 0xc0135761, v18
	v_mul_f32_e32 v18, 0x3d372713, v8
	v_mul_f32_e32 v19, v10, v19
	v_exp_f32_e32 v21, v20
	v_mul_f32_e32 v20, 0x3d372713, v11
	v_mul_f32_e32 v6, v12, v6
	v_mul_f32_e32 v18, v8, v18
	v_fma_f32 v19, v10, v19, v10
	v_mul_f32_e32 v20, v11, v20
	v_fma_f32 v6, v12, v6, v12
	v_fma_f32 v18, v8, v18, v8
	v_mul_f32_e32 v19, 0xc0135761, v19
	v_fma_f32 v20, v11, v20, v11
	v_mul_f32_e32 v6, 0xc0135761, v6
	v_mul_f32_e32 v18, 0xc0135761, v18
	v_exp_f32_e32 v19, v19
	v_mul_f32_e32 v20, 0xc0135761, v20
	v_exp_f32_e32 v6, v6
	v_exp_f32_e32 v17, v17
	v_exp_f32_e32 v18, v18
	v_exp_f32_e32 v22, v20
	v_add_f32_e32 v19, 1.0, v19
	v_add_f32_e32 v6, 1.0, v6
	v_add_f32_e32 v17, 1.0, v17
	v_add_f32_e32 v18, 1.0, v18
	v_rcp_f32_e32 v20, v19
	v_add_f32_e32 v19, 1.0, v21
	v_add_f32_e32 v21, 1.0, v22
	v_rcp_f32_e32 v6, v6
	v_rcp_f32_e32 v7, v7
	v_rcp_f32_e32 v18, v18
	v_rcp_f32_e32 v19, v19
	v_rcp_f32_e32 v21, v21
	v_rcp_f32_e32 v17, v17
	v_pk_mul_f32 v[12:13], v[12:13], v[6:7]
	v_pk_mul_f32 v[8:9], v[8:9], v[18:19]
	v_pk_mul_f32 v[10:11], v[10:11], v[20:21]
	v_pk_mul_f32 v[14:15], v[14:15], v[16:17]
; __device__ __forceinline__ unsigned cvt_pk_bf16(float lo, float hi) { unsigned r; asm volatile("v_cvt_pk_bf16_f32 %0, %1, %2" : "=v"(r) : "v"(lo), "v"(hi)); return r; }
; __device__ __forceinline__ float gelu_tanh(float x) { const float y = x + 0.044715f * x * x * x; return x * __builtin_amdgcn_rcpf(1.0f + __builtin_amdgcn_exp2f(-2.302208198f * y)); }
;     __device__ __forceinline__ void operator()(const f32x4 (&acc)[2][2][4][2], const Unit& u, int wr, int wc, int fr, int fq) const {
;     ...
;             for (int m = 0; m < 4; ++m) { bf16_t* rowp = O + (size_t)u.ks * ks_stride + (size_t)(row0 + ai * HALF + m * 16) * ldc + col0;
; #pragma unroll
;                 for (int bj = 0; bj < 2; ++bj) { f32x4 v0 = acc[ai][bj][m][0] * ascale, v1 = acc[ai][bj][m][1] * ascale;
;                     if (act) {
; #pragma unroll
;                         for (int j = 0; j < 4; ++j) { v0[j] = gelu_tanh(v0[j]); v1[j] = gelu_tanh(v1[j]); } }
;                     u32x4 w; w.x = cvt_pk_bf16(v0[0], v0[1]); w.y = cvt_pk_bf16(v0[2], v0[3]); w.z = cvt_pk_bf16(v1[0], v1[1]); w.w = cvt_pk_bf16(v1[2], v1[3]);
;                     *(u32x4*)(rowp + bj * HALF) = w; } }
.LBB0_2060:
	v_lshlrev_b64 v[6:7], 12, v[4:5]
	v_lshl_add_u64 v[6:7], s[16:17], 0, v[6:7]
	v_lshl_add_u64 v[6:7], v[2:3], 1, v[6:7]
	v_cvt_pk_bf16_f32 v12, v12, v13
	v_cvt_pk_bf16_f32 v13, v8, v9
	v_add_co_u32_e32 v8, vcc, s68, v6
	v_cvt_pk_bf16_f32 v14, v14, v15
	v_cvt_pk_bf16_f32 v15, v10, v11
	v_pk_mul_f32 v[10:11], v[52:53], s[10:11] op_sel_hi:[1,0]
	s_nop 0
	v_addc_co_u32_e32 v9, vcc, 0, v7, vcc
	global_store_dwordx4 v[8:9], v[12:15], off sc0 sc1
	v_pk_mul_f32 v[8:9], v[56:57], s[10:11] op_sel_hi:[1,0]
	s_and_b64 vcc, exec, s[2:3]
	v_pk_mul_f32 v[12:13], v[54:55], s[10:11] op_sel_hi:[1,0]
	v_pk_mul_f32 v[14:15], v[50:51], s[10:11] op_sel_hi:[1,0]
	s_cbranch_vccnz .LBB0_2062
	v_mul_f32_e32 v17, 0x3d372713, v14
	v_mul_f32_e32 v17, v14, v17
	v_mul_f32_e32 v18, 0x3d372713, v13
	v_fma_f32 v17, v14, v17, v14
	v_mul_f32_e32 v18, v13, v18
	v_mov_b32_e32 v19, v13
	v_mul_f32_e32 v17, 0xc0135761, v17
	v_fmac_f32_e32 v19, v19, v18
	v_exp_f32_e32 v17, v17
	v_mul_f32_e32 v18, 0xc0135761, v19
	v_exp_f32_e32 v19, v18
	v_mul_f32_e32 v22, 0x3d372713, v9
	v_add_f32_e32 v17, 1.0, v17
	v_rcp_f32_e32 v18, v17
	v_add_f32_e32 v17, 1.0, v19
	v_mul_f32_e32 v19, 0x3d372713, v15
	v_mul_f32_e32 v22, v9, v22
	v_mul_f32_e32 v19, v15, v19
	v_mov_b32_e32 v20, v15
	v_fma_f32 v22, v9, v22, v9
	v_fmac_f32_e32 v20, v20, v19
	v_mul_f32_e32 v21, 0x3d372713, v10
	v_mul_f32_e32 v22, 0xc0135761, v22
	v_mul_f32_e32 v16, 0x3d372713, v12
	v_mul_f32_e32 v19, 0xc0135761, v20
	v_mul_f32_e32 v20, 0x3d372713, v8
	v_mul_f32_e32 v21, v10, v21
	v_exp_f32_e32 v23, v22
	v_mul_f32_e32 v22, 0x3d372713, v11
	v_mul_f32_e32 v16, v12, v16
	v_mul_f32_e32 v20, v8, v20
	v_fma_f32 v21, v10, v21, v10
	v_mul_f32_e32 v22, v11, v22
	v_fma_f32 v16, v12, v16, v12
	v_fma_f32 v20, v8, v20, v8
	v_mul_f32_e32 v21, 0xc0135761, v21
	v_fma_f32 v22, v11, v22, v11
	v_mul_f32_e32 v16, 0xc0135761, v16
	v_mul_f32_e32 v20, 0xc0135761, v20
	v_exp_f32_e32 v21, v21
	v_mul_f32_e32 v22, 0xc0135761, v22
	v_exp_f32_e32 v16, v16
	v_exp_f32_e32 v19, v19
	v_exp_f32_e32 v20, v20
	v_exp_f32_e32 v24, v22
	v_add_f32_e32 v21, 1.0, v21
	v_add_f32_e32 v16, 1.0, v16
	v_add_f32_e32 v19, 1.0, v19
	v_add_f32_e32 v20, 1.0, v20
	v_rcp_f32_e32 v22, v21
	v_add_f32_e32 v21, 1.0, v23
	v_add_f32_e32 v23, 1.0, v24
	v_rcp_f32_e32 v16, v16
	v_rcp_f32_e32 v17, v17
	v_rcp_f32_e32 v20, v20
	v_rcp_f32_e32 v21, v21
	v_rcp_f32_e32 v23, v23
	v_rcp_f32_e32 v19, v19
	v_pk_mul_f32 v[12:13], v[12:13], v[16:17]
	v_pk_mul_f32 v[8:9], v[8:9], v[20:21]
	v_pk_mul_f32 v[10:11], v[10:11], v[22:23]
	v_pk_mul_f32 v[14:15], v[14:15], v[18:19]
.LBB0_2062:
	v_lshl_add_u64 v[16:17], v[6:7], 0, s[30:31]
	v_cvt_pk_bf16_f32 v6, v12, v13
	v_cvt_pk_bf16_f32 v7, v8, v9
	v_cvt_pk_bf16_f32 v8, v14, v15
	v_cvt_pk_bf16_f32 v9, v10, v11
	global_store_dwordx4 v[16:17], v[6:9], off offset:256 sc0 sc1
	v_pk_mul_f32 v[10:11], v[46:47], s[10:11] op_sel_hi:[1,0]
	s_and_b64 vcc, exec, s[2:3]
	v_pk_mul_f32 v[6:7], v[48:49], s[10:11] op_sel_hi:[1,0]
	v_pk_mul_f32 v[8:9], v[44:45], s[10:11] op_sel_hi:[1,0]
	v_pk_mul_f32 v[12:13], v[42:43], s[10:11] op_sel_hi:[1,0]
	s_cbranch_vccnz .LBB0_2064
	v_mul_f32_e32 v15, 0x3d372713, v12
	v_mul_f32_e32 v15, v12, v15
	v_mul_f32_e32 v16, 0x3d372713, v11
	v_fma_f32 v15, v12, v15, v12
	v_mul_f32_e32 v16, v11, v16
	v_mov_b32_e32 v17, v11
	v_mul_f32_e32 v15, 0xc0135761, v15
	v_fmac_f32_e32 v17, v17, v16
	v_exp_f32_e32 v15, v15
	v_mul_f32_e32 v16, 0xc0135761, v17
	v_exp_f32_e32 v17, v16
	v_mul_f32_e32 v20, 0x3d372713, v7
	v_add_f32_e32 v15, 1.0, v15
	v_rcp_f32_e32 v16, v15
	v_add_f32_e32 v15, 1.0, v17
	v_mul_f32_e32 v17, 0x3d372713, v13
	v_mul_f32_e32 v20, v7, v20
	v_mul_f32_e32 v17, v13, v17
	v_mov_b32_e32 v18, v13
	v_fma_f32 v20, v7, v20, v7
	v_fmac_f32_e32 v18, v18, v17
	v_mul_f32_e32 v19, 0x3d372713, v8
	v_mul_f32_e32 v20, 0xc0135761, v20
	v_mul_f32_e32 v14, 0x3d372713, v10
	v_mul_f32_e32 v17, 0xc0135761, v18
	v_mul_f32_e32 v18, 0x3d372713, v6
	v_mul_f32_e32 v19, v8, v19
	v_exp_f32_e32 v21, v20
	v_mul_f32_e32 v20, 0x3d372713, v9
	v_mul_f32_e32 v14, v10, v14
	v_mul_f32_e32 v18, v6, v18
	v_fma_f32 v19, v8, v19, v8
	v_mul_f32_e32 v20, v9, v20
	v_fma_f32 v14, v10, v14, v10
	v_fma_f32 v18, v6, v18, v6
	v_mul_f32_e32 v19, 0xc0135761, v19
	v_fma_f32 v20, v9, v20, v9
	v_mul_f32_e32 v14, 0xc0135761, v14
	v_mul_f32_e32 v18, 0xc0135761, v18
	v_exp_f32_e32 v19, v19
	v_mul_f32_e32 v20, 0xc0135761, v20
	v_exp_f32_e32 v14, v14
	v_exp_f32_e32 v17, v17
	v_exp_f32_e32 v18, v18
	v_exp_f32_e32 v22, v20
	v_add_f32_e32 v19, 1.0, v19
	v_add_f32_e32 v14, 1.0, v14
	v_add_f32_e32 v17, 1.0, v17
	v_add_f32_e32 v18, 1.0, v18
	v_rcp_f32_e32 v20, v19
	v_add_f32_e32 v19, 1.0, v21
	v_add_f32_e32 v21, 1.0, v22
	v_rcp_f32_e32 v14, v14
	v_rcp_f32_e32 v15, v15
	v_rcp_f32_e32 v18, v18
	v_rcp_f32_e32 v19, v19
	v_rcp_f32_e32 v21, v21
	v_rcp_f32_e32 v17, v17
	v_pk_mul_f32 v[10:11], v[10:11], v[14:15]
	v_pk_mul_f32 v[6:7], v[6:7], v[18:19]
	v_pk_mul_f32 v[8:9], v[8:9], v[20:21]
	v_pk_mul_f32 v[12:13], v[12:13], v[16:17]
; __device__ __forceinline__ unsigned cvt_pk_bf16(float lo, float hi) { unsigned r; asm volatile("v_cvt_pk_bf16_f32 %0, %1, %2" : "=v"(r) : "v"(lo), "v"(hi)); return r; }
; __device__ __forceinline__ float gelu_tanh(float x) { const float y = x + 0.044715f * x * x * x; return x * __builtin_amdgcn_rcpf(1.0f + __builtin_amdgcn_exp2f(-2.302208198f * y)); }
; #define PG8_BAR __builtin_amdgcn_s_barrier()
;     __device__ __forceinline__ void operator()(const f32x4 (&acc)[2][2][4][2], const Unit& u, int wr, int wc, int fr, int fq) const {
;     ...
;             for (int m = 0; m < 4; ++m) { bf16_t* rowp = O + (size_t)u.ks * ks_stride + (size_t)(row0 + ai * HALF + m * 16) * ldc + col0;
; #pragma unroll
;                 for (int bj = 0; bj < 2; ++bj) { f32x4 v0 = acc[ai][bj][m][0] * ascale, v1 = acc[ai][bj][m][1] * ascale;
;                     if (act) {
; #pragma unroll
;                         for (int j = 0; j < 4; ++j) { v0[j] = gelu_tanh(v0[j]); v1[j] = gelu_tanh(v1[j]); } }
;                     u32x4 w; w.x = cvt_pk_bf16(v0[0], v0[1]); w.y = cvt_pk_bf16(v0[2], v0[3]); w.z = cvt_pk_bf16(v1[0], v1[1]); w.w = cvt_pk_bf16(v1[2], v1[3]);
;                     *(u32x4*)(rowp + bj * HALF) = w; } }
; template <class Epi, class Sched, bool ALIGN_EPI = false, bool SP2 = false, bool FP8 = false>
; __device__ __forceinline__ void gemm_phase(PG8_LAS unsigned char* lds, const Gemm g, const Sched& S, const Epi& E) {
;     ...
;         if constexpr (!Epi::AFTER_DRAIN) { E(acc, cur, wr, wc, fr, fq); S.done(cur); }
;         if (!has_next) break;
; #pragma unroll
;         for (int a = 0; a < 2; ++a)
; #pragma unroll
;             for (int b = 0; b < 2; ++b)
; #pragma unroll
;                 for (int m = 0; m < 4; ++m)
; #pragma unroll
;                     for (int n = 0; n < 2; ++n) acc[a][b][m][n] = (f32x4){0.f, 0.f, 0.f, 0.f};
;         cur = nxt; cA = nA; cB = nB; ++ui;
;         if constexpr (ALIGN_EPI) { if (wr == 1) PG8_BAR; }
.LBB0_2064:
	v_lshlrev_b64 v[4:5], 12, v[4:5]
	v_lshl_add_u64 v[4:5], s[16:17], 0, v[4:5]
	v_lshl_add_u64 v[2:3], v[2:3], 1, v[4:5]
	v_cvt_pk_bf16_f32 v4, v10, v11
	v_cvt_pk_bf16_f32 v5, v6, v7
	v_cvt_pk_bf16_f32 v6, v12, v13
	v_cvt_pk_bf16_f32 v7, v8, v9
	v_add_co_u32_e32 v8, vcc, s69, v2
	v_pk_mul_f32 v[10:11], v[34:35], s[10:11] op_sel_hi:[1,0]
	s_nop 0
	v_addc_co_u32_e32 v9, vcc, 0, v3, vcc
	global_store_dwordx4 v[8:9], v[4:7], off sc0 sc1
	v_pk_mul_f32 v[8:9], v[38:39], s[10:11] op_sel_hi:[1,0]
	s_and_b64 vcc, exec, s[2:3]
	v_pk_mul_f32 v[4:5], v[40:41], s[10:11] op_sel_hi:[1,0]
	v_pk_mul_f32 v[6:7], v[36:37], s[10:11] op_sel_hi:[1,0]
	s_cbranch_vccnz .LBB0_2066
	v_mul_f32_e32 v13, 0x3d372713, v10
	v_mul_f32_e32 v13, v10, v13
	v_mul_f32_e32 v14, 0x3d372713, v9
	v_fma_f32 v13, v10, v13, v10
	v_mul_f32_e32 v14, v9, v14
	v_mov_b32_e32 v15, v9
	v_mul_f32_e32 v13, 0xc0135761, v13
	v_fmac_f32_e32 v15, v15, v14
	v_exp_f32_e32 v13, v13
	v_mul_f32_e32 v14, 0xc0135761, v15
	v_exp_f32_e32 v15, v14
	v_mul_f32_e32 v18, 0x3d372713, v5
	v_add_f32_e32 v13, 1.0, v13
	v_rcp_f32_e32 v14, v13
	v_add_f32_e32 v13, 1.0, v15
	v_mul_f32_e32 v15, 0x3d372713, v11
	v_mul_f32_e32 v18, v5, v18
	v_mul_f32_e32 v15, v11, v15
	v_mov_b32_e32 v16, v11
	v_fma_f32 v18, v5, v18, v5
	v_fmac_f32_e32 v16, v16, v15
	v_mul_f32_e32 v17, 0x3d372713, v6
	v_mul_f32_e32 v18, 0xc0135761, v18
	v_mul_f32_e32 v12, 0x3d372713, v8
	v_mul_f32_e32 v15, 0xc0135761, v16
	v_mul_f32_e32 v16, 0x3d372713, v4
	v_mul_f32_e32 v17, v6, v17
	v_exp_f32_e32 v19, v18
	v_mul_f32_e32 v18, 0x3d372713, v7
	v_mul_f32_e32 v12, v8, v12
	v_mul_f32_e32 v16, v4, v16
	v_fma_f32 v17, v6, v17, v6
	v_mul_f32_e32 v18, v7, v18
	v_fma_f32 v12, v8, v12, v8
	v_fma_f32 v16, v4, v16, v4
	v_mul_f32_e32 v17, 0xc0135761, v17
	v_fma_f32 v18, v7, v18, v7
	v_mul_f32_e32 v12, 0xc0135761, v12
	v_mul_f32_e32 v16, 0xc0135761, v16
	v_exp_f32_e32 v17, v17
	v_mul_f32_e32 v18, 0xc0135761, v18
	v_exp_f32_e32 v12, v12
	v_exp_f32_e32 v15, v15
	v_exp_f32_e32 v16, v16
	v_exp_f32_e32 v20, v18
	v_add_f32_e32 v17, 1.0, v17
	v_add_f32_e32 v12, 1.0, v12
	v_add_f32_e32 v15, 1.0, v15
	v_add_f32_e32 v16, 1.0, v16
	v_rcp_f32_e32 v18, v17
	v_add_f32_e32 v17, 1.0, v19
	v_add_f32_e32 v19, 1.0, v20
	v_rcp_f32_e32 v12, v12
	v_rcp_f32_e32 v13, v13
	v_rcp_f32_e32 v16, v16
	v_rcp_f32_e32 v17, v17
	v_rcp_f32_e32 v19, v19
	v_rcp_f32_e32 v15, v15
	v_pk_mul_f32 v[8:9], v[8:9], v[12:13]
	v_pk_mul_f32 v[4:5], v[4:5], v[16:17]
	v_pk_mul_f32 v[6:7], v[6:7], v[18:19]
	v_pk_mul_f32 v[10:11], v[10:11], v[14:15]
.LBB0_2066:
	v_lshl_add_u64 v[12:13], v[2:3], 0, s[34:35]
	s_and_b64 vcc, exec, s[0:1]
	s_mov_b64 s[0:1], -1
	v_cvt_pk_bf16_f32 v2, v8, v9
	v_cvt_pk_bf16_f32 v3, v4, v5
	v_cvt_pk_bf16_f32 v4, v10, v11
	v_cvt_pk_bf16_f32 v5, v6, v7
	global_store_dwordx4 v[12:13], v[2:5], off offset:256 sc0 sc1
	s_cbranch_vccnz .LBB0_2019
	s_andn2_b64 vcc, exec, s[14:15]
	s_cbranch_vccnz .LBB0_2018
	s_barrier
	s_branch .LBB0_2018

; __device__ __forceinline__ unsigned cvt_pk_bf16(float lo, float hi) { unsigned r; asm volatile("v_cvt_pk_bf16_f32 %0, %1, %2" : "=v"(r) : "v"(lo), "v"(hi)); return r; }
; __device__ __forceinline__ float gelu_tanh(float x) { const float y = x + 0.044715f * x * x * x; return x * __builtin_amdgcn_rcpf(1.0f + __builtin_amdgcn_exp2f(-2.302208198f * y)); }
;     __device__ __forceinline__ void operator()(const f32x4 (&acc)[2][2][4][2], const Unit& u, int wr, int wc, int fr, int fq) const {
;         const int row0 = u.pm * BM + wr * 64 + fr, col0 = u.pn * BM + wc * 32 + 8 * fq; const bool act = u.pn < nact;
; #pragma unroll
;         for (int ai = 0; ai < 2; ++ai)
; #pragma unroll
;             for (int m = 0; m < 4; ++m) { bf16_t* rowp = O + (size_t)u.ks * ks_stride + (size_t)(row0 + ai * HALF + m * 16) * ldc + col0;
; #pragma unroll
;                 for (int bj = 0; bj < 2; ++bj) { f32x4 v0 = acc[ai][bj][m][0] * ascale, v1 = acc[ai][bj][m][1] * ascale;
;                     if (act) {
; #pragma unroll
;                         for (int j = 0; j < 4; ++j) { v0[j] = gelu_tanh(v0[j]); v1[j] = gelu_tanh(v1[j]); } }
;                     u32x4 w; w.x = cvt_pk_bf16(v0[0], v0[1]); w.y = cvt_pk_bf16(v0[2], v0[3]); w.z = cvt_pk_bf16(v1[0], v1[1]); w.w = cvt_pk_bf16(v1[2], v1[3]);
;                     *(u32x4*)(rowp + bj * HALF) = w; } }
.LBB0_2098:
	s_ashr_i32 s37, s36, 31
	v_lshl_add_u32 v4, s74, 8, v1
	s_lshl_b64 s[2:3], s[36:37], 23
	s_add_u32 s36, s55, s2
	v_ashrrev_i32_e32 v5, 31, v4
	v_lshl_or_b32 v2, s75, 8, v192
	s_addc_u32 s37, s56, s3
	v_lshlrev_b64 v[6:7], 12, v[4:5]
	v_ashrrev_i32_e32 v3, 31, v2
	v_lshl_add_u64 v[6:7], s[36:37], 0, v[6:7]
	v_lshl_add_u64 v[6:7], v[2:3], 1, v[6:7]
	v_cvt_pk_bf16_f32 v12, v12, v13
	v_cvt_pk_bf16_f32 v13, v8, v9
	v_cvt_pk_bf16_f32 v14, v14, v15
	v_cvt_pk_bf16_f32 v15, v10, v11
	global_store_dwordx4 v[6:7], v[12:15], off sc0 sc1
	v_pk_mul_f32 v[8:9], v[152:153], s[20:21] op_sel_hi:[1,0]
	v_pk_mul_f32 v[10:11], v[148:149], s[20:21] op_sel_hi:[1,0]
	v_cndmask_b32_e64 v14, 0, 1, s[38:39]
	v_pk_mul_f32 v[12:13], v[150:151], s[20:21] op_sel_hi:[1,0]
	v_cmp_ne_u32_e64 s[2:3], 1, v14
	s_andn2_b64 vcc, exec, s[38:39]
	v_pk_mul_f32 v[14:15], v[146:147], s[20:21] op_sel_hi:[1,0]
	s_cbranch_vccnz .LBB0_2100
	v_mul_f32_e32 v17, 0x3d372713, v14
	v_mul_f32_e32 v17, v14, v17
	v_mul_f32_e32 v18, 0x3d372713, v13
	v_fma_f32 v17, v14, v17, v14
	v_mul_f32_e32 v18, v13, v18
	v_mov_b32_e32 v19, v13
	v_mul_f32_e32 v17, 0xc0135761, v17
	v_fmac_f32_e32 v19, v19, v18
	v_exp_f32_e32 v17, v17
	v_mul_f32_e32 v18, 0xc0135761, v19
	v_exp_f32_e32 v19, v18
	v_mul_f32_e32 v22, 0x3d372713, v9
	v_add_f32_e32 v17, 1.0, v17
	v_rcp_f32_e32 v18, v17
	v_add_f32_e32 v17, 1.0, v19
	v_mul_f32_e32 v19, 0x3d372713, v15
	v_mul_f32_e32 v22, v9, v22
	v_mul_f32_e32 v19, v15, v19
	v_mov_b32_e32 v20, v15
	v_fma_f32 v22, v9, v22, v9
	v_fmac_f32_e32 v20, v20, v19
	v_mul_f32_e32 v21, 0x3d372713, v10
	v_mul_f32_e32 v22, 0xc0135761, v22
	v_mul_f32_e32 v16, 0x3d372713, v12
	v_mul_f32_e32 v19, 0xc0135761, v20
	v_mul_f32_e32 v20, 0x3d372713, v8
	v_mul_f32_e32 v21, v10, v21
	v_exp_f32_e32 v23, v22
	v_mul_f32_e32 v22, 0x3d372713, v11
	v_mul_f32_e32 v16, v12, v16
	v_mul_f32_e32 v20, v8, v20
	v_fma_f32 v21, v10, v21, v10
	v_mul_f32_e32 v22, v11, v22
	v_fma_f32 v16, v12, v16, v12
	v_fma_f32 v20, v8, v20, v8
	v_mul_f32_e32 v21, 0xc0135761, v21
	v_fma_f32 v22, v11, v22, v11
	v_mul_f32_e32 v16, 0xc0135761, v16
	v_mul_f32_e32 v20, 0xc0135761, v20
	v_exp_f32_e32 v21, v21
	v_mul_f32_e32 v22, 0xc0135761, v22
	v_exp_f32_e32 v16, v16
	v_exp_f32_e32 v19, v19
	v_exp_f32_e32 v20, v20
	v_exp_f32_e32 v24, v22
	v_add_f32_e32 v21, 1.0, v21
	v_add_f32_e32 v16, 1.0, v16
	v_add_f32_e32 v19, 1.0, v19
	v_add_f32_e32 v20, 1.0, v20
	v_rcp_f32_e32 v22, v21
	v_add_f32_e32 v21, 1.0, v23
	v_add_f32_e32 v23, 1.0, v24
	v_rcp_f32_e32 v16, v16
	v_rcp_f32_e32 v17, v17
	v_rcp_f32_e32 v20, v20
	v_rcp_f32_e32 v21, v21
	v_rcp_f32_e32 v23, v23
	v_rcp_f32_e32 v19, v19
	v_pk_mul_f32 v[12:13], v[12:13], v[16:17]
	v_pk_mul_f32 v[8:9], v[8:9], v[20:21]
	v_pk_mul_f32 v[10:11], v[10:11], v[22:23]
	v_pk_mul_f32 v[14:15], v[14:15], v[18:19]
.LBB0_2100:
	v_cvt_pk_bf16_f32 v12, v12, v13
	v_cvt_pk_bf16_f32 v13, v8, v9
	s_nop 0
	v_cvt_pk_bf16_f32 v14, v14, v15
	v_cvt_pk_bf16_f32 v15, v10, v11
	global_store_dwordx4 v[6:7], v[12:15], off offset:256 sc0 sc1
	v_pk_mul_f32 v[8:9], v[144:145], s[20:21] op_sel_hi:[1,0]
	v_pk_mul_f32 v[10:11], v[140:141], s[20:21] op_sel_hi:[1,0]
	v_pk_mul_f32 v[12:13], v[142:143], s[20:21] op_sel_hi:[1,0]
	s_and_b64 vcc, exec, s[2:3]
	v_pk_mul_f32 v[14:15], v[138:139], s[20:21] op_sel_hi:[1,0]
	s_cbranch_vccnz .LBB0_2102
	v_mul_f32_e32 v7, 0x3d372713, v14
	v_mul_f32_e32 v7, v14, v7
	v_mul_f32_e32 v16, 0x3d372713, v13
	v_fma_f32 v7, v14, v7, v14
	v_mul_f32_e32 v16, v13, v16
	v_mov_b32_e32 v17, v13
	v_mul_f32_e32 v7, 0xc0135761, v7
	v_fmac_f32_e32 v17, v17, v16
	v_exp_f32_e32 v7, v7
	v_mul_f32_e32 v16, 0xc0135761, v17
	v_exp_f32_e32 v17, v16
	v_mul_f32_e32 v20, 0x3d372713, v9
	v_add_f32_e32 v7, 1.0, v7
	v_rcp_f32_e32 v16, v7
	v_add_f32_e32 v7, 1.0, v17
	v_mul_f32_e32 v17, 0x3d372713, v15
	v_mul_f32_e32 v20, v9, v20
	v_mul_f32_e32 v17, v15, v17
	v_mov_b32_e32 v18, v15
	v_fma_f32 v20, v9, v20, v9
	v_fmac_f32_e32 v18, v18, v17
	v_mul_f32_e32 v19, 0x3d372713, v10
	v_mul_f32_e32 v20, 0xc0135761, v20
	v_mul_f32_e32 v6, 0x3d372713, v12
	v_mul_f32_e32 v17, 0xc0135761, v18
	v_mul_f32_e32 v18, 0x3d372713, v8
	v_mul_f32_e32 v19, v10, v19
	v_exp_f32_e32 v21, v20
	v_mul_f32_e32 v20, 0x3d372713, v11
	v_mul_f32_e32 v6, v12, v6
	v_mul_f32_e32 v18, v8, v18
	v_fma_f32 v19, v10, v19, v10
	v_mul_f32_e32 v20, v11, v20
	v_fma_f32 v6, v12, v6, v12
	v_fma_f32 v18, v8, v18, v8
	v_mul_f32_e32 v19, 0xc0135761, v19
	v_fma_f32 v20, v11, v20, v11
	v_mul_f32_e32 v6, 0xc0135761, v6
	v_mul_f32_e32 v18, 0xc0135761, v18
	v_exp_f32_e32 v19, v19
	v_mul_f32_e32 v20, 0xc0135761, v20
	v_exp_f32_e32 v6, v6
	v_exp_f32_e32 v17, v17
	v_exp_f32_e32 v18, v18
	v_exp_f32_e32 v22, v20
	v_add_f32_e32 v19, 1.0, v19
	v_add_f32_e32 v6, 1.0, v6
	v_add_f32_e32 v17, 1.0, v17
	v_add_f32_e32 v18, 1.0, v18
	v_rcp_f32_e32 v20, v19
	v_add_f32_e32 v19, 1.0, v21
	v_add_f32_e32 v21, 1.0, v22
	v_rcp_f32_e32 v6, v6
	v_rcp_f32_e32 v7, v7
	v_rcp_f32_e32 v18, v18
	v_rcp_f32_e32 v19, v19
	v_rcp_f32_e32 v21, v21
	v_rcp_f32_e32 v17, v17
	v_pk_mul_f32 v[12:13], v[12:13], v[6:7]
	v_pk_mul_f32 v[8:9], v[8:9], v[18:19]
	v_pk_mul_f32 v[10:11], v[10:11], v[20:21]
	v_pk_mul_f32 v[14:15], v[14:15], v[16:17]
; __device__ __forceinline__ unsigned cvt_pk_bf16(float lo, float hi) { unsigned r; asm volatile("v_cvt_pk_bf16_f32 %0, %1, %2" : "=v"(r) : "v"(lo), "v"(hi)); return r; }
; __device__ __forceinline__ float gelu_tanh(float x) { const float y = x + 0.044715f * x * x * x; return x * __builtin_amdgcn_rcpf(1.0f + __builtin_amdgcn_exp2f(-2.302208198f * y)); }
;     __device__ __forceinline__ void operator()(const f32x4 (&acc)[2][2][4][2], const Unit& u, int wr, int wc, int fr, int fq) const {
;     ...
;             for (int m = 0; m < 4; ++m) { bf16_t* rowp = O + (size_t)u.ks * ks_stride + (size_t)(row0 + ai * HALF + m * 16) * ldc + col0;
; #pragma unroll
;                 for (int bj = 0; bj < 2; ++bj) { f32x4 v0 = acc[ai][bj][m][0] * ascale, v1 = acc[ai][bj][m][1] * ascale;
;                     if (act) {
; #pragma unroll
;                         for (int j = 0; j < 4; ++j) { v0[j] = gelu_tanh(v0[j]); v1[j] = gelu_tanh(v1[j]); } }
;                     u32x4 w; w.x = cvt_pk_bf16(v0[0], v0[1]); w.y = cvt_pk_bf16(v0[2], v0[3]); w.z = cvt_pk_bf16(v1[0], v1[1]); w.w = cvt_pk_bf16(v1[2], v1[3]);
;                     *(u32x4*)(rowp + bj * HALF) = w; } }
.LBB0_2102:
	v_or_b32_e32 v6, 16, v4
	v_ashrrev_i32_e32 v7, 31, v6
	v_lshlrev_b64 v[6:7], 12, v[6:7]
	v_lshl_add_u64 v[6:7], s[36:37], 0, v[6:7]
	v_lshl_add_u64 v[6:7], v[2:3], 1, v[6:7]
	v_cvt_pk_bf16_f32 v12, v12, v13
	v_cvt_pk_bf16_f32 v13, v8, v9
	v_cvt_pk_bf16_f32 v14, v14, v15
	v_cvt_pk_bf16_f32 v15, v10, v11
	global_store_dwordx4 v[6:7], v[12:15], off sc0 sc1
	v_pk_mul_f32 v[8:9], v[136:137], s[20:21] op_sel_hi:[1,0]
	v_pk_mul_f32 v[10:11], v[132:133], s[20:21] op_sel_hi:[1,0]
	v_pk_mul_f32 v[12:13], v[134:135], s[20:21] op_sel_hi:[1,0]
	s_and_b64 vcc, exec, s[2:3]
	v_pk_mul_f32 v[14:15], v[130:131], s[20:21] op_sel_hi:[1,0]
	s_cbranch_vccnz .LBB0_2104
	v_mul_f32_e32 v17, 0x3d372713, v14
	v_mul_f32_e32 v17, v14, v17
	v_mul_f32_e32 v18, 0x3d372713, v13
	v_fma_f32 v17, v14, v17, v14
	v_mul_f32_e32 v18, v13, v18
	v_mov_b32_e32 v19, v13
	v_mul_f32_e32 v17, 0xc0135761, v17
	v_fmac_f32_e32 v19, v19, v18
	v_exp_f32_e32 v17, v17
	v_mul_f32_e32 v18, 0xc0135761, v19
	v_exp_f32_e32 v19, v18
	v_mul_f32_e32 v22, 0x3d372713, v9
	v_add_f32_e32 v17, 1.0, v17
	v_rcp_f32_e32 v18, v17
	v_add_f32_e32 v17, 1.0, v19
	v_mul_f32_e32 v19, 0x3d372713, v15
	v_mul_f32_e32 v22, v9, v22
	v_mul_f32_e32 v19, v15, v19
	v_mov_b32_e32 v20, v15
	v_fma_f32 v22, v9, v22, v9
	v_fmac_f32_e32 v20, v20, v19
	v_mul_f32_e32 v21, 0x3d372713, v10
	v_mul_f32_e32 v22, 0xc0135761, v22
	v_mul_f32_e32 v16, 0x3d372713, v12
	v_mul_f32_e32 v19, 0xc0135761, v20
	v_mul_f32_e32 v20, 0x3d372713, v8
	v_mul_f32_e32 v21, v10, v21
	v_exp_f32_e32 v23, v22
	v_mul_f32_e32 v22, 0x3d372713, v11
	v_mul_f32_e32 v16, v12, v16
	v_mul_f32_e32 v20, v8, v20
	v_fma_f32 v21, v10, v21, v10
	v_mul_f32_e32 v22, v11, v22
	v_fma_f32 v16, v12, v16, v12
	v_fma_f32 v20, v8, v20, v8
	v_mul_f32_e32 v21, 0xc0135761, v21
	v_fma_f32 v22, v11, v22, v11
	v_mul_f32_e32 v16, 0xc0135761, v16
	v_mul_f32_e32 v20, 0xc0135761, v20
	v_exp_f32_e32 v21, v21
	v_mul_f32_e32 v22, 0xc0135761, v22
	v_exp_f32_e32 v16, v16
	v_exp_f32_e32 v19, v19
	v_exp_f32_e32 v20, v20
	v_exp_f32_e32 v24, v22
	v_add_f32_e32 v21, 1.0, v21
	v_add_f32_e32 v16, 1.0, v16
	v_add_f32_e32 v19, 1.0, v19
	v_add_f32_e32 v20, 1.0, v20
	v_rcp_f32_e32 v22, v21
	v_add_f32_e32 v21, 1.0, v23
	v_add_f32_e32 v23, 1.0, v24
	v_rcp_f32_e32 v16, v16
	v_rcp_f32_e32 v17, v17
	v_rcp_f32_e32 v20, v20
	v_rcp_f32_e32 v21, v21
	v_rcp_f32_e32 v23, v23
	v_rcp_f32_e32 v19, v19
	v_pk_mul_f32 v[12:13], v[12:13], v[16:17]
	v_pk_mul_f32 v[8:9], v[8:9], v[20:21]
	v_pk_mul_f32 v[10:11], v[10:11], v[22:23]
	v_pk_mul_f32 v[14:15], v[14:15], v[18:19]
.LBB0_2104:
	v_cvt_pk_bf16_f32 v12, v12, v13
	v_cvt_pk_bf16_f32 v13, v8, v9
	s_nop 0
	v_cvt_pk_bf16_f32 v14, v14, v15
	v_cvt_pk_bf16_f32 v15, v10, v11
	global_store_dwordx4 v[6:7], v[12:15], off offset:256 sc0 sc1
	v_pk_mul_f32 v[8:9], v[128:129], s[20:21] op_sel_hi:[1,0]
	v_pk_mul_f32 v[10:11], v[124:125], s[20:21] op_sel_hi:[1,0]
	v_pk_mul_f32 v[12:13], v[126:127], s[20:21] op_sel_hi:[1,0]
	s_and_b64 vcc, exec, s[2:3]
	v_pk_mul_f32 v[14:15], v[122:123], s[20:21] op_sel_hi:[1,0]
	s_cbranch_vccnz .LBB0_2106
	v_mul_f32_e32 v7, 0x3d372713, v14
	v_mul_f32_e32 v7, v14, v7
	v_mul_f32_e32 v16, 0x3d372713, v13
	v_fma_f32 v7, v14, v7, v14
	v_mul_f32_e32 v16, v13, v16
	v_mov_b32_e32 v17, v13
	v_mul_f32_e32 v7, 0xc0135761, v7
	v_fmac_f32_e32 v17, v17, v16
	v_exp_f32_e32 v7, v7
	v_mul_f32_e32 v16, 0xc0135761, v17
	v_exp_f32_e32 v17, v16
	v_mul_f32_e32 v20, 0x3d372713, v9
	v_add_f32_e32 v7, 1.0, v7
	v_rcp_f32_e32 v16, v7
	v_add_f32_e32 v7, 1.0, v17
	v_mul_f32_e32 v17, 0x3d372713, v15
	v_mul_f32_e32 v20, v9, v20
	v_mul_f32_e32 v17, v15, v17
	v_mov_b32_e32 v18, v15
	v_fma_f32 v20, v9, v20, v9
	v_fmac_f32_e32 v18, v18, v17
	v_mul_f32_e32 v19, 0x3d372713, v10
	v_mul_f32_e32 v20, 0xc0135761, v20
	v_mul_f32_e32 v6, 0x3d372713, v12
	v_mul_f32_e32 v17, 0xc0135761, v18
	v_mul_f32_e32 v18, 0x3d372713, v8
	v_mul_f32_e32 v19, v10, v19
	v_exp_f32_e32 v21, v20
	v_mul_f32_e32 v20, 0x3d372713, v11
	v_mul_f32_e32 v6, v12, v6
	v_mul_f32_e32 v18, v8, v18
	v_fma_f32 v19, v10, v19, v10
	v_mul_f32_e32 v20, v11, v20
	v_fma_f32 v6, v12, v6, v12
	v_fma_f32 v18, v8, v18, v8
	v_mul_f32_e32 v19, 0xc0135761, v19
	v_fma_f32 v20, v11, v20, v11
	v_mul_f32_e32 v6, 0xc0135761, v6
	v_mul_f32_e32 v18, 0xc0135761, v18
	v_exp_f32_e32 v19, v19
	v_mul_f32_e32 v20, 0xc0135761, v20
	v_exp_f32_e32 v6, v6
	v_exp_f32_e32 v17, v17
	v_exp_f32_e32 v18, v18
	v_exp_f32_e32 v22, v20
	v_add_f32_e32 v19, 1.0, v19
	v_add_f32_e32 v6, 1.0, v6
	v_add_f32_e32 v17, 1.0, v17
	v_add_f32_e32 v18, 1.0, v18
	v_rcp_f32_e32 v20, v19
	v_add_f32_e32 v19, 1.0, v21
	v_add_f32_e32 v21, 1.0, v22
	v_rcp_f32_e32 v6, v6
	v_rcp_f32_e32 v7, v7
	v_rcp_f32_e32 v18, v18
	v_rcp_f32_e32 v19, v19
	v_rcp_f32_e32 v21, v21
	v_rcp_f32_e32 v17, v17
	v_pk_mul_f32 v[12:13], v[12:13], v[6:7]
	v_pk_mul_f32 v[8:9], v[8:9], v[18:19]
	v_pk_mul_f32 v[10:11], v[10:11], v[20:21]
	v_pk_mul_f32 v[14:15], v[14:15], v[16:17]
; __device__ __forceinline__ unsigned cvt_pk_bf16(float lo, float hi) { unsigned r; asm volatile("v_cvt_pk_bf16_f32 %0, %1, %2" : "=v"(r) : "v"(lo), "v"(hi)); return r; }
; __device__ __forceinline__ float gelu_tanh(float x) { const float y = x + 0.044715f * x * x * x; return x * __builtin_amdgcn_rcpf(1.0f + __builtin_amdgcn_exp2f(-2.302208198f * y)); }
;     __device__ __forceinline__ void operator()(const f32x4 (&acc)[2][2][4][2], const Unit& u, int wr, int wc, int fr, int fq) const {
;     ...
;             for (int m = 0; m < 4; ++m) { bf16_t* rowp = O + (size_t)u.ks * ks_stride + (size_t)(row0 + ai * HALF + m * 16) * ldc + col0;
; #pragma unroll
;                 for (int bj = 0; bj < 2; ++bj) { f32x4 v0 = acc[ai][bj][m][0] * ascale, v1 = acc[ai][bj][m][1] * ascale;
;                     if (act) {
; #pragma unroll
;                         for (int j = 0; j < 4; ++j) { v0[j] = gelu_tanh(v0[j]); v1[j] = gelu_tanh(v1[j]); } }
;                     u32x4 w; w.x = cvt_pk_bf16(v0[0], v0[1]); w.y = cvt_pk_bf16(v0[2], v0[3]); w.z = cvt_pk_bf16(v1[0], v1[1]); w.w = cvt_pk_bf16(v1[2], v1[3]);
;                     *(u32x4*)(rowp + bj * HALF) = w; } }
.LBB0_2106:
	v_or_b32_e32 v6, 32, v4
	v_ashrrev_i32_e32 v7, 31, v6
	v_lshlrev_b64 v[6:7], 12, v[6:7]
	v_lshl_add_u64 v[6:7], s[36:37], 0, v[6:7]
	v_lshl_add_u64 v[6:7], v[2:3], 1, v[6:7]
	v_cvt_pk_bf16_f32 v12, v12, v13
	v_cvt_pk_bf16_f32 v13, v8, v9
	v_cvt_pk_bf16_f32 v14, v14, v15
	v_cvt_pk_bf16_f32 v15, v10, v11
	global_store_dwordx4 v[6:7], v[12:15], off sc0 sc1
	v_pk_mul_f32 v[8:9], v[120:121], s[20:21] op_sel_hi:[1,0]
	v_pk_mul_f32 v[10:11], v[116:117], s[20:21] op_sel_hi:[1,0]
	v_pk_mul_f32 v[12:13], v[118:119], s[20:21] op_sel_hi:[1,0]
	s_and_b64 vcc, exec, s[2:3]
	v_pk_mul_f32 v[14:15], v[114:115], s[20:21] op_sel_hi:[1,0]
	s_cbranch_vccnz .LBB0_2108
	v_mul_f32_e32 v17, 0x3d372713, v14
	v_mul_f32_e32 v17, v14, v17
	v_mul_f32_e32 v18, 0x3d372713, v13
	v_fma_f32 v17, v14, v17, v14
	v_mul_f32_e32 v18, v13, v18
	v_mov_b32_e32 v19, v13
	v_mul_f32_e32 v17, 0xc0135761, v17
	v_fmac_f32_e32 v19, v19, v18
	v_exp_f32_e32 v17, v17
	v_mul_f32_e32 v18, 0xc0135761, v19
	v_exp_f32_e32 v19, v18
	v_mul_f32_e32 v22, 0x3d372713, v9
	v_add_f32_e32 v17, 1.0, v17
	v_rcp_f32_e32 v18, v17
	v_add_f32_e32 v17, 1.0, v19
	v_mul_f32_e32 v19, 0x3d372713, v15
	v_mul_f32_e32 v22, v9, v22
	v_mul_f32_e32 v19, v15, v19
	v_mov_b32_e32 v20, v15
	v_fma_f32 v22, v9, v22, v9
	v_fmac_f32_e32 v20, v20, v19
	v_mul_f32_e32 v21, 0x3d372713, v10
	v_mul_f32_e32 v22, 0xc0135761, v22
	v_mul_f32_e32 v16, 0x3d372713, v12
	v_mul_f32_e32 v19, 0xc0135761, v20
	v_mul_f32_e32 v20, 0x3d372713, v8
	v_mul_f32_e32 v21, v10, v21
	v_exp_f32_e32 v23, v22
	v_mul_f32_e32 v22, 0x3d372713, v11
	v_mul_f32_e32 v16, v12, v16
	v_mul_f32_e32 v20, v8, v20
	v_fma_f32 v21, v10, v21, v10
	v_mul_f32_e32 v22, v11, v22
	v_fma_f32 v16, v12, v16, v12
	v_fma_f32 v20, v8, v20, v8
	v_mul_f32_e32 v21, 0xc0135761, v21
	v_fma_f32 v22, v11, v22, v11
	v_mul_f32_e32 v16, 0xc0135761, v16
	v_mul_f32_e32 v20, 0xc0135761, v20
	v_exp_f32_e32 v21, v21
	v_mul_f32_e32 v22, 0xc0135761, v22
	v_exp_f32_e32 v16, v16
	v_exp_f32_e32 v19, v19
	v_exp_f32_e32 v20, v20
	v_exp_f32_e32 v24, v22
	v_add_f32_e32 v21, 1.0, v21
	v_add_f32_e32 v16, 1.0, v16
	v_add_f32_e32 v19, 1.0, v19
	v_add_f32_e32 v20, 1.0, v20
	v_rcp_f32_e32 v22, v21
	v_add_f32_e32 v21, 1.0, v23
	v_add_f32_e32 v23, 1.0, v24
	v_rcp_f32_e32 v16, v16
	v_rcp_f32_e32 v17, v17
	v_rcp_f32_e32 v20, v20
	v_rcp_f32_e32 v21, v21
	v_rcp_f32_e32 v23, v23
	v_rcp_f32_e32 v19, v19
	v_pk_mul_f32 v[12:13], v[12:13], v[16:17]
	v_pk_mul_f32 v[8:9], v[8:9], v[20:21]
	v_pk_mul_f32 v[10:11], v[10:11], v[22:23]
	v_pk_mul_f32 v[14:15], v[14:15], v[18:19]
.LBB0_2108:
	v_cvt_pk_bf16_f32 v12, v12, v13
	v_cvt_pk_bf16_f32 v13, v8, v9
	s_nop 0
	v_cvt_pk_bf16_f32 v14, v14, v15
	v_cvt_pk_bf16_f32 v15, v10, v11
	global_store_dwordx4 v[6:7], v[12:15], off offset:256 sc0 sc1
	v_pk_mul_f32 v[8:9], v[112:113], s[20:21] op_sel_hi:[1,0]
	v_pk_mul_f32 v[10:11], v[108:109], s[20:21] op_sel_hi:[1,0]
	v_pk_mul_f32 v[12:13], v[110:111], s[20:21] op_sel_hi:[1,0]
	s_and_b64 vcc, exec, s[2:3]
	v_pk_mul_f32 v[14:15], v[106:107], s[20:21] op_sel_hi:[1,0]
	s_cbranch_vccnz .LBB0_2110
	v_mul_f32_e32 v7, 0x3d372713, v14
	v_mul_f32_e32 v7, v14, v7
	v_mul_f32_e32 v16, 0x3d372713, v13
	v_fma_f32 v7, v14, v7, v14
	v_mul_f32_e32 v16, v13, v16
	v_mov_b32_e32 v17, v13
	v_mul_f32_e32 v7, 0xc0135761, v7
	v_fmac_f32_e32 v17, v17, v16
	v_exp_f32_e32 v7, v7
	v_mul_f32_e32 v16, 0xc0135761, v17
	v_exp_f32_e32 v17, v16
	v_mul_f32_e32 v20, 0x3d372713, v9
	v_add_f32_e32 v7, 1.0, v7
	v_rcp_f32_e32 v16, v7
	v_add_f32_e32 v7, 1.0, v17
	v_mul_f32_e32 v17, 0x3d372713, v15
	v_mul_f32_e32 v20, v9, v20
	v_mul_f32_e32 v17, v15, v17
	v_mov_b32_e32 v18, v15
	v_fma_f32 v20, v9, v20, v9
	v_fmac_f32_e32 v18, v18, v17
	v_mul_f32_e32 v19, 0x3d372713, v10
	v_mul_f32_e32 v20, 0xc0135761, v20
	v_mul_f32_e32 v6, 0x3d372713, v12
	v_mul_f32_e32 v17, 0xc0135761, v18
	v_mul_f32_e32 v18, 0x3d372713, v8
	v_mul_f32_e32 v19, v10, v19
	v_exp_f32_e32 v21, v20
	v_mul_f32_e32 v20, 0x3d372713, v11
	v_mul_f32_e32 v6, v12, v6
	v_mul_f32_e32 v18, v8, v18
	v_fma_f32 v19, v10, v19, v10
	v_mul_f32_e32 v20, v11, v20
	v_fma_f32 v6, v12, v6, v12
	v_fma_f32 v18, v8, v18, v8
	v_mul_f32_e32 v19, 0xc0135761, v19
	v_fma_f32 v20, v11, v20, v11
	v_mul_f32_e32 v6, 0xc0135761, v6
	v_mul_f32_e32 v18, 0xc0135761, v18
	v_exp_f32_e32 v19, v19
	v_mul_f32_e32 v20, 0xc0135761, v20
	v_exp_f32_e32 v6, v6
	v_exp_f32_e32 v17, v17
	v_exp_f32_e32 v18, v18
	v_exp_f32_e32 v22, v20
	v_add_f32_e32 v19, 1.0, v19
	v_add_f32_e32 v6, 1.0, v6
	v_add_f32_e32 v17, 1.0, v17
	v_add_f32_e32 v18, 1.0, v18
	v_rcp_f32_e32 v20, v19
	v_add_f32_e32 v19, 1.0, v21
	v_add_f32_e32 v21, 1.0, v22
	v_rcp_f32_e32 v6, v6
	v_rcp_f32_e32 v7, v7
	v_rcp_f32_e32 v18, v18
	v_rcp_f32_e32 v19, v19
	v_rcp_f32_e32 v21, v21
	v_rcp_f32_e32 v17, v17
	v_pk_mul_f32 v[12:13], v[12:13], v[6:7]
	v_pk_mul_f32 v[8:9], v[8:9], v[18:19]
	v_pk_mul_f32 v[10:11], v[10:11], v[20:21]
	v_pk_mul_f32 v[14:15], v[14:15], v[16:17]
; __device__ __forceinline__ unsigned cvt_pk_bf16(float lo, float hi) { unsigned r; asm volatile("v_cvt_pk_bf16_f32 %0, %1, %2" : "=v"(r) : "v"(lo), "v"(hi)); return r; }
; __device__ __forceinline__ float gelu_tanh(float x) { const float y = x + 0.044715f * x * x * x; return x * __builtin_amdgcn_rcpf(1.0f + __builtin_amdgcn_exp2f(-2.302208198f * y)); }
;     __device__ __forceinline__ void operator()(const f32x4 (&acc)[2][2][4][2], const Unit& u, int wr, int wc, int fr, int fq) const {
;     ...
;             for (int m = 0; m < 4; ++m) { bf16_t* rowp = O + (size_t)u.ks * ks_stride + (size_t)(row0 + ai * HALF + m * 16) * ldc + col0;
; #pragma unroll
;                 for (int bj = 0; bj < 2; ++bj) { f32x4 v0 = acc[ai][bj][m][0] * ascale, v1 = acc[ai][bj][m][1] * ascale;
;                     if (act) {
; #pragma unroll
;                         for (int j = 0; j < 4; ++j) { v0[j] = gelu_tanh(v0[j]); v1[j] = gelu_tanh(v1[j]); } }
;                     u32x4 w; w.x = cvt_pk_bf16(v0[0], v0[1]); w.y = cvt_pk_bf16(v0[2], v0[3]); w.z = cvt_pk_bf16(v1[0], v1[1]); w.w = cvt_pk_bf16(v1[2], v1[3]);
;                     *(u32x4*)(rowp + bj * HALF) = w; } }
.LBB0_2110:
	v_or_b32_e32 v6, 48, v4
	v_ashrrev_i32_e32 v7, 31, v6
	v_lshlrev_b64 v[6:7], 12, v[6:7]
	v_lshl_add_u64 v[6:7], s[36:37], 0, v[6:7]
	v_lshl_add_u64 v[6:7], v[2:3], 1, v[6:7]
	v_cvt_pk_bf16_f32 v12, v12, v13
	v_cvt_pk_bf16_f32 v13, v8, v9
	v_cvt_pk_bf16_f32 v14, v14, v15
	v_cvt_pk_bf16_f32 v15, v10, v11
	global_store_dwordx4 v[6:7], v[12:15], off sc0 sc1
	v_pk_mul_f32 v[8:9], v[104:105], s[20:21] op_sel_hi:[1,0]
	v_pk_mul_f32 v[10:11], v[100:101], s[20:21] op_sel_hi:[1,0]
	v_pk_mul_f32 v[12:13], v[102:103], s[20:21] op_sel_hi:[1,0]
	s_and_b64 vcc, exec, s[2:3]
	v_pk_mul_f32 v[14:15], v[98:99], s[20:21] op_sel_hi:[1,0]
	s_cbranch_vccnz .LBB0_2112
	v_mul_f32_e32 v17, 0x3d372713, v14
	v_mul_f32_e32 v17, v14, v17
	v_mul_f32_e32 v18, 0x3d372713, v13
	v_fma_f32 v17, v14, v17, v14
	v_mul_f32_e32 v18, v13, v18
	v_mov_b32_e32 v19, v13
	v_mul_f32_e32 v17, 0xc0135761, v17
	v_fmac_f32_e32 v19, v19, v18
	v_exp_f32_e32 v17, v17
	v_mul_f32_e32 v18, 0xc0135761, v19
	v_exp_f32_e32 v19, v18
	v_mul_f32_e32 v22, 0x3d372713, v9
	v_add_f32_e32 v17, 1.0, v17
	v_rcp_f32_e32 v18, v17
	v_add_f32_e32 v17, 1.0, v19
	v_mul_f32_e32 v19, 0x3d372713, v15
	v_mul_f32_e32 v22, v9, v22
	v_mul_f32_e32 v19, v15, v19
	v_mov_b32_e32 v20, v15
	v_fma_f32 v22, v9, v22, v9
	v_fmac_f32_e32 v20, v20, v19
	v_mul_f32_e32 v21, 0x3d372713, v10
	v_mul_f32_e32 v22, 0xc0135761, v22
	v_mul_f32_e32 v16, 0x3d372713, v12
	v_mul_f32_e32 v19, 0xc0135761, v20
	v_mul_f32_e32 v20, 0x3d372713, v8
	v_mul_f32_e32 v21, v10, v21
	v_exp_f32_e32 v23, v22
	v_mul_f32_e32 v22, 0x3d372713, v11
	v_mul_f32_e32 v16, v12, v16
	v_mul_f32_e32 v20, v8, v20
	v_fma_f32 v21, v10, v21, v10
	v_mul_f32_e32 v22, v11, v22
	v_fma_f32 v16, v12, v16, v12
	v_fma_f32 v20, v8, v20, v8
	v_mul_f32_e32 v21, 0xc0135761, v21
	v_fma_f32 v22, v11, v22, v11
	v_mul_f32_e32 v16, 0xc0135761, v16
	v_mul_f32_e32 v20, 0xc0135761, v20
	v_exp_f32_e32 v21, v21
	v_mul_f32_e32 v22, 0xc0135761, v22
	v_exp_f32_e32 v16, v16
	v_exp_f32_e32 v19, v19
	v_exp_f32_e32 v20, v20
	v_exp_f32_e32 v24, v22
	v_add_f32_e32 v21, 1.0, v21
	v_add_f32_e32 v16, 1.0, v16
	v_add_f32_e32 v19, 1.0, v19
	v_add_f32_e32 v20, 1.0, v20
	v_rcp_f32_e32 v22, v21
	v_add_f32_e32 v21, 1.0, v23
	v_add_f32_e32 v23, 1.0, v24
	v_rcp_f32_e32 v16, v16
	v_rcp_f32_e32 v17, v17
	v_rcp_f32_e32 v20, v20
	v_rcp_f32_e32 v21, v21
	v_rcp_f32_e32 v23, v23
	v_rcp_f32_e32 v19, v19
	v_pk_mul_f32 v[12:13], v[12:13], v[16:17]
	v_pk_mul_f32 v[8:9], v[8:9], v[20:21]
	v_pk_mul_f32 v[10:11], v[10:11], v[22:23]
	v_pk_mul_f32 v[14:15], v[14:15], v[18:19]
.LBB0_2112:
	v_cvt_pk_bf16_f32 v12, v12, v13
	v_cvt_pk_bf16_f32 v13, v8, v9
	s_nop 0
	v_cvt_pk_bf16_f32 v14, v14, v15
	v_cvt_pk_bf16_f32 v15, v10, v11
	global_store_dwordx4 v[6:7], v[12:15], off offset:256 sc0 sc1
	v_pk_mul_f32 v[8:9], v[96:97], s[20:21] op_sel_hi:[1,0]
	v_pk_mul_f32 v[10:11], v[92:93], s[20:21] op_sel_hi:[1,0]
	v_pk_mul_f32 v[12:13], v[94:95], s[20:21] op_sel_hi:[1,0]
	s_and_b64 vcc, exec, s[2:3]
	v_pk_mul_f32 v[14:15], v[90:91], s[20:21] op_sel_hi:[1,0]
	s_cbranch_vccnz .LBB0_2114
	v_mul_f32_e32 v7, 0x3d372713, v14
	v_mul_f32_e32 v7, v14, v7
	v_mul_f32_e32 v16, 0x3d372713, v13
	v_fma_f32 v7, v14, v7, v14
	v_mul_f32_e32 v16, v13, v16
	v_mov_b32_e32 v17, v13
	v_mul_f32_e32 v7, 0xc0135761, v7
	v_fmac_f32_e32 v17, v17, v16
	v_exp_f32_e32 v7, v7
	v_mul_f32_e32 v16, 0xc0135761, v17
	v_exp_f32_e32 v17, v16
	v_mul_f32_e32 v20, 0x3d372713, v9
	v_add_f32_e32 v7, 1.0, v7
	v_rcp_f32_e32 v16, v7
	v_add_f32_e32 v7, 1.0, v17
	v_mul_f32_e32 v17, 0x3d372713, v15
	v_mul_f32_e32 v20, v9, v20
	v_mul_f32_e32 v17, v15, v17
	v_mov_b32_e32 v18, v15
	v_fma_f32 v20, v9, v20, v9
	v_fmac_f32_e32 v18, v18, v17
	v_mul_f32_e32 v19, 0x3d372713, v10
	v_mul_f32_e32 v20, 0xc0135761, v20
	v_mul_f32_e32 v6, 0x3d372713, v12
	v_mul_f32_e32 v17, 0xc0135761, v18
	v_mul_f32_e32 v18, 0x3d372713, v8
	v_mul_f32_e32 v19, v10, v19
	v_exp_f32_e32 v21, v20
	v_mul_f32_e32 v20, 0x3d372713, v11
	v_mul_f32_e32 v6, v12, v6
	v_mul_f32_e32 v18, v8, v18
	v_fma_f32 v19, v10, v19, v10
	v_mul_f32_e32 v20, v11, v20
	v_fma_f32 v6, v12, v6, v12
	v_fma_f32 v18, v8, v18, v8
	v_mul_f32_e32 v19, 0xc0135761, v19
	v_fma_f32 v20, v11, v20, v11
	v_mul_f32_e32 v6, 0xc0135761, v6
	v_mul_f32_e32 v18, 0xc0135761, v18
	v_exp_f32_e32 v19, v19
	v_mul_f32_e32 v20, 0xc0135761, v20
	v_exp_f32_e32 v6, v6
	v_exp_f32_e32 v17, v17
	v_exp_f32_e32 v18, v18
	v_exp_f32_e32 v22, v20
	v_add_f32_e32 v19, 1.0, v19
	v_add_f32_e32 v6, 1.0, v6
	v_add_f32_e32 v17, 1.0, v17
	v_add_f32_e32 v18, 1.0, v18
	v_rcp_f32_e32 v20, v19
	v_add_f32_e32 v19, 1.0, v21
	v_add_f32_e32 v21, 1.0, v22
	v_rcp_f32_e32 v6, v6
	v_rcp_f32_e32 v7, v7
	v_rcp_f32_e32 v18, v18
	v_rcp_f32_e32 v19, v19
	v_rcp_f32_e32 v21, v21
	v_rcp_f32_e32 v17, v17
	v_pk_mul_f32 v[12:13], v[12:13], v[6:7]
	v_pk_mul_f32 v[8:9], v[8:9], v[18:19]
	v_pk_mul_f32 v[10:11], v[10:11], v[20:21]
	v_pk_mul_f32 v[14:15], v[14:15], v[16:17]
; __device__ __forceinline__ unsigned cvt_pk_bf16(float lo, float hi) { unsigned r; asm volatile("v_cvt_pk_bf16_f32 %0, %1, %2" : "=v"(r) : "v"(lo), "v"(hi)); return r; }
; __device__ __forceinline__ float gelu_tanh(float x) { const float y = x + 0.044715f * x * x * x; return x * __builtin_amdgcn_rcpf(1.0f + __builtin_amdgcn_exp2f(-2.302208198f * y)); }
;     __device__ __forceinline__ void operator()(const f32x4 (&acc)[2][2][4][2], const Unit& u, int wr, int wc, int fr, int fq) const {
;     ...
;             for (int m = 0; m < 4; ++m) { bf16_t* rowp = O + (size_t)u.ks * ks_stride + (size_t)(row0 + ai * HALF + m * 16) * ldc + col0;
; #pragma unroll
;                 for (int bj = 0; bj < 2; ++bj) { f32x4 v0 = acc[ai][bj][m][0] * ascale, v1 = acc[ai][bj][m][1] * ascale;
;                     if (act) {
; #pragma unroll
;                         for (int j = 0; j < 4; ++j) { v0[j] = gelu_tanh(v0[j]); v1[j] = gelu_tanh(v1[j]); } }
;                     u32x4 w; w.x = cvt_pk_bf16(v0[0], v0[1]); w.y = cvt_pk_bf16(v0[2], v0[3]); w.z = cvt_pk_bf16(v1[0], v1[1]); w.w = cvt_pk_bf16(v1[2], v1[3]);
;                     *(u32x4*)(rowp + bj * HALF) = w; } }
.LBB0_2114:
	v_lshlrev_b64 v[6:7], 12, v[4:5]
	v_lshl_add_u64 v[6:7], s[36:37], 0, v[6:7]
	v_lshl_add_u64 v[6:7], v[2:3], 1, v[6:7]
	v_cvt_pk_bf16_f32 v12, v12, v13
	v_cvt_pk_bf16_f32 v13, v8, v9
	v_add_co_u32_e32 v8, vcc, s68, v6
	v_cvt_pk_bf16_f32 v14, v14, v15
	v_cvt_pk_bf16_f32 v15, v10, v11
	v_pk_mul_f32 v[10:11], v[84:85], s[20:21] op_sel_hi:[1,0]
	s_nop 0
	v_addc_co_u32_e32 v9, vcc, 0, v7, vcc
	global_store_dwordx4 v[8:9], v[12:15], off sc0 sc1
	v_pk_mul_f32 v[8:9], v[88:89], s[20:21] op_sel_hi:[1,0]
	s_and_b64 vcc, exec, s[2:3]
	v_pk_mul_f32 v[12:13], v[86:87], s[20:21] op_sel_hi:[1,0]
	v_pk_mul_f32 v[14:15], v[82:83], s[20:21] op_sel_hi:[1,0]
	s_cbranch_vccnz .LBB0_2116
	v_mul_f32_e32 v17, 0x3d372713, v14
	v_mul_f32_e32 v17, v14, v17
	v_mul_f32_e32 v18, 0x3d372713, v13
	v_fma_f32 v17, v14, v17, v14
	v_mul_f32_e32 v18, v13, v18
	v_mov_b32_e32 v19, v13
	v_mul_f32_e32 v17, 0xc0135761, v17
	v_fmac_f32_e32 v19, v19, v18
	v_exp_f32_e32 v17, v17
	v_mul_f32_e32 v18, 0xc0135761, v19
	v_exp_f32_e32 v19, v18
	v_mul_f32_e32 v22, 0x3d372713, v9
	v_add_f32_e32 v17, 1.0, v17
	v_rcp_f32_e32 v18, v17
	v_add_f32_e32 v17, 1.0, v19
	v_mul_f32_e32 v19, 0x3d372713, v15
	v_mul_f32_e32 v22, v9, v22
	v_mul_f32_e32 v19, v15, v19
	v_mov_b32_e32 v20, v15
	v_fma_f32 v22, v9, v22, v9
	v_fmac_f32_e32 v20, v20, v19
	v_mul_f32_e32 v21, 0x3d372713, v10
	v_mul_f32_e32 v22, 0xc0135761, v22
	v_mul_f32_e32 v16, 0x3d372713, v12
	v_mul_f32_e32 v19, 0xc0135761, v20
	v_mul_f32_e32 v20, 0x3d372713, v8
	v_mul_f32_e32 v21, v10, v21
	v_exp_f32_e32 v23, v22
	v_mul_f32_e32 v22, 0x3d372713, v11
	v_mul_f32_e32 v16, v12, v16
	v_mul_f32_e32 v20, v8, v20
	v_fma_f32 v21, v10, v21, v10
	v_mul_f32_e32 v22, v11, v22
	v_fma_f32 v16, v12, v16, v12
	v_fma_f32 v20, v8, v20, v8
	v_mul_f32_e32 v21, 0xc0135761, v21
	v_fma_f32 v22, v11, v22, v11
	v_mul_f32_e32 v16, 0xc0135761, v16
	v_mul_f32_e32 v20, 0xc0135761, v20
	v_exp_f32_e32 v21, v21
	v_mul_f32_e32 v22, 0xc0135761, v22
	v_exp_f32_e32 v16, v16
	v_exp_f32_e32 v19, v19
	v_exp_f32_e32 v20, v20
	v_exp_f32_e32 v24, v22
	v_add_f32_e32 v21, 1.0, v21
	v_add_f32_e32 v16, 1.0, v16
	v_add_f32_e32 v19, 1.0, v19
	v_add_f32_e32 v20, 1.0, v20
	v_rcp_f32_e32 v22, v21
	v_add_f32_e32 v21, 1.0, v23
	v_add_f32_e32 v23, 1.0, v24
	v_rcp_f32_e32 v16, v16
	v_rcp_f32_e32 v17, v17
	v_rcp_f32_e32 v20, v20
	v_rcp_f32_e32 v21, v21
	v_rcp_f32_e32 v23, v23
	v_rcp_f32_e32 v19, v19
	v_pk_mul_f32 v[12:13], v[12:13], v[16:17]
	v_pk_mul_f32 v[8:9], v[8:9], v[20:21]
	v_pk_mul_f32 v[10:11], v[10:11], v[22:23]
	v_pk_mul_f32 v[14:15], v[14:15], v[18:19]
.LBB0_2116:
	v_lshl_add_u64 v[16:17], v[6:7], 0, s[22:23]
	v_cvt_pk_bf16_f32 v6, v12, v13
	v_cvt_pk_bf16_f32 v7, v8, v9
	v_cvt_pk_bf16_f32 v8, v14, v15
	v_cvt_pk_bf16_f32 v9, v10, v11
	global_store_dwordx4 v[16:17], v[6:9], off offset:256 sc0 sc1
	v_pk_mul_f32 v[12:13], v[78:79], s[20:21] op_sel_hi:[1,0]
	v_pk_mul_f32 v[10:11], v[76:77], s[20:21] op_sel_hi:[1,0]
	v_pk_mul_f32 v[8:9], v[80:81], s[20:21] op_sel_hi:[1,0]
	s_and_b64 vcc, exec, s[2:3]
	v_pk_mul_f32 v[14:15], v[74:75], s[20:21] op_sel_hi:[1,0]
	s_cbranch_vccnz .LBB0_2118
	v_mul_f32_e32 v7, 0x3d372713, v14
	v_mul_f32_e32 v7, v14, v7
	v_mul_f32_e32 v16, 0x3d372713, v13
	v_fma_f32 v7, v14, v7, v14
	v_mul_f32_e32 v16, v13, v16
	v_mov_b32_e32 v17, v13
	v_mul_f32_e32 v7, 0xc0135761, v7
	v_fmac_f32_e32 v17, v17, v16
	v_exp_f32_e32 v7, v7
	v_mul_f32_e32 v16, 0xc0135761, v17
	v_exp_f32_e32 v17, v16
	v_mul_f32_e32 v20, 0x3d372713, v9
	v_add_f32_e32 v7, 1.0, v7
	v_rcp_f32_e32 v16, v7
	v_add_f32_e32 v7, 1.0, v17
	v_mul_f32_e32 v17, 0x3d372713, v15
	v_mul_f32_e32 v20, v9, v20
	v_mul_f32_e32 v17, v15, v17
	v_mov_b32_e32 v18, v15
	v_fma_f32 v20, v9, v20, v9
	v_fmac_f32_e32 v18, v18, v17
	v_mul_f32_e32 v19, 0x3d372713, v10
	v_mul_f32_e32 v20, 0xc0135761, v20
	v_mul_f32_e32 v6, 0x3d372713, v12
	v_mul_f32_e32 v17, 0xc0135761, v18
	v_mul_f32_e32 v18, 0x3d372713, v8
	v_mul_f32_e32 v19, v10, v19
	v_exp_f32_e32 v21, v20
	v_mul_f32_e32 v20, 0x3d372713, v11
	v_mul_f32_e32 v6, v12, v6
	v_mul_f32_e32 v18, v8, v18
	v_fma_f32 v19, v10, v19, v10
	v_mul_f32_e32 v20, v11, v20
	v_fma_f32 v6, v12, v6, v12
	v_fma_f32 v18, v8, v18, v8
	v_mul_f32_e32 v19, 0xc0135761, v19
	v_fma_f32 v20, v11, v20, v11
	v_mul_f32_e32 v6, 0xc0135761, v6
	v_mul_f32_e32 v18, 0xc0135761, v18
	v_exp_f32_e32 v19, v19
	v_mul_f32_e32 v20, 0xc0135761, v20
	v_exp_f32_e32 v6, v6
	v_exp_f32_e32 v17, v17
	v_exp_f32_e32 v18, v18
	v_exp_f32_e32 v22, v20
	v_add_f32_e32 v19, 1.0, v19
	v_add_f32_e32 v6, 1.0, v6
	v_add_f32_e32 v17, 1.0, v17
	v_add_f32_e32 v18, 1.0, v18
	v_rcp_f32_e32 v20, v19
	v_add_f32_e32 v19, 1.0, v21
	v_add_f32_e32 v21, 1.0, v22
	v_rcp_f32_e32 v6, v6
	v_rcp_f32_e32 v7, v7
	v_rcp_f32_e32 v18, v18
	v_rcp_f32_e32 v19, v19
	v_rcp_f32_e32 v21, v21
	v_rcp_f32_e32 v17, v17
	v_pk_mul_f32 v[12:13], v[12:13], v[6:7]
	v_pk_mul_f32 v[8:9], v[8:9], v[18:19]
	v_pk_mul_f32 v[10:11], v[10:11], v[20:21]
	v_pk_mul_f32 v[14:15], v[14:15], v[16:17]
; __device__ __forceinline__ unsigned cvt_pk_bf16(float lo, float hi) { unsigned r; asm volatile("v_cvt_pk_bf16_f32 %0, %1, %2" : "=v"(r) : "v"(lo), "v"(hi)); return r; }
; __device__ __forceinline__ float gelu_tanh(float x) { const float y = x + 0.044715f * x * x * x; return x * __builtin_amdgcn_rcpf(1.0f + __builtin_amdgcn_exp2f(-2.302208198f * y)); }
;     __device__ __forceinline__ void operator()(const f32x4 (&acc)[2][2][4][2], const Unit& u, int wr, int wc, int fr, int fq) const {
;     ...
;             for (int m = 0; m < 4; ++m) { bf16_t* rowp = O + (size_t)u.ks * ks_stride + (size_t)(row0 + ai * HALF + m * 16) * ldc + col0;
; #pragma unroll
;                 for (int bj = 0; bj < 2; ++bj) { f32x4 v0 = acc[ai][bj][m][0] * ascale, v1 = acc[ai][bj][m][1] * ascale;
;                     if (act) {
; #pragma unroll
;                         for (int j = 0; j < 4; ++j) { v0[j] = gelu_tanh(v0[j]); v1[j] = gelu_tanh(v1[j]); } }
;                     u32x4 w; w.x = cvt_pk_bf16(v0[0], v0[1]); w.y = cvt_pk_bf16(v0[2], v0[3]); w.z = cvt_pk_bf16(v1[0], v1[1]); w.w = cvt_pk_bf16(v1[2], v1[3]);
;                     *(u32x4*)(rowp + bj * HALF) = w; } }
.LBB0_2118:
	v_lshlrev_b64 v[6:7], 12, v[4:5]
	v_lshl_add_u64 v[6:7], s[36:37], 0, v[6:7]
	v_lshl_add_u64 v[6:7], v[2:3], 1, v[6:7]
	v_cvt_pk_bf16_f32 v12, v12, v13
	v_cvt_pk_bf16_f32 v13, v8, v9
	v_add_co_u32_e32 v8, vcc, s69, v6
	v_cvt_pk_bf16_f32 v14, v14, v15
	v_cvt_pk_bf16_f32 v15, v10, v11
	v_pk_mul_f32 v[10:11], v[68:69], s[20:21] op_sel_hi:[1,0]
	s_nop 0
	v_addc_co_u32_e32 v9, vcc, 0, v7, vcc
	global_store_dwordx4 v[8:9], v[12:15], off sc0 sc1
	v_pk_mul_f32 v[8:9], v[72:73], s[20:21] op_sel_hi:[1,0]
	s_and_b64 vcc, exec, s[2:3]
	v_pk_mul_f32 v[12:13], v[70:71], s[20:21] op_sel_hi:[1,0]
	v_pk_mul_f32 v[14:15], v[66:67], s[20:21] op_sel_hi:[1,0]
	s_cbranch_vccnz .LBB0_2120
	v_mul_f32_e32 v17, 0x3d372713, v14
	v_mul_f32_e32 v17, v14, v17
	v_mul_f32_e32 v18, 0x3d372713, v13
	v_fma_f32 v17, v14, v17, v14
	v_mul_f32_e32 v18, v13, v18
	v_mov_b32_e32 v19, v13
	v_mul_f32_e32 v17, 0xc0135761, v17
	v_fmac_f32_e32 v19, v19, v18
	v_exp_f32_e32 v17, v17
	v_mul_f32_e32 v18, 0xc0135761, v19
	v_exp_f32_e32 v19, v18
	v_mul_f32_e32 v22, 0x3d372713, v9
	v_add_f32_e32 v17, 1.0, v17
	v_rcp_f32_e32 v18, v17
	v_add_f32_e32 v17, 1.0, v19
	v_mul_f32_e32 v19, 0x3d372713, v15
	v_mul_f32_e32 v22, v9, v22
	v_mul_f32_e32 v19, v15, v19
	v_mov_b32_e32 v20, v15
	v_fma_f32 v22, v9, v22, v9
	v_fmac_f32_e32 v20, v20, v19
	v_mul_f32_e32 v21, 0x3d372713, v10
	v_mul_f32_e32 v22, 0xc0135761, v22
	v_mul_f32_e32 v16, 0x3d372713, v12
	v_mul_f32_e32 v19, 0xc0135761, v20
	v_mul_f32_e32 v20, 0x3d372713, v8
	v_mul_f32_e32 v21, v10, v21
	v_exp_f32_e32 v23, v22
	v_mul_f32_e32 v22, 0x3d372713, v11
	v_mul_f32_e32 v16, v12, v16
	v_mul_f32_e32 v20, v8, v20
	v_fma_f32 v21, v10, v21, v10
	v_mul_f32_e32 v22, v11, v22
	v_fma_f32 v16, v12, v16, v12
	v_fma_f32 v20, v8, v20, v8
	v_mul_f32_e32 v21, 0xc0135761, v21
	v_fma_f32 v22, v11, v22, v11
	v_mul_f32_e32 v16, 0xc0135761, v16
	v_mul_f32_e32 v20, 0xc0135761, v20
	v_exp_f32_e32 v21, v21
	v_mul_f32_e32 v22, 0xc0135761, v22
	v_exp_f32_e32 v16, v16
	v_exp_f32_e32 v19, v19
	v_exp_f32_e32 v20, v20
	v_exp_f32_e32 v24, v22
	v_add_f32_e32 v21, 1.0, v21
	v_add_f32_e32 v16, 1.0, v16
	v_add_f32_e32 v19, 1.0, v19
	v_add_f32_e32 v20, 1.0, v20
	v_rcp_f32_e32 v22, v21
	v_add_f32_e32 v21, 1.0, v23
	v_add_f32_e32 v23, 1.0, v24
	v_rcp_f32_e32 v16, v16
	v_rcp_f32_e32 v17, v17
	v_rcp_f32_e32 v20, v20
	v_rcp_f32_e32 v21, v21
	v_rcp_f32_e32 v23, v23
	v_rcp_f32_e32 v19, v19
	v_pk_mul_f32 v[12:13], v[12:13], v[16:17]
	v_pk_mul_f32 v[8:9], v[8:9], v[20:21]
	v_pk_mul_f32 v[10:11], v[10:11], v[22:23]
	v_pk_mul_f32 v[14:15], v[14:15], v[18:19]
.LBB0_2120:
	v_lshl_add_u64 v[16:17], v[6:7], 0, s[24:25]
	v_cvt_pk_bf16_f32 v6, v12, v13
	v_cvt_pk_bf16_f32 v7, v8, v9
	v_cvt_pk_bf16_f32 v8, v14, v15
	v_cvt_pk_bf16_f32 v9, v10, v11
	global_store_dwordx4 v[16:17], v[6:9], off offset:256 sc0 sc1
	v_pk_mul_f32 v[12:13], v[62:63], s[20:21] op_sel_hi:[1,0]
	v_pk_mul_f32 v[10:11], v[60:61], s[20:21] op_sel_hi:[1,0]
	v_pk_mul_f32 v[8:9], v[64:65], s[20:21] op_sel_hi:[1,0]
	s_and_b64 vcc, exec, s[2:3]
	v_pk_mul_f32 v[14:15], v[58:59], s[20:21] op_sel_hi:[1,0]
	s_cbranch_vccnz .LBB0_2122
	v_mul_f32_e32 v7, 0x3d372713, v14
	v_mul_f32_e32 v7, v14, v7
	v_mul_f32_e32 v16, 0x3d372713, v13
	v_fma_f32 v7, v14, v7, v14
	v_mul_f32_e32 v16, v13, v16
	v_mov_b32_e32 v17, v13
	v_mul_f32_e32 v7, 0xc0135761, v7
	v_fmac_f32_e32 v17, v17, v16
	v_exp_f32_e32 v7, v7
	v_mul_f32_e32 v16, 0xc0135761, v17
	v_exp_f32_e32 v17, v16
	v_mul_f32_e32 v20, 0x3d372713, v9
	v_add_f32_e32 v7, 1.0, v7
	v_rcp_f32_e32 v16, v7
	v_add_f32_e32 v7, 1.0, v17
	v_mul_f32_e32 v17, 0x3d372713, v15
	v_mul_f32_e32 v20, v9, v20
	v_mul_f32_e32 v17, v15, v17
	v_mov_b32_e32 v18, v15
	v_fma_f32 v20, v9, v20, v9
	v_fmac_f32_e32 v18, v18, v17
	v_mul_f32_e32 v19, 0x3d372713, v10
	v_mul_f32_e32 v20, 0xc0135761, v20
	v_mul_f32_e32 v6, 0x3d372713, v12
	v_mul_f32_e32 v17, 0xc0135761, v18
	v_mul_f32_e32 v18, 0x3d372713, v8
	v_mul_f32_e32 v19, v10, v19
	v_exp_f32_e32 v21, v20
	v_mul_f32_e32 v20, 0x3d372713, v11
	v_mul_f32_e32 v6, v12, v6
	v_mul_f32_e32 v18, v8, v18
	v_fma_f32 v19, v10, v19, v10
	v_mul_f32_e32 v20, v11, v20
	v_fma_f32 v6, v12, v6, v12
	v_fma_f32 v18, v8, v18, v8
	v_mul_f32_e32 v19, 0xc0135761, v19
	v_fma_f32 v20, v11, v20, v11
	v_mul_f32_e32 v6, 0xc0135761, v6
	v_mul_f32_e32 v18, 0xc0135761, v18
	v_exp_f32_e32 v19, v19
	v_mul_f32_e32 v20, 0xc0135761, v20
	v_exp_f32_e32 v6, v6
	v_exp_f32_e32 v17, v17
	v_exp_f32_e32 v18, v18
	v_exp_f32_e32 v22, v20
	v_add_f32_e32 v19, 1.0, v19
	v_add_f32_e32 v6, 1.0, v6
	v_add_f32_e32 v17, 1.0, v17
	v_add_f32_e32 v18, 1.0, v18
	v_rcp_f32_e32 v20, v19
	v_add_f32_e32 v19, 1.0, v21
	v_add_f32_e32 v21, 1.0, v22
	v_rcp_f32_e32 v6, v6
	v_rcp_f32_e32 v7, v7
	v_rcp_f32_e32 v18, v18
	v_rcp_f32_e32 v19, v19
	v_rcp_f32_e32 v21, v21
	v_rcp_f32_e32 v17, v17
	v_pk_mul_f32 v[12:13], v[12:13], v[6:7]
	v_pk_mul_f32 v[8:9], v[8:9], v[18:19]
	v_pk_mul_f32 v[10:11], v[10:11], v[20:21]
	v_pk_mul_f32 v[14:15], v[14:15], v[16:17]
; __device__ __forceinline__ unsigned cvt_pk_bf16(float lo, float hi) { unsigned r; asm volatile("v_cvt_pk_bf16_f32 %0, %1, %2" : "=v"(r) : "v"(lo), "v"(hi)); return r; }
; __device__ __forceinline__ float gelu_tanh(float x) { const float y = x + 0.044715f * x * x * x; return x * __builtin_amdgcn_rcpf(1.0f + __builtin_amdgcn_exp2f(-2.302208198f * y)); }
;     __device__ __forceinline__ void operator()(const f32x4 (&acc)[2][2][4][2], const Unit& u, int wr, int wc, int fr, int fq) const {
;     ...
;             for (int m = 0; m < 4; ++m) { bf16_t* rowp = O + (size_t)u.ks * ks_stride + (size_t)(row0 + ai * HALF + m * 16) * ldc + col0;
; #pragma unroll
;                 for (int bj = 0; bj < 2; ++bj) { f32x4 v0 = acc[ai][bj][m][0] * ascale, v1 = acc[ai][bj][m][1] * ascale;
;                     if (act) {
; #pragma unroll
;                         for (int j = 0; j < 4; ++j) { v0[j] = gelu_tanh(v0[j]); v1[j] = gelu_tanh(v1[j]); } }
;                     u32x4 w; w.x = cvt_pk_bf16(v0[0], v0[1]); w.y = cvt_pk_bf16(v0[2], v0[3]); w.z = cvt_pk_bf16(v1[0], v1[1]); w.w = cvt_pk_bf16(v1[2], v1[3]);
;                     *(u32x4*)(rowp + bj * HALF) = w; } }
.LBB0_2122:
	v_lshlrev_b64 v[6:7], 12, v[4:5]
	v_lshl_add_u64 v[6:7], s[36:37], 0, v[6:7]
	v_lshl_add_u64 v[6:7], v[2:3], 1, v[6:7]
	v_cvt_pk_bf16_f32 v12, v12, v13
	v_cvt_pk_bf16_f32 v13, v8, v9
	v_add_co_u32_e32 v8, vcc, s70, v6
	v_cvt_pk_bf16_f32 v14, v14, v15
	v_cvt_pk_bf16_f32 v15, v10, v11
	v_pk_mul_f32 v[10:11], v[52:53], s[20:21] op_sel_hi:[1,0]
	s_nop 0
	v_addc_co_u32_e32 v9, vcc, 0, v7, vcc
	global_store_dwordx4 v[8:9], v[12:15], off sc0 sc1
	v_pk_mul_f32 v[8:9], v[56:57], s[20:21] op_sel_hi:[1,0]
	s_and_b64 vcc, exec, s[2:3]
	v_pk_mul_f32 v[12:13], v[54:55], s[20:21] op_sel_hi:[1,0]
	v_pk_mul_f32 v[14:15], v[50:51], s[20:21] op_sel_hi:[1,0]
	s_cbranch_vccnz .LBB0_2124
	v_mul_f32_e32 v17, 0x3d372713, v14
	v_mul_f32_e32 v17, v14, v17
	v_mul_f32_e32 v18, 0x3d372713, v13
	v_fma_f32 v17, v14, v17, v14
	v_mul_f32_e32 v18, v13, v18
	v_mov_b32_e32 v19, v13
	v_mul_f32_e32 v17, 0xc0135761, v17
	v_fmac_f32_e32 v19, v19, v18
	v_exp_f32_e32 v17, v17
	v_mul_f32_e32 v18, 0xc0135761, v19
	v_exp_f32_e32 v19, v18
	v_mul_f32_e32 v22, 0x3d372713, v9
	v_add_f32_e32 v17, 1.0, v17
	v_rcp_f32_e32 v18, v17
	v_add_f32_e32 v17, 1.0, v19
	v_mul_f32_e32 v19, 0x3d372713, v15
	v_mul_f32_e32 v22, v9, v22
	v_mul_f32_e32 v19, v15, v19
	v_mov_b32_e32 v20, v15
	v_fma_f32 v22, v9, v22, v9
	v_fmac_f32_e32 v20, v20, v19
	v_mul_f32_e32 v21, 0x3d372713, v10
	v_mul_f32_e32 v22, 0xc0135761, v22
	v_mul_f32_e32 v16, 0x3d372713, v12
	v_mul_f32_e32 v19, 0xc0135761, v20
	v_mul_f32_e32 v20, 0x3d372713, v8
	v_mul_f32_e32 v21, v10, v21
	v_exp_f32_e32 v23, v22
	v_mul_f32_e32 v22, 0x3d372713, v11
	v_mul_f32_e32 v16, v12, v16
	v_mul_f32_e32 v20, v8, v20
	v_fma_f32 v21, v10, v21, v10
	v_mul_f32_e32 v22, v11, v22
	v_fma_f32 v16, v12, v16, v12
	v_fma_f32 v20, v8, v20, v8
	v_mul_f32_e32 v21, 0xc0135761, v21
	v_fma_f32 v22, v11, v22, v11
	v_mul_f32_e32 v16, 0xc0135761, v16
	v_mul_f32_e32 v20, 0xc0135761, v20
	v_exp_f32_e32 v21, v21
	v_mul_f32_e32 v22, 0xc0135761, v22
	v_exp_f32_e32 v16, v16
	v_exp_f32_e32 v19, v19
	v_exp_f32_e32 v20, v20
	v_exp_f32_e32 v24, v22
	v_add_f32_e32 v21, 1.0, v21
	v_add_f32_e32 v16, 1.0, v16
	v_add_f32_e32 v19, 1.0, v19
	v_add_f32_e32 v20, 1.0, v20
	v_rcp_f32_e32 v22, v21
	v_add_f32_e32 v21, 1.0, v23
	v_add_f32_e32 v23, 1.0, v24
	v_rcp_f32_e32 v16, v16
	v_rcp_f32_e32 v17, v17
	v_rcp_f32_e32 v20, v20
	v_rcp_f32_e32 v21, v21
	v_rcp_f32_e32 v23, v23
	v_rcp_f32_e32 v19, v19
	v_pk_mul_f32 v[12:13], v[12:13], v[16:17]
	v_pk_mul_f32 v[8:9], v[8:9], v[20:21]
	v_pk_mul_f32 v[10:11], v[10:11], v[22:23]
	v_pk_mul_f32 v[14:15], v[14:15], v[18:19]
.LBB0_2124:
	v_lshl_add_u64 v[16:17], v[6:7], 0, s[26:27]
	v_cvt_pk_bf16_f32 v6, v12, v13
	v_cvt_pk_bf16_f32 v7, v8, v9
	v_cvt_pk_bf16_f32 v8, v14, v15
	v_cvt_pk_bf16_f32 v9, v10, v11
	global_store_dwordx4 v[16:17], v[6:9], off offset:256 sc0 sc1
	v_pk_mul_f32 v[10:11], v[46:47], s[20:21] op_sel_hi:[1,0]
	s_and_b64 vcc, exec, s[2:3]
	v_pk_mul_f32 v[6:7], v[48:49], s[20:21] op_sel_hi:[1,0]
	v_pk_mul_f32 v[8:9], v[44:45], s[20:21] op_sel_hi:[1,0]
	v_pk_mul_f32 v[12:13], v[42:43], s[20:21] op_sel_hi:[1,0]
	s_cbranch_vccnz .LBB0_2126
	v_mul_f32_e32 v15, 0x3d372713, v12
	v_mul_f32_e32 v15, v12, v15
	v_mul_f32_e32 v16, 0x3d372713, v11
	v_fma_f32 v15, v12, v15, v12
	v_mul_f32_e32 v16, v11, v16
	v_mov_b32_e32 v17, v11
	v_mul_f32_e32 v15, 0xc0135761, v15
	v_fmac_f32_e32 v17, v17, v16
	v_exp_f32_e32 v15, v15
	v_mul_f32_e32 v16, 0xc0135761, v17
	v_exp_f32_e32 v17, v16
	v_mul_f32_e32 v20, 0x3d372713, v7
	v_add_f32_e32 v15, 1.0, v15
	v_rcp_f32_e32 v16, v15
	v_add_f32_e32 v15, 1.0, v17
	v_mul_f32_e32 v17, 0x3d372713, v13
	v_mul_f32_e32 v20, v7, v20
	v_mul_f32_e32 v17, v13, v17
	v_mov_b32_e32 v18, v13
	v_fma_f32 v20, v7, v20, v7
	v_fmac_f32_e32 v18, v18, v17
	v_mul_f32_e32 v19, 0x3d372713, v8
	v_mul_f32_e32 v20, 0xc0135761, v20
	v_mul_f32_e32 v14, 0x3d372713, v10
	v_mul_f32_e32 v17, 0xc0135761, v18
	v_mul_f32_e32 v18, 0x3d372713, v6
	v_mul_f32_e32 v19, v8, v19
	v_exp_f32_e32 v21, v20
	v_mul_f32_e32 v20, 0x3d372713, v9
	v_mul_f32_e32 v14, v10, v14
	v_mul_f32_e32 v18, v6, v18
	v_fma_f32 v19, v8, v19, v8
	v_mul_f32_e32 v20, v9, v20
	v_fma_f32 v14, v10, v14, v10
	v_fma_f32 v18, v6, v18, v6
	v_mul_f32_e32 v19, 0xc0135761, v19
	v_fma_f32 v20, v9, v20, v9
	v_mul_f32_e32 v14, 0xc0135761, v14
	v_mul_f32_e32 v18, 0xc0135761, v18
	v_exp_f32_e32 v19, v19
	v_mul_f32_e32 v20, 0xc0135761, v20
	v_exp_f32_e32 v14, v14
	v_exp_f32_e32 v17, v17
	v_exp_f32_e32 v18, v18
	v_exp_f32_e32 v22, v20
	v_add_f32_e32 v19, 1.0, v19
	v_add_f32_e32 v14, 1.0, v14
	v_add_f32_e32 v17, 1.0, v17
	v_add_f32_e32 v18, 1.0, v18
	v_rcp_f32_e32 v20, v19
	v_add_f32_e32 v19, 1.0, v21
	v_add_f32_e32 v21, 1.0, v22
	v_rcp_f32_e32 v14, v14
	v_rcp_f32_e32 v15, v15
	v_rcp_f32_e32 v18, v18
	v_rcp_f32_e32 v19, v19
	v_rcp_f32_e32 v21, v21
	v_rcp_f32_e32 v17, v17
	v_pk_mul_f32 v[10:11], v[10:11], v[14:15]
	v_pk_mul_f32 v[6:7], v[6:7], v[18:19]
	v_pk_mul_f32 v[8:9], v[8:9], v[20:21]
	v_pk_mul_f32 v[12:13], v[12:13], v[16:17]
; __device__ __forceinline__ unsigned cvt_pk_bf16(float lo, float hi) { unsigned r; asm volatile("v_cvt_pk_bf16_f32 %0, %1, %2" : "=v"(r) : "v"(lo), "v"(hi)); return r; }
; __device__ __forceinline__ float gelu_tanh(float x) { const float y = x + 0.044715f * x * x * x; return x * __builtin_amdgcn_rcpf(1.0f + __builtin_amdgcn_exp2f(-2.302208198f * y)); }
; #define PG8_BAR __builtin_amdgcn_s_barrier()
;     __device__ __forceinline__ void operator()(const f32x4 (&acc)[2][2][4][2], const Unit& u, int wr, int wc, int fr, int fq) const {
;     ...
;             for (int m = 0; m < 4; ++m) { bf16_t* rowp = O + (size_t)u.ks * ks_stride + (size_t)(row0 + ai * HALF + m * 16) * ldc + col0;
; #pragma unroll
;                 for (int bj = 0; bj < 2; ++bj) { f32x4 v0 = acc[ai][bj][m][0] * ascale, v1 = acc[ai][bj][m][1] * ascale;
;                     if (act) {
; #pragma unroll
;                         for (int j = 0; j < 4; ++j) { v0[j] = gelu_tanh(v0[j]); v1[j] = gelu_tanh(v1[j]); } }
;                     u32x4 w; w.x = cvt_pk_bf16(v0[0], v0[1]); w.y = cvt_pk_bf16(v0[2], v0[3]); w.z = cvt_pk_bf16(v1[0], v1[1]); w.w = cvt_pk_bf16(v1[2], v1[3]);
;                     *(u32x4*)(rowp + bj * HALF) = w; } }
; template <class Epi, class Sched, bool ALIGN_EPI = false, bool SP2 = false, bool FP8 = false>
; __device__ __forceinline__ void gemm_phase(PG8_LAS unsigned char* lds, const Gemm g, const Sched& S, const Epi& E) {
;     ...
;         if constexpr (!Epi::AFTER_DRAIN) { E(acc, cur, wr, wc, fr, fq); S.done(cur); }
;         if (!has_next) break;
; #pragma unroll
;         for (int a = 0; a < 2; ++a)
; #pragma unroll
;             for (int b = 0; b < 2; ++b)
; #pragma unroll
;                 for (int m = 0; m < 4; ++m)
; #pragma unroll
;                     for (int n = 0; n < 2; ++n) acc[a][b][m][n] = (f32x4){0.f, 0.f, 0.f, 0.f};
;         cur = nxt; cA = nA; cB = nB; ++ui;
;         if constexpr (ALIGN_EPI) { if (wr == 1) PG8_BAR; }
.LBB0_2126:
	v_lshlrev_b64 v[4:5], 12, v[4:5]
	v_lshl_add_u64 v[4:5], s[36:37], 0, v[4:5]
	v_lshl_add_u64 v[2:3], v[2:3], 1, v[4:5]
	v_cvt_pk_bf16_f32 v4, v10, v11
	v_cvt_pk_bf16_f32 v5, v6, v7
	v_cvt_pk_bf16_f32 v6, v12, v13
	v_cvt_pk_bf16_f32 v7, v8, v9
	v_add_co_u32_e32 v8, vcc, s71, v2
	v_pk_mul_f32 v[10:11], v[34:35], s[20:21] op_sel_hi:[1,0]
	s_nop 0
	v_addc_co_u32_e32 v9, vcc, 0, v3, vcc
	global_store_dwordx4 v[8:9], v[4:7], off sc0 sc1
	v_pk_mul_f32 v[8:9], v[38:39], s[20:21] op_sel_hi:[1,0]
	s_and_b64 vcc, exec, s[2:3]
	v_pk_mul_f32 v[4:5], v[40:41], s[20:21] op_sel_hi:[1,0]
	v_pk_mul_f32 v[6:7], v[36:37], s[20:21] op_sel_hi:[1,0]
	s_cbranch_vccnz .LBB0_2128
	v_mul_f32_e32 v13, 0x3d372713, v10
	v_mul_f32_e32 v13, v10, v13
	v_mul_f32_e32 v14, 0x3d372713, v9
	v_fma_f32 v13, v10, v13, v10
	v_mul_f32_e32 v14, v9, v14
	v_mov_b32_e32 v15, v9
	v_mul_f32_e32 v13, 0xc0135761, v13
	v_fmac_f32_e32 v15, v15, v14
	v_exp_f32_e32 v13, v13
	v_mul_f32_e32 v14, 0xc0135761, v15
	v_exp_f32_e32 v15, v14
	v_mul_f32_e32 v18, 0x3d372713, v5
	v_add_f32_e32 v13, 1.0, v13
	v_rcp_f32_e32 v14, v13
	v_add_f32_e32 v13, 1.0, v15
	v_mul_f32_e32 v15, 0x3d372713, v11
	v_mul_f32_e32 v18, v5, v18
	v_mul_f32_e32 v15, v11, v15
	v_mov_b32_e32 v16, v11
	v_fma_f32 v18, v5, v18, v5
	v_fmac_f32_e32 v16, v16, v15
	v_mul_f32_e32 v17, 0x3d372713, v6
	v_mul_f32_e32 v18, 0xc0135761, v18
	v_mul_f32_e32 v12, 0x3d372713, v8
	v_mul_f32_e32 v15, 0xc0135761, v16
	v_mul_f32_e32 v16, 0x3d372713, v4
	v_mul_f32_e32 v17, v6, v17
	v_exp_f32_e32 v19, v18
	v_mul_f32_e32 v18, 0x3d372713, v7
	v_mul_f32_e32 v12, v8, v12
	v_mul_f32_e32 v16, v4, v16
	v_fma_f32 v17, v6, v17, v6
	v_mul_f32_e32 v18, v7, v18
	v_fma_f32 v12, v8, v12, v8
	v_fma_f32 v16, v4, v16, v4
	v_mul_f32_e32 v17, 0xc0135761, v17
	v_fma_f32 v18, v7, v18, v7
	v_mul_f32_e32 v12, 0xc0135761, v12
	v_mul_f32_e32 v16, 0xc0135761, v16
	v_exp_f32_e32 v17, v17
	v_mul_f32_e32 v18, 0xc0135761, v18
	v_exp_f32_e32 v12, v12
	v_exp_f32_e32 v15, v15
	v_exp_f32_e32 v16, v16
	v_exp_f32_e32 v20, v18
	v_add_f32_e32 v17, 1.0, v17
	v_add_f32_e32 v12, 1.0, v12
	v_add_f32_e32 v15, 1.0, v15
	v_add_f32_e32 v16, 1.0, v16
	v_rcp_f32_e32 v18, v17
	v_add_f32_e32 v17, 1.0, v19
	v_add_f32_e32 v19, 1.0, v20
	v_rcp_f32_e32 v12, v12
	v_rcp_f32_e32 v13, v13
	v_rcp_f32_e32 v16, v16
	v_rcp_f32_e32 v17, v17
	v_rcp_f32_e32 v19, v19
	v_rcp_f32_e32 v15, v15
	v_pk_mul_f32 v[8:9], v[8:9], v[12:13]
	v_pk_mul_f32 v[4:5], v[4:5], v[16:17]
	v_pk_mul_f32 v[6:7], v[6:7], v[18:19]
	v_pk_mul_f32 v[10:11], v[10:11], v[14:15]
.LBB0_2128:
	v_lshl_add_u64 v[12:13], v[2:3], 0, s[28:29]
	s_and_b64 vcc, exec, s[0:1]
	s_mov_b64 s[0:1], -1
	v_cvt_pk_bf16_f32 v2, v8, v9
	v_cvt_pk_bf16_f32 v3, v4, v5
	v_cvt_pk_bf16_f32 v4, v10, v11
	v_cvt_pk_bf16_f32 v5, v6, v7
	global_store_dwordx4 v[12:13], v[2:5], off offset:256 sc0 sc1
	s_cbranch_vccnz .LBB0_2081
	s_andn2_b64 vcc, exec, s[10:11]
	s_cbranch_vccnz .LBB0_2080
	s_barrier
	s_branch .LBB0_2080
